# E6 plus nt (non-temporal) cache policy on all dwordx4 global stores
# baseline (speedup 1.0000x reference)
.LBB0_65:
	ds_read2_b32 v[214:215], v140 offset1:32
	s_andn2_b64 vcc, exec, s[12:13]
	s_mov_b32 s20, s62
	s_waitcnt vmcnt(0) lgkmcnt(0)
	v_mul_f32_e32 v77, v68, v214
	ds_read_b32 v210, v152
	ds_read_b32 v211, v162
	ds_read_b32 v212, v170
	ds_read_b32 v213, v178
	ds_read_b32 v214, v186
	ds_read_b32 v216, v194
	ds_read_b32 v217, v202
	ds_read_b32 v218, v142
	s_waitcnt lgkmcnt(7)
	v_mul_f32_e32 v210, v69, v210
	v_cvt_pk_bf16_f32 v210, v77, v210
	s_waitcnt lgkmcnt(6)
	v_mul_f32_e32 v77, v70, v211
	s_waitcnt lgkmcnt(5)
	v_mul_f32_e32 v211, v71, v212
	v_cvt_pk_bf16_f32 v211, v77, v211
	s_waitcnt lgkmcnt(4)
	v_mul_f32_e32 v77, v64, v213
	s_waitcnt lgkmcnt(3)
	v_mul_f32_e32 v212, v65, v214
	v_cvt_pk_bf16_f32 v212, v77, v212
	s_waitcnt lgkmcnt(2)
	v_mul_f32_e32 v77, v66, v216
	s_waitcnt lgkmcnt(1)
	v_mul_f32_e32 v213, v67, v217
	v_cvt_pk_bf16_f32 v213, v77, v213
	v_add_u32_e32 v77, s43, v139
	v_mad_i64_i32 v[216:217], s[6:7], s42, v77, 0
	v_lshl_add_u64 v[216:217], v[216:217], 1, s[4:5]
	s_lshl_b64 s[6:7], s[8:9], 1
	v_lshl_add_u64 v[216:217], v[216:217], 0, s[6:7]
	v_lshl_add_u64 v[216:217], v[216:217], 0, v[72:73]
	global_store_dwordx4 v[216:217], v[210:213], off nt
	s_waitcnt lgkmcnt(0)
	v_mul_f32_e32 v77, v68, v218
	ds_read_b32 v210, v153
	ds_read_b32 v211, v163
	ds_read_b32 v212, v171
	ds_read_b32 v213, v179
	ds_read_b32 v214, v187
	ds_read_b32 v216, v195
	ds_read_b32 v217, v203
	ds_read_b32 v218, v144
	s_waitcnt lgkmcnt(7)
	v_mul_f32_e32 v210, v69, v210
	v_cvt_pk_bf16_f32 v210, v77, v210
	s_waitcnt lgkmcnt(6)
	v_mul_f32_e32 v77, v70, v211
	s_waitcnt lgkmcnt(5)
	v_mul_f32_e32 v211, v71, v212
	v_cvt_pk_bf16_f32 v211, v77, v211
	s_waitcnt lgkmcnt(4)
	v_mul_f32_e32 v77, v64, v213
	s_waitcnt lgkmcnt(3)
	v_mul_f32_e32 v212, v65, v214
	v_cvt_pk_bf16_f32 v212, v77, v212
	s_waitcnt lgkmcnt(2)
	v_mul_f32_e32 v77, v66, v216
	s_waitcnt lgkmcnt(1)
	v_mul_f32_e32 v213, v67, v217
	v_cvt_pk_bf16_f32 v213, v77, v213
	v_add_u32_e32 v77, s43, v141
	v_mad_i64_i32 v[216:217], s[8:9], s42, v77, 0
	v_lshl_add_u64 v[216:217], v[216:217], 1, s[4:5]
	v_lshl_add_u64 v[216:217], v[216:217], 0, s[6:7]
	v_lshl_add_u64 v[216:217], v[216:217], 0, v[72:73]
	global_store_dwordx4 v[216:217], v[210:213], off nt
	s_waitcnt lgkmcnt(0)
	v_mul_f32_e32 v77, v68, v218
	ds_read_b32 v210, v154
	ds_read_b32 v211, v164
	ds_read_b32 v212, v172
	ds_read_b32 v213, v180
	ds_read_b32 v214, v188
	ds_read_b32 v216, v196
	ds_read_b32 v217, v204
	ds_read_b32 v218, v145
	s_waitcnt lgkmcnt(7)
	v_mul_f32_e32 v210, v69, v210
	v_cvt_pk_bf16_f32 v210, v77, v210
	s_waitcnt lgkmcnt(6)
	v_mul_f32_e32 v77, v70, v211
	s_waitcnt lgkmcnt(5)
	v_mul_f32_e32 v211, v71, v212
	v_cvt_pk_bf16_f32 v211, v77, v211
	s_waitcnt lgkmcnt(4)
	v_mul_f32_e32 v77, v64, v213
	s_waitcnt lgkmcnt(3)
	v_mul_f32_e32 v212, v65, v214
	v_cvt_pk_bf16_f32 v212, v77, v212
	s_waitcnt lgkmcnt(2)
	v_mul_f32_e32 v77, v66, v216
	s_waitcnt lgkmcnt(1)
	v_mul_f32_e32 v213, v67, v217
	v_cvt_pk_bf16_f32 v213, v77, v213
	v_add_u32_e32 v77, s43, v143
	v_mad_i64_i32 v[216:217], s[8:9], s42, v77, 0
	v_lshl_add_u64 v[216:217], v[216:217], 1, s[4:5]
	v_lshl_add_u64 v[216:217], v[216:217], 0, s[6:7]
	v_lshl_add_u64 v[216:217], v[216:217], 0, v[72:73]
	global_store_dwordx4 v[216:217], v[210:213], off nt
	s_waitcnt lgkmcnt(0)
	v_mul_f32_e32 v77, v68, v218
	ds_read_b32 v210, v156
	ds_read_b32 v211, v165
	ds_read_b32 v212, v173
	ds_read_b32 v213, v181
	ds_read_b32 v214, v189
	ds_read_b32 v216, v197
	ds_read_b32 v217, v205
	ds_read_b32 v218, v158
	s_waitcnt lgkmcnt(7)
	v_mul_f32_e32 v210, v69, v210
	v_cvt_pk_bf16_f32 v210, v77, v210
	s_waitcnt lgkmcnt(6)
	v_mul_f32_e32 v77, v70, v211
	s_waitcnt lgkmcnt(5)
	v_mul_f32_e32 v211, v71, v212
	v_cvt_pk_bf16_f32 v211, v77, v211
	s_waitcnt lgkmcnt(4)
	v_mul_f32_e32 v77, v64, v213
	s_waitcnt lgkmcnt(3)
	v_mul_f32_e32 v212, v65, v214
	v_cvt_pk_bf16_f32 v212, v77, v212
	s_waitcnt lgkmcnt(2)
	v_mul_f32_e32 v77, v66, v216
	s_waitcnt lgkmcnt(1)
	v_mul_f32_e32 v213, v67, v217
	v_cvt_pk_bf16_f32 v213, v77, v213
	v_add_u32_e32 v77, s43, v155
	v_mad_i64_i32 v[216:217], s[8:9], s42, v77, 0
	v_lshl_add_u64 v[216:217], v[216:217], 1, s[4:5]
	v_lshl_add_u64 v[216:217], v[216:217], 0, s[6:7]
	v_lshl_add_u64 v[216:217], v[216:217], 0, v[72:73]
	global_store_dwordx4 v[216:217], v[210:213], off nt
	v_mul_f32_e32 v77, v68, v215
	s_waitcnt lgkmcnt(0)
	v_mul_f32_e32 v210, v69, v218
	v_cvt_pk_bf16_f32 v210, v77, v210
	ds_read_b32 v77, v166
	ds_read_b32 v211, v174
	ds_read_b32 v212, v182
	ds_read_b32 v213, v190
	ds_read_b32 v214, v198
	ds_read_b32 v215, v206
	ds_read_b32 v216, v147
	ds_read_b32 v217, v159
	s_waitcnt lgkmcnt(7)
	v_mul_f32_e32 v77, v70, v77
	s_waitcnt lgkmcnt(6)
	v_mul_f32_e32 v211, v71, v211
	v_cvt_pk_bf16_f32 v211, v77, v211
	s_waitcnt lgkmcnt(5)
	v_mul_f32_e32 v77, v64, v212
	s_waitcnt lgkmcnt(4)
	v_mul_f32_e32 v212, v65, v213
	v_cvt_pk_bf16_f32 v212, v77, v212
	s_waitcnt lgkmcnt(3)
	v_mul_f32_e32 v77, v66, v214
	s_waitcnt lgkmcnt(2)
	v_mul_f32_e32 v213, v67, v215
	v_cvt_pk_bf16_f32 v213, v77, v213
	v_add_u32_e32 v77, s43, v157
	v_mad_i64_i32 v[214:215], s[8:9], s42, v77, 0
	v_lshl_add_u64 v[214:215], v[214:215], 1, s[4:5]
	v_lshl_add_u64 v[214:215], v[214:215], 0, s[6:7]
	v_lshl_add_u64 v[214:215], v[214:215], 0, v[72:73]
	global_store_dwordx4 v[214:215], v[210:213], off nt
	s_waitcnt lgkmcnt(1)
	v_mul_f32_e32 v77, v68, v216
	s_waitcnt lgkmcnt(0)
	v_mul_f32_e32 v210, v69, v217
	v_cvt_pk_bf16_f32 v210, v77, v210
	ds_read_b32 v77, v167
	ds_read_b32 v211, v175
	ds_read_b32 v212, v183
	ds_read_b32 v213, v191
	ds_read_b32 v214, v199
	ds_read_b32 v215, v207
	ds_read_b32 v216, v149
	ds_read_b32 v217, v160
	s_waitcnt lgkmcnt(7)
	v_mul_f32_e32 v77, v70, v77
	s_waitcnt lgkmcnt(6)
	v_mul_f32_e32 v211, v71, v211
	v_cvt_pk_bf16_f32 v211, v77, v211
	s_waitcnt lgkmcnt(5)
	v_mul_f32_e32 v77, v64, v212
	s_waitcnt lgkmcnt(4)
	v_mul_f32_e32 v212, v65, v213
	v_cvt_pk_bf16_f32 v212, v77, v212
	s_waitcnt lgkmcnt(3)
	v_mul_f32_e32 v77, v66, v214
	s_waitcnt lgkmcnt(2)
	v_mul_f32_e32 v213, v67, v215
	v_cvt_pk_bf16_f32 v213, v77, v213
	v_add_u32_e32 v77, s43, v146
	v_mad_i64_i32 v[214:215], s[8:9], s42, v77, 0
	v_lshl_add_u64 v[214:215], v[214:215], 1, s[4:5]
	v_lshl_add_u64 v[214:215], v[214:215], 0, s[6:7]
	v_lshl_add_u64 v[214:215], v[214:215], 0, v[72:73]
	global_store_dwordx4 v[214:215], v[210:213], off nt
	s_waitcnt lgkmcnt(1)
	v_mul_f32_e32 v77, v68, v216
	s_waitcnt lgkmcnt(0)
	v_mul_f32_e32 v210, v69, v217
	v_cvt_pk_bf16_f32 v210, v77, v210
	ds_read_b32 v77, v168
	ds_read_b32 v211, v176
	ds_read_b32 v212, v184
	ds_read_b32 v213, v192
	ds_read_b32 v214, v200
	ds_read_b32 v215, v208
	ds_read_b32 v216, v151
	ds_read_b32 v217, v161
	s_waitcnt lgkmcnt(7)
	v_mul_f32_e32 v77, v70, v77
	s_waitcnt lgkmcnt(6)
	v_mul_f32_e32 v211, v71, v211
	v_cvt_pk_bf16_f32 v211, v77, v211
	s_waitcnt lgkmcnt(5)
	v_mul_f32_e32 v77, v64, v212
	s_waitcnt lgkmcnt(4)
	v_mul_f32_e32 v212, v65, v213
	v_cvt_pk_bf16_f32 v212, v77, v212
	s_waitcnt lgkmcnt(3)
	v_mul_f32_e32 v77, v66, v214
	s_waitcnt lgkmcnt(2)
	v_mul_f32_e32 v213, v67, v215
	v_cvt_pk_bf16_f32 v213, v77, v213
	v_add_u32_e32 v77, s43, v148
	v_mad_i64_i32 v[214:215], s[8:9], s42, v77, 0
	v_lshl_add_u64 v[214:215], v[214:215], 1, s[4:5]
	v_lshl_add_u64 v[214:215], v[214:215], 0, s[6:7]
	v_lshl_add_u64 v[214:215], v[214:215], 0, v[72:73]
	global_store_dwordx4 v[214:215], v[210:213], off nt
	ds_read_b32 v77, v169
	ds_read_b32 v210, v177
	ds_read_b32 v211, v185
	ds_read_b32 v212, v193
	ds_read_b32 v213, v201
	ds_read_b32 v214, v209
	s_waitcnt lgkmcnt(7)
	v_mul_f32_e32 v68, v68, v216
	s_waitcnt lgkmcnt(6)
	v_mul_f32_e32 v69, v69, v217
	v_cvt_pk_bf16_f32 v68, v68, v69
	s_waitcnt lgkmcnt(5)
	v_mul_f32_e32 v69, v70, v77
	s_waitcnt lgkmcnt(4)
	v_mul_f32_e32 v70, v71, v210
	s_waitcnt lgkmcnt(3)
	v_mul_f32_e32 v64, v64, v211
	v_cvt_pk_bf16_f32 v69, v69, v70
	s_waitcnt lgkmcnt(2)
	v_mul_f32_e32 v65, v65, v212
	v_cvt_pk_bf16_f32 v70, v64, v65
	s_waitcnt lgkmcnt(1)
	v_mul_f32_e32 v64, v66, v213
	s_waitcnt lgkmcnt(0)
	v_mul_f32_e32 v65, v67, v214
	v_cvt_pk_bf16_f32 v71, v64, v65
	v_add_u32_e32 v64, s43, v150
	v_mad_i64_i32 v[64:65], s[8:9], s42, v64, 0
	v_lshl_add_u64 v[64:65], v[64:65], 1, s[4:5]
	v_lshl_add_u64 v[64:65], v[64:65], 0, s[6:7]
	v_lshl_add_u64 v[64:65], v[64:65], 0, v[72:73]
	global_store_dwordx4 v[64:65], v[68:71], off nt
	s_waitcnt lgkmcnt(0)
	s_mov_b32 s43, s26
	s_mov_b64 s[4:5], s[14:15]
	s_mov_b64 s[6:7], s[16:17]
	s_mov_b32 s42, s63
	s_mov_b32 s8, s21
	s_cbranch_vccz .LBB0_99

.LBB0_101:
	s_or_b64 exec, exec, s[20:21]
	v_lshlrev_b64 v[6:7], 19, v[6:7]
	v_lshl_add_u64 v[6:7], s[14:15], 0, v[6:7]
	v_lshlrev_b32_e32 v4, 11, v12
	v_add_u32_e32 v11, s23, v11
	v_lshl_add_u64 v[6:7], v[6:7], 0, v[4:5]
	v_lshlrev_b32_e32 v4, 1, v13
	v_cmp_lt_i32_e32 vcc, s26, v11
	v_lshl_add_u64 v[6:7], v[6:7], 0, v[4:5]
	s_or_b64 s[16:17], vcc, s[16:17]
	v_add_u32_e32 v10, s24, v10
	global_store_dwordx4 v[6:7], v[0:3], off nt
	s_andn2_b64 exec, exec, s[16:17]
	s_cbranch_execz .LBB0_104

.LBB0_106:
	v_ashrrev_i32_e32 v3, 13, v8
	v_lshrrev_b32_e32 v0, 7, v8
	v_mul_i32_i24_e32 v10, 0x300, v3
	v_and_or_b32 v0, v0, 63, v2
	v_ashrrev_i32_e32 v11, 31, v10
	v_lshl_add_u64 v[10:11], v[0:1], 0, v[10:11]
	v_and_b32_e32 v12, 0x3f8, v9
	v_add_u32_e32 v8, s23, v8
	v_lshlrev_b64 v[10:11], 11, v[10:11]
	v_cmp_lt_i32_e32 vcc, s13, v8
	v_lshlrev_b32_e32 v0, 1, v12
	v_lshl_add_u64 v[10:11], s[6:7], 0, v[10:11]
	v_add_u32_e32 v9, s12, v9
	s_or_b64 s[8:9], vcc, s[8:9]
	v_lshl_add_u64 v[10:11], v[10:11], 0, v[0:1]
	global_store_dwordx4 v[10:11], v[4:7], off nt
	s_andn2_b64 exec, exec, s[8:9]
	s_cbranch_execnz .LBB0_106

.LBB0_262:
	v_lshl_add_u32 v150, s28, 8, v147
	v_ashrrev_i32_e32 v151, 31, v150
	v_or_b32_e32 v158, 16, v150
	v_or_b32_e32 v166, 32, v150
	v_or_b32_e32 v178, 48, v150
	v_lshl_add_u64 v[154:155], v[150:151], 2, s[14:15]
	v_ashrrev_i32_e32 v159, 31, v158
	v_ashrrev_i32_e32 v167, 31, v166
	v_ashrrev_i32_e32 v179, 31, v178
	v_lshl_add_u64 v[162:163], v[158:159], 2, s[14:15]
	v_lshl_add_u64 v[170:171], v[166:167], 2, s[14:15]
	v_lshl_add_u64 v[174:175], v[178:179], 2, s[14:15]
	global_load_dword v172, v[154:155], off
	global_load_dword v168, v[162:163], off
	global_load_dword v164, v[170:171], off
	global_load_dword v160, v[174:175], off
	global_load_dword v156, v[154:155], off offset:512
	global_load_dword v152, v[154:155], off offset:576
	global_load_dword v148, v[154:155], off offset:640
	global_load_dword v146, v[154:155], off offset:704
	v_add_u32_e32 v154, 0x80, v150
	v_add_u32_e32 v180, 0x90, v150
	v_add_u32_e32 v182, 0xa0, v150
	v_add_u32_e32 v184, 0xb0, v150
	v_ashrrev_i32_e32 v155, 31, v154
	v_ashrrev_i32_e32 v181, 31, v180
	v_ashrrev_i32_e32 v183, 31, v182
	v_ashrrev_i32_e32 v185, 31, v184
	s_cmp_gt_i32 s63, 3
	v_lshlrev_b64 v[176:177], 11, v[150:151]
	s_mov_b64 s[28:29], -1
	v_lshlrev_b64 v[174:175], 11, v[158:159]
	v_lshlrev_b64 v[170:171], 11, v[166:167]
	v_lshlrev_b64 v[166:167], 11, v[178:179]
	v_lshlrev_b64 v[162:163], 11, v[154:155]
	v_lshlrev_b64 v[158:159], 11, v[180:181]
	v_lshlrev_b64 v[154:155], 11, v[182:183]
	v_lshlrev_b64 v[150:151], 11, v[184:185]
	s_cbranch_scc0 .LBB0_265
	v_lshl_add_u32 v136, s63, 7, v157
	v_lshl_add_u64 v[180:181], s[12:13], 0, v[176:177]
	v_lshlrev_b64 v[178:179], 1, v[136:137]
	v_lshl_add_u64 v[184:185], v[180:181], 0, v[178:179]
	s_waitcnt vmcnt(0)
	v_mul_f32_e32 v136, v172, v172
	v_pk_mul_f32 v[180:181], v[126:127], v[118:119]
	v_pk_mul_f32 v[182:183], v[124:125], v[116:117]
	v_pk_mul_f32 v[186:187], v[180:181], v[136:137] op_sel_hi:[1,0]
	v_pk_mul_f32 v[180:181], v[182:183], v[136:137] op_sel_hi:[1,0]
	v_pk_mul_f32 v[182:183], v[122:123], v[110:111]
	v_pk_mul_f32 v[188:189], v[120:121], v[108:109]
	v_pk_mul_f32 v[190:191], v[182:183], v[136:137] op_sel_hi:[1,0]
	v_pk_mul_f32 v[182:183], v[188:189], v[136:137] op_sel_hi:[1,0]
	v_cvt_pk_bf16_f32 v180, v180, v181
	v_cvt_pk_bf16_f32 v181, v186, v187
	v_mul_f32_e32 v136, v168, v168
	v_cvt_pk_bf16_f32 v182, v182, v183
	v_cvt_pk_bf16_f32 v183, v190, v191
	global_store_dwordx4 v[184:185], v[180:183], off nt
	v_pk_mul_f32 v[188:189], v[104:105], v[92:93]
	s_nop 0
	v_lshl_add_u64 v[180:181], s[12:13], 0, v[174:175]
	v_lshl_add_u64 v[184:185], v[180:181], 0, v[178:179]
	v_pk_mul_f32 v[180:181], v[114:115], v[102:103]
	v_pk_mul_f32 v[182:183], v[112:113], v[100:101]
	v_pk_mul_f32 v[186:187], v[180:181], v[136:137] op_sel_hi:[1,0]
	v_pk_mul_f32 v[180:181], v[182:183], v[136:137] op_sel_hi:[1,0]
	v_pk_mul_f32 v[182:183], v[106:107], v[94:95]
	v_cvt_pk_bf16_f32 v180, v180, v181
	v_cvt_pk_bf16_f32 v181, v186, v187
	s_nop 0
	v_pk_mul_f32 v[190:191], v[182:183], v[136:137] op_sel_hi:[1,0]
	v_pk_mul_f32 v[182:183], v[188:189], v[136:137] op_sel_hi:[1,0]
	v_mul_f32_e32 v136, v164, v164
	v_cvt_pk_bf16_f32 v182, v182, v183
	v_cvt_pk_bf16_f32 v183, v190, v191
	global_store_dwordx4 v[184:185], v[180:183], off nt
	v_pk_mul_f32 v[188:189], v[88:89], v[76:77]
	s_nop 0
	v_lshl_add_u64 v[180:181], s[12:13], 0, v[170:171]
	v_lshl_add_u64 v[184:185], v[180:181], 0, v[178:179]
	v_pk_mul_f32 v[180:181], v[98:99], v[86:87]
	v_pk_mul_f32 v[182:183], v[96:97], v[84:85]
	v_pk_mul_f32 v[186:187], v[180:181], v[136:137] op_sel_hi:[1,0]
	v_pk_mul_f32 v[180:181], v[182:183], v[136:137] op_sel_hi:[1,0]
	v_pk_mul_f32 v[182:183], v[90:91], v[78:79]
	v_cvt_pk_bf16_f32 v180, v180, v181
	v_cvt_pk_bf16_f32 v181, v186, v187
	s_nop 0
	v_pk_mul_f32 v[190:191], v[182:183], v[136:137] op_sel_hi:[1,0]
	v_pk_mul_f32 v[182:183], v[188:189], v[136:137] op_sel_hi:[1,0]
	v_mul_f32_e32 v136, v160, v160
	v_cvt_pk_bf16_f32 v182, v182, v183
	v_cvt_pk_bf16_f32 v183, v190, v191
	global_store_dwordx4 v[184:185], v[180:183], off nt
	v_pk_mul_f32 v[188:189], v[72:73], v[64:65]
	s_nop 0
	v_lshl_add_u64 v[180:181], s[12:13], 0, v[166:167]
	v_lshl_add_u64 v[184:185], v[180:181], 0, v[178:179]
	v_pk_mul_f32 v[180:181], v[82:83], v[70:71]
	v_pk_mul_f32 v[182:183], v[80:81], v[68:69]
	v_pk_mul_f32 v[186:187], v[180:181], v[136:137] op_sel_hi:[1,0]
	v_pk_mul_f32 v[180:181], v[182:183], v[136:137] op_sel_hi:[1,0]
	v_pk_mul_f32 v[182:183], v[74:75], v[66:67]
	v_cvt_pk_bf16_f32 v180, v180, v181
	v_cvt_pk_bf16_f32 v181, v186, v187
	s_nop 0
	v_pk_mul_f32 v[190:191], v[182:183], v[136:137] op_sel_hi:[1,0]
	v_pk_mul_f32 v[182:183], v[188:189], v[136:137] op_sel_hi:[1,0]
	v_mul_f32_e32 v136, v156, v156
	v_cvt_pk_bf16_f32 v182, v182, v183
	v_cvt_pk_bf16_f32 v183, v190, v191
	global_store_dwordx4 v[184:185], v[180:183], off nt
	v_pk_mul_f32 v[188:189], v[56:57], v[44:45]
	s_nop 0
	v_lshl_add_u64 v[180:181], s[12:13], 0, v[162:163]
	v_lshl_add_u64 v[184:185], v[180:181], 0, v[178:179]
	v_pk_mul_f32 v[180:181], v[62:63], v[54:55]
	v_pk_mul_f32 v[182:183], v[60:61], v[52:53]
	v_pk_mul_f32 v[186:187], v[180:181], v[136:137] op_sel_hi:[1,0]
	v_pk_mul_f32 v[180:181], v[182:183], v[136:137] op_sel_hi:[1,0]
	v_pk_mul_f32 v[182:183], v[58:59], v[46:47]
	v_cvt_pk_bf16_f32 v180, v180, v181
	v_cvt_pk_bf16_f32 v181, v186, v187
	s_nop 0
	v_pk_mul_f32 v[190:191], v[182:183], v[136:137] op_sel_hi:[1,0]
	v_pk_mul_f32 v[182:183], v[188:189], v[136:137] op_sel_hi:[1,0]
	v_mul_f32_e32 v136, v152, v152
	v_cvt_pk_bf16_f32 v182, v182, v183
	v_cvt_pk_bf16_f32 v183, v190, v191
	global_store_dwordx4 v[184:185], v[180:183], off nt
	v_pk_mul_f32 v[188:189], v[40:41], v[28:29]
	s_nop 0
	v_lshl_add_u64 v[180:181], s[12:13], 0, v[158:159]
	v_lshl_add_u64 v[184:185], v[180:181], 0, v[178:179]
	v_pk_mul_f32 v[180:181], v[50:51], v[38:39]
	v_pk_mul_f32 v[182:183], v[48:49], v[36:37]
	v_pk_mul_f32 v[186:187], v[180:181], v[136:137] op_sel_hi:[1,0]
	v_pk_mul_f32 v[180:181], v[182:183], v[136:137] op_sel_hi:[1,0]
	v_pk_mul_f32 v[182:183], v[42:43], v[30:31]
	v_cvt_pk_bf16_f32 v180, v180, v181
	v_cvt_pk_bf16_f32 v181, v186, v187
	s_nop 0
	v_pk_mul_f32 v[190:191], v[182:183], v[136:137] op_sel_hi:[1,0]
	v_pk_mul_f32 v[182:183], v[188:189], v[136:137] op_sel_hi:[1,0]
	v_mul_f32_e32 v136, v148, v148
	v_cvt_pk_bf16_f32 v182, v182, v183
	v_cvt_pk_bf16_f32 v183, v190, v191
	global_store_dwordx4 v[184:185], v[180:183], off nt
	v_pk_mul_f32 v[188:189], v[24:25], v[12:13]
	s_nop 0
	v_lshl_add_u64 v[180:181], s[12:13], 0, v[154:155]
	v_lshl_add_u64 v[184:185], v[180:181], 0, v[178:179]
	v_pk_mul_f32 v[180:181], v[34:35], v[22:23]
	v_pk_mul_f32 v[182:183], v[32:33], v[20:21]
	v_pk_mul_f32 v[186:187], v[180:181], v[136:137] op_sel_hi:[1,0]
	v_pk_mul_f32 v[180:181], v[182:183], v[136:137] op_sel_hi:[1,0]
	v_pk_mul_f32 v[182:183], v[26:27], v[14:15]
	v_cvt_pk_bf16_f32 v180, v180, v181
	v_cvt_pk_bf16_f32 v181, v186, v187
	v_pk_mul_f32 v[186:187], v[8:9], v[0:1]
	v_pk_mul_f32 v[190:191], v[182:183], v[136:137] op_sel_hi:[1,0]
	v_pk_mul_f32 v[182:183], v[188:189], v[136:137] op_sel_hi:[1,0]
	v_mul_f32_e32 v136, v146, v146
	v_cvt_pk_bf16_f32 v182, v182, v183
	v_cvt_pk_bf16_f32 v183, v190, v191
	global_store_dwordx4 v[184:185], v[180:183], off nt
	s_nop 1
	v_lshl_add_u64 v[180:181], s[12:13], 0, v[150:151]
	v_lshl_add_u64 v[182:183], v[180:181], 0, v[178:179]
	v_pk_mul_f32 v[178:179], v[18:19], v[6:7]
	v_pk_mul_f32 v[180:181], v[16:17], v[4:5]
	v_pk_mul_f32 v[184:185], v[178:179], v[136:137] op_sel_hi:[1,0]
	v_pk_mul_f32 v[178:179], v[180:181], v[136:137] op_sel_hi:[1,0]
	v_pk_mul_f32 v[180:181], v[10:11], v[2:3]
	v_cvt_pk_bf16_f32 v178, v178, v179
	v_cvt_pk_bf16_f32 v179, v184, v185
	s_nop 0
	v_pk_mul_f32 v[188:189], v[180:181], v[136:137] op_sel_hi:[1,0]
	v_pk_mul_f32 v[180:181], v[186:187], v[136:137] op_sel_hi:[1,0]
	s_nop 0
	v_cvt_pk_bf16_f32 v180, v180, v181
	v_cvt_pk_bf16_f32 v181, v188, v189
	global_store_dwordx4 v[182:183], v[178:181], off nt
	s_cbranch_execz .LBB0_266

.LBB0_266:
	s_nop 0
	v_lshl_or_b32 v178, s63, 8, v153
	v_ashrrev_i32_e32 v179, 31, v178
	v_lshl_add_u64 v[180:181], s[8:9], 0, v[176:177]
	v_lshlrev_b64 v[176:177], 1, v[178:179]
	v_lshl_add_u64 v[178:179], v[180:181], 0, v[176:177]
	s_waitcnt vmcnt(0)
	v_pk_mul_f32 v[126:127], v[126:127], v[172:173] op_sel_hi:[1,0]
	v_pk_mul_f32 v[124:125], v[124:125], v[172:173] op_sel_hi:[1,0]
	v_pk_mul_f32 v[180:181], v[122:123], v[172:173] op_sel_hi:[1,0]
	v_pk_mul_f32 v[122:123], v[120:121], v[172:173] op_sel_hi:[1,0]
	v_cvt_pk_bf16_f32 v120, v124, v125
	v_cvt_pk_bf16_f32 v121, v126, v127
	v_pk_mul_f32 v[118:119], v[118:119], v[172:173] op_sel_hi:[1,0]
	v_cvt_pk_bf16_f32 v122, v122, v123
	v_cvt_pk_bf16_f32 v123, v180, v181
	global_store_dwordx4 v[178:179], v[120:123], off nt
	v_pk_mul_f32 v[116:117], v[116:117], v[172:173] op_sel_hi:[1,0]
	v_pk_mul_f32 v[112:113], v[112:113], v[168:169] op_sel_hi:[1,0]
	v_pk_mul_f32 v[120:121], v[110:111], v[172:173] op_sel_hi:[1,0]
	v_pk_mul_f32 v[110:111], v[108:109], v[172:173] op_sel_hi:[1,0]
	v_cvt_pk_bf16_f32 v108, v116, v117
	v_cvt_pk_bf16_f32 v109, v118, v119
	v_pk_mul_f32 v[102:103], v[102:103], v[168:169] op_sel_hi:[1,0]
	v_cvt_pk_bf16_f32 v110, v110, v111
	v_cvt_pk_bf16_f32 v111, v120, v121
	global_store_dwordx4 v[178:179], v[108:111], off offset:256 nt
	v_pk_mul_f32 v[100:101], v[100:101], v[168:169] op_sel_hi:[1,0]
	v_pk_mul_f32 v[96:97], v[96:97], v[164:165] op_sel_hi:[1,0]
	v_lshl_add_u64 v[108:109], s[8:9], 0, v[174:175]
	v_lshl_add_u64 v[108:109], v[108:109], 0, v[176:177]
	v_pk_mul_f32 v[110:111], v[114:115], v[168:169] op_sel_hi:[1,0]
	v_pk_mul_f32 v[114:115], v[106:107], v[168:169] op_sel_hi:[1,0]
	v_pk_mul_f32 v[106:107], v[104:105], v[168:169] op_sel_hi:[1,0]
	v_cvt_pk_bf16_f32 v104, v112, v113
	v_cvt_pk_bf16_f32 v105, v110, v111
	v_pk_mul_f32 v[86:87], v[86:87], v[164:165] op_sel_hi:[1,0]
	v_cvt_pk_bf16_f32 v106, v106, v107
	v_cvt_pk_bf16_f32 v107, v114, v115
	global_store_dwordx4 v[108:109], v[104:107], off nt
	v_pk_mul_f32 v[84:85], v[84:85], v[164:165] op_sel_hi:[1,0]
	v_pk_mul_f32 v[80:81], v[80:81], v[160:161] op_sel_hi:[1,0]
	v_pk_mul_f32 v[104:105], v[94:95], v[168:169] op_sel_hi:[1,0]
	v_pk_mul_f32 v[94:95], v[92:93], v[168:169] op_sel_hi:[1,0]
	v_cvt_pk_bf16_f32 v92, v100, v101
	v_cvt_pk_bf16_f32 v93, v102, v103
	v_pk_mul_f32 v[70:71], v[70:71], v[160:161] op_sel_hi:[1,0]
	v_cvt_pk_bf16_f32 v94, v94, v95
	v_cvt_pk_bf16_f32 v95, v104, v105
	global_store_dwordx4 v[108:109], v[92:95], off offset:256 nt
	v_pk_mul_f32 v[68:69], v[68:69], v[160:161] op_sel_hi:[1,0]
	v_pk_mul_f32 v[62:63], v[62:63], v[156:157] op_sel_hi:[1,0]
	v_lshl_add_u64 v[92:93], s[8:9], 0, v[170:171]
	v_lshl_add_u64 v[92:93], v[92:93], 0, v[176:177]
	v_pk_mul_f32 v[94:95], v[98:99], v[164:165] op_sel_hi:[1,0]
	v_pk_mul_f32 v[98:99], v[90:91], v[164:165] op_sel_hi:[1,0]
	v_pk_mul_f32 v[90:91], v[88:89], v[164:165] op_sel_hi:[1,0]
	v_cvt_pk_bf16_f32 v88, v96, v97
	v_cvt_pk_bf16_f32 v89, v94, v95
	v_pk_mul_f32 v[60:61], v[60:61], v[156:157] op_sel_hi:[1,0]
	v_cvt_pk_bf16_f32 v90, v90, v91
	v_cvt_pk_bf16_f32 v91, v98, v99
	global_store_dwordx4 v[92:93], v[88:91], off nt
	v_pk_mul_f32 v[54:55], v[54:55], v[156:157] op_sel_hi:[1,0]
	v_pk_mul_f32 v[52:53], v[52:53], v[156:157] op_sel_hi:[1,0]
	v_pk_mul_f32 v[88:89], v[78:79], v[164:165] op_sel_hi:[1,0]
	v_pk_mul_f32 v[78:79], v[76:77], v[164:165] op_sel_hi:[1,0]
	v_cvt_pk_bf16_f32 v76, v84, v85
	v_cvt_pk_bf16_f32 v77, v86, v87
	v_pk_mul_f32 v[48:49], v[48:49], v[152:153] op_sel_hi:[1,0]
	v_cvt_pk_bf16_f32 v78, v78, v79
	v_cvt_pk_bf16_f32 v79, v88, v89
	global_store_dwordx4 v[92:93], v[76:79], off offset:256 nt
	v_pk_mul_f32 v[38:39], v[38:39], v[152:153] op_sel_hi:[1,0]
	v_pk_mul_f32 v[36:37], v[36:37], v[152:153] op_sel_hi:[1,0]
	v_lshl_add_u64 v[76:77], s[8:9], 0, v[166:167]
	v_lshl_add_u64 v[76:77], v[76:77], 0, v[176:177]
	v_pk_mul_f32 v[78:79], v[82:83], v[160:161] op_sel_hi:[1,0]
	v_pk_mul_f32 v[82:83], v[74:75], v[160:161] op_sel_hi:[1,0]
	v_pk_mul_f32 v[74:75], v[72:73], v[160:161] op_sel_hi:[1,0]
	v_cvt_pk_bf16_f32 v72, v80, v81
	v_cvt_pk_bf16_f32 v73, v78, v79
	v_pk_mul_f32 v[32:33], v[32:33], v[148:149] op_sel_hi:[1,0]
	v_cvt_pk_bf16_f32 v74, v74, v75
	v_cvt_pk_bf16_f32 v75, v82, v83
	global_store_dwordx4 v[76:77], v[72:75], off nt
	v_pk_mul_f32 v[22:23], v[22:23], v[148:149] op_sel_hi:[1,0]
	v_pk_mul_f32 v[20:21], v[20:21], v[148:149] op_sel_hi:[1,0]
	v_pk_mul_f32 v[72:73], v[66:67], v[160:161] op_sel_hi:[1,0]
	v_pk_mul_f32 v[66:67], v[64:65], v[160:161] op_sel_hi:[1,0]
	v_cvt_pk_bf16_f32 v64, v68, v69
	v_cvt_pk_bf16_f32 v65, v70, v71
	v_pk_mul_f32 v[16:17], v[16:17], v[146:147] op_sel_hi:[1,0]
	v_cvt_pk_bf16_f32 v66, v66, v67
	v_cvt_pk_bf16_f32 v67, v72, v73
	global_store_dwordx4 v[76:77], v[64:67], off offset:256 nt
	v_pk_mul_f32 v[6:7], v[6:7], v[146:147] op_sel_hi:[1,0]
	v_pk_mul_f32 v[4:5], v[4:5], v[146:147] op_sel_hi:[1,0]
	v_lshl_add_u64 v[64:65], s[8:9], 0, v[162:163]
	v_lshl_add_u64 v[64:65], v[64:65], 0, v[176:177]
	v_pk_mul_f32 v[66:67], v[58:59], v[156:157] op_sel_hi:[1,0]
	v_pk_mul_f32 v[58:59], v[56:57], v[156:157] op_sel_hi:[1,0]
	v_cvt_pk_bf16_f32 v56, v60, v61
	v_cvt_pk_bf16_f32 v57, v62, v63
	s_nop 0
	v_cvt_pk_bf16_f32 v58, v58, v59
	v_cvt_pk_bf16_f32 v59, v66, v67
	global_store_dwordx4 v[64:65], v[56:59], off nt
	s_nop 1
	v_pk_mul_f32 v[56:57], v[46:47], v[156:157] op_sel_hi:[1,0]
	v_pk_mul_f32 v[46:47], v[44:45], v[156:157] op_sel_hi:[1,0]
	v_cvt_pk_bf16_f32 v44, v52, v53
	v_cvt_pk_bf16_f32 v45, v54, v55
	s_nop 0
	v_cvt_pk_bf16_f32 v46, v46, v47
	v_cvt_pk_bf16_f32 v47, v56, v57
	global_store_dwordx4 v[64:65], v[44:47], off offset:256 nt
	s_nop 1
	v_lshl_add_u64 v[44:45], s[8:9], 0, v[158:159]
	v_lshl_add_u64 v[44:45], v[44:45], 0, v[176:177]
	v_pk_mul_f32 v[46:47], v[50:51], v[152:153] op_sel_hi:[1,0]
	v_pk_mul_f32 v[50:51], v[42:43], v[152:153] op_sel_hi:[1,0]
	v_pk_mul_f32 v[42:43], v[40:41], v[152:153] op_sel_hi:[1,0]
	v_cvt_pk_bf16_f32 v40, v48, v49
	v_cvt_pk_bf16_f32 v41, v46, v47
	s_nop 0
	v_cvt_pk_bf16_f32 v42, v42, v43
	v_cvt_pk_bf16_f32 v43, v50, v51
	global_store_dwordx4 v[44:45], v[40:43], off nt
	s_nop 1
	v_pk_mul_f32 v[40:41], v[30:31], v[152:153] op_sel_hi:[1,0]
	v_pk_mul_f32 v[30:31], v[28:29], v[152:153] op_sel_hi:[1,0]
	v_cvt_pk_bf16_f32 v28, v36, v37
	v_cvt_pk_bf16_f32 v29, v38, v39
	s_nop 0
	v_cvt_pk_bf16_f32 v30, v30, v31
	v_cvt_pk_bf16_f32 v31, v40, v41
	global_store_dwordx4 v[44:45], v[28:31], off offset:256 nt
	s_nop 1
	v_lshl_add_u64 v[28:29], s[8:9], 0, v[154:155]
	v_lshl_add_u64 v[28:29], v[28:29], 0, v[176:177]
	v_pk_mul_f32 v[30:31], v[34:35], v[148:149] op_sel_hi:[1,0]
	v_pk_mul_f32 v[34:35], v[26:27], v[148:149] op_sel_hi:[1,0]
	v_pk_mul_f32 v[26:27], v[24:25], v[148:149] op_sel_hi:[1,0]
	v_cvt_pk_bf16_f32 v24, v32, v33
	v_cvt_pk_bf16_f32 v25, v30, v31
	s_nop 0
	v_cvt_pk_bf16_f32 v26, v26, v27
	v_cvt_pk_bf16_f32 v27, v34, v35
	global_store_dwordx4 v[28:29], v[24:27], off nt
	s_nop 1
	v_pk_mul_f32 v[24:25], v[14:15], v[148:149] op_sel_hi:[1,0]
	v_pk_mul_f32 v[14:15], v[12:13], v[148:149] op_sel_hi:[1,0]
	v_cvt_pk_bf16_f32 v12, v20, v21
	v_cvt_pk_bf16_f32 v13, v22, v23
	s_nop 0
	v_cvt_pk_bf16_f32 v14, v14, v15
	v_cvt_pk_bf16_f32 v15, v24, v25
	global_store_dwordx4 v[28:29], v[12:15], off offset:256 nt
	s_nop 1
	v_lshl_add_u64 v[12:13], s[8:9], 0, v[150:151]
	v_lshl_add_u64 v[12:13], v[12:13], 0, v[176:177]
	v_pk_mul_f32 v[14:15], v[18:19], v[146:147] op_sel_hi:[1,0]
	v_pk_mul_f32 v[18:19], v[10:11], v[146:147] op_sel_hi:[1,0]
	v_pk_mul_f32 v[10:11], v[8:9], v[146:147] op_sel_hi:[1,0]
	v_cvt_pk_bf16_f32 v8, v16, v17
	v_cvt_pk_bf16_f32 v9, v14, v15
	s_nop 0
	v_cvt_pk_bf16_f32 v10, v10, v11
	v_cvt_pk_bf16_f32 v11, v18, v19
	global_store_dwordx4 v[12:13], v[8:11], off nt
	s_nop 1
	v_pk_mul_f32 v[8:9], v[2:3], v[146:147] op_sel_hi:[1,0]
	v_pk_mul_f32 v[2:3], v[0:1], v[146:147] op_sel_hi:[1,0]
	v_cvt_pk_bf16_f32 v0, v4, v5
	v_cvt_pk_bf16_f32 v1, v6, v7
	s_nop 0
	v_cvt_pk_bf16_f32 v2, v2, v3
	v_cvt_pk_bf16_f32 v3, v8, v9
	global_store_dwordx4 v[12:13], v[0:3], off offset:256 nt
	s_andn2_b64 vcc, exec, s[2:3]
	s_mov_b64 s[2:3], -1
	s_cbranch_vccnz .LBB0_255

.LBB0_339:
	s_or_b64 exec, exec, s[22:23]
	v_lshlrev_b32_e32 v46, 2, v22
	global_load_dwordx4 v[22:25], v46, s[2:3]
	global_load_dwordx4 v[26:29], v46, s[18:19]
	global_load_dwordx4 v[30:33], v46, s[2:3] offset:16
	global_load_dwordx4 v[34:37], v46, s[18:19] offset:16
	global_load_dwordx4 v[38:41], v46, s[16:17]
	global_load_dwordx4 v[42:45], v46, s[16:17] offset:16
	s_waitcnt vmcnt(0)
	v_lshlrev_b32_e32 v52, 16, v4
	v_lshlrev_b32_e32 v53, 16, v0
	v_lshlrev_b32_e32 v47, 16, v12
	v_lshlrev_b32_e32 v46, 16, v8
	v_and_b32_e32 v54, 0xffff0000, v4
	v_and_b32_e32 v55, 0xffff0000, v0
	v_and_b32_e32 v49, 0xffff0000, v12
	v_and_b32_e32 v48, 0xffff0000, v8
	v_lshlrev_b32_e32 v56, 16, v5
	v_lshlrev_b32_e32 v57, 16, v1
	v_lshlrev_b32_e32 v50, 16, v9
	v_lshlrev_b32_e32 v51, 16, v13
	v_and_b32_e32 v58, 0xffff0000, v5
	v_and_b32_e32 v59, 0xffff0000, v1
	v_and_b32_e32 v1, 0xffff0000, v13
	v_and_b32_e32 v0, 0xffff0000, v9
	v_lshlrev_b32_e32 v60, 16, v6
	v_lshlrev_b32_e32 v61, 16, v2
	v_lshlrev_b32_e32 v5, 16, v14
	v_lshlrev_b32_e32 v4, 16, v10
	v_and_b32_e32 v62, 0xffff0000, v6
	v_and_b32_e32 v63, 0xffff0000, v2
	v_and_b32_e32 v9, 0xffff0000, v14
	v_and_b32_e32 v8, 0xffff0000, v10
	v_lshlrev_b32_e32 v64, 16, v7
	v_lshlrev_b32_e32 v65, 16, v3
	v_lshlrev_b32_e32 v12, 16, v11
	v_lshlrev_b32_e32 v13, 16, v15
	v_and_b32_e32 v66, 0xffff0000, v7
	v_and_b32_e32 v67, 0xffff0000, v3
	v_and_b32_e32 v3, 0xffff0000, v15
	v_and_b32_e32 v2, 0xffff0000, v11
	v_lshlrev_b64 v[18:19], 10, v[18:19]
	v_add_u32_e32 v20, s26, v20
	v_cmp_lt_i32_e32 vcc, s29, v20
	s_or_b64 s[20:21], vcc, s[20:21]
	v_add_u32_e32 v21, s27, v21
	v_mov_b32_e32 v6, v22
	v_mov_b32_e32 v7, v26
	v_mov_b32_e32 v26, v23
	v_mov_b32_e32 v11, v28
	v_mov_b32_e32 v28, v25
	v_mov_b32_e32 v14, v30
	v_mov_b32_e32 v15, v34
	v_mov_b32_e32 v34, v31
	v_mov_b32_e32 v22, v32
	v_mov_b32_e32 v23, v36
	v_mov_b32_e32 v10, v24
	v_mov_b32_e32 v36, v33
	v_pk_mul_f32 v[6:7], v[6:7], v[46:47]
	v_pk_mul_f32 v[0:1], v[28:29], v[0:1]
	v_pk_mul_f32 v[4:5], v[14:15], v[4:5]
	v_pk_mul_f32 v[8:9], v[34:35], v[8:9]
	v_pk_mul_f32 v[12:13], v[22:23], v[12:13]
	v_pk_mul_f32 v[24:25], v[26:27], v[48:49]
	v_pk_mul_f32 v[10:11], v[10:11], v[50:51]
	v_pk_mul_f32 v[2:3], v[36:37], v[2:3]
	v_fma_f32 v6, v38, v53, v6
	v_fma_f32 v0, v41, v59, v0
	v_fma_f32 v4, v42, v61, v4
	v_fma_f32 v8, v43, v63, v8
	v_fma_f32 v12, v44, v65, v12
	v_fma_f32 v14, v39, v55, v24
	v_fma_f32 v10, v40, v57, v10
	v_fma_f32 v2, v45, v67, v2
	v_add_f32_e32 v6, v6, v7
	v_add_f32_e32 v0, v0, v1
	v_add_f32_e32 v1, v4, v5
	v_add_f32_e32 v4, v8, v9
	v_add_f32_e32 v5, v12, v13
	v_add_f32_e32 v7, v14, v25
	v_add_f32_e32 v10, v10, v11
	v_add_f32_e32 v2, v2, v3
	v_mul_f32_e32 v3, v6, v52
	v_mul_f32_e32 v4, v4, v62
	v_mul_f32_e32 v5, v5, v64
	v_mul_f32_e32 v6, v7, v54
	v_mul_f32_e32 v7, v10, v56
	v_mul_f32_e32 v8, v0, v58
	v_mul_f32_e32 v9, v1, v60
	v_mul_f32_e32 v10, v2, v66
	v_cvt_pk_bf16_f32 v0, v3, v6
	v_cvt_pk_bf16_f32 v2, v9, v4
	v_cvt_pk_bf16_f32 v3, v5, v10
	v_lshl_add_u64 v[4:5], v[18:19], 1, s[14:15]
	v_lshl_add_u64 v[4:5], v[4:5], 0, v[16:17]
	v_cvt_pk_bf16_f32 v1, v7, v8
	global_store_dwordx4 v[4:5], v[0:3], off nt
	s_andn2_b64 exec, exec, s[20:21]
	s_cbranch_execz .LBB0_344

.LBB0_433:
	v_lshl_or_b32 v208, s63, 8, v242
	v_lshl_add_u32 v236, s8, 8, v240
	v_ashrrev_i32_e32 v209, 31, v208
	v_lshlrev_b64 v[248:249], 1, v[208:209]
	v_ashrrev_i32_e32 v237, 31, v236
	v_lshl_add_u64 v[112:113], s[14:15], 0, v[248:249]
	v_lshlrev_b64 v[250:251], 11, v[236:237]
	v_lshl_add_u64 v[114:115], v[112:113], 0, v[250:251]
	global_load_dwordx4 v[188:191], v[114:115], off
	global_load_dwordx4 v[184:187], v[114:115], off offset:256
	v_or_b32_e32 v232, 16, v236
	v_ashrrev_i32_e32 v233, 31, v232
	v_or_b32_e32 v228, 32, v236
	v_lshlrev_b64 v[238:239], 11, v[232:233]
	v_ashrrev_i32_e32 v229, 31, v228
	v_or_b32_e32 v224, 48, v236
	v_lshl_add_u64 v[114:115], v[112:113], 0, v[238:239]
	v_lshlrev_b64 v[234:235], 11, v[228:229]
	v_ashrrev_i32_e32 v225, 31, v224
	v_add_u32_e32 v220, 0x80, v236
	global_load_dwordx4 v[180:183], v[114:115], off
	global_load_dwordx4 v[176:179], v[114:115], off offset:256
	v_lshl_add_u64 v[114:115], v[112:113], 0, v[234:235]
	v_lshlrev_b64 v[230:231], 11, v[224:225]
	v_ashrrev_i32_e32 v221, 31, v220
	v_add_u32_e32 v216, 0x90, v236
	global_load_dwordx4 v[172:175], v[114:115], off
	global_load_dwordx4 v[168:171], v[114:115], off offset:256
	v_lshl_add_u64 v[114:115], v[112:113], 0, v[230:231]
	v_lshlrev_b64 v[226:227], 11, v[220:221]
	v_ashrrev_i32_e32 v217, 31, v216
	v_add_u32_e32 v212, 0xa0, v236
	v_add_u32_e32 v210, 0xb0, v236
	global_load_dwordx4 v[164:167], v[114:115], off
	global_load_dwordx4 v[160:163], v[114:115], off offset:256
	v_lshl_add_u64 v[114:115], v[112:113], 0, v[226:227]
	v_lshlrev_b64 v[222:223], 11, v[216:217]
	v_ashrrev_i32_e32 v213, 31, v212
	v_ashrrev_i32_e32 v211, 31, v210
	global_load_dwordx4 v[156:159], v[114:115], off
	global_load_dwordx4 v[148:151], v[114:115], off offset:256
	v_lshl_add_u64 v[114:115], v[112:113], 0, v[222:223]
	v_lshlrev_b64 v[218:219], 11, v[212:213]
	v_lshlrev_b64 v[214:215], 11, v[210:211]
	global_load_dwordx4 v[140:143], v[114:115], off
	global_load_dwordx4 v[136:139], v[114:115], off offset:256
	v_lshl_add_u64 v[114:115], v[112:113], 0, v[218:219]
	v_lshl_add_u64 v[112:113], v[112:113], 0, v[214:215]
	global_load_dwordx4 v[128:131], v[114:115], off
	global_load_dwordx4 v[116:119], v[114:115], off offset:256
	global_load_dwordx4 v[124:127], v[112:113], off
	s_nop 0
	global_load_dwordx4 v[112:115], v[112:113], off offset:256
	v_lshl_add_u64 v[250:251], s[14:15], 0, v[250:251]
	v_lshl_add_u64 v[248:249], v[250:251], 0, v[248:249]
	s_lshl_b32 s30, s63, 2
	s_ashr_i32 s31, s30, 31
	s_waitcnt vmcnt(0)
	v_lshlrev_b32_e32 v250, 16, v188
	v_and_b32_e32 v251, 0xffff0000, v188
	v_lshlrev_b32_e32 v188, 16, v189
	v_and_b32_e32 v189, 0xffff0000, v189
	v_pk_add_f32 v[154:155], v[154:155], v[188:189]
	v_pk_add_f32 v[152:153], v[152:153], v[250:251]
	v_lshlrev_b32_e32 v188, 16, v190
	v_and_b32_e32 v189, 0xffff0000, v190
	v_lshlrev_b32_e32 v190, 16, v191
	v_and_b32_e32 v191, 0xffff0000, v191
	v_pk_add_f32 v[190:191], v[146:147], v[190:191]
	v_pk_add_f32 v[146:147], v[144:145], v[188:189]
	v_mul_f32_e32 v144, v153, v153
	v_mul_f32_e32 v145, v155, v155
	v_fmac_f32_e32 v144, v152, v152
	v_fmac_f32_e32 v145, v154, v154
	v_add_f32_e32 v144, v144, v145
	v_mul_f32_e32 v145, v147, v147
	v_fmac_f32_e32 v145, v146, v146
	v_add_f32_e32 v144, v145, v144
	v_mul_f32_e32 v145, v191, v191
	v_fmac_f32_e32 v145, v190, v190
	v_add_f32_e32 v188, v145, v144
	v_cvt_pk_bf16_f32 v144, v152, v153
	v_cvt_pk_bf16_f32 v145, v154, v155
	v_cvt_pk_bf16_f32 v146, v146, v147
	v_cvt_pk_bf16_f32 v147, v190, v191
	global_store_dwordx4 v[248:249], v[144:147], off nt
	s_nop 1
	v_lshlrev_b32_e32 v144, 16, v184
	v_and_b32_e32 v145, 0xffff0000, v184
	v_lshlrev_b32_e32 v146, 16, v185
	v_and_b32_e32 v147, 0xffff0000, v185
	v_pk_add_f32 v[134:135], v[134:135], v[146:147]
	v_pk_add_f32 v[132:133], v[132:133], v[144:145]
	v_lshlrev_b32_e32 v144, 16, v186
	v_and_b32_e32 v145, 0xffff0000, v186
	v_lshlrev_b32_e32 v146, 16, v187
	v_and_b32_e32 v147, 0xffff0000, v187
	v_pk_add_f32 v[146:147], v[122:123], v[146:147]
	v_pk_add_f32 v[122:123], v[120:121], v[144:145]
	v_mul_f32_e32 v120, v133, v133
	v_mul_f32_e32 v121, v135, v135
	v_fmac_f32_e32 v120, v132, v132
	v_fmac_f32_e32 v121, v134, v134
	v_add_f32_e32 v120, v120, v121
	v_mul_f32_e32 v121, v123, v123
	v_fmac_f32_e32 v121, v122, v122
	v_add_f32_e32 v120, v121, v120
	v_mul_f32_e32 v121, v147, v147
	v_fmac_f32_e32 v121, v146, v146
	v_add_f32_e32 v120, v121, v120
	v_add_f32_e32 v144, v188, v120
	v_cvt_pk_bf16_f32 v120, v132, v133
	v_cvt_pk_bf16_f32 v121, v134, v135
	v_cvt_pk_bf16_f32 v122, v122, v123
	v_cvt_pk_bf16_f32 v123, v146, v147
	global_store_dwordx4 v[248:249], v[120:123], off offset:256 nt
	ds_bpermute_b32 v120, v243, v144
	s_waitcnt lgkmcnt(0)
	v_add_f32_e32 v120, v144, v120
	ds_bpermute_b32 v121, v244, v120
	s_and_saveexec_b64 s[36:37], s[2:3]
	s_cbranch_execz .LBB0_435
	s_waitcnt lgkmcnt(0)
	v_add_f32_e32 v122, v120, v121
	v_lshlrev_b64 v[120:121], 6, v[236:237]
	v_lshl_add_u64 v[120:121], s[16:17], 0, v[120:121]
	v_lshl_add_u64 v[120:121], s[30:31], 2, v[120:121]
	s_lshl_b32 s8, s55, 2
	v_lshl_add_u64 v[120:121], v[120:121], 0, s[8:9]
	global_store_dword v[120:121], v122, off
.LBB0_435:
	s_or_b64 exec, exec, s[36:37]
	v_lshlrev_b32_e32 v122, 16, v180
	v_and_b32_e32 v123, 0xffff0000, v180
	v_lshlrev_b32_e32 v132, 16, v181
	v_and_b32_e32 v133, 0xffff0000, v181
	v_pk_add_f32 v[110:111], v[110:111], v[132:133]
	v_pk_add_f32 v[108:109], v[108:109], v[122:123]
	v_lshlrev_b32_e32 v122, 16, v182
	v_and_b32_e32 v123, 0xffff0000, v182
	v_lshlrev_b32_e32 v132, 16, v183
	v_and_b32_e32 v133, 0xffff0000, v183
	v_pk_add_f32 v[132:133], v[106:107], v[132:133]
	v_pk_add_f32 v[106:107], v[104:105], v[122:123]
	v_mul_f32_e32 v104, v109, v109
	v_mul_f32_e32 v105, v111, v111
	v_fmac_f32_e32 v104, v108, v108
	v_fmac_f32_e32 v105, v110, v110
	v_add_f32_e32 v104, v104, v105
	v_mul_f32_e32 v105, v107, v107
	v_fmac_f32_e32 v105, v106, v106
	v_add_f32_e32 v104, v105, v104
	v_mul_f32_e32 v105, v133, v133
	v_fmac_f32_e32 v105, v132, v132
	v_add_f32_e32 v122, v105, v104
	v_cvt_pk_bf16_f32 v104, v108, v109
	v_cvt_pk_bf16_f32 v105, v110, v111
	v_lshlrev_b32_e32 v108, 16, v176
	v_and_b32_e32 v109, 0xffff0000, v176
	v_lshlrev_b32_e32 v110, 16, v177
	v_and_b32_e32 v111, 0xffff0000, v177
	v_pk_add_f32 v[102:103], v[102:103], v[110:111]
	v_pk_add_f32 v[100:101], v[100:101], v[108:109]
	v_lshlrev_b32_e32 v108, 16, v178
	v_and_b32_e32 v109, 0xffff0000, v178
	v_pk_add_f32 v[108:109], v[96:97], v[108:109]
	v_mul_f32_e32 v96, v101, v101
	v_mul_f32_e32 v97, v103, v103
	v_fmac_f32_e32 v96, v100, v100
	v_fmac_f32_e32 v97, v102, v102
	v_lshlrev_b32_e32 v110, 16, v179
	v_and_b32_e32 v111, 0xffff0000, v179
	v_add_f32_e32 v96, v96, v97
	v_mul_f32_e32 v97, v109, v109
	v_pk_add_f32 v[110:111], v[98:99], v[110:111]
	v_fmac_f32_e32 v97, v108, v108
	v_add_f32_e32 v96, v97, v96
	v_mul_f32_e32 v97, v111, v111
	v_fmac_f32_e32 v97, v110, v110
	v_add_f32_e32 v96, v97, v96
	v_add_f32_e32 v96, v122, v96
	ds_bpermute_b32 v97, v243, v96
	s_waitcnt lgkmcnt(1)
	v_lshl_add_u64 v[120:121], s[14:15], 0, v[238:239]
	v_lshl_add_u64 v[120:121], v[208:209], 1, v[120:121]
	v_cvt_pk_bf16_f32 v106, v106, v107
	v_cvt_pk_bf16_f32 v107, v132, v133
	s_waitcnt lgkmcnt(0)
	v_add_f32_e32 v96, v96, v97
	ds_bpermute_b32 v97, v244, v96
	global_store_dwordx4 v[120:121], v[104:107], off nt
	v_cvt_pk_bf16_f32 v98, v100, v101
	v_cvt_pk_bf16_f32 v99, v102, v103
	v_cvt_pk_bf16_f32 v100, v108, v109
	v_cvt_pk_bf16_f32 v101, v110, v111
	global_store_dwordx4 v[120:121], v[98:101], off offset:256 nt
	s_and_saveexec_b64 s[36:37], s[2:3]
	s_cbranch_execz .LBB0_437
	s_waitcnt lgkmcnt(0)
	v_add_f32_e32 v98, v96, v97
	v_lshlrev_b64 v[96:97], 6, v[232:233]
	v_lshl_add_u64 v[96:97], s[16:17], 0, v[96:97]
	v_lshl_add_u64 v[96:97], s[30:31], 2, v[96:97]
	s_lshl_b32 s8, s55, 2
	v_lshl_add_u64 v[96:97], v[96:97], 0, s[8:9]
	global_store_dword v[96:97], v98, off
.LBB0_437:
	s_or_b64 exec, exec, s[36:37]
	v_lshlrev_b32_e32 v98, 16, v172
	v_and_b32_e32 v99, 0xffff0000, v172
	v_lshlrev_b32_e32 v100, 16, v173
	v_and_b32_e32 v101, 0xffff0000, v173
	v_pk_add_f32 v[94:95], v[94:95], v[100:101]
	v_pk_add_f32 v[92:93], v[92:93], v[98:99]
	v_lshlrev_b32_e32 v98, 16, v174
	v_and_b32_e32 v99, 0xffff0000, v174
	v_lshlrev_b32_e32 v100, 16, v175
	v_and_b32_e32 v101, 0xffff0000, v175
	v_pk_add_f32 v[100:101], v[90:91], v[100:101]
	v_pk_add_f32 v[90:91], v[88:89], v[98:99]
	v_mul_f32_e32 v88, v93, v93
	v_mul_f32_e32 v89, v95, v95
	v_fmac_f32_e32 v88, v92, v92
	v_fmac_f32_e32 v89, v94, v94
	v_add_f32_e32 v88, v88, v89
	v_mul_f32_e32 v89, v91, v91
	v_fmac_f32_e32 v89, v90, v90
	v_add_f32_e32 v88, v89, v88
	v_mul_f32_e32 v89, v101, v101
	v_fmac_f32_e32 v89, v100, v100
	v_add_f32_e32 v98, v89, v88
	v_cvt_pk_bf16_f32 v88, v92, v93
	v_cvt_pk_bf16_f32 v89, v94, v95
	v_lshlrev_b32_e32 v92, 16, v168
	v_and_b32_e32 v93, 0xffff0000, v168
	v_lshlrev_b32_e32 v94, 16, v169
	v_and_b32_e32 v95, 0xffff0000, v169
	v_pk_add_f32 v[86:87], v[86:87], v[94:95]
	v_pk_add_f32 v[84:85], v[84:85], v[92:93]
	v_lshlrev_b32_e32 v92, 16, v170
	v_and_b32_e32 v93, 0xffff0000, v170
	v_pk_add_f32 v[92:93], v[80:81], v[92:93]
	v_mul_f32_e32 v80, v85, v85
	v_mul_f32_e32 v81, v87, v87
	v_fmac_f32_e32 v80, v84, v84
	v_fmac_f32_e32 v81, v86, v86
	v_lshlrev_b32_e32 v94, 16, v171
	v_and_b32_e32 v95, 0xffff0000, v171
	v_add_f32_e32 v80, v80, v81
	v_mul_f32_e32 v81, v93, v93
	v_pk_add_f32 v[94:95], v[82:83], v[94:95]
	v_fmac_f32_e32 v81, v92, v92
	v_add_f32_e32 v80, v81, v80
	v_mul_f32_e32 v81, v95, v95
	v_fmac_f32_e32 v81, v94, v94
	v_add_f32_e32 v80, v81, v80
	v_add_f32_e32 v80, v98, v80
	ds_bpermute_b32 v81, v243, v80
	s_waitcnt lgkmcnt(1)
	v_lshl_add_u64 v[96:97], s[14:15], 0, v[234:235]
	v_lshl_add_u64 v[96:97], v[208:209], 1, v[96:97]
	v_cvt_pk_bf16_f32 v90, v90, v91
	v_cvt_pk_bf16_f32 v91, v100, v101
	s_waitcnt lgkmcnt(0)
	v_add_f32_e32 v80, v80, v81
	ds_bpermute_b32 v81, v244, v80
	global_store_dwordx4 v[96:97], v[88:91], off nt
	v_cvt_pk_bf16_f32 v82, v84, v85
	v_cvt_pk_bf16_f32 v83, v86, v87
	v_cvt_pk_bf16_f32 v84, v92, v93
	v_cvt_pk_bf16_f32 v85, v94, v95
	global_store_dwordx4 v[96:97], v[82:85], off offset:256 nt
	s_and_saveexec_b64 s[36:37], s[2:3]
	s_cbranch_execz .LBB0_439
	s_waitcnt lgkmcnt(0)
	v_add_f32_e32 v82, v80, v81
	v_lshlrev_b64 v[80:81], 6, v[228:229]
	v_lshl_add_u64 v[80:81], s[16:17], 0, v[80:81]
	v_lshl_add_u64 v[80:81], s[30:31], 2, v[80:81]
	s_lshl_b32 s8, s55, 2
	v_lshl_add_u64 v[80:81], v[80:81], 0, s[8:9]
	global_store_dword v[80:81], v82, off
.LBB0_439:
	s_or_b64 exec, exec, s[36:37]
	v_lshlrev_b32_e32 v82, 16, v164
	v_and_b32_e32 v83, 0xffff0000, v164
	v_lshlrev_b32_e32 v84, 16, v165
	v_and_b32_e32 v85, 0xffff0000, v165
	v_pk_add_f32 v[78:79], v[78:79], v[84:85]
	v_pk_add_f32 v[76:77], v[76:77], v[82:83]
	v_lshlrev_b32_e32 v82, 16, v166
	v_and_b32_e32 v83, 0xffff0000, v166
	v_lshlrev_b32_e32 v84, 16, v167
	v_and_b32_e32 v85, 0xffff0000, v167
	v_pk_add_f32 v[84:85], v[74:75], v[84:85]
	v_pk_add_f32 v[74:75], v[72:73], v[82:83]
	v_mul_f32_e32 v72, v77, v77
	v_mul_f32_e32 v73, v79, v79
	v_fmac_f32_e32 v72, v76, v76
	v_fmac_f32_e32 v73, v78, v78
	v_add_f32_e32 v72, v72, v73
	v_mul_f32_e32 v73, v75, v75
	v_fmac_f32_e32 v73, v74, v74
	v_add_f32_e32 v72, v73, v72
	v_mul_f32_e32 v73, v85, v85
	v_fmac_f32_e32 v73, v84, v84
	v_add_f32_e32 v82, v73, v72
	v_cvt_pk_bf16_f32 v72, v76, v77
	v_cvt_pk_bf16_f32 v73, v78, v79
	v_lshlrev_b32_e32 v76, 16, v160
	v_and_b32_e32 v77, 0xffff0000, v160
	v_lshlrev_b32_e32 v78, 16, v161
	v_and_b32_e32 v79, 0xffff0000, v161
	v_pk_add_f32 v[70:71], v[70:71], v[78:79]
	v_pk_add_f32 v[68:69], v[68:69], v[76:77]
	v_lshlrev_b32_e32 v76, 16, v162
	v_and_b32_e32 v77, 0xffff0000, v162
	v_pk_add_f32 v[76:77], v[64:65], v[76:77]
	v_mul_f32_e32 v64, v69, v69
	v_mul_f32_e32 v65, v71, v71
	v_fmac_f32_e32 v64, v68, v68
	v_fmac_f32_e32 v65, v70, v70
	v_lshlrev_b32_e32 v78, 16, v163
	v_and_b32_e32 v79, 0xffff0000, v163
	v_add_f32_e32 v64, v64, v65
	v_mul_f32_e32 v65, v77, v77
	v_pk_add_f32 v[78:79], v[66:67], v[78:79]
	v_fmac_f32_e32 v65, v76, v76
	v_add_f32_e32 v64, v65, v64
	v_mul_f32_e32 v65, v79, v79
	v_fmac_f32_e32 v65, v78, v78
	v_add_f32_e32 v64, v65, v64
	v_add_f32_e32 v64, v82, v64
	ds_bpermute_b32 v65, v243, v64
	s_waitcnt lgkmcnt(1)
	v_lshl_add_u64 v[80:81], s[14:15], 0, v[230:231]
	v_lshl_add_u64 v[80:81], v[208:209], 1, v[80:81]
	v_cvt_pk_bf16_f32 v74, v74, v75
	v_cvt_pk_bf16_f32 v75, v84, v85
	s_waitcnt lgkmcnt(0)
	v_add_f32_e32 v64, v64, v65
	ds_bpermute_b32 v65, v244, v64
	global_store_dwordx4 v[80:81], v[72:75], off nt
	v_cvt_pk_bf16_f32 v66, v68, v69
	v_cvt_pk_bf16_f32 v67, v70, v71
	v_cvt_pk_bf16_f32 v68, v76, v77
	v_cvt_pk_bf16_f32 v69, v78, v79
	global_store_dwordx4 v[80:81], v[66:69], off offset:256 nt
	s_and_saveexec_b64 s[36:37], s[2:3]
	s_cbranch_execz .LBB0_441
	s_waitcnt lgkmcnt(0)
	v_add_f32_e32 v66, v64, v65
	v_lshlrev_b64 v[64:65], 6, v[224:225]
	v_lshl_add_u64 v[64:65], s[16:17], 0, v[64:65]
	v_lshl_add_u64 v[64:65], s[30:31], 2, v[64:65]
	s_lshl_b32 s8, s55, 2
	v_lshl_add_u64 v[64:65], v[64:65], 0, s[8:9]
	global_store_dword v[64:65], v66, off
.LBB0_441:
	s_or_b64 exec, exec, s[36:37]
	v_lshlrev_b32_e32 v66, 16, v156
	v_and_b32_e32 v67, 0xffff0000, v156
	v_lshlrev_b32_e32 v68, 16, v157
	v_and_b32_e32 v69, 0xffff0000, v157
	v_pk_add_f32 v[62:63], v[62:63], v[68:69]
	v_pk_add_f32 v[60:61], v[60:61], v[66:67]
	v_lshlrev_b32_e32 v66, 16, v158
	v_and_b32_e32 v67, 0xffff0000, v158
	v_lshlrev_b32_e32 v68, 16, v159
	v_and_b32_e32 v69, 0xffff0000, v159
	v_pk_add_f32 v[68:69], v[58:59], v[68:69]
	v_pk_add_f32 v[58:59], v[56:57], v[66:67]
	v_mul_f32_e32 v56, v61, v61
	v_mul_f32_e32 v57, v63, v63
	v_fmac_f32_e32 v56, v60, v60
	v_fmac_f32_e32 v57, v62, v62
	v_add_f32_e32 v56, v56, v57
	v_mul_f32_e32 v57, v59, v59
	v_fmac_f32_e32 v57, v58, v58
	v_add_f32_e32 v56, v57, v56
	v_mul_f32_e32 v57, v69, v69
	v_fmac_f32_e32 v57, v68, v68
	v_add_f32_e32 v66, v57, v56
	v_cvt_pk_bf16_f32 v56, v60, v61
	v_cvt_pk_bf16_f32 v57, v62, v63
	v_lshlrev_b32_e32 v60, 16, v148
	v_and_b32_e32 v61, 0xffff0000, v148
	v_lshlrev_b32_e32 v62, 16, v149
	v_and_b32_e32 v63, 0xffff0000, v149
	v_pk_add_f32 v[54:55], v[54:55], v[62:63]
	v_pk_add_f32 v[52:53], v[52:53], v[60:61]
	v_lshlrev_b32_e32 v60, 16, v150
	v_and_b32_e32 v61, 0xffff0000, v150
	v_pk_add_f32 v[60:61], v[48:49], v[60:61]
	v_mul_f32_e32 v48, v53, v53
	v_mul_f32_e32 v49, v55, v55
	v_fmac_f32_e32 v48, v52, v52
	v_fmac_f32_e32 v49, v54, v54
	v_lshlrev_b32_e32 v62, 16, v151
	v_and_b32_e32 v63, 0xffff0000, v151
	v_add_f32_e32 v48, v48, v49
	v_mul_f32_e32 v49, v61, v61
	v_pk_add_f32 v[62:63], v[50:51], v[62:63]
	v_fmac_f32_e32 v49, v60, v60
	v_add_f32_e32 v48, v49, v48
	v_mul_f32_e32 v49, v63, v63
	v_fmac_f32_e32 v49, v62, v62
	v_add_f32_e32 v48, v49, v48
	v_add_f32_e32 v48, v66, v48
	ds_bpermute_b32 v49, v243, v48
	s_waitcnt lgkmcnt(1)
	v_lshl_add_u64 v[64:65], s[14:15], 0, v[226:227]
	v_lshl_add_u64 v[64:65], v[208:209], 1, v[64:65]
	v_cvt_pk_bf16_f32 v58, v58, v59
	v_cvt_pk_bf16_f32 v59, v68, v69
	s_waitcnt lgkmcnt(0)
	v_add_f32_e32 v48, v48, v49
	ds_bpermute_b32 v49, v244, v48
	global_store_dwordx4 v[64:65], v[56:59], off nt
	v_cvt_pk_bf16_f32 v50, v52, v53
	v_cvt_pk_bf16_f32 v51, v54, v55
	v_cvt_pk_bf16_f32 v52, v60, v61
	v_cvt_pk_bf16_f32 v53, v62, v63
	global_store_dwordx4 v[64:65], v[50:53], off offset:256 nt
	s_and_saveexec_b64 s[36:37], s[2:3]
	s_cbranch_execz .LBB0_443
	s_waitcnt lgkmcnt(0)
	v_add_f32_e32 v50, v48, v49
	v_lshlrev_b64 v[48:49], 6, v[220:221]
	v_lshl_add_u64 v[48:49], s[16:17], 0, v[48:49]
	v_lshl_add_u64 v[48:49], s[30:31], 2, v[48:49]
	s_lshl_b32 s8, s55, 2
	v_lshl_add_u64 v[48:49], v[48:49], 0, s[8:9]
	global_store_dword v[48:49], v50, off
.LBB0_443:
	s_or_b64 exec, exec, s[36:37]
	v_lshlrev_b32_e32 v50, 16, v140
	v_and_b32_e32 v51, 0xffff0000, v140
	v_lshlrev_b32_e32 v52, 16, v141
	v_and_b32_e32 v53, 0xffff0000, v141
	v_pk_add_f32 v[46:47], v[46:47], v[52:53]
	v_pk_add_f32 v[44:45], v[44:45], v[50:51]
	v_lshlrev_b32_e32 v50, 16, v142
	v_and_b32_e32 v51, 0xffff0000, v142
	v_lshlrev_b32_e32 v52, 16, v143
	v_and_b32_e32 v53, 0xffff0000, v143
	v_pk_add_f32 v[52:53], v[42:43], v[52:53]
	v_pk_add_f32 v[42:43], v[40:41], v[50:51]
	v_mul_f32_e32 v40, v45, v45
	v_mul_f32_e32 v41, v47, v47
	v_fmac_f32_e32 v40, v44, v44
	v_fmac_f32_e32 v41, v46, v46
	v_add_f32_e32 v40, v40, v41
	v_mul_f32_e32 v41, v43, v43
	v_fmac_f32_e32 v41, v42, v42
	v_add_f32_e32 v40, v41, v40
	v_mul_f32_e32 v41, v53, v53
	v_fmac_f32_e32 v41, v52, v52
	v_add_f32_e32 v50, v41, v40
	v_cvt_pk_bf16_f32 v40, v44, v45
	v_cvt_pk_bf16_f32 v41, v46, v47
	v_lshlrev_b32_e32 v44, 16, v136
	v_and_b32_e32 v45, 0xffff0000, v136
	v_lshlrev_b32_e32 v46, 16, v137
	v_and_b32_e32 v47, 0xffff0000, v137
	v_pk_add_f32 v[38:39], v[38:39], v[46:47]
	v_pk_add_f32 v[36:37], v[36:37], v[44:45]
	v_lshlrev_b32_e32 v44, 16, v138
	v_and_b32_e32 v45, 0xffff0000, v138
	v_pk_add_f32 v[44:45], v[32:33], v[44:45]
	v_mul_f32_e32 v32, v37, v37
	v_mul_f32_e32 v33, v39, v39
	v_fmac_f32_e32 v32, v36, v36
	v_fmac_f32_e32 v33, v38, v38
	v_lshlrev_b32_e32 v46, 16, v139
	v_and_b32_e32 v47, 0xffff0000, v139
	v_add_f32_e32 v32, v32, v33
	v_mul_f32_e32 v33, v45, v45
	v_pk_add_f32 v[46:47], v[34:35], v[46:47]
	v_fmac_f32_e32 v33, v44, v44
	v_add_f32_e32 v32, v33, v32
	v_mul_f32_e32 v33, v47, v47
	v_fmac_f32_e32 v33, v46, v46
	v_add_f32_e32 v32, v33, v32
	v_add_f32_e32 v32, v50, v32
	ds_bpermute_b32 v33, v243, v32
	s_waitcnt lgkmcnt(1)
	v_lshl_add_u64 v[48:49], s[14:15], 0, v[222:223]
	v_lshl_add_u64 v[48:49], v[208:209], 1, v[48:49]
	v_cvt_pk_bf16_f32 v42, v42, v43
	v_cvt_pk_bf16_f32 v43, v52, v53
	s_waitcnt lgkmcnt(0)
	v_add_f32_e32 v32, v32, v33
	ds_bpermute_b32 v33, v244, v32
	global_store_dwordx4 v[48:49], v[40:43], off nt
	v_cvt_pk_bf16_f32 v34, v36, v37
	v_cvt_pk_bf16_f32 v35, v38, v39
	v_cvt_pk_bf16_f32 v36, v44, v45
	v_cvt_pk_bf16_f32 v37, v46, v47
	global_store_dwordx4 v[48:49], v[34:37], off offset:256 nt
	s_and_saveexec_b64 s[36:37], s[2:3]
	s_cbranch_execz .LBB0_445
	s_waitcnt lgkmcnt(0)
	v_add_f32_e32 v34, v32, v33
	v_lshlrev_b64 v[32:33], 6, v[216:217]
	v_lshl_add_u64 v[32:33], s[16:17], 0, v[32:33]
	v_lshl_add_u64 v[32:33], s[30:31], 2, v[32:33]
	s_lshl_b32 s8, s55, 2
	v_lshl_add_u64 v[32:33], v[32:33], 0, s[8:9]
	global_store_dword v[32:33], v34, off
.LBB0_445:
	s_or_b64 exec, exec, s[36:37]
	v_lshlrev_b32_e32 v34, 16, v128
	v_and_b32_e32 v35, 0xffff0000, v128
	v_lshlrev_b32_e32 v36, 16, v129
	v_and_b32_e32 v37, 0xffff0000, v129
	v_pk_add_f32 v[30:31], v[30:31], v[36:37]
	v_pk_add_f32 v[28:29], v[28:29], v[34:35]
	v_lshlrev_b32_e32 v34, 16, v130
	v_and_b32_e32 v35, 0xffff0000, v130
	v_lshlrev_b32_e32 v36, 16, v131
	v_and_b32_e32 v37, 0xffff0000, v131
	v_pk_add_f32 v[36:37], v[26:27], v[36:37]
	v_pk_add_f32 v[26:27], v[24:25], v[34:35]
	v_mul_f32_e32 v24, v29, v29
	v_mul_f32_e32 v25, v31, v31
	v_fmac_f32_e32 v24, v28, v28
	v_fmac_f32_e32 v25, v30, v30
	v_add_f32_e32 v24, v24, v25
	v_mul_f32_e32 v25, v27, v27
	v_fmac_f32_e32 v25, v26, v26
	v_add_f32_e32 v24, v25, v24
	v_mul_f32_e32 v25, v37, v37
	v_fmac_f32_e32 v25, v36, v36
	v_add_f32_e32 v34, v25, v24
	v_cvt_pk_bf16_f32 v24, v28, v29
	v_cvt_pk_bf16_f32 v25, v30, v31
	v_lshlrev_b32_e32 v28, 16, v116
	v_and_b32_e32 v29, 0xffff0000, v116
	v_lshlrev_b32_e32 v30, 16, v117
	v_and_b32_e32 v31, 0xffff0000, v117
	v_pk_add_f32 v[22:23], v[22:23], v[30:31]
	v_pk_add_f32 v[20:21], v[20:21], v[28:29]
	v_lshlrev_b32_e32 v28, 16, v118
	v_and_b32_e32 v29, 0xffff0000, v118
	v_pk_add_f32 v[28:29], v[16:17], v[28:29]
	v_mul_f32_e32 v16, v21, v21
	v_mul_f32_e32 v17, v23, v23
	v_fmac_f32_e32 v16, v20, v20
	v_fmac_f32_e32 v17, v22, v22
	v_lshlrev_b32_e32 v30, 16, v119
	v_and_b32_e32 v31, 0xffff0000, v119
	v_add_f32_e32 v16, v16, v17
	v_mul_f32_e32 v17, v29, v29
	v_pk_add_f32 v[30:31], v[18:19], v[30:31]
	v_fmac_f32_e32 v17, v28, v28
	v_add_f32_e32 v16, v17, v16
	v_mul_f32_e32 v17, v31, v31
	v_fmac_f32_e32 v17, v30, v30
	v_add_f32_e32 v16, v17, v16
	v_add_f32_e32 v16, v34, v16
	ds_bpermute_b32 v17, v243, v16
	s_waitcnt lgkmcnt(1)
	v_lshl_add_u64 v[32:33], s[14:15], 0, v[218:219]
	v_lshl_add_u64 v[32:33], v[208:209], 1, v[32:33]
	v_cvt_pk_bf16_f32 v26, v26, v27
	v_cvt_pk_bf16_f32 v27, v36, v37
	s_waitcnt lgkmcnt(0)
	v_add_f32_e32 v16, v16, v17
	ds_bpermute_b32 v17, v244, v16
	global_store_dwordx4 v[32:33], v[24:27], off nt
	v_cvt_pk_bf16_f32 v18, v20, v21
	v_cvt_pk_bf16_f32 v19, v22, v23
	v_cvt_pk_bf16_f32 v20, v28, v29
	v_cvt_pk_bf16_f32 v21, v30, v31
	global_store_dwordx4 v[32:33], v[18:21], off offset:256 nt
	s_and_saveexec_b64 s[36:37], s[2:3]
	s_cbranch_execz .LBB0_447
	s_waitcnt lgkmcnt(0)
	v_add_f32_e32 v18, v16, v17
	v_lshlrev_b64 v[16:17], 6, v[212:213]
	v_lshl_add_u64 v[16:17], s[16:17], 0, v[16:17]
	v_lshl_add_u64 v[16:17], s[30:31], 2, v[16:17]
	s_lshl_b32 s8, s55, 2
	v_lshl_add_u64 v[16:17], v[16:17], 0, s[8:9]
	global_store_dword v[16:17], v18, off
.LBB0_447:
	s_or_b64 exec, exec, s[36:37]
	v_lshlrev_b32_e32 v18, 16, v124
	v_and_b32_e32 v19, 0xffff0000, v124
	v_lshlrev_b32_e32 v20, 16, v125
	v_and_b32_e32 v21, 0xffff0000, v125
	v_pk_add_f32 v[14:15], v[14:15], v[20:21]
	v_pk_add_f32 v[12:13], v[12:13], v[18:19]
	v_lshlrev_b32_e32 v18, 16, v126
	v_and_b32_e32 v19, 0xffff0000, v126
	v_lshlrev_b32_e32 v20, 16, v127
	v_and_b32_e32 v21, 0xffff0000, v127
	v_pk_add_f32 v[20:21], v[10:11], v[20:21]
	v_pk_add_f32 v[10:11], v[8:9], v[18:19]
	v_mul_f32_e32 v8, v13, v13
	v_mul_f32_e32 v9, v15, v15
	v_fmac_f32_e32 v8, v12, v12
	v_fmac_f32_e32 v9, v14, v14
	v_add_f32_e32 v8, v8, v9
	v_mul_f32_e32 v9, v11, v11
	v_fmac_f32_e32 v9, v10, v10
	v_add_f32_e32 v8, v9, v8
	v_mul_f32_e32 v9, v21, v21
	v_fmac_f32_e32 v9, v20, v20
	v_add_f32_e32 v18, v9, v8
	v_cvt_pk_bf16_f32 v8, v12, v13
	v_cvt_pk_bf16_f32 v9, v14, v15
	v_lshlrev_b32_e32 v12, 16, v112
	v_and_b32_e32 v13, 0xffff0000, v112
	v_lshlrev_b32_e32 v14, 16, v113
	v_and_b32_e32 v15, 0xffff0000, v113
	v_pk_add_f32 v[6:7], v[6:7], v[14:15]
	v_pk_add_f32 v[4:5], v[4:5], v[12:13]
	v_lshlrev_b32_e32 v12, 16, v114
	v_and_b32_e32 v13, 0xffff0000, v114
	v_pk_add_f32 v[12:13], v[0:1], v[12:13]
	v_mul_f32_e32 v0, v5, v5
	v_mul_f32_e32 v1, v7, v7
	v_fmac_f32_e32 v0, v4, v4
	v_fmac_f32_e32 v1, v6, v6
	v_lshlrev_b32_e32 v14, 16, v115
	v_and_b32_e32 v15, 0xffff0000, v115
	v_add_f32_e32 v0, v0, v1
	v_mul_f32_e32 v1, v13, v13
	v_pk_add_f32 v[14:15], v[2:3], v[14:15]
	v_fmac_f32_e32 v1, v12, v12
	v_add_f32_e32 v0, v1, v0
	v_mul_f32_e32 v1, v15, v15
	v_fmac_f32_e32 v1, v14, v14
	v_add_f32_e32 v0, v1, v0
	v_add_f32_e32 v0, v18, v0
	ds_bpermute_b32 v1, v243, v0
	s_waitcnt lgkmcnt(1)
	v_lshl_add_u64 v[16:17], s[14:15], 0, v[214:215]
	v_lshl_add_u64 v[16:17], v[208:209], 1, v[16:17]
	v_cvt_pk_bf16_f32 v10, v10, v11
	v_cvt_pk_bf16_f32 v11, v20, v21
	s_waitcnt lgkmcnt(0)
	v_add_f32_e32 v0, v0, v1
	ds_bpermute_b32 v1, v244, v0
	global_store_dwordx4 v[16:17], v[8:11], off nt
	v_cvt_pk_bf16_f32 v2, v4, v5
	v_cvt_pk_bf16_f32 v3, v6, v7
	v_cvt_pk_bf16_f32 v4, v12, v13
	v_cvt_pk_bf16_f32 v5, v14, v15
	global_store_dwordx4 v[16:17], v[2:5], off offset:256 nt
	s_and_saveexec_b64 s[36:37], s[2:3]
	s_cbranch_execz .LBB0_449
	s_waitcnt lgkmcnt(0)
	v_add_f32_e32 v2, v0, v1
	v_lshlrev_b64 v[0:1], 6, v[210:211]
	v_lshl_add_u64 v[0:1], s[16:17], 0, v[0:1]
	v_lshl_add_u64 v[0:1], s[30:31], 2, v[0:1]
	s_lshl_b32 s8, s55, 2
	v_lshl_add_u64 v[0:1], v[0:1], 0, s[8:9]
	global_store_dword v[0:1], v2, off

.LBB0_642:
	ds_read2_b32 v[214:215], v146 offset1:32
	s_addk_i32 s24, 0x400
	s_addk_i32 s52, 0x400
	s_add_i32 s53, s53, 0x10000
	s_waitcnt vmcnt(0) lgkmcnt(0)
	v_mul_f32_e32 v77, v68, v214
	ds_read_b32 v209, v147
	ds_read_b32 v211, v148
	ds_read_b32 v212, v149
	ds_read_b32 v213, v150
	ds_read_b32 v214, v151
	ds_read_b32 v216, v152
	ds_read_b32 v217, v153
	ds_read_b32 v218, v154
	s_waitcnt lgkmcnt(7)
	v_mul_f32_e32 v209, v69, v209
	v_cvt_pk_bf16_f32 v210, v77, v209
	s_waitcnt lgkmcnt(6)
	v_mul_f32_e32 v77, v70, v211
	s_waitcnt lgkmcnt(5)
	v_mul_f32_e32 v209, v71, v212
	v_cvt_pk_bf16_f32 v211, v77, v209
	s_waitcnt lgkmcnt(4)
	v_mul_f32_e32 v77, v64, v213
	s_waitcnt lgkmcnt(3)
	v_mul_f32_e32 v209, v65, v214
	v_cvt_pk_bf16_f32 v212, v77, v209
	s_waitcnt lgkmcnt(2)
	v_mul_f32_e32 v77, v66, v216
	s_waitcnt lgkmcnt(1)
	v_mul_f32_e32 v209, v67, v217
	v_cvt_pk_bf16_f32 v213, v77, v209
	v_add_u32_e32 v77, s26, v138
	v_mad_i64_i32 v[216:217], s[4:5], s25, v77, 0
	v_lshl_add_u64 v[216:217], v[216:217], 1, s[2:3]
	s_lshl_b64 s[4:5], s[6:7], 1
	v_lshl_add_u64 v[216:217], v[216:217], 0, s[4:5]
	v_lshl_add_u64 v[216:217], v[216:217], 0, v[72:73]
	global_store_dwordx4 v[216:217], v[210:213], off nt
	s_waitcnt lgkmcnt(0)
	v_mul_f32_e32 v77, v68, v218
	ds_read_b32 v209, v155
	ds_read_b32 v211, v156
	ds_read_b32 v212, v157
	ds_read_b32 v213, v158
	ds_read_b32 v214, v159
	ds_read_b32 v216, v160
	ds_read_b32 v217, v161
	ds_read_b32 v218, v162
	s_waitcnt lgkmcnt(7)
	v_mul_f32_e32 v209, v69, v209
	v_cvt_pk_bf16_f32 v210, v77, v209
	s_waitcnt lgkmcnt(6)
	v_mul_f32_e32 v77, v70, v211
	s_waitcnt lgkmcnt(5)
	v_mul_f32_e32 v209, v71, v212
	v_cvt_pk_bf16_f32 v211, v77, v209
	s_waitcnt lgkmcnt(4)
	v_mul_f32_e32 v77, v64, v213
	s_waitcnt lgkmcnt(3)
	v_mul_f32_e32 v209, v65, v214
	v_cvt_pk_bf16_f32 v212, v77, v209
	s_waitcnt lgkmcnt(2)
	v_mul_f32_e32 v77, v66, v216
	s_waitcnt lgkmcnt(1)
	v_mul_f32_e32 v209, v67, v217
	v_cvt_pk_bf16_f32 v213, v77, v209
	v_add_u32_e32 v77, s26, v139
	v_mad_i64_i32 v[216:217], s[6:7], s25, v77, 0
	v_lshl_add_u64 v[216:217], v[216:217], 1, s[2:3]
	v_lshl_add_u64 v[216:217], v[216:217], 0, s[4:5]
	v_lshl_add_u64 v[216:217], v[216:217], 0, v[72:73]
	global_store_dwordx4 v[216:217], v[210:213], off nt
	s_waitcnt lgkmcnt(0)
	v_mul_f32_e32 v77, v68, v218
	ds_read_b32 v209, v163
	ds_read_b32 v211, v164
	ds_read_b32 v212, v165
	ds_read_b32 v213, v166
	ds_read_b32 v214, v167
	ds_read_b32 v216, v168
	ds_read_b32 v217, v169
	ds_read_b32 v218, v170
	s_waitcnt lgkmcnt(7)
	v_mul_f32_e32 v209, v69, v209
	v_cvt_pk_bf16_f32 v210, v77, v209
	s_waitcnt lgkmcnt(6)
	v_mul_f32_e32 v77, v70, v211
	s_waitcnt lgkmcnt(5)
	v_mul_f32_e32 v209, v71, v212
	v_cvt_pk_bf16_f32 v211, v77, v209
	s_waitcnt lgkmcnt(4)
	v_mul_f32_e32 v77, v64, v213
	s_waitcnt lgkmcnt(3)
	v_mul_f32_e32 v209, v65, v214
	v_cvt_pk_bf16_f32 v212, v77, v209
	s_waitcnt lgkmcnt(2)
	v_mul_f32_e32 v77, v66, v216
	s_waitcnt lgkmcnt(1)
	v_mul_f32_e32 v209, v67, v217
	v_cvt_pk_bf16_f32 v213, v77, v209
	v_add_u32_e32 v77, s26, v140
	v_mad_i64_i32 v[216:217], s[6:7], s25, v77, 0
	v_lshl_add_u64 v[216:217], v[216:217], 1, s[2:3]
	v_lshl_add_u64 v[216:217], v[216:217], 0, s[4:5]
	v_lshl_add_u64 v[216:217], v[216:217], 0, v[72:73]
	global_store_dwordx4 v[216:217], v[210:213], off nt
	s_waitcnt lgkmcnt(0)
	v_mul_f32_e32 v77, v68, v218
	ds_read_b32 v209, v171
	ds_read_b32 v211, v172
	ds_read_b32 v212, v173
	ds_read_b32 v213, v174
	ds_read_b32 v214, v175
	ds_read_b32 v216, v176
	ds_read_b32 v217, v177
	ds_read_b32 v218, v178
	s_waitcnt lgkmcnt(7)
	v_mul_f32_e32 v209, v69, v209
	v_cvt_pk_bf16_f32 v210, v77, v209
	s_waitcnt lgkmcnt(6)
	v_mul_f32_e32 v77, v70, v211
	s_waitcnt lgkmcnt(5)
	v_mul_f32_e32 v209, v71, v212
	v_cvt_pk_bf16_f32 v211, v77, v209
	s_waitcnt lgkmcnt(4)
	v_mul_f32_e32 v77, v64, v213
	s_waitcnt lgkmcnt(3)
	v_mul_f32_e32 v209, v65, v214
	v_cvt_pk_bf16_f32 v212, v77, v209
	s_waitcnt lgkmcnt(2)
	v_mul_f32_e32 v77, v66, v216
	s_waitcnt lgkmcnt(1)
	v_mul_f32_e32 v209, v67, v217
	v_cvt_pk_bf16_f32 v213, v77, v209
	v_add_u32_e32 v77, s26, v141
	v_mad_i64_i32 v[216:217], s[6:7], s25, v77, 0
	v_lshl_add_u64 v[216:217], v[216:217], 1, s[2:3]
	v_lshl_add_u64 v[216:217], v[216:217], 0, s[4:5]
	v_lshl_add_u64 v[216:217], v[216:217], 0, v[72:73]
	global_store_dwordx4 v[216:217], v[210:213], off nt
	v_mul_f32_e32 v77, v68, v215
	s_waitcnt lgkmcnt(0)
	v_mul_f32_e32 v209, v69, v218
	v_cvt_pk_bf16_f32 v210, v77, v209
	ds_read_b32 v77, v179
	ds_read_b32 v209, v180
	ds_read_b32 v212, v181
	ds_read_b32 v213, v182
	ds_read_b32 v214, v183
	ds_read_b32 v215, v184
	ds_read_b32 v216, v185
	ds_read_b32 v217, v186
	s_waitcnt lgkmcnt(7)
	v_mul_f32_e32 v77, v70, v77
	s_waitcnt lgkmcnt(6)
	v_mul_f32_e32 v209, v71, v209
	v_cvt_pk_bf16_f32 v211, v77, v209
	s_waitcnt lgkmcnt(5)
	v_mul_f32_e32 v77, v64, v212
	s_waitcnt lgkmcnt(4)
	v_mul_f32_e32 v209, v65, v213
	v_cvt_pk_bf16_f32 v212, v77, v209
	s_waitcnt lgkmcnt(3)
	v_mul_f32_e32 v77, v66, v214
	s_waitcnt lgkmcnt(2)
	v_mul_f32_e32 v209, v67, v215
	v_cvt_pk_bf16_f32 v213, v77, v209
	v_add_u32_e32 v77, s26, v142
	v_mad_i64_i32 v[214:215], s[6:7], s25, v77, 0
	v_lshl_add_u64 v[214:215], v[214:215], 1, s[2:3]
	v_lshl_add_u64 v[214:215], v[214:215], 0, s[4:5]
	v_lshl_add_u64 v[214:215], v[214:215], 0, v[72:73]
	global_store_dwordx4 v[214:215], v[210:213], off nt
	s_waitcnt lgkmcnt(1)
	v_mul_f32_e32 v77, v68, v216
	s_waitcnt lgkmcnt(0)
	v_mul_f32_e32 v209, v69, v217
	v_cvt_pk_bf16_f32 v210, v77, v209
	ds_read_b32 v77, v187
	ds_read_b32 v209, v188
	ds_read_b32 v212, v189
	ds_read_b32 v213, v190
	ds_read_b32 v214, v191
	ds_read_b32 v215, v192
	ds_read_b32 v216, v193
	ds_read_b32 v217, v194
	s_waitcnt lgkmcnt(7)
	v_mul_f32_e32 v77, v70, v77
	s_waitcnt lgkmcnt(6)
	v_mul_f32_e32 v209, v71, v209
	v_cvt_pk_bf16_f32 v211, v77, v209
	s_waitcnt lgkmcnt(5)
	v_mul_f32_e32 v77, v64, v212
	s_waitcnt lgkmcnt(4)
	v_mul_f32_e32 v209, v65, v213
	v_cvt_pk_bf16_f32 v212, v77, v209
	s_waitcnt lgkmcnt(3)
	v_mul_f32_e32 v77, v66, v214
	s_waitcnt lgkmcnt(2)
	v_mul_f32_e32 v209, v67, v215
	v_cvt_pk_bf16_f32 v213, v77, v209
	v_add_u32_e32 v77, s26, v143
	v_mad_i64_i32 v[214:215], s[6:7], s25, v77, 0
	v_lshl_add_u64 v[214:215], v[214:215], 1, s[2:3]
	v_lshl_add_u64 v[214:215], v[214:215], 0, s[4:5]
	v_lshl_add_u64 v[214:215], v[214:215], 0, v[72:73]
	global_store_dwordx4 v[214:215], v[210:213], off nt
	s_waitcnt lgkmcnt(1)
	v_mul_f32_e32 v77, v68, v216
	s_waitcnt lgkmcnt(0)
	v_mul_f32_e32 v209, v69, v217
	v_cvt_pk_bf16_f32 v210, v77, v209
	ds_read_b32 v77, v195
	ds_read_b32 v209, v196
	ds_read_b32 v212, v197
	ds_read_b32 v213, v198
	ds_read_b32 v214, v199
	ds_read_b32 v215, v200
	ds_read_b32 v216, v201
	ds_read_b32 v217, v202
	s_waitcnt lgkmcnt(7)
	v_mul_f32_e32 v77, v70, v77
	s_waitcnt lgkmcnt(6)
	v_mul_f32_e32 v209, v71, v209
	v_cvt_pk_bf16_f32 v211, v77, v209
	s_waitcnt lgkmcnt(5)
	v_mul_f32_e32 v77, v64, v212
	s_waitcnt lgkmcnt(4)
	v_mul_f32_e32 v209, v65, v213
	v_cvt_pk_bf16_f32 v212, v77, v209
	s_waitcnt lgkmcnt(3)
	v_mul_f32_e32 v77, v66, v214
	s_waitcnt lgkmcnt(2)
	v_mul_f32_e32 v209, v67, v215
	v_cvt_pk_bf16_f32 v213, v77, v209
	v_add_u32_e32 v77, s26, v144
	v_mad_i64_i32 v[214:215], s[6:7], s25, v77, 0
	v_lshl_add_u64 v[214:215], v[214:215], 1, s[2:3]
	v_lshl_add_u64 v[214:215], v[214:215], 0, s[4:5]
	v_lshl_add_u64 v[214:215], v[214:215], 0, v[72:73]
	global_store_dwordx4 v[214:215], v[210:213], off nt
	ds_read_b32 v77, v203
	ds_read_b32 v209, v204
	ds_read_b32 v210, v205
	ds_read_b32 v211, v206
	ds_read_b32 v212, v207
	ds_read_b32 v213, v208
	s_waitcnt lgkmcnt(7)
	v_mul_f32_e32 v68, v68, v216
	s_waitcnt lgkmcnt(6)
	v_mul_f32_e32 v69, v69, v217
	v_cvt_pk_bf16_f32 v68, v68, v69
	s_waitcnt lgkmcnt(5)
	v_mul_f32_e32 v69, v70, v77
	s_waitcnt lgkmcnt(4)
	v_mul_f32_e32 v70, v71, v209
	s_waitcnt lgkmcnt(3)
	v_mul_f32_e32 v64, v64, v210
	v_cvt_pk_bf16_f32 v69, v69, v70
	s_waitcnt lgkmcnt(2)
	v_mul_f32_e32 v65, v65, v211
	v_cvt_pk_bf16_f32 v70, v64, v65
	s_waitcnt lgkmcnt(1)
	v_mul_f32_e32 v64, v66, v212
	s_waitcnt lgkmcnt(0)
	v_mul_f32_e32 v65, v67, v213
	v_cvt_pk_bf16_f32 v71, v64, v65
	v_add_u32_e32 v64, s26, v145
	v_mad_i64_i32 v[64:65], s[6:7], s25, v64, 0
	v_lshl_add_u64 v[64:65], v[64:65], 1, s[2:3]
	v_lshl_add_u64 v[64:65], v[64:65], 0, s[4:5]
	v_lshl_add_u64 v[64:65], v[64:65], 0, v[72:73]
	global_store_dwordx4 v[64:65], v[68:71], off nt
	s_waitcnt lgkmcnt(0)
	s_cmpk_lt_i32 s54, 0x400
	s_mov_b32 s26, s22
	s_mov_b64 s[2:3], s[8:9]
	s_mov_b64 s[4:5], s[12:13]
	s_mov_b32 s25, s55
	s_mov_b32 s6, s16
	s_cbranch_scc0 .LBB0_676

.LBB0_794:
	v_add_u32_e32 v140, s65, v137
	v_ashrrev_i32_e32 v141, 31, v140
	v_lshl_add_u64 v[134:135], v[140:141], 2, s[16:17]
	global_load_dword v142, v[134:135], off
	v_mov_b32_e32 v162, v120
	v_add_u32_e32 v120, 16, v140
	v_mov_b32_e32 v163, v112
	v_mov_b32_e32 v112, v121
	v_ashrrev_i32_e32 v121, 31, v120
	v_lshl_add_u64 v[120:121], v[120:121], 2, s[16:17]
	global_load_dword v174, v[120:121], off
	v_mov_b32_e32 v160, v124
	v_mov_b32_e32 v164, v126
	v_mov_b32_e32 v166, v122
	v_add_u32_e32 v122, 32, v140
	v_add_u32_e32 v124, 48, v140
	v_add_u32_e32 v126, 0x80, v140
	v_mov_b32_e32 v161, v116
	v_mov_b32_e32 v116, v125
	v_mov_b32_e32 v165, v118
	v_mov_b32_e32 v167, v114
	v_mov_b32_e32 v118, v127
	v_mov_b32_e32 v114, v123
	v_add_u32_e32 v168, 0x90, v140
	v_add_u32_e32 v170, 0xa0, v140
	v_add_u32_e32 v140, 0xb0, v140
	v_ashrrev_i32_e32 v123, 31, v122
	v_ashrrev_i32_e32 v125, 31, v124
	v_ashrrev_i32_e32 v127, 31, v126
	v_ashrrev_i32_e32 v169, 31, v168
	v_ashrrev_i32_e32 v171, 31, v170
	v_ashrrev_i32_e32 v141, 31, v140
	v_lshl_add_u64 v[120:121], v[122:123], 2, s[16:17]
	v_lshl_add_u64 v[122:123], v[124:125], 2, s[16:17]
	v_lshl_add_u64 v[124:125], v[126:127], 2, s[16:17]
	v_lshl_add_u64 v[168:169], v[168:169], 2, s[16:17]
	v_lshl_add_u64 v[170:171], v[170:171], 2, s[16:17]
	v_lshl_add_u64 v[140:141], v[140:141], 2, s[16:17]
	global_load_dword v136, v[120:121], off
	global_load_dword v132, v[122:123], off
	global_load_dword v126, v[124:125], off
	s_nop 0
	global_load_dword v124, v[168:169], off
	global_load_dword v122, v[170:171], off
	global_load_dword v120, v[140:141], off
	v_lshl_or_b32 v144, s28, 7, v151
	v_lshl_add_u32 v138, s64, 8, v137
	v_mov_b64_e32 v[134:135], s[14:15]
	v_ashrrev_i32_e32 v145, 31, v144
	v_mad_i64_i32 v[172:173], s[30:31], v138, s59, v[134:135]
	s_and_b64 vcc, exec, s[2:3]
	s_mov_b64 s[2:3], -1
	s_waitcnt vmcnt(0)
	v_pk_mul_f32 v[116:117], v[116:117], v[142:143] op_sel_hi:[1,0]
	v_pk_mul_f32 v[112:113], v[112:113], v[142:143] op_sel_hi:[1,0]
	v_mul_f32_e32 v125, 0xbfb8aa3b, v117
	v_mul_f32_e32 v127, 0xbfb8aa3b, v113
	v_exp_f32_e32 v125, v125
	v_exp_f32_e32 v127, v127
	v_pk_mul_f32 v[140:141], v[160:161], v[142:143] op_sel_hi:[1,0]
	v_pk_mul_f32 v[160:161], v[162:163], v[142:143] op_sel_hi:[1,0]
	v_pk_mul_f32 v[162:163], v[164:165], v[142:143] op_sel_hi:[1,0]
	v_pk_mul_f32 v[164:165], v[166:167], v[142:143] op_sel_hi:[1,0]
	v_pk_mul_f32 v[118:119], v[118:119], v[142:143] op_sel_hi:[1,0]
	v_pk_mul_f32 v[114:115], v[114:115], v[142:143] op_sel_hi:[1,0]
	v_mul_f32_e32 v121, 0xbfb8aa3b, v141
	v_mul_f32_e32 v143, 0xbfb8aa3b, v165
	v_add_f32_e32 v125, 1.0, v125
	v_add_f32_e32 v127, 1.0, v127
	v_mul_f32_e32 v159, 0xbfb8aa3b, v119
	v_exp_f32_e32 v121, v121
	v_exp_f32_e32 v143, v143
	v_rcp_f32_e32 v125, v125
	v_rcp_f32_e32 v127, v127
	v_mul_f32_e32 v166, 0xbfb8aa3b, v115
	v_exp_f32_e32 v159, v159
	v_mul_f32_e32 v142, 0xbfb8aa3b, v163
	v_exp_f32_e32 v166, v166
	v_mul_f32_e32 v123, 0xbfb8aa3b, v161
	v_exp_f32_e32 v142, v142
	v_exp_f32_e32 v123, v123
	v_add_f32_e32 v121, 1.0, v121
	v_add_f32_e32 v143, 1.0, v143
	v_mul_f32_e32 v117, v117, v125
	v_mul_f32_e32 v113, v113, v127
	v_rcp_f32_e32 v121, v121
	v_rcp_f32_e32 v143, v143
	v_mul_f32_e32 v116, v116, v117
	v_mul_f32_e32 v117, v112, v113
	v_add_f32_e32 v113, 1.0, v159
	v_rcp_f32_e32 v113, v113
	v_add_f32_e32 v127, 1.0, v166
	v_add_f32_e32 v142, 1.0, v142
	v_rcp_f32_e32 v127, v127
	v_add_f32_e32 v123, 1.0, v123
	v_rcp_f32_e32 v142, v142
	v_rcp_f32_e32 v123, v123
	v_mul_f32_e32 v121, v141, v121
	v_mul_f32_e32 v112, v165, v143
	v_mul_f32_e32 v121, v140, v121
	v_mul_f32_e32 v140, v164, v112
	v_mul_f32_e32 v112, v119, v113
	v_mul_f32_e32 v141, v118, v112
	v_mul_f32_e32 v112, v115, v127
	v_mul_f32_e32 v125, v163, v142
	v_mul_f32_e32 v127, v114, v112
	v_lshlrev_b64 v[112:113], 1, v[144:145]
	v_mul_f32_e32 v123, v161, v123
	v_mul_f32_e32 v125, v162, v125
	v_lshl_add_u64 v[118:119], v[172:173], 0, v[112:113]
	v_cvt_pk_bf16_f32 v114, v121, v116
	v_cvt_pk_bf16_f32 v115, v125, v141
	v_mul_f32_e32 v123, v160, v123
	v_cvt_pk_bf16_f32 v116, v123, v117
	v_cvt_pk_bf16_f32 v117, v140, v127
	global_store_dwordx4 v[118:119], v[114:117], off nt
	s_nop 1
	v_mov_b32_e32 v114, v100
	v_mov_b32_e32 v115, v108
	v_pk_mul_f32 v[114:115], v[114:115], v[174:175] op_sel_hi:[1,0]
	v_mov_b32_e32 v116, v96
	v_mul_f32_e32 v100, 0xbfb8aa3b, v115
	v_mov_b32_e32 v117, v104
	v_exp_f32_e32 v100, v100
	v_pk_mul_f32 v[116:117], v[116:117], v[174:175] op_sel_hi:[1,0]
	v_mov_b32_e32 v108, v101
	v_mul_f32_e32 v96, 0xbfb8aa3b, v117
	v_exp_f32_e32 v96, v96
	v_add_f32_e32 v100, 1.0, v100
	v_rcp_f32_e32 v100, v100
	v_or_b32_e32 v104, 16, v138
	v_add_f32_e32 v96, 1.0, v96
	v_rcp_f32_e32 v96, v96
	v_mul_f32_e32 v100, v115, v100
	v_mul_f32_e32 v114, v114, v100
	v_pk_mul_f32 v[100:101], v[108:109], v[174:175] op_sel_hi:[1,0]
	v_mad_i64_i32 v[118:119], s[30:31], v104, s59, v[134:135]
	v_mul_f32_e32 v115, v117, v96
	v_mul_f32_e32 v96, 0xbfb8aa3b, v101
	v_mov_b32_e32 v104, v97
	v_exp_f32_e32 v108, v96
	v_pk_mul_f32 v[96:97], v[104:105], v[174:175] op_sel_hi:[1,0]
	v_mul_f32_e32 v109, v116, v115
	v_mul_f32_e32 v104, 0xbfb8aa3b, v97
	v_exp_f32_e32 v104, v104
	v_add_f32_e32 v105, 1.0, v108
	v_rcp_f32_e32 v108, v105
	v_mov_b32_e32 v105, v110
	v_add_f32_e32 v104, 1.0, v104
	v_rcp_f32_e32 v115, v104
	v_mov_b32_e32 v104, v102
	v_pk_mul_f32 v[104:105], v[104:105], v[174:175] op_sel_hi:[1,0]
	v_mul_f32_e32 v101, v101, v108
	v_mul_f32_e32 v102, 0xbfb8aa3b, v105
	v_exp_f32_e32 v102, v102
	v_mul_f32_e32 v108, v100, v101
	v_mov_b32_e32 v101, v106
	v_mul_f32_e32 v97, v97, v115
	v_add_f32_e32 v100, 1.0, v102
	v_rcp_f32_e32 v102, v100
	v_mov_b32_e32 v100, v98
	v_pk_mul_f32 v[100:101], v[100:101], v[174:175] op_sel_hi:[1,0]
	v_mul_f32_e32 v115, v96, v97
	v_mul_f32_e32 v98, 0xbfb8aa3b, v101
	v_exp_f32_e32 v98, v98
	v_mul_f32_e32 v96, v105, v102
	v_mul_f32_e32 v102, v104, v96
	v_mov_b32_e32 v110, v103
	v_add_f32_e32 v96, 1.0, v98
	v_rcp_f32_e32 v104, v96
	v_pk_mul_f32 v[96:97], v[110:111], v[174:175] op_sel_hi:[1,0]
	v_mov_b32_e32 v106, v99
	v_mul_f32_e32 v98, 0xbfb8aa3b, v97
	v_exp_f32_e32 v103, v98
	v_pk_mul_f32 v[98:99], v[106:107], v[174:175] op_sel_hi:[1,0]
	v_mul_f32_e32 v101, v101, v104
	v_mul_f32_e32 v105, 0xbfb8aa3b, v99
	v_exp_f32_e32 v105, v105
	v_add_f32_e32 v103, 1.0, v103
	v_rcp_f32_e32 v103, v103
	v_add_f32_e32 v104, 1.0, v105
	v_rcp_f32_e32 v104, v104
	v_mul_f32_e32 v97, v97, v103
	v_mul_f32_e32 v97, v96, v97
	v_mul_f32_e32 v105, v100, v101
	v_mul_f32_e32 v96, v99, v104
	v_mul_f32_e32 v99, v98, v96
	v_lshl_add_u64 v[100:101], v[118:119], 0, v[112:113]
	v_cvt_pk_bf16_f32 v96, v114, v108
	v_cvt_pk_bf16_f32 v97, v102, v97
	v_cvt_pk_bf16_f32 v98, v109, v115
	v_cvt_pk_bf16_f32 v99, v105, v99
	global_store_dwordx4 v[100:101], v[96:99], off nt
	s_nop 1
	v_mov_b32_e32 v96, v84
	v_mov_b32_e32 v97, v92
	v_pk_mul_f32 v[96:97], v[96:97], v[136:137] op_sel_hi:[1,0]
	v_mov_b32_e32 v98, v80
	v_mul_f32_e32 v84, 0xbfb8aa3b, v97
	v_mov_b32_e32 v99, v88
	v_exp_f32_e32 v84, v84
	v_pk_mul_f32 v[98:99], v[98:99], v[136:137] op_sel_hi:[1,0]
	v_mov_b32_e32 v92, v85
	v_mul_f32_e32 v80, 0xbfb8aa3b, v99
	v_exp_f32_e32 v80, v80
	v_add_f32_e32 v84, 1.0, v84
	v_rcp_f32_e32 v84, v84
	v_or_b32_e32 v88, 32, v138
	v_add_f32_e32 v80, 1.0, v80
	v_rcp_f32_e32 v80, v80
	v_mul_f32_e32 v84, v97, v84
	v_mul_f32_e32 v96, v96, v84
	v_pk_mul_f32 v[84:85], v[92:93], v[136:137] op_sel_hi:[1,0]
	v_mad_i64_i32 v[100:101], s[30:31], v88, s59, v[134:135]
	v_mul_f32_e32 v97, v99, v80
	v_mul_f32_e32 v80, 0xbfb8aa3b, v85
	v_mov_b32_e32 v88, v81
	v_exp_f32_e32 v92, v80
	v_pk_mul_f32 v[80:81], v[88:89], v[136:137] op_sel_hi:[1,0]
	v_mul_f32_e32 v93, v98, v97
	v_mul_f32_e32 v88, 0xbfb8aa3b, v81
	v_exp_f32_e32 v88, v88
	v_add_f32_e32 v89, 1.0, v92
	v_rcp_f32_e32 v92, v89
	v_mov_b32_e32 v89, v94
	v_add_f32_e32 v88, 1.0, v88
	v_rcp_f32_e32 v97, v88
	v_mov_b32_e32 v88, v86
	v_pk_mul_f32 v[88:89], v[88:89], v[136:137] op_sel_hi:[1,0]
	v_mul_f32_e32 v85, v85, v92
	v_mul_f32_e32 v86, 0xbfb8aa3b, v89
	v_exp_f32_e32 v86, v86
	v_mul_f32_e32 v92, v84, v85
	v_mov_b32_e32 v85, v90
	v_mul_f32_e32 v81, v81, v97
	v_add_f32_e32 v84, 1.0, v86
	v_rcp_f32_e32 v86, v84
	v_mov_b32_e32 v84, v82
	v_pk_mul_f32 v[84:85], v[84:85], v[136:137] op_sel_hi:[1,0]
	v_mul_f32_e32 v97, v80, v81
	v_mul_f32_e32 v82, 0xbfb8aa3b, v85
	v_exp_f32_e32 v82, v82
	v_mul_f32_e32 v80, v89, v86
	v_mul_f32_e32 v86, v88, v80
	v_mov_b32_e32 v94, v87
	v_add_f32_e32 v80, 1.0, v82
	v_rcp_f32_e32 v88, v80
	v_pk_mul_f32 v[80:81], v[94:95], v[136:137] op_sel_hi:[1,0]
	v_mov_b32_e32 v90, v83
	v_mul_f32_e32 v82, 0xbfb8aa3b, v81
	v_exp_f32_e32 v87, v82
	v_pk_mul_f32 v[82:83], v[90:91], v[136:137] op_sel_hi:[1,0]
	v_mul_f32_e32 v85, v85, v88
	v_mul_f32_e32 v89, 0xbfb8aa3b, v83
	v_exp_f32_e32 v89, v89
	v_add_f32_e32 v87, 1.0, v87
	v_rcp_f32_e32 v87, v87
	v_add_f32_e32 v88, 1.0, v89
	v_rcp_f32_e32 v88, v88
	v_mul_f32_e32 v81, v81, v87
	v_mul_f32_e32 v81, v80, v81
	v_mul_f32_e32 v89, v84, v85
	v_mul_f32_e32 v80, v83, v88
	v_mul_f32_e32 v83, v82, v80
	v_lshl_add_u64 v[84:85], v[100:101], 0, v[112:113]
	v_cvt_pk_bf16_f32 v80, v96, v92
	v_cvt_pk_bf16_f32 v81, v86, v81
	v_cvt_pk_bf16_f32 v82, v93, v97
	v_cvt_pk_bf16_f32 v83, v89, v83
	global_store_dwordx4 v[84:85], v[80:83], off nt
	s_nop 1
	v_mov_b32_e32 v80, v68
	v_mov_b32_e32 v81, v76
	v_pk_mul_f32 v[80:81], v[80:81], v[132:133] op_sel_hi:[1,0]
	v_mov_b32_e32 v82, v64
	v_mul_f32_e32 v68, 0xbfb8aa3b, v81
	v_mov_b32_e32 v83, v72
	v_exp_f32_e32 v68, v68
	v_pk_mul_f32 v[82:83], v[82:83], v[132:133] op_sel_hi:[1,0]
	v_mov_b32_e32 v76, v69
	v_mul_f32_e32 v64, 0xbfb8aa3b, v83
	v_exp_f32_e32 v64, v64
	v_add_f32_e32 v68, 1.0, v68
	v_rcp_f32_e32 v68, v68
	v_or_b32_e32 v72, 48, v138
	v_add_f32_e32 v64, 1.0, v64
	v_rcp_f32_e32 v64, v64
	v_mul_f32_e32 v68, v81, v68
	v_mul_f32_e32 v80, v80, v68
	v_pk_mul_f32 v[68:69], v[76:77], v[132:133] op_sel_hi:[1,0]
	v_mad_i64_i32 v[84:85], s[30:31], v72, s59, v[134:135]
	v_mul_f32_e32 v81, v83, v64
	v_mul_f32_e32 v64, 0xbfb8aa3b, v69
	v_mov_b32_e32 v72, v65
	v_exp_f32_e32 v76, v64
	v_pk_mul_f32 v[64:65], v[72:73], v[132:133] op_sel_hi:[1,0]
	v_mul_f32_e32 v77, v82, v81
	v_mul_f32_e32 v72, 0xbfb8aa3b, v65
	v_exp_f32_e32 v72, v72
	v_add_f32_e32 v73, 1.0, v76
	v_rcp_f32_e32 v76, v73
	v_mov_b32_e32 v73, v78
	v_add_f32_e32 v72, 1.0, v72
	v_rcp_f32_e32 v81, v72
	v_mov_b32_e32 v72, v70
	v_pk_mul_f32 v[72:73], v[72:73], v[132:133] op_sel_hi:[1,0]
	v_mul_f32_e32 v69, v69, v76
	v_mul_f32_e32 v70, 0xbfb8aa3b, v73
	v_exp_f32_e32 v70, v70
	v_mul_f32_e32 v76, v68, v69
	v_mov_b32_e32 v69, v74
	v_mul_f32_e32 v65, v65, v81
	v_add_f32_e32 v68, 1.0, v70
	v_rcp_f32_e32 v70, v68
	v_mov_b32_e32 v68, v66
	v_pk_mul_f32 v[68:69], v[68:69], v[132:133] op_sel_hi:[1,0]
	v_mul_f32_e32 v81, v64, v65
	v_mul_f32_e32 v66, 0xbfb8aa3b, v69
	v_exp_f32_e32 v66, v66
	v_mul_f32_e32 v64, v73, v70
	v_mul_f32_e32 v70, v72, v64
	v_mov_b32_e32 v78, v71
	v_add_f32_e32 v64, 1.0, v66
	v_rcp_f32_e32 v72, v64
	v_pk_mul_f32 v[64:65], v[78:79], v[132:133] op_sel_hi:[1,0]
	v_mov_b32_e32 v74, v67
	v_mul_f32_e32 v66, 0xbfb8aa3b, v65
	v_exp_f32_e32 v71, v66
	v_pk_mul_f32 v[66:67], v[74:75], v[132:133] op_sel_hi:[1,0]
	v_mul_f32_e32 v69, v69, v72
	v_mul_f32_e32 v73, 0xbfb8aa3b, v67
	v_exp_f32_e32 v73, v73
	v_add_f32_e32 v71, 1.0, v71
	v_rcp_f32_e32 v71, v71
	v_add_f32_e32 v72, 1.0, v73
	v_rcp_f32_e32 v72, v72
	v_mul_f32_e32 v65, v65, v71
	v_mul_f32_e32 v65, v64, v65
	v_mul_f32_e32 v73, v68, v69
	v_mul_f32_e32 v64, v67, v72
	v_mul_f32_e32 v67, v66, v64
	v_lshl_add_u64 v[68:69], v[84:85], 0, v[112:113]
	v_cvt_pk_bf16_f32 v64, v80, v76
	v_cvt_pk_bf16_f32 v65, v70, v65
	v_cvt_pk_bf16_f32 v66, v77, v81
	v_cvt_pk_bf16_f32 v67, v73, v67
	global_store_dwordx4 v[68:69], v[64:67], off nt
	s_nop 1
	v_mov_b32_e32 v64, v52
	v_mov_b32_e32 v65, v60
	v_pk_mul_f32 v[64:65], v[64:65], v[126:127] op_sel_hi:[1,0]
	v_mov_b32_e32 v66, v48
	v_mul_f32_e32 v52, 0xbfb8aa3b, v65
	v_mov_b32_e32 v67, v56
	v_exp_f32_e32 v52, v52
	v_pk_mul_f32 v[66:67], v[66:67], v[126:127] op_sel_hi:[1,0]
	v_mov_b32_e32 v60, v53
	v_mul_f32_e32 v48, 0xbfb8aa3b, v67
	v_exp_f32_e32 v48, v48
	v_add_f32_e32 v52, 1.0, v52
	v_rcp_f32_e32 v52, v52
	v_add_u32_e32 v56, 0x80, v138
	v_add_f32_e32 v48, 1.0, v48
	v_rcp_f32_e32 v48, v48
	v_mul_f32_e32 v52, v65, v52
	v_mul_f32_e32 v64, v64, v52
	v_pk_mul_f32 v[52:53], v[60:61], v[126:127] op_sel_hi:[1,0]
	v_mad_i64_i32 v[68:69], s[30:31], v56, s59, v[134:135]
	v_mul_f32_e32 v65, v67, v48
	v_mul_f32_e32 v48, 0xbfb8aa3b, v53
	v_mov_b32_e32 v56, v49
	v_exp_f32_e32 v60, v48
	v_pk_mul_f32 v[48:49], v[56:57], v[126:127] op_sel_hi:[1,0]
	v_mul_f32_e32 v61, v66, v65
	v_mul_f32_e32 v56, 0xbfb8aa3b, v49
	v_exp_f32_e32 v56, v56
	v_add_f32_e32 v57, 1.0, v60
	v_rcp_f32_e32 v60, v57
	v_mov_b32_e32 v57, v62
	v_add_f32_e32 v56, 1.0, v56
	v_rcp_f32_e32 v65, v56
	v_mov_b32_e32 v56, v54
	v_pk_mul_f32 v[56:57], v[56:57], v[126:127] op_sel_hi:[1,0]
	v_mul_f32_e32 v53, v53, v60
	v_mul_f32_e32 v54, 0xbfb8aa3b, v57
	v_exp_f32_e32 v54, v54
	v_mul_f32_e32 v60, v52, v53
	v_mov_b32_e32 v53, v58
	v_mul_f32_e32 v49, v49, v65
	v_add_f32_e32 v52, 1.0, v54
	v_rcp_f32_e32 v54, v52
	v_mov_b32_e32 v52, v50
	v_pk_mul_f32 v[52:53], v[52:53], v[126:127] op_sel_hi:[1,0]
	v_mul_f32_e32 v65, v48, v49
	v_mul_f32_e32 v50, 0xbfb8aa3b, v53
	v_exp_f32_e32 v50, v50
	v_mul_f32_e32 v48, v57, v54
	v_mul_f32_e32 v54, v56, v48
	v_mov_b32_e32 v62, v55
	v_add_f32_e32 v48, 1.0, v50
	v_rcp_f32_e32 v56, v48
	v_pk_mul_f32 v[48:49], v[62:63], v[126:127] op_sel_hi:[1,0]
	v_mov_b32_e32 v58, v51
	v_mul_f32_e32 v50, 0xbfb8aa3b, v49
	v_exp_f32_e32 v55, v50
	v_pk_mul_f32 v[50:51], v[58:59], v[126:127] op_sel_hi:[1,0]
	v_mul_f32_e32 v53, v53, v56
	v_mul_f32_e32 v57, 0xbfb8aa3b, v51
	v_exp_f32_e32 v57, v57
	v_add_f32_e32 v55, 1.0, v55
	v_rcp_f32_e32 v55, v55
	v_add_f32_e32 v56, 1.0, v57
	v_rcp_f32_e32 v56, v56
	v_mul_f32_e32 v49, v49, v55
	v_mul_f32_e32 v49, v48, v49
	v_mul_f32_e32 v57, v52, v53
	v_mul_f32_e32 v48, v51, v56
	v_mul_f32_e32 v51, v50, v48
	v_lshl_add_u64 v[52:53], v[68:69], 0, v[112:113]
	v_cvt_pk_bf16_f32 v48, v64, v60
	v_cvt_pk_bf16_f32 v49, v54, v49
	v_cvt_pk_bf16_f32 v50, v61, v65
	v_cvt_pk_bf16_f32 v51, v57, v51
	global_store_dwordx4 v[52:53], v[48:51], off nt
	s_nop 1
	v_mov_b32_e32 v48, v36
	v_mov_b32_e32 v49, v44
	v_pk_mul_f32 v[48:49], v[48:49], v[124:125] op_sel_hi:[1,0]
	v_mov_b32_e32 v50, v32
	v_mul_f32_e32 v36, 0xbfb8aa3b, v49
	v_mov_b32_e32 v51, v40
	v_exp_f32_e32 v36, v36
	v_pk_mul_f32 v[50:51], v[50:51], v[124:125] op_sel_hi:[1,0]
	v_mov_b32_e32 v44, v37
	v_mul_f32_e32 v32, 0xbfb8aa3b, v51
	v_exp_f32_e32 v32, v32
	v_add_f32_e32 v36, 1.0, v36
	v_rcp_f32_e32 v36, v36
	v_add_u32_e32 v40, 0x90, v138
	v_add_f32_e32 v32, 1.0, v32
	v_rcp_f32_e32 v32, v32
	v_mul_f32_e32 v36, v49, v36
	v_mul_f32_e32 v48, v48, v36
	v_pk_mul_f32 v[36:37], v[44:45], v[124:125] op_sel_hi:[1,0]
	v_mad_i64_i32 v[52:53], s[30:31], v40, s59, v[134:135]
	v_mul_f32_e32 v49, v51, v32
	v_mul_f32_e32 v32, 0xbfb8aa3b, v37
	v_mov_b32_e32 v40, v33
	v_exp_f32_e32 v44, v32
	v_pk_mul_f32 v[32:33], v[40:41], v[124:125] op_sel_hi:[1,0]
	v_mul_f32_e32 v45, v50, v49
	v_mul_f32_e32 v40, 0xbfb8aa3b, v33
	v_exp_f32_e32 v40, v40
	v_add_f32_e32 v41, 1.0, v44
	v_rcp_f32_e32 v44, v41
	v_mov_b32_e32 v41, v46
	v_add_f32_e32 v40, 1.0, v40
	v_rcp_f32_e32 v49, v40
	v_mov_b32_e32 v40, v38
	v_pk_mul_f32 v[40:41], v[40:41], v[124:125] op_sel_hi:[1,0]
	v_mul_f32_e32 v37, v37, v44
	v_mul_f32_e32 v38, 0xbfb8aa3b, v41
	v_exp_f32_e32 v38, v38
	v_mul_f32_e32 v44, v36, v37
	v_mov_b32_e32 v37, v42
	v_mul_f32_e32 v33, v33, v49
	v_add_f32_e32 v36, 1.0, v38
	v_rcp_f32_e32 v38, v36
	v_mov_b32_e32 v36, v34
	v_pk_mul_f32 v[36:37], v[36:37], v[124:125] op_sel_hi:[1,0]
	v_mul_f32_e32 v49, v32, v33
	v_mul_f32_e32 v34, 0xbfb8aa3b, v37
	v_exp_f32_e32 v34, v34
	v_mul_f32_e32 v32, v41, v38
	v_mul_f32_e32 v38, v40, v32
	v_mov_b32_e32 v46, v39
	v_add_f32_e32 v32, 1.0, v34
	v_rcp_f32_e32 v40, v32
	v_pk_mul_f32 v[32:33], v[46:47], v[124:125] op_sel_hi:[1,0]
	v_mov_b32_e32 v42, v35
	v_mul_f32_e32 v34, 0xbfb8aa3b, v33
	v_exp_f32_e32 v39, v34
	v_pk_mul_f32 v[34:35], v[42:43], v[124:125] op_sel_hi:[1,0]
	v_mul_f32_e32 v37, v37, v40
	v_mul_f32_e32 v41, 0xbfb8aa3b, v35
	v_exp_f32_e32 v41, v41
	v_add_f32_e32 v39, 1.0, v39
	v_rcp_f32_e32 v39, v39
	v_add_f32_e32 v40, 1.0, v41
	v_rcp_f32_e32 v40, v40
	v_mul_f32_e32 v33, v33, v39
	v_mul_f32_e32 v33, v32, v33
	v_mul_f32_e32 v41, v36, v37
	v_mul_f32_e32 v32, v35, v40
	v_mul_f32_e32 v35, v34, v32
	v_lshl_add_u64 v[36:37], v[52:53], 0, v[112:113]
	v_cvt_pk_bf16_f32 v32, v48, v44
	v_cvt_pk_bf16_f32 v33, v38, v33
	v_cvt_pk_bf16_f32 v34, v45, v49
	v_cvt_pk_bf16_f32 v35, v41, v35
	global_store_dwordx4 v[36:37], v[32:35], off nt
	s_nop 1
	v_mov_b32_e32 v32, v20
	v_mov_b32_e32 v33, v28
	v_pk_mul_f32 v[32:33], v[32:33], v[122:123] op_sel_hi:[1,0]
	v_mov_b32_e32 v34, v16
	v_mul_f32_e32 v20, 0xbfb8aa3b, v33
	v_mov_b32_e32 v35, v24
	v_exp_f32_e32 v20, v20
	v_pk_mul_f32 v[34:35], v[34:35], v[122:123] op_sel_hi:[1,0]
	v_mov_b32_e32 v28, v21
	v_mul_f32_e32 v16, 0xbfb8aa3b, v35
	v_exp_f32_e32 v16, v16
	v_add_f32_e32 v20, 1.0, v20
	v_rcp_f32_e32 v20, v20
	v_add_u32_e32 v24, 0xa0, v138
	v_add_f32_e32 v16, 1.0, v16
	v_rcp_f32_e32 v16, v16
	v_mul_f32_e32 v20, v33, v20
	v_mul_f32_e32 v32, v32, v20
	v_pk_mul_f32 v[20:21], v[28:29], v[122:123] op_sel_hi:[1,0]
	v_mad_i64_i32 v[36:37], s[30:31], v24, s59, v[134:135]
	v_mul_f32_e32 v33, v35, v16
	v_mul_f32_e32 v16, 0xbfb8aa3b, v21
	v_mov_b32_e32 v24, v17
	v_exp_f32_e32 v28, v16
	v_pk_mul_f32 v[16:17], v[24:25], v[122:123] op_sel_hi:[1,0]
	v_mul_f32_e32 v29, v34, v33
	v_mul_f32_e32 v24, 0xbfb8aa3b, v17
	v_exp_f32_e32 v24, v24
	v_add_f32_e32 v25, 1.0, v28
	v_rcp_f32_e32 v28, v25
	v_mov_b32_e32 v25, v30
	v_add_f32_e32 v24, 1.0, v24
	v_rcp_f32_e32 v33, v24
	v_mov_b32_e32 v24, v22
	v_pk_mul_f32 v[24:25], v[24:25], v[122:123] op_sel_hi:[1,0]
	v_mul_f32_e32 v21, v21, v28
	v_mul_f32_e32 v22, 0xbfb8aa3b, v25
	v_exp_f32_e32 v22, v22
	v_mul_f32_e32 v28, v20, v21
	v_mov_b32_e32 v21, v26
	v_mul_f32_e32 v17, v17, v33
	v_add_f32_e32 v20, 1.0, v22
	v_rcp_f32_e32 v22, v20
	v_mov_b32_e32 v20, v18
	v_pk_mul_f32 v[20:21], v[20:21], v[122:123] op_sel_hi:[1,0]
	v_mul_f32_e32 v33, v16, v17
	v_mul_f32_e32 v18, 0xbfb8aa3b, v21
	v_exp_f32_e32 v18, v18
	v_mul_f32_e32 v16, v25, v22
	v_mul_f32_e32 v22, v24, v16
	v_mov_b32_e32 v30, v23
	v_add_f32_e32 v16, 1.0, v18
	v_rcp_f32_e32 v24, v16
	v_pk_mul_f32 v[16:17], v[30:31], v[122:123] op_sel_hi:[1,0]
	v_mov_b32_e32 v26, v19
	v_mul_f32_e32 v18, 0xbfb8aa3b, v17
	v_exp_f32_e32 v23, v18
	v_pk_mul_f32 v[18:19], v[26:27], v[122:123] op_sel_hi:[1,0]
	v_mul_f32_e32 v21, v21, v24
	v_mul_f32_e32 v25, 0xbfb8aa3b, v19
	v_exp_f32_e32 v25, v25
	v_add_f32_e32 v23, 1.0, v23
	v_rcp_f32_e32 v23, v23
	v_add_f32_e32 v24, 1.0, v25
	v_rcp_f32_e32 v24, v24
	v_mul_f32_e32 v17, v17, v23
	v_mul_f32_e32 v17, v16, v17
	v_mul_f32_e32 v25, v20, v21
	v_mul_f32_e32 v16, v19, v24
	v_mul_f32_e32 v19, v18, v16
	v_lshl_add_u64 v[20:21], v[36:37], 0, v[112:113]
	v_cvt_pk_bf16_f32 v16, v32, v28
	v_cvt_pk_bf16_f32 v17, v22, v17
	v_cvt_pk_bf16_f32 v18, v29, v33
	v_cvt_pk_bf16_f32 v19, v25, v19
	global_store_dwordx4 v[20:21], v[16:19], off nt
	s_nop 1
	v_mov_b32_e32 v16, v4
	v_mov_b32_e32 v17, v12
	v_pk_mul_f32 v[16:17], v[16:17], v[120:121] op_sel_hi:[1,0]
	v_mov_b32_e32 v18, v0
	v_mul_f32_e32 v4, 0xbfb8aa3b, v17
	v_mov_b32_e32 v19, v8
	v_exp_f32_e32 v4, v4
	v_pk_mul_f32 v[18:19], v[18:19], v[120:121] op_sel_hi:[1,0]
	v_mov_b32_e32 v12, v5
	v_mul_f32_e32 v0, 0xbfb8aa3b, v19
	v_exp_f32_e32 v0, v0
	v_add_f32_e32 v4, 1.0, v4
	v_rcp_f32_e32 v4, v4
	v_add_u32_e32 v8, 0xb0, v138
	v_add_f32_e32 v0, 1.0, v0
	v_rcp_f32_e32 v0, v0
	v_mul_f32_e32 v4, v17, v4
	v_mul_f32_e32 v16, v16, v4
	v_pk_mul_f32 v[4:5], v[12:13], v[120:121] op_sel_hi:[1,0]
	v_mad_i64_i32 v[20:21], s[30:31], v8, s59, v[134:135]
	v_mul_f32_e32 v17, v19, v0
	v_mul_f32_e32 v0, 0xbfb8aa3b, v5
	v_mov_b32_e32 v8, v1
	v_exp_f32_e32 v12, v0
	v_pk_mul_f32 v[0:1], v[8:9], v[120:121] op_sel_hi:[1,0]
	v_mul_f32_e32 v13, v18, v17
	v_mul_f32_e32 v8, 0xbfb8aa3b, v1
	v_exp_f32_e32 v8, v8
	v_add_f32_e32 v9, 1.0, v12
	v_rcp_f32_e32 v12, v9
	v_mov_b32_e32 v9, v14
	v_add_f32_e32 v8, 1.0, v8
	v_rcp_f32_e32 v17, v8
	v_mov_b32_e32 v8, v6
	v_pk_mul_f32 v[8:9], v[8:9], v[120:121] op_sel_hi:[1,0]
	v_mul_f32_e32 v5, v5, v12
	v_mul_f32_e32 v6, 0xbfb8aa3b, v9
	v_exp_f32_e32 v6, v6
	v_mul_f32_e32 v12, v4, v5
	v_mov_b32_e32 v5, v10
	v_mul_f32_e32 v1, v1, v17
	v_add_f32_e32 v4, 1.0, v6
	v_rcp_f32_e32 v6, v4
	v_mov_b32_e32 v4, v2
	v_pk_mul_f32 v[4:5], v[4:5], v[120:121] op_sel_hi:[1,0]
	v_mul_f32_e32 v17, v0, v1
	v_mul_f32_e32 v2, 0xbfb8aa3b, v5
	v_exp_f32_e32 v2, v2
	v_mul_f32_e32 v0, v9, v6
	v_mul_f32_e32 v6, v8, v0
	v_mov_b32_e32 v14, v7
	v_add_f32_e32 v0, 1.0, v2
	v_rcp_f32_e32 v8, v0
	v_pk_mul_f32 v[0:1], v[14:15], v[120:121] op_sel_hi:[1,0]
	v_mov_b32_e32 v10, v3
	v_mul_f32_e32 v2, 0xbfb8aa3b, v1
	v_exp_f32_e32 v7, v2
	v_pk_mul_f32 v[2:3], v[10:11], v[120:121] op_sel_hi:[1,0]
	v_mul_f32_e32 v5, v5, v8
	v_mul_f32_e32 v9, 0xbfb8aa3b, v3
	v_exp_f32_e32 v9, v9
	v_add_f32_e32 v7, 1.0, v7
	v_rcp_f32_e32 v7, v7
	v_add_f32_e32 v8, 1.0, v9
	v_rcp_f32_e32 v8, v8
	v_mul_f32_e32 v1, v1, v7
	v_mul_f32_e32 v1, v0, v1
	v_mul_f32_e32 v9, v4, v5
	v_mul_f32_e32 v0, v3, v8
	v_mul_f32_e32 v3, v2, v0
	v_lshl_add_u64 v[4:5], v[20:21], 0, v[112:113]
	v_cvt_pk_bf16_f32 v0, v16, v12
	v_cvt_pk_bf16_f32 v1, v6, v1
	v_cvt_pk_bf16_f32 v2, v13, v17
	v_cvt_pk_bf16_f32 v3, v9, v3
	global_store_dwordx4 v[4:5], v[0:3], off nt
	s_cbranch_vccnz .LBB0_777
	s_andn2_b64 vcc, exec, s[12:13]
	s_cbranch_vccnz .LBB0_776
	s_barrier
	s_branch .LBB0_776

.LBB0_851:
	ds_read2_b32 v[214:215], v146 offset1:32
	s_addk_i32 s30, 0x800
	s_addk_i32 s56, 0x800
	s_add_i32 s57, s57, 0x20000
	s_andn2_b64 vcc, exec, s[12:13]
	s_waitcnt vmcnt(0) lgkmcnt(0)
	v_mul_f32_e32 v77, v68, v214
	ds_read_b32 v209, v147
	ds_read_b32 v211, v148
	ds_read_b32 v212, v149
	ds_read_b32 v213, v150
	ds_read_b32 v214, v151
	ds_read_b32 v216, v152
	ds_read_b32 v217, v153
	ds_read_b32 v218, v154
	s_waitcnt lgkmcnt(7)
	v_mul_f32_e32 v209, v69, v209
	v_cvt_pk_bf16_f32 v210, v77, v209
	s_waitcnt lgkmcnt(6)
	v_mul_f32_e32 v77, v70, v211
	s_waitcnt lgkmcnt(5)
	v_mul_f32_e32 v209, v71, v212
	v_cvt_pk_bf16_f32 v211, v77, v209
	s_waitcnt lgkmcnt(4)
	v_mul_f32_e32 v77, v64, v213
	s_waitcnt lgkmcnt(3)
	v_mul_f32_e32 v209, v65, v214
	v_cvt_pk_bf16_f32 v212, v77, v209
	s_waitcnt lgkmcnt(2)
	v_mul_f32_e32 v77, v66, v216
	s_waitcnt lgkmcnt(1)
	v_mul_f32_e32 v209, v67, v217
	v_cvt_pk_bf16_f32 v213, v77, v209
	v_add_u32_e32 v77, s36, v138
	v_mad_i64_i32 v[216:217], s[6:7], s31, v77, 0
	v_lshl_add_u64 v[216:217], v[216:217], 1, s[2:3]
	s_lshl_b64 s[6:7], s[8:9], 1
	v_lshl_add_u64 v[216:217], v[216:217], 0, s[6:7]
	v_lshl_add_u64 v[216:217], v[216:217], 0, v[72:73]
	global_store_dwordx4 v[216:217], v[210:213], off nt
	s_waitcnt lgkmcnt(0)
	v_mul_f32_e32 v77, v68, v218
	ds_read_b32 v209, v155
	ds_read_b32 v211, v156
	ds_read_b32 v212, v157
	ds_read_b32 v213, v158
	ds_read_b32 v214, v159
	ds_read_b32 v216, v160
	ds_read_b32 v217, v161
	ds_read_b32 v218, v162
	s_waitcnt lgkmcnt(7)
	v_mul_f32_e32 v209, v69, v209
	v_cvt_pk_bf16_f32 v210, v77, v209
	s_waitcnt lgkmcnt(6)
	v_mul_f32_e32 v77, v70, v211
	s_waitcnt lgkmcnt(5)
	v_mul_f32_e32 v209, v71, v212
	v_cvt_pk_bf16_f32 v211, v77, v209
	s_waitcnt lgkmcnt(4)
	v_mul_f32_e32 v77, v64, v213
	s_waitcnt lgkmcnt(3)
	v_mul_f32_e32 v209, v65, v214
	v_cvt_pk_bf16_f32 v212, v77, v209
	s_waitcnt lgkmcnt(2)
	v_mul_f32_e32 v77, v66, v216
	s_waitcnt lgkmcnt(1)
	v_mul_f32_e32 v209, v67, v217
	v_cvt_pk_bf16_f32 v213, v77, v209
	v_add_u32_e32 v77, s36, v139
	v_mad_i64_i32 v[216:217], s[8:9], s31, v77, 0
	v_lshl_add_u64 v[216:217], v[216:217], 1, s[2:3]
	v_lshl_add_u64 v[216:217], v[216:217], 0, s[6:7]
	v_lshl_add_u64 v[216:217], v[216:217], 0, v[72:73]
	global_store_dwordx4 v[216:217], v[210:213], off nt
	s_waitcnt lgkmcnt(0)
	v_mul_f32_e32 v77, v68, v218
	ds_read_b32 v209, v163
	ds_read_b32 v211, v164
	ds_read_b32 v212, v165
	ds_read_b32 v213, v166
	ds_read_b32 v214, v167
	ds_read_b32 v216, v168
	ds_read_b32 v217, v169
	ds_read_b32 v218, v170
	s_waitcnt lgkmcnt(7)
	v_mul_f32_e32 v209, v69, v209
	v_cvt_pk_bf16_f32 v210, v77, v209
	s_waitcnt lgkmcnt(6)
	v_mul_f32_e32 v77, v70, v211
	s_waitcnt lgkmcnt(5)
	v_mul_f32_e32 v209, v71, v212
	v_cvt_pk_bf16_f32 v211, v77, v209
	s_waitcnt lgkmcnt(4)
	v_mul_f32_e32 v77, v64, v213
	s_waitcnt lgkmcnt(3)
	v_mul_f32_e32 v209, v65, v214
	v_cvt_pk_bf16_f32 v212, v77, v209
	s_waitcnt lgkmcnt(2)
	v_mul_f32_e32 v77, v66, v216
	s_waitcnt lgkmcnt(1)
	v_mul_f32_e32 v209, v67, v217
	v_cvt_pk_bf16_f32 v213, v77, v209
	v_add_u32_e32 v77, s36, v140
	v_mad_i64_i32 v[216:217], s[8:9], s31, v77, 0
	v_lshl_add_u64 v[216:217], v[216:217], 1, s[2:3]
	v_lshl_add_u64 v[216:217], v[216:217], 0, s[6:7]
	v_lshl_add_u64 v[216:217], v[216:217], 0, v[72:73]
	global_store_dwordx4 v[216:217], v[210:213], off nt
	s_waitcnt lgkmcnt(0)
	v_mul_f32_e32 v77, v68, v218
	ds_read_b32 v209, v171
	ds_read_b32 v211, v172
	ds_read_b32 v212, v173
	ds_read_b32 v213, v174
	ds_read_b32 v214, v175
	ds_read_b32 v216, v176
	ds_read_b32 v217, v177
	ds_read_b32 v218, v178
	s_waitcnt lgkmcnt(7)
	v_mul_f32_e32 v209, v69, v209
	v_cvt_pk_bf16_f32 v210, v77, v209
	s_waitcnt lgkmcnt(6)
	v_mul_f32_e32 v77, v70, v211
	s_waitcnt lgkmcnt(5)
	v_mul_f32_e32 v209, v71, v212
	v_cvt_pk_bf16_f32 v211, v77, v209
	s_waitcnt lgkmcnt(4)
	v_mul_f32_e32 v77, v64, v213
	s_waitcnt lgkmcnt(3)
	v_mul_f32_e32 v209, v65, v214
	v_cvt_pk_bf16_f32 v212, v77, v209
	s_waitcnt lgkmcnt(2)
	v_mul_f32_e32 v77, v66, v216
	s_waitcnt lgkmcnt(1)
	v_mul_f32_e32 v209, v67, v217
	v_cvt_pk_bf16_f32 v213, v77, v209
	v_add_u32_e32 v77, s36, v141
	v_mad_i64_i32 v[216:217], s[8:9], s31, v77, 0
	v_lshl_add_u64 v[216:217], v[216:217], 1, s[2:3]
	v_lshl_add_u64 v[216:217], v[216:217], 0, s[6:7]
	v_lshl_add_u64 v[216:217], v[216:217], 0, v[72:73]
	global_store_dwordx4 v[216:217], v[210:213], off nt
	v_mul_f32_e32 v77, v68, v215
	s_waitcnt lgkmcnt(0)
	v_mul_f32_e32 v209, v69, v218
	v_cvt_pk_bf16_f32 v210, v77, v209
	ds_read_b32 v77, v179
	ds_read_b32 v209, v180
	ds_read_b32 v212, v181
	ds_read_b32 v213, v182
	ds_read_b32 v214, v183
	ds_read_b32 v215, v184
	ds_read_b32 v216, v185
	ds_read_b32 v217, v186
	s_waitcnt lgkmcnt(7)
	v_mul_f32_e32 v77, v70, v77
	s_waitcnt lgkmcnt(6)
	v_mul_f32_e32 v209, v71, v209
	v_cvt_pk_bf16_f32 v211, v77, v209
	s_waitcnt lgkmcnt(5)
	v_mul_f32_e32 v77, v64, v212
	s_waitcnt lgkmcnt(4)
	v_mul_f32_e32 v209, v65, v213
	v_cvt_pk_bf16_f32 v212, v77, v209
	s_waitcnt lgkmcnt(3)
	v_mul_f32_e32 v77, v66, v214
	s_waitcnt lgkmcnt(2)
	v_mul_f32_e32 v209, v67, v215
	v_cvt_pk_bf16_f32 v213, v77, v209
	v_add_u32_e32 v77, s36, v142
	v_mad_i64_i32 v[214:215], s[8:9], s31, v77, 0
	v_lshl_add_u64 v[214:215], v[214:215], 1, s[2:3]
	v_lshl_add_u64 v[214:215], v[214:215], 0, s[6:7]
	v_lshl_add_u64 v[214:215], v[214:215], 0, v[72:73]
	global_store_dwordx4 v[214:215], v[210:213], off nt
	s_waitcnt lgkmcnt(1)
	v_mul_f32_e32 v77, v68, v216
	s_waitcnt lgkmcnt(0)
	v_mul_f32_e32 v209, v69, v217
	v_cvt_pk_bf16_f32 v210, v77, v209
	ds_read_b32 v77, v187
	ds_read_b32 v209, v188
	ds_read_b32 v212, v189
	ds_read_b32 v213, v190
	ds_read_b32 v214, v191
	ds_read_b32 v215, v192
	ds_read_b32 v216, v193
	ds_read_b32 v217, v194
	s_waitcnt lgkmcnt(7)
	v_mul_f32_e32 v77, v70, v77
	s_waitcnt lgkmcnt(6)
	v_mul_f32_e32 v209, v71, v209
	v_cvt_pk_bf16_f32 v211, v77, v209
	s_waitcnt lgkmcnt(5)
	v_mul_f32_e32 v77, v64, v212
	s_waitcnt lgkmcnt(4)
	v_mul_f32_e32 v209, v65, v213
	v_cvt_pk_bf16_f32 v212, v77, v209
	s_waitcnt lgkmcnt(3)
	v_mul_f32_e32 v77, v66, v214
	s_waitcnt lgkmcnt(2)
	v_mul_f32_e32 v209, v67, v215
	v_cvt_pk_bf16_f32 v213, v77, v209
	v_add_u32_e32 v77, s36, v143
	v_mad_i64_i32 v[214:215], s[8:9], s31, v77, 0
	v_lshl_add_u64 v[214:215], v[214:215], 1, s[2:3]
	v_lshl_add_u64 v[214:215], v[214:215], 0, s[6:7]
	v_lshl_add_u64 v[214:215], v[214:215], 0, v[72:73]
	global_store_dwordx4 v[214:215], v[210:213], off nt
	s_waitcnt lgkmcnt(1)
	v_mul_f32_e32 v77, v68, v216
	s_waitcnt lgkmcnt(0)
	v_mul_f32_e32 v209, v69, v217
	v_cvt_pk_bf16_f32 v210, v77, v209
	ds_read_b32 v77, v195
	ds_read_b32 v209, v196
	ds_read_b32 v212, v197
	ds_read_b32 v213, v198
	ds_read_b32 v214, v199
	ds_read_b32 v215, v200
	ds_read_b32 v216, v201
	ds_read_b32 v217, v202
	s_waitcnt lgkmcnt(7)
	v_mul_f32_e32 v77, v70, v77
	s_waitcnt lgkmcnt(6)
	v_mul_f32_e32 v209, v71, v209
	v_cvt_pk_bf16_f32 v211, v77, v209
	s_waitcnt lgkmcnt(5)
	v_mul_f32_e32 v77, v64, v212
	s_waitcnt lgkmcnt(4)
	v_mul_f32_e32 v209, v65, v213
	v_cvt_pk_bf16_f32 v212, v77, v209
	s_waitcnt lgkmcnt(3)
	v_mul_f32_e32 v77, v66, v214
	s_waitcnt lgkmcnt(2)
	v_mul_f32_e32 v209, v67, v215
	v_cvt_pk_bf16_f32 v213, v77, v209
	v_add_u32_e32 v77, s36, v144
	v_mad_i64_i32 v[214:215], s[8:9], s31, v77, 0
	v_lshl_add_u64 v[214:215], v[214:215], 1, s[2:3]
	v_lshl_add_u64 v[214:215], v[214:215], 0, s[6:7]
	v_lshl_add_u64 v[214:215], v[214:215], 0, v[72:73]
	global_store_dwordx4 v[214:215], v[210:213], off nt
	ds_read_b32 v77, v203
	ds_read_b32 v209, v204
	ds_read_b32 v210, v205
	ds_read_b32 v211, v206
	ds_read_b32 v212, v207
	ds_read_b32 v213, v208
	s_waitcnt lgkmcnt(7)
	v_mul_f32_e32 v68, v68, v216
	s_waitcnt lgkmcnt(6)
	v_mul_f32_e32 v69, v69, v217
	v_cvt_pk_bf16_f32 v68, v68, v69
	s_waitcnt lgkmcnt(5)
	v_mul_f32_e32 v69, v70, v77
	s_waitcnt lgkmcnt(4)
	v_mul_f32_e32 v70, v71, v209
	s_waitcnt lgkmcnt(3)
	v_mul_f32_e32 v64, v64, v210
	v_cvt_pk_bf16_f32 v69, v69, v70
	s_waitcnt lgkmcnt(2)
	v_mul_f32_e32 v65, v65, v211
	v_cvt_pk_bf16_f32 v70, v64, v65
	s_waitcnt lgkmcnt(1)
	v_mul_f32_e32 v64, v66, v212
	s_waitcnt lgkmcnt(0)
	v_mul_f32_e32 v65, v67, v213
	v_cvt_pk_bf16_f32 v71, v64, v65
	v_add_u32_e32 v64, s36, v145
	v_mad_i64_i32 v[64:65], s[8:9], s31, v64, 0
	v_lshl_add_u64 v[64:65], v[64:65], 1, s[2:3]
	v_lshl_add_u64 v[64:65], v[64:65], 0, s[6:7]
	v_lshl_add_u64 v[64:65], v[64:65], 0, v[72:73]
	global_store_dwordx4 v[64:65], v[68:71], off nt
	s_waitcnt lgkmcnt(0)
	s_mov_b32 s36, s26
	s_mov_b64 s[2:3], s[14:15]
	s_mov_b64 s[6:7], s[16:17]
	s_mov_b32 s31, s58
	s_mov_b32 s8, s20
	s_cbranch_vccz .LBB0_885

.LBB0_938:
	ds_read2_b32 v[214:215], v146 offset1:32
	s_add_i32 s57, s57, s29
	s_add_i32 s28, s28, s29
	s_add_i32 s54, s54, s55
	s_add_i32 s56, s56, s44
	s_waitcnt vmcnt(0) lgkmcnt(0)
	v_mul_f32_e32 v77, v68, v214
	ds_read_b32 v209, v147
	ds_read_b32 v211, v148
	ds_read_b32 v212, v149
	ds_read_b32 v213, v150
	ds_read_b32 v214, v151
	ds_read_b32 v216, v152
	ds_read_b32 v217, v153
	ds_read_b32 v218, v154
	s_waitcnt lgkmcnt(7)
	v_mul_f32_e32 v209, v69, v209
	v_cvt_pk_bf16_f32 v210, v77, v209
	s_waitcnt lgkmcnt(6)
	v_mul_f32_e32 v77, v70, v211
	s_waitcnt lgkmcnt(5)
	v_mul_f32_e32 v209, v71, v212
	v_cvt_pk_bf16_f32 v211, v77, v209
	s_waitcnt lgkmcnt(4)
	v_mul_f32_e32 v77, v64, v213
	s_waitcnt lgkmcnt(3)
	v_mul_f32_e32 v209, v65, v214
	v_cvt_pk_bf16_f32 v212, v77, v209
	s_waitcnt lgkmcnt(2)
	v_mul_f32_e32 v77, v66, v216
	s_waitcnt lgkmcnt(1)
	v_mul_f32_e32 v209, v67, v217
	v_cvt_pk_bf16_f32 v213, v77, v209
	v_add_u32_e32 v77, s27, v138
	v_mad_i64_i32 v[216:217], s[6:7], s26, v77, 0
	v_lshl_add_u64 v[216:217], v[216:217], 1, s[2:3]
	s_lshl_b64 s[6:7], s[8:9], 1
	v_lshl_add_u64 v[216:217], v[216:217], 0, s[6:7]
	v_lshl_add_u64 v[216:217], v[216:217], 0, v[72:73]
	global_store_dwordx4 v[216:217], v[210:213], off nt
	s_waitcnt lgkmcnt(0)
	v_mul_f32_e32 v77, v68, v218
	ds_read_b32 v209, v155
	ds_read_b32 v211, v156
	ds_read_b32 v212, v157
	ds_read_b32 v213, v158
	ds_read_b32 v214, v159
	ds_read_b32 v216, v160
	ds_read_b32 v217, v161
	ds_read_b32 v218, v162
	s_waitcnt lgkmcnt(7)
	v_mul_f32_e32 v209, v69, v209
	v_cvt_pk_bf16_f32 v210, v77, v209
	s_waitcnt lgkmcnt(6)
	v_mul_f32_e32 v77, v70, v211
	s_waitcnt lgkmcnt(5)
	v_mul_f32_e32 v209, v71, v212
	v_cvt_pk_bf16_f32 v211, v77, v209
	s_waitcnt lgkmcnt(4)
	v_mul_f32_e32 v77, v64, v213
	s_waitcnt lgkmcnt(3)
	v_mul_f32_e32 v209, v65, v214
	v_cvt_pk_bf16_f32 v212, v77, v209
	s_waitcnt lgkmcnt(2)
	v_mul_f32_e32 v77, v66, v216
	s_waitcnt lgkmcnt(1)
	v_mul_f32_e32 v209, v67, v217
	v_cvt_pk_bf16_f32 v213, v77, v209
	v_add_u32_e32 v77, s27, v139
	v_mad_i64_i32 v[216:217], s[8:9], s26, v77, 0
	v_lshl_add_u64 v[216:217], v[216:217], 1, s[2:3]
	v_lshl_add_u64 v[216:217], v[216:217], 0, s[6:7]
	v_lshl_add_u64 v[216:217], v[216:217], 0, v[72:73]
	global_store_dwordx4 v[216:217], v[210:213], off nt
	s_waitcnt lgkmcnt(0)
	v_mul_f32_e32 v77, v68, v218
	ds_read_b32 v209, v163
	ds_read_b32 v211, v164
	ds_read_b32 v212, v165
	ds_read_b32 v213, v166
	ds_read_b32 v214, v167
	ds_read_b32 v216, v168
	ds_read_b32 v217, v169
	ds_read_b32 v218, v170
	s_waitcnt lgkmcnt(7)
	v_mul_f32_e32 v209, v69, v209
	v_cvt_pk_bf16_f32 v210, v77, v209
	s_waitcnt lgkmcnt(6)
	v_mul_f32_e32 v77, v70, v211
	s_waitcnt lgkmcnt(5)
	v_mul_f32_e32 v209, v71, v212
	v_cvt_pk_bf16_f32 v211, v77, v209
	s_waitcnt lgkmcnt(4)
	v_mul_f32_e32 v77, v64, v213
	s_waitcnt lgkmcnt(3)
	v_mul_f32_e32 v209, v65, v214
	v_cvt_pk_bf16_f32 v212, v77, v209
	s_waitcnt lgkmcnt(2)
	v_mul_f32_e32 v77, v66, v216
	s_waitcnt lgkmcnt(1)
	v_mul_f32_e32 v209, v67, v217
	v_cvt_pk_bf16_f32 v213, v77, v209
	v_add_u32_e32 v77, s27, v140
	v_mad_i64_i32 v[216:217], s[8:9], s26, v77, 0
	v_lshl_add_u64 v[216:217], v[216:217], 1, s[2:3]
	v_lshl_add_u64 v[216:217], v[216:217], 0, s[6:7]
	v_lshl_add_u64 v[216:217], v[216:217], 0, v[72:73]
	global_store_dwordx4 v[216:217], v[210:213], off nt
	s_waitcnt lgkmcnt(0)
	v_mul_f32_e32 v77, v68, v218
	ds_read_b32 v209, v171
	ds_read_b32 v211, v172
	ds_read_b32 v212, v173
	ds_read_b32 v213, v174
	ds_read_b32 v214, v175
	ds_read_b32 v216, v176
	ds_read_b32 v217, v177
	ds_read_b32 v218, v178
	s_waitcnt lgkmcnt(7)
	v_mul_f32_e32 v209, v69, v209
	v_cvt_pk_bf16_f32 v210, v77, v209
	s_waitcnt lgkmcnt(6)
	v_mul_f32_e32 v77, v70, v211
	s_waitcnt lgkmcnt(5)
	v_mul_f32_e32 v209, v71, v212
	v_cvt_pk_bf16_f32 v211, v77, v209
	s_waitcnt lgkmcnt(4)
	v_mul_f32_e32 v77, v64, v213
	s_waitcnt lgkmcnt(3)
	v_mul_f32_e32 v209, v65, v214
	v_cvt_pk_bf16_f32 v212, v77, v209
	s_waitcnt lgkmcnt(2)
	v_mul_f32_e32 v77, v66, v216
	s_waitcnt lgkmcnt(1)
	v_mul_f32_e32 v209, v67, v217
	v_cvt_pk_bf16_f32 v213, v77, v209
	v_add_u32_e32 v77, s27, v141
	v_mad_i64_i32 v[216:217], s[8:9], s26, v77, 0
	v_lshl_add_u64 v[216:217], v[216:217], 1, s[2:3]
	v_lshl_add_u64 v[216:217], v[216:217], 0, s[6:7]
	v_lshl_add_u64 v[216:217], v[216:217], 0, v[72:73]
	global_store_dwordx4 v[216:217], v[210:213], off nt
	v_mul_f32_e32 v77, v68, v215
	s_waitcnt lgkmcnt(0)
	v_mul_f32_e32 v209, v69, v218
	v_cvt_pk_bf16_f32 v210, v77, v209
	ds_read_b32 v77, v179
	ds_read_b32 v209, v180
	ds_read_b32 v212, v181
	ds_read_b32 v213, v182
	ds_read_b32 v214, v183
	ds_read_b32 v215, v184
	ds_read_b32 v216, v185
	ds_read_b32 v217, v186
	s_waitcnt lgkmcnt(7)
	v_mul_f32_e32 v77, v70, v77
	s_waitcnt lgkmcnt(6)
	v_mul_f32_e32 v209, v71, v209
	v_cvt_pk_bf16_f32 v211, v77, v209
	s_waitcnt lgkmcnt(5)
	v_mul_f32_e32 v77, v64, v212
	s_waitcnt lgkmcnt(4)
	v_mul_f32_e32 v209, v65, v213
	v_cvt_pk_bf16_f32 v212, v77, v209
	s_waitcnt lgkmcnt(3)
	v_mul_f32_e32 v77, v66, v214
	s_waitcnt lgkmcnt(2)
	v_mul_f32_e32 v209, v67, v215
	v_cvt_pk_bf16_f32 v213, v77, v209
	v_add_u32_e32 v77, s27, v142
	v_mad_i64_i32 v[214:215], s[8:9], s26, v77, 0
	v_lshl_add_u64 v[214:215], v[214:215], 1, s[2:3]
	v_lshl_add_u64 v[214:215], v[214:215], 0, s[6:7]
	v_lshl_add_u64 v[214:215], v[214:215], 0, v[72:73]
	global_store_dwordx4 v[214:215], v[210:213], off nt
	s_waitcnt lgkmcnt(1)
	v_mul_f32_e32 v77, v68, v216
	s_waitcnt lgkmcnt(0)
	v_mul_f32_e32 v209, v69, v217
	v_cvt_pk_bf16_f32 v210, v77, v209
	ds_read_b32 v77, v187
	ds_read_b32 v209, v188
	ds_read_b32 v212, v189
	ds_read_b32 v213, v190
	ds_read_b32 v214, v191
	ds_read_b32 v215, v192
	ds_read_b32 v216, v193
	ds_read_b32 v217, v194
	s_waitcnt lgkmcnt(7)
	v_mul_f32_e32 v77, v70, v77
	s_waitcnt lgkmcnt(6)
	v_mul_f32_e32 v209, v71, v209
	v_cvt_pk_bf16_f32 v211, v77, v209
	s_waitcnt lgkmcnt(5)
	v_mul_f32_e32 v77, v64, v212
	s_waitcnt lgkmcnt(4)
	v_mul_f32_e32 v209, v65, v213
	v_cvt_pk_bf16_f32 v212, v77, v209
	s_waitcnt lgkmcnt(3)
	v_mul_f32_e32 v77, v66, v214
	s_waitcnt lgkmcnt(2)
	v_mul_f32_e32 v209, v67, v215
	v_cvt_pk_bf16_f32 v213, v77, v209
	v_add_u32_e32 v77, s27, v143
	v_mad_i64_i32 v[214:215], s[8:9], s26, v77, 0
	v_lshl_add_u64 v[214:215], v[214:215], 1, s[2:3]
	v_lshl_add_u64 v[214:215], v[214:215], 0, s[6:7]
	v_lshl_add_u64 v[214:215], v[214:215], 0, v[72:73]
	global_store_dwordx4 v[214:215], v[210:213], off nt
	s_waitcnt lgkmcnt(1)
	v_mul_f32_e32 v77, v68, v216
	s_waitcnt lgkmcnt(0)
	v_mul_f32_e32 v209, v69, v217
	v_cvt_pk_bf16_f32 v210, v77, v209
	ds_read_b32 v77, v195
	ds_read_b32 v209, v196
	ds_read_b32 v212, v197
	ds_read_b32 v213, v198
	ds_read_b32 v214, v199
	ds_read_b32 v215, v200
	ds_read_b32 v216, v201
	ds_read_b32 v217, v202
	s_waitcnt lgkmcnt(7)
	v_mul_f32_e32 v77, v70, v77
	s_waitcnt lgkmcnt(6)
	v_mul_f32_e32 v209, v71, v209
	v_cvt_pk_bf16_f32 v211, v77, v209
	s_waitcnt lgkmcnt(5)
	v_mul_f32_e32 v77, v64, v212
	s_waitcnt lgkmcnt(4)
	v_mul_f32_e32 v209, v65, v213
	v_cvt_pk_bf16_f32 v212, v77, v209
	s_waitcnt lgkmcnt(3)
	v_mul_f32_e32 v77, v66, v214
	s_waitcnt lgkmcnt(2)
	v_mul_f32_e32 v209, v67, v215
	v_cvt_pk_bf16_f32 v213, v77, v209
	v_add_u32_e32 v77, s27, v144
	v_mad_i64_i32 v[214:215], s[8:9], s26, v77, 0
	v_lshl_add_u64 v[214:215], v[214:215], 1, s[2:3]
	v_lshl_add_u64 v[214:215], v[214:215], 0, s[6:7]
	v_lshl_add_u64 v[214:215], v[214:215], 0, v[72:73]
	global_store_dwordx4 v[214:215], v[210:213], off nt
	ds_read_b32 v77, v203
	ds_read_b32 v209, v204
	ds_read_b32 v210, v205
	ds_read_b32 v211, v206
	ds_read_b32 v212, v207
	ds_read_b32 v213, v208
	s_waitcnt lgkmcnt(7)
	v_mul_f32_e32 v68, v68, v216
	s_waitcnt lgkmcnt(6)
	v_mul_f32_e32 v69, v69, v217
	v_cvt_pk_bf16_f32 v68, v68, v69
	s_waitcnt lgkmcnt(5)
	v_mul_f32_e32 v69, v70, v77
	s_waitcnt lgkmcnt(4)
	v_mul_f32_e32 v70, v71, v209
	s_waitcnt lgkmcnt(3)
	v_mul_f32_e32 v64, v64, v210
	v_cvt_pk_bf16_f32 v69, v69, v70
	s_waitcnt lgkmcnt(2)
	v_mul_f32_e32 v65, v65, v211
	v_cvt_pk_bf16_f32 v70, v64, v65
	s_waitcnt lgkmcnt(1)
	v_mul_f32_e32 v64, v66, v212
	s_waitcnt lgkmcnt(0)
	v_mul_f32_e32 v65, v67, v213
	v_cvt_pk_bf16_f32 v71, v64, v65
	v_add_u32_e32 v64, s27, v145
	v_mad_i64_i32 v[64:65], s[8:9], s26, v64, 0
	v_lshl_add_u64 v[64:65], v[64:65], 1, s[2:3]
	v_lshl_add_u64 v[64:65], v[64:65], 0, s[6:7]
	v_lshl_add_u64 v[64:65], v[64:65], 0, v[72:73]
	global_store_dwordx4 v[64:65], v[68:71], off nt
	s_waitcnt lgkmcnt(0)
	s_add_i32 s2, s53, s57
	s_cmpk_gt_i32 s2, 0x13ff
	s_mov_b32 s27, s24
	s_mov_b64 s[2:3], s[12:13]
	s_mov_b64 s[6:7], s[14:15]
	s_mov_b32 s26, s58
	s_mov_b32 s8, s18
	s_cbranch_scc1 .LBB0_972

.LBB0_1070:
	v_lshl_or_b32 v136, s67, 8, v148
	v_ashrrev_i32_e32 v137, 31, v136
	v_add_u32_e32 v192, s49, v138
	v_ashrrev_i32_e32 v193, 31, v192
	v_lshlrev_b64 v[192:193], 2, v[192:193]
	v_lshl_add_u64 v[194:195], s[12:13], 0, v[192:193]
	v_lshl_add_u64 v[192:193], s[8:9], 0, v[192:193]
	v_cmp_gt_i32_e32 vcc, s52, v138
	s_and_saveexec_b64 s[36:37], vcc
	global_load_dword v160, v[192:193], off
	global_load_dword v162, v[194:195], off
	s_or_b64 exec, exec, s[36:37]
	v_add_u32_e32 v196, 16, v138
	v_cmp_gt_i32_e32 vcc, s52, v196
	s_and_saveexec_b64 s[36:37], vcc
	global_load_dword v164, v[192:193], off offset:64
	global_load_dword v166, v[194:195], off offset:64
	s_or_b64 exec, exec, s[36:37]
	v_add_u32_e32 v196, 32, v138
	v_cmp_gt_i32_e32 vcc, s52, v196
	s_and_saveexec_b64 s[36:37], vcc
	global_load_dword v168, v[192:193], off offset:128
	global_load_dword v170, v[194:195], off offset:128
	s_or_b64 exec, exec, s[36:37]
	v_add_u32_e32 v196, 48, v138
	v_cmp_gt_i32_e32 vcc, s52, v196
	s_and_saveexec_b64 s[36:37], vcc
	global_load_dword v172, v[192:193], off offset:192
	global_load_dword v174, v[194:195], off offset:192
	s_or_b64 exec, exec, s[36:37]
	v_add_u32_e32 v196, 128, v138
	v_cmp_gt_i32_e32 vcc, s52, v196
	s_and_saveexec_b64 s[36:37], vcc
	global_load_dword v176, v[192:193], off offset:512
	global_load_dword v178, v[194:195], off offset:512
	s_or_b64 exec, exec, s[36:37]
	v_add_u32_e32 v196, 144, v138
	v_cmp_gt_i32_e32 vcc, s52, v196
	s_and_saveexec_b64 s[36:37], vcc
	global_load_dword v180, v[192:193], off offset:576
	global_load_dword v182, v[194:195], off offset:576
	s_or_b64 exec, exec, s[36:37]
	v_add_u32_e32 v196, 160, v138
	v_cmp_gt_i32_e32 vcc, s52, v196
	s_and_saveexec_b64 s[36:37], vcc
	global_load_dword v184, v[192:193], off offset:640
	global_load_dword v186, v[194:195], off offset:640
	s_or_b64 exec, exec, s[36:37]
	v_add_u32_e32 v196, 176, v138
	v_cmp_gt_i32_e32 vcc, s52, v196
	s_and_saveexec_b64 s[36:37], vcc
	global_load_dword v188, v[192:193], off offset:704
	global_load_dword v190, v[194:195], off offset:704
	s_or_b64 exec, exec, s[36:37]
	s_waitcnt vmcnt(0)
	v_cmp_gt_i32_e32 vcc, s52, v138
	s_and_saveexec_b64 s[36:37], vcc
	s_cbranch_execz .LBB0_1072
	v_mov_b32_e32 v152, 0
	v_mov_b32_e32 v153, 0
	v_mov_b32_e32 v154, 0
	v_mov_b32_e32 v155, 0
	v_ashrrev_i32_e32 v161, 31, v160
	v_mul_f32_e32 v162, 0x41800000, v162
	v_pk_mul_f32 v[112:113], v[112:113], v[162:163] op_sel_hi:[1,0]
	v_pk_mul_f32 v[116:117], v[116:117], v[162:163] op_sel_hi:[1,0]
	v_pk_mul_f32 v[120:121], v[120:121], v[162:163] op_sel_hi:[1,0]
	v_pk_mul_f32 v[124:125], v[124:125], v[162:163] op_sel_hi:[1,0]
	v_cvt_pk_fp8_f32 v152, v112, v113
	v_cvt_pk_fp8_f32 v153, v116, v117
	v_cvt_pk_fp8_f32 v154, v120, v121
	v_cvt_pk_fp8_f32 v155, v124, v125
	v_pk_mul_f32 v[114:115], v[114:115], v[162:163] op_sel_hi:[1,0]
	v_pk_mul_f32 v[118:119], v[118:119], v[162:163] op_sel_hi:[1,0]
	v_pk_mul_f32 v[122:123], v[122:123], v[162:163] op_sel_hi:[1,0]
	v_pk_mul_f32 v[126:127], v[126:127], v[162:163] op_sel_hi:[1,0]
	v_cvt_pk_fp8_f32 v152, v114, v115 op_sel:[0,0,1]
	v_cvt_pk_fp8_f32 v153, v118, v119 op_sel:[0,0,1]
	v_cvt_pk_fp8_f32 v154, v122, v123 op_sel:[0,0,1]
	v_cvt_pk_fp8_f32 v155, v126, v127 op_sel:[0,0,1]
	v_lshlrev_b64 v[112:113], 10, v[160:161]
	v_lshl_add_u64 v[112:113], s[6:7], 0, v[112:113]
	v_lshl_add_u64 v[112:113], v[112:113], 0, v[136:137]
	global_store_dwordx4 v[112:113], v[152:155], off nt
.LBB0_1072:
	s_or_b64 exec, exec, s[36:37]
	v_or_b32_e32 v112, 16, v138
	v_cmp_gt_i32_e32 vcc, s52, v112
	s_and_saveexec_b64 s[36:37], vcc
	s_cbranch_execz .LBB0_1074
	v_mov_b32_e32 v112, 0
	v_mov_b32_e32 v113, 0
	v_mov_b32_e32 v114, 0
	v_mov_b32_e32 v115, 0
	v_ashrrev_i32_e32 v165, 31, v164
	v_mul_f32_e32 v166, 0x41800000, v166
	v_pk_mul_f32 v[96:97], v[96:97], v[166:167] op_sel_hi:[1,0]
	v_pk_mul_f32 v[100:101], v[100:101], v[166:167] op_sel_hi:[1,0]
	v_pk_mul_f32 v[104:105], v[104:105], v[166:167] op_sel_hi:[1,0]
	v_pk_mul_f32 v[108:109], v[108:109], v[166:167] op_sel_hi:[1,0]
	v_cvt_pk_fp8_f32 v112, v96, v97
	v_cvt_pk_fp8_f32 v113, v100, v101
	v_cvt_pk_fp8_f32 v114, v104, v105
	v_cvt_pk_fp8_f32 v115, v108, v109
	v_pk_mul_f32 v[98:99], v[98:99], v[166:167] op_sel_hi:[1,0]
	v_pk_mul_f32 v[102:103], v[102:103], v[166:167] op_sel_hi:[1,0]
	v_pk_mul_f32 v[106:107], v[106:107], v[166:167] op_sel_hi:[1,0]
	v_pk_mul_f32 v[110:111], v[110:111], v[166:167] op_sel_hi:[1,0]
	v_cvt_pk_fp8_f32 v112, v98, v99 op_sel:[0,0,1]
	v_cvt_pk_fp8_f32 v113, v102, v103 op_sel:[0,0,1]
	v_cvt_pk_fp8_f32 v114, v106, v107 op_sel:[0,0,1]
	v_cvt_pk_fp8_f32 v115, v110, v111 op_sel:[0,0,1]
	v_lshlrev_b64 v[96:97], 10, v[164:165]
	v_lshl_add_u64 v[96:97], s[6:7], 0, v[96:97]
	v_lshl_add_u64 v[96:97], v[96:97], 0, v[136:137]
	global_store_dwordx4 v[96:97], v[112:115], off nt
.LBB0_1074:
	s_or_b64 exec, exec, s[36:37]
	v_or_b32_e32 v96, 32, v138
	v_cmp_gt_i32_e32 vcc, s52, v96
	s_and_saveexec_b64 s[36:37], vcc
	s_cbranch_execz .LBB0_1076
	v_mov_b32_e32 v96, 0
	v_mov_b32_e32 v97, 0
	v_mov_b32_e32 v98, 0
	v_mov_b32_e32 v99, 0
	v_ashrrev_i32_e32 v169, 31, v168
	v_mul_f32_e32 v170, 0x41800000, v170
	v_pk_mul_f32 v[80:81], v[80:81], v[170:171] op_sel_hi:[1,0]
	v_pk_mul_f32 v[84:85], v[84:85], v[170:171] op_sel_hi:[1,0]
	v_pk_mul_f32 v[88:89], v[88:89], v[170:171] op_sel_hi:[1,0]
	v_pk_mul_f32 v[92:93], v[92:93], v[170:171] op_sel_hi:[1,0]
	v_cvt_pk_fp8_f32 v96, v80, v81
	v_cvt_pk_fp8_f32 v97, v84, v85
	v_cvt_pk_fp8_f32 v98, v88, v89
	v_cvt_pk_fp8_f32 v99, v92, v93
	v_pk_mul_f32 v[82:83], v[82:83], v[170:171] op_sel_hi:[1,0]
	v_pk_mul_f32 v[86:87], v[86:87], v[170:171] op_sel_hi:[1,0]
	v_pk_mul_f32 v[90:91], v[90:91], v[170:171] op_sel_hi:[1,0]
	v_pk_mul_f32 v[94:95], v[94:95], v[170:171] op_sel_hi:[1,0]
	v_cvt_pk_fp8_f32 v96, v82, v83 op_sel:[0,0,1]
	v_cvt_pk_fp8_f32 v97, v86, v87 op_sel:[0,0,1]
	v_cvt_pk_fp8_f32 v98, v90, v91 op_sel:[0,0,1]
	v_cvt_pk_fp8_f32 v99, v94, v95 op_sel:[0,0,1]
	v_lshlrev_b64 v[80:81], 10, v[168:169]
	v_lshl_add_u64 v[80:81], s[6:7], 0, v[80:81]
	v_lshl_add_u64 v[80:81], v[80:81], 0, v[136:137]
	global_store_dwordx4 v[80:81], v[96:99], off nt
.LBB0_1076:
	s_or_b64 exec, exec, s[36:37]
	v_or_b32_e32 v80, 48, v138
	v_cmp_gt_i32_e32 vcc, s52, v80
	s_and_saveexec_b64 s[36:37], vcc
	s_cbranch_execz .LBB0_1078
	v_mov_b32_e32 v80, 0
	v_mov_b32_e32 v81, 0
	v_mov_b32_e32 v82, 0
	v_mov_b32_e32 v83, 0
	v_ashrrev_i32_e32 v173, 31, v172
	v_mul_f32_e32 v174, 0x41800000, v174
	v_pk_mul_f32 v[64:65], v[64:65], v[174:175] op_sel_hi:[1,0]
	v_pk_mul_f32 v[68:69], v[68:69], v[174:175] op_sel_hi:[1,0]
	v_pk_mul_f32 v[72:73], v[72:73], v[174:175] op_sel_hi:[1,0]
	v_pk_mul_f32 v[76:77], v[76:77], v[174:175] op_sel_hi:[1,0]
	v_cvt_pk_fp8_f32 v80, v64, v65
	v_cvt_pk_fp8_f32 v81, v68, v69
	v_cvt_pk_fp8_f32 v82, v72, v73
	v_cvt_pk_fp8_f32 v83, v76, v77
	v_pk_mul_f32 v[66:67], v[66:67], v[174:175] op_sel_hi:[1,0]
	v_pk_mul_f32 v[70:71], v[70:71], v[174:175] op_sel_hi:[1,0]
	v_pk_mul_f32 v[74:75], v[74:75], v[174:175] op_sel_hi:[1,0]
	v_pk_mul_f32 v[78:79], v[78:79], v[174:175] op_sel_hi:[1,0]
	v_cvt_pk_fp8_f32 v80, v66, v67 op_sel:[0,0,1]
	v_cvt_pk_fp8_f32 v81, v70, v71 op_sel:[0,0,1]
	v_cvt_pk_fp8_f32 v82, v74, v75 op_sel:[0,0,1]
	v_cvt_pk_fp8_f32 v83, v78, v79 op_sel:[0,0,1]
	v_lshlrev_b64 v[64:65], 10, v[172:173]
	v_lshl_add_u64 v[64:65], s[6:7], 0, v[64:65]
	v_lshl_add_u64 v[64:65], v[64:65], 0, v[136:137]
	global_store_dwordx4 v[64:65], v[80:83], off nt
.LBB0_1078:
	s_or_b64 exec, exec, s[36:37]
	v_add_u32_e32 v64, 0x80, v138
	v_cmp_gt_i32_e32 vcc, s52, v64
	s_and_saveexec_b64 s[36:37], vcc
	s_cbranch_execz .LBB0_1080
	v_mov_b32_e32 v64, 0
	v_mov_b32_e32 v65, 0
	v_mov_b32_e32 v66, 0
	v_mov_b32_e32 v67, 0
	v_ashrrev_i32_e32 v177, 31, v176
	v_mul_f32_e32 v178, 0x41800000, v178
	v_pk_mul_f32 v[48:49], v[48:49], v[178:179] op_sel_hi:[1,0]
	v_pk_mul_f32 v[52:53], v[52:53], v[178:179] op_sel_hi:[1,0]
	v_pk_mul_f32 v[56:57], v[56:57], v[178:179] op_sel_hi:[1,0]
	v_pk_mul_f32 v[60:61], v[60:61], v[178:179] op_sel_hi:[1,0]
	v_cvt_pk_fp8_f32 v64, v48, v49
	v_cvt_pk_fp8_f32 v65, v52, v53
	v_cvt_pk_fp8_f32 v66, v56, v57
	v_cvt_pk_fp8_f32 v67, v60, v61
	v_pk_mul_f32 v[50:51], v[50:51], v[178:179] op_sel_hi:[1,0]
	v_pk_mul_f32 v[54:55], v[54:55], v[178:179] op_sel_hi:[1,0]
	v_pk_mul_f32 v[58:59], v[58:59], v[178:179] op_sel_hi:[1,0]
	v_pk_mul_f32 v[62:63], v[62:63], v[178:179] op_sel_hi:[1,0]
	v_cvt_pk_fp8_f32 v64, v50, v51 op_sel:[0,0,1]
	v_cvt_pk_fp8_f32 v65, v54, v55 op_sel:[0,0,1]
	v_cvt_pk_fp8_f32 v66, v58, v59 op_sel:[0,0,1]
	v_cvt_pk_fp8_f32 v67, v62, v63 op_sel:[0,0,1]
	v_lshlrev_b64 v[48:49], 10, v[176:177]
	v_lshl_add_u64 v[48:49], s[6:7], 0, v[48:49]
	v_lshl_add_u64 v[48:49], v[48:49], 0, v[136:137]
	global_store_dwordx4 v[48:49], v[64:67], off nt
.LBB0_1080:
	s_or_b64 exec, exec, s[36:37]
	v_add_u32_e32 v48, 0x90, v138
	v_cmp_gt_i32_e32 vcc, s52, v48
	s_and_saveexec_b64 s[36:37], vcc
	s_cbranch_execz .LBB0_1082
	v_mov_b32_e32 v48, 0
	v_mov_b32_e32 v49, 0
	v_mov_b32_e32 v50, 0
	v_mov_b32_e32 v51, 0
	v_ashrrev_i32_e32 v181, 31, v180
	v_mul_f32_e32 v182, 0x41800000, v182
	v_pk_mul_f32 v[32:33], v[32:33], v[182:183] op_sel_hi:[1,0]
	v_pk_mul_f32 v[36:37], v[36:37], v[182:183] op_sel_hi:[1,0]
	v_pk_mul_f32 v[40:41], v[40:41], v[182:183] op_sel_hi:[1,0]
	v_pk_mul_f32 v[44:45], v[44:45], v[182:183] op_sel_hi:[1,0]
	v_cvt_pk_fp8_f32 v48, v32, v33
	v_cvt_pk_fp8_f32 v49, v36, v37
	v_cvt_pk_fp8_f32 v50, v40, v41
	v_cvt_pk_fp8_f32 v51, v44, v45
	v_pk_mul_f32 v[34:35], v[34:35], v[182:183] op_sel_hi:[1,0]
	v_pk_mul_f32 v[38:39], v[38:39], v[182:183] op_sel_hi:[1,0]
	v_pk_mul_f32 v[42:43], v[42:43], v[182:183] op_sel_hi:[1,0]
	v_pk_mul_f32 v[46:47], v[46:47], v[182:183] op_sel_hi:[1,0]
	v_cvt_pk_fp8_f32 v48, v34, v35 op_sel:[0,0,1]
	v_cvt_pk_fp8_f32 v49, v38, v39 op_sel:[0,0,1]
	v_cvt_pk_fp8_f32 v50, v42, v43 op_sel:[0,0,1]
	v_cvt_pk_fp8_f32 v51, v46, v47 op_sel:[0,0,1]
	v_lshlrev_b64 v[32:33], 10, v[180:181]
	v_lshl_add_u64 v[32:33], s[6:7], 0, v[32:33]
	v_lshl_add_u64 v[32:33], v[32:33], 0, v[136:137]
	global_store_dwordx4 v[32:33], v[48:51], off nt
.LBB0_1082:
	s_or_b64 exec, exec, s[36:37]
	v_cmp_gt_i32_e32 vcc, s52, v151
	s_and_saveexec_b64 s[36:37], vcc
	s_cbranch_execz .LBB0_1084
	v_mov_b32_e32 v32, 0
	v_mov_b32_e32 v33, 0
	v_mov_b32_e32 v34, 0
	v_mov_b32_e32 v35, 0
	v_ashrrev_i32_e32 v185, 31, v184
	v_mul_f32_e32 v186, 0x41800000, v186
	v_pk_mul_f32 v[16:17], v[16:17], v[186:187] op_sel_hi:[1,0]
	v_pk_mul_f32 v[20:21], v[20:21], v[186:187] op_sel_hi:[1,0]
	v_pk_mul_f32 v[24:25], v[24:25], v[186:187] op_sel_hi:[1,0]
	v_pk_mul_f32 v[28:29], v[28:29], v[186:187] op_sel_hi:[1,0]
	v_cvt_pk_fp8_f32 v32, v16, v17
	v_cvt_pk_fp8_f32 v33, v20, v21
	v_cvt_pk_fp8_f32 v34, v24, v25
	v_cvt_pk_fp8_f32 v35, v28, v29
	v_pk_mul_f32 v[18:19], v[18:19], v[186:187] op_sel_hi:[1,0]
	v_pk_mul_f32 v[22:23], v[22:23], v[186:187] op_sel_hi:[1,0]
	v_pk_mul_f32 v[26:27], v[26:27], v[186:187] op_sel_hi:[1,0]
	v_pk_mul_f32 v[30:31], v[30:31], v[186:187] op_sel_hi:[1,0]
	v_cvt_pk_fp8_f32 v32, v18, v19 op_sel:[0,0,1]
	v_cvt_pk_fp8_f32 v33, v22, v23 op_sel:[0,0,1]
	v_cvt_pk_fp8_f32 v34, v26, v27 op_sel:[0,0,1]
	v_cvt_pk_fp8_f32 v35, v30, v31 op_sel:[0,0,1]
	v_lshlrev_b64 v[16:17], 10, v[184:185]
	v_lshl_add_u64 v[16:17], s[6:7], 0, v[16:17]
	v_lshl_add_u64 v[16:17], v[16:17], 0, v[136:137]
	global_store_dwordx4 v[16:17], v[32:35], off nt
.LBB0_1084:
	s_or_b64 exec, exec, s[36:37]
	v_cmp_gt_i32_e32 vcc, s52, v141
	s_and_saveexec_b64 s[36:37], vcc
	s_cbranch_execz .LBB0_1086
	v_mov_b32_e32 v16, 0
	v_mov_b32_e32 v17, 0
	v_mov_b32_e32 v18, 0
	v_mov_b32_e32 v19, 0
	v_ashrrev_i32_e32 v189, 31, v188
	v_mul_f32_e32 v190, 0x41800000, v190
	v_pk_mul_f32 v[0:1], v[0:1], v[190:191] op_sel_hi:[1,0]
	v_pk_mul_f32 v[4:5], v[4:5], v[190:191] op_sel_hi:[1,0]
	v_pk_mul_f32 v[8:9], v[8:9], v[190:191] op_sel_hi:[1,0]
	v_pk_mul_f32 v[12:13], v[12:13], v[190:191] op_sel_hi:[1,0]
	v_cvt_pk_fp8_f32 v16, v0, v1
	v_cvt_pk_fp8_f32 v17, v4, v5
	v_cvt_pk_fp8_f32 v18, v8, v9
	v_cvt_pk_fp8_f32 v19, v12, v13
	v_pk_mul_f32 v[2:3], v[2:3], v[190:191] op_sel_hi:[1,0]
	v_pk_mul_f32 v[6:7], v[6:7], v[190:191] op_sel_hi:[1,0]
	v_pk_mul_f32 v[10:11], v[10:11], v[190:191] op_sel_hi:[1,0]
	v_pk_mul_f32 v[14:15], v[14:15], v[190:191] op_sel_hi:[1,0]
	v_cvt_pk_fp8_f32 v16, v2, v3 op_sel:[0,0,1]
	v_cvt_pk_fp8_f32 v17, v6, v7 op_sel:[0,0,1]
	v_cvt_pk_fp8_f32 v18, v10, v11 op_sel:[0,0,1]
	v_cvt_pk_fp8_f32 v19, v14, v15 op_sel:[0,0,1]
	v_lshlrev_b64 v[0:1], 10, v[188:189]
	v_lshl_add_u64 v[0:1], s[6:7], 0, v[0:1]
	v_lshl_add_u64 v[0:1], v[0:1], 0, v[136:137]
	global_store_dwordx4 v[0:1], v[16:19], off nt

.LBB0_1246:
	v_lshl_add_u32 v146, s26, 8, v149
	v_ashrrev_i32_e32 v147, 31, v146
	v_lshl_add_u64 v[158:159], v[146:147], 2, s[12:13]
	global_load_dword v160, v[158:159], off
	global_load_dword v162, v[158:159], off offset:64
	global_load_dword v164, v[158:159], off offset:128
	global_load_dword v152, v[158:159], off offset:192
	v_mov_b64_e32 v[144:145], s[8:9]
	v_or_b32_e32 v148, 16, v146
	v_mad_i64_i32 v[168:169], s[28:29], v148, s59, v[144:145]
	global_load_dword v174, v[158:159], off offset:512
	global_load_dword v176, v[158:159], off offset:576
	global_load_dword v178, v[158:159], off offset:640
	global_load_dword v148, v[158:159], off offset:704
	v_lshl_or_b32 v150, s60, 8, v154
	v_ashrrev_i32_e32 v151, 31, v150
	v_add_u32_e32 v165, 0xb0, v146
	v_mad_i64_i32 v[166:167], s[28:29], v146, s59, v[144:145]
	v_or_b32_e32 v161, 32, v146
	v_or_b32_e32 v163, 48, v146
	v_lshlrev_b64 v[150:151], 1, v[150:151]
	v_mad_i64_i32 v[172:173], s[28:29], v163, s59, v[144:145]
	v_lshl_add_u64 v[158:159], v[166:167], 0, v[150:151]
	v_mad_i64_i32 v[170:171], s[28:29], v161, s59, v[144:145]
	v_lshl_add_u64 v[166:167], v[168:169], 0, v[150:151]
	v_lshl_add_u64 v[168:169], v[170:171], 0, v[150:151]
	v_lshl_add_u64 v[170:171], v[172:173], 0, v[150:151]
	v_add_u32_e32 v147, 0x80, v146
	s_andn2_b64 vcc, exec, s[2:3]
	s_mov_b64 s[2:3], -1
	s_waitcnt vmcnt(0)
	v_pk_mul_f32 v[126:127], v[126:127], v[160:161] op_sel_hi:[1,0]
	v_pk_mul_f32 v[124:125], v[124:125], v[160:161] op_sel_hi:[1,0]
	v_pk_mul_f32 v[118:119], v[118:119], v[162:163] op_sel_hi:[1,0]
	v_pk_mul_f32 v[116:117], v[116:117], v[162:163] op_sel_hi:[1,0]
	v_pk_mul_f32 v[114:115], v[114:115], v[162:163] op_sel_hi:[1,0]
	v_pk_mul_f32 v[112:113], v[112:113], v[162:163] op_sel_hi:[1,0]
	v_pk_mul_f32 v[90:91], v[90:91], v[162:163] op_sel_hi:[1,0]
	v_pk_mul_f32 v[88:89], v[88:89], v[162:163] op_sel_hi:[1,0]
	v_pk_mul_f32 v[86:87], v[86:87], v[162:163] op_sel_hi:[1,0]
	v_pk_mul_f32 v[84:85], v[84:85], v[162:163] op_sel_hi:[1,0]
	v_pk_mul_f32 v[162:163], v[72:73], v[164:165] op_sel_hi:[1,0]
	v_cvt_pk_bf16_f32 v72, v124, v125
	v_cvt_pk_bf16_f32 v73, v126, v127
	v_pk_mul_f32 v[122:123], v[122:123], v[160:161] op_sel_hi:[1,0]
	v_pk_mul_f32 v[120:121], v[120:121], v[160:161] op_sel_hi:[1,0]
	v_pk_mul_f32 v[106:107], v[106:107], v[160:161] op_sel_hi:[1,0]
	v_pk_mul_f32 v[104:105], v[104:105], v[160:161] op_sel_hi:[1,0]
	v_pk_mul_f32 v[98:99], v[98:99], v[160:161] op_sel_hi:[1,0]
	v_pk_mul_f32 v[96:97], v[96:97], v[160:161] op_sel_hi:[1,0]
	v_pk_mul_f32 v[160:161], v[74:75], v[164:165] op_sel_hi:[1,0]
	v_cvt_pk_bf16_f32 v74, v120, v121
	v_cvt_pk_bf16_f32 v75, v122, v123
	global_store_dwordx4 v[158:159], v[72:75], off nt
	v_pk_mul_f32 v[110:111], v[110:111], v[164:165] op_sel_hi:[1,0]
	v_pk_mul_f32 v[108:109], v[108:109], v[164:165] op_sel_hi:[1,0]
	v_cvt_pk_bf16_f32 v72, v104, v105
	v_cvt_pk_bf16_f32 v73, v106, v107
	v_cvt_pk_bf16_f32 v74, v96, v97
	v_cvt_pk_bf16_f32 v75, v98, v99
	global_store_dwordx4 v[158:159], v[72:75], off offset:256 nt
	v_pk_mul_f32 v[102:103], v[102:103], v[164:165] op_sel_hi:[1,0]
	v_pk_mul_f32 v[100:101], v[100:101], v[164:165] op_sel_hi:[1,0]
	v_cvt_pk_bf16_f32 v72, v116, v117
	v_cvt_pk_bf16_f32 v73, v118, v119
	v_cvt_pk_bf16_f32 v74, v112, v113
	v_cvt_pk_bf16_f32 v75, v114, v115
	global_store_dwordx4 v[166:167], v[72:75], off nt
	v_pk_mul_f32 v[78:79], v[78:79], v[164:165] op_sel_hi:[1,0]
	v_pk_mul_f32 v[76:77], v[76:77], v[164:165] op_sel_hi:[1,0]
	v_cvt_pk_bf16_f32 v72, v88, v89
	v_cvt_pk_bf16_f32 v73, v90, v91
	v_cvt_pk_bf16_f32 v74, v84, v85
	v_cvt_pk_bf16_f32 v75, v86, v87
	global_store_dwordx4 v[166:167], v[72:75], off offset:256 nt
	v_pk_mul_f32 v[94:95], v[94:95], v[152:153] op_sel_hi:[1,0]
	v_pk_mul_f32 v[92:93], v[92:93], v[152:153] op_sel_hi:[1,0]
	v_cvt_pk_bf16_f32 v72, v108, v109
	v_cvt_pk_bf16_f32 v73, v110, v111
	v_cvt_pk_bf16_f32 v74, v100, v101
	v_cvt_pk_bf16_f32 v75, v102, v103
	global_store_dwordx4 v[168:169], v[72:75], off nt
	v_pk_mul_f32 v[82:83], v[82:83], v[152:153] op_sel_hi:[1,0]
	v_pk_mul_f32 v[80:81], v[80:81], v[152:153] op_sel_hi:[1,0]
	v_cvt_pk_bf16_f32 v72, v76, v77
	v_cvt_pk_bf16_f32 v73, v78, v79
	v_cvt_pk_bf16_f32 v74, v162, v163
	v_cvt_pk_bf16_f32 v75, v160, v161
	global_store_dwordx4 v[168:169], v[72:75], off offset:256 nt
	v_pk_mul_f32 v[70:71], v[70:71], v[152:153] op_sel_hi:[1,0]
	v_pk_mul_f32 v[68:69], v[68:69], v[152:153] op_sel_hi:[1,0]
	v_cvt_pk_bf16_f32 v72, v92, v93
	v_cvt_pk_bf16_f32 v73, v94, v95
	v_cvt_pk_bf16_f32 v74, v80, v81
	v_cvt_pk_bf16_f32 v75, v82, v83
	global_store_dwordx4 v[170:171], v[72:75], off nt
	v_pk_mul_f32 v[62:63], v[62:63], v[174:175] op_sel_hi:[1,0]
	v_pk_mul_f32 v[60:61], v[60:61], v[174:175] op_sel_hi:[1,0]
	v_pk_mul_f32 v[72:73], v[66:67], v[152:153] op_sel_hi:[1,0]
	v_pk_mul_f32 v[66:67], v[64:65], v[152:153] op_sel_hi:[1,0]
	v_cvt_pk_bf16_f32 v64, v68, v69
	v_cvt_pk_bf16_f32 v65, v70, v71
	v_pk_mul_f32 v[52:53], v[52:53], v[174:175] op_sel_hi:[1,0]
	v_cvt_pk_bf16_f32 v66, v66, v67
	v_cvt_pk_bf16_f32 v67, v72, v73
	global_store_dwordx4 v[170:171], v[64:67], off offset:256 nt
	v_pk_mul_f32 v[54:55], v[54:55], v[174:175] op_sel_hi:[1,0]
	v_pk_mul_f32 v[48:49], v[48:49], v[176:177] op_sel_hi:[1,0]
	v_mad_i64_i32 v[64:65], s[28:29], v147, s59, v[144:145]
	v_lshl_add_u64 v[64:65], v[64:65], 0, v[150:151]
	v_pk_mul_f32 v[66:67], v[58:59], v[174:175] op_sel_hi:[1,0]
	v_pk_mul_f32 v[58:59], v[56:57], v[174:175] op_sel_hi:[1,0]
	v_cvt_pk_bf16_f32 v56, v60, v61
	v_cvt_pk_bf16_f32 v57, v62, v63
	v_pk_mul_f32 v[36:37], v[36:37], v[176:177] op_sel_hi:[1,0]
	v_cvt_pk_bf16_f32 v58, v58, v59
	v_cvt_pk_bf16_f32 v59, v66, v67
	global_store_dwordx4 v[64:65], v[56:59], off nt
	v_pk_mul_f32 v[38:39], v[38:39], v[176:177] op_sel_hi:[1,0]
	v_pk_mul_f32 v[32:33], v[32:33], v[178:179] op_sel_hi:[1,0]
	v_pk_mul_f32 v[56:57], v[46:47], v[174:175] op_sel_hi:[1,0]
	v_pk_mul_f32 v[46:47], v[44:45], v[174:175] op_sel_hi:[1,0]
	v_cvt_pk_bf16_f32 v44, v52, v53
	v_cvt_pk_bf16_f32 v45, v54, v55
	v_pk_mul_f32 v[22:23], v[22:23], v[178:179] op_sel_hi:[1,0]
	v_cvt_pk_bf16_f32 v46, v46, v47
	v_cvt_pk_bf16_f32 v47, v56, v57
	global_store_dwordx4 v[64:65], v[44:47], off offset:256 nt
	v_pk_mul_f32 v[20:21], v[20:21], v[178:179] op_sel_hi:[1,0]
	v_pk_mul_f32 v[16:17], v[16:17], v[148:149] op_sel_hi:[1,0]
	v_add_u32_e32 v44, 0x90, v146
	v_mad_i64_i32 v[44:45], s[28:29], v44, s59, v[144:145]
	v_lshl_add_u64 v[44:45], v[44:45], 0, v[150:151]
	v_pk_mul_f32 v[46:47], v[50:51], v[176:177] op_sel_hi:[1,0]
	v_pk_mul_f32 v[50:51], v[42:43], v[176:177] op_sel_hi:[1,0]
	v_pk_mul_f32 v[42:43], v[40:41], v[176:177] op_sel_hi:[1,0]
	v_cvt_pk_bf16_f32 v40, v48, v49
	v_cvt_pk_bf16_f32 v41, v46, v47
	v_pk_mul_f32 v[6:7], v[6:7], v[148:149] op_sel_hi:[1,0]
	v_cvt_pk_bf16_f32 v42, v42, v43
	v_cvt_pk_bf16_f32 v43, v50, v51
	global_store_dwordx4 v[44:45], v[40:43], off nt
	v_pk_mul_f32 v[4:5], v[4:5], v[148:149] op_sel_hi:[1,0]
	s_nop 0
	v_pk_mul_f32 v[40:41], v[30:31], v[176:177] op_sel_hi:[1,0]
	v_pk_mul_f32 v[30:31], v[28:29], v[176:177] op_sel_hi:[1,0]
	v_cvt_pk_bf16_f32 v28, v36, v37
	v_cvt_pk_bf16_f32 v29, v38, v39
	s_nop 0
	v_cvt_pk_bf16_f32 v30, v30, v31
	v_cvt_pk_bf16_f32 v31, v40, v41
	global_store_dwordx4 v[44:45], v[28:31], off offset:256 nt
	s_nop 1
	v_add_u32_e32 v28, 0xa0, v146
	v_mad_i64_i32 v[28:29], s[28:29], v28, s59, v[144:145]
	v_lshl_add_u64 v[28:29], v[28:29], 0, v[150:151]
	v_pk_mul_f32 v[30:31], v[34:35], v[178:179] op_sel_hi:[1,0]
	v_pk_mul_f32 v[34:35], v[26:27], v[178:179] op_sel_hi:[1,0]
	v_pk_mul_f32 v[26:27], v[24:25], v[178:179] op_sel_hi:[1,0]
	v_cvt_pk_bf16_f32 v24, v32, v33
	v_cvt_pk_bf16_f32 v25, v30, v31
	s_nop 0
	v_cvt_pk_bf16_f32 v26, v26, v27
	v_cvt_pk_bf16_f32 v27, v34, v35
	global_store_dwordx4 v[28:29], v[24:27], off nt
	s_nop 1
	v_pk_mul_f32 v[24:25], v[14:15], v[178:179] op_sel_hi:[1,0]
	v_pk_mul_f32 v[14:15], v[12:13], v[178:179] op_sel_hi:[1,0]
	v_cvt_pk_bf16_f32 v12, v20, v21
	v_cvt_pk_bf16_f32 v13, v22, v23
	s_nop 0
	v_cvt_pk_bf16_f32 v14, v14, v15
	v_cvt_pk_bf16_f32 v15, v24, v25
	global_store_dwordx4 v[28:29], v[12:15], off offset:256 nt
	s_nop 1
	v_mad_i64_i32 v[12:13], s[28:29], v165, s59, v[144:145]
	v_lshl_add_u64 v[12:13], v[12:13], 0, v[150:151]
	v_pk_mul_f32 v[14:15], v[18:19], v[148:149] op_sel_hi:[1,0]
	v_pk_mul_f32 v[18:19], v[10:11], v[148:149] op_sel_hi:[1,0]
	v_pk_mul_f32 v[10:11], v[8:9], v[148:149] op_sel_hi:[1,0]
	v_cvt_pk_bf16_f32 v8, v16, v17
	v_cvt_pk_bf16_f32 v9, v14, v15
	s_nop 0
	v_cvt_pk_bf16_f32 v10, v10, v11
	v_cvt_pk_bf16_f32 v11, v18, v19
	global_store_dwordx4 v[12:13], v[8:11], off nt
	s_nop 1
	v_pk_mul_f32 v[8:9], v[2:3], v[148:149] op_sel_hi:[1,0]
	v_pk_mul_f32 v[2:3], v[0:1], v[148:149] op_sel_hi:[1,0]
	v_cvt_pk_bf16_f32 v0, v4, v5
	v_cvt_pk_bf16_f32 v1, v6, v7
	s_nop 0
	v_cvt_pk_bf16_f32 v2, v2, v3
	v_cvt_pk_bf16_f32 v3, v8, v9
	global_store_dwordx4 v[12:13], v[0:3], off offset:256 nt
	s_cbranch_vccnz .LBB0_1239
	s_andn2_b64 vcc, exec, s[6:7]
	s_cbranch_vccnz .LBB0_1238
	s_barrier
	s_branch .LBB0_1238

.LBB0_1295:
	ds_read2_b32 v[214:215], v146 offset1:32
	s_addk_i32 s26, 0x400
	s_addk_i32 s51, 0x400
	s_add_i32 s52, s52, 0x10000
	s_waitcnt vmcnt(0) lgkmcnt(0)
	v_mul_f32_e32 v77, v68, v214
	ds_read_b32 v209, v147
	ds_read_b32 v211, v148
	ds_read_b32 v212, v149
	ds_read_b32 v213, v150
	ds_read_b32 v214, v151
	ds_read_b32 v216, v152
	ds_read_b32 v217, v153
	ds_read_b32 v218, v154
	s_waitcnt lgkmcnt(7)
	v_mul_f32_e32 v209, v69, v209
	v_cvt_pk_bf16_f32 v210, v77, v209
	s_waitcnt lgkmcnt(6)
	v_mul_f32_e32 v77, v70, v211
	s_waitcnt lgkmcnt(5)
	v_mul_f32_e32 v209, v71, v212
	v_cvt_pk_bf16_f32 v211, v77, v209
	s_waitcnt lgkmcnt(4)
	v_mul_f32_e32 v77, v64, v213
	s_waitcnt lgkmcnt(3)
	v_mul_f32_e32 v209, v65, v214
	v_cvt_pk_bf16_f32 v212, v77, v209
	s_waitcnt lgkmcnt(2)
	v_mul_f32_e32 v77, v66, v216
	s_waitcnt lgkmcnt(1)
	v_mul_f32_e32 v209, v67, v217
	v_cvt_pk_bf16_f32 v213, v77, v209
	v_add_u32_e32 v77, s28, v138
	v_mad_i64_i32 v[216:217], s[6:7], s27, v77, 0
	v_lshl_add_u64 v[216:217], v[216:217], 1, s[2:3]
	s_lshl_b64 s[6:7], s[8:9], 1
	v_lshl_add_u64 v[216:217], v[216:217], 0, s[6:7]
	v_lshl_add_u64 v[216:217], v[216:217], 0, v[72:73]
	global_store_dwordx4 v[216:217], v[210:213], off nt
	s_waitcnt lgkmcnt(0)
	v_mul_f32_e32 v77, v68, v218
	ds_read_b32 v209, v155
	ds_read_b32 v211, v156
	ds_read_b32 v212, v157
	ds_read_b32 v213, v158
	ds_read_b32 v214, v159
	ds_read_b32 v216, v160
	ds_read_b32 v217, v161
	ds_read_b32 v218, v162
	s_waitcnt lgkmcnt(7)
	v_mul_f32_e32 v209, v69, v209
	v_cvt_pk_bf16_f32 v210, v77, v209
	s_waitcnt lgkmcnt(6)
	v_mul_f32_e32 v77, v70, v211
	s_waitcnt lgkmcnt(5)
	v_mul_f32_e32 v209, v71, v212
	v_cvt_pk_bf16_f32 v211, v77, v209
	s_waitcnt lgkmcnt(4)
	v_mul_f32_e32 v77, v64, v213
	s_waitcnt lgkmcnt(3)
	v_mul_f32_e32 v209, v65, v214
	v_cvt_pk_bf16_f32 v212, v77, v209
	s_waitcnt lgkmcnt(2)
	v_mul_f32_e32 v77, v66, v216
	s_waitcnt lgkmcnt(1)
	v_mul_f32_e32 v209, v67, v217
	v_cvt_pk_bf16_f32 v213, v77, v209
	v_add_u32_e32 v77, s28, v139
	v_mad_i64_i32 v[216:217], s[8:9], s27, v77, 0
	v_lshl_add_u64 v[216:217], v[216:217], 1, s[2:3]
	v_lshl_add_u64 v[216:217], v[216:217], 0, s[6:7]
	v_lshl_add_u64 v[216:217], v[216:217], 0, v[72:73]
	global_store_dwordx4 v[216:217], v[210:213], off nt
	s_waitcnt lgkmcnt(0)
	v_mul_f32_e32 v77, v68, v218
	ds_read_b32 v209, v163
	ds_read_b32 v211, v164
	ds_read_b32 v212, v165
	ds_read_b32 v213, v166
	ds_read_b32 v214, v167
	ds_read_b32 v216, v168
	ds_read_b32 v217, v169
	ds_read_b32 v218, v170
	s_waitcnt lgkmcnt(7)
	v_mul_f32_e32 v209, v69, v209
	v_cvt_pk_bf16_f32 v210, v77, v209
	s_waitcnt lgkmcnt(6)
	v_mul_f32_e32 v77, v70, v211
	s_waitcnt lgkmcnt(5)
	v_mul_f32_e32 v209, v71, v212
	v_cvt_pk_bf16_f32 v211, v77, v209
	s_waitcnt lgkmcnt(4)
	v_mul_f32_e32 v77, v64, v213
	s_waitcnt lgkmcnt(3)
	v_mul_f32_e32 v209, v65, v214
	v_cvt_pk_bf16_f32 v212, v77, v209
	s_waitcnt lgkmcnt(2)
	v_mul_f32_e32 v77, v66, v216
	s_waitcnt lgkmcnt(1)
	v_mul_f32_e32 v209, v67, v217
	v_cvt_pk_bf16_f32 v213, v77, v209
	v_add_u32_e32 v77, s28, v140
	v_mad_i64_i32 v[216:217], s[8:9], s27, v77, 0
	v_lshl_add_u64 v[216:217], v[216:217], 1, s[2:3]
	v_lshl_add_u64 v[216:217], v[216:217], 0, s[6:7]
	v_lshl_add_u64 v[216:217], v[216:217], 0, v[72:73]
	global_store_dwordx4 v[216:217], v[210:213], off nt
	s_waitcnt lgkmcnt(0)
	v_mul_f32_e32 v77, v68, v218
	ds_read_b32 v209, v171
	ds_read_b32 v211, v172
	ds_read_b32 v212, v173
	ds_read_b32 v213, v174
	ds_read_b32 v214, v175
	ds_read_b32 v216, v176
	ds_read_b32 v217, v177
	ds_read_b32 v218, v178
	s_waitcnt lgkmcnt(7)
	v_mul_f32_e32 v209, v69, v209
	v_cvt_pk_bf16_f32 v210, v77, v209
	s_waitcnt lgkmcnt(6)
	v_mul_f32_e32 v77, v70, v211
	s_waitcnt lgkmcnt(5)
	v_mul_f32_e32 v209, v71, v212
	v_cvt_pk_bf16_f32 v211, v77, v209
	s_waitcnt lgkmcnt(4)
	v_mul_f32_e32 v77, v64, v213
	s_waitcnt lgkmcnt(3)
	v_mul_f32_e32 v209, v65, v214
	v_cvt_pk_bf16_f32 v212, v77, v209
	s_waitcnt lgkmcnt(2)
	v_mul_f32_e32 v77, v66, v216
	s_waitcnt lgkmcnt(1)
	v_mul_f32_e32 v209, v67, v217
	v_cvt_pk_bf16_f32 v213, v77, v209
	v_add_u32_e32 v77, s28, v141
	v_mad_i64_i32 v[216:217], s[8:9], s27, v77, 0
	v_lshl_add_u64 v[216:217], v[216:217], 1, s[2:3]
	v_lshl_add_u64 v[216:217], v[216:217], 0, s[6:7]
	v_lshl_add_u64 v[216:217], v[216:217], 0, v[72:73]
	global_store_dwordx4 v[216:217], v[210:213], off nt
	v_mul_f32_e32 v77, v68, v215
	s_waitcnt lgkmcnt(0)
	v_mul_f32_e32 v209, v69, v218
	v_cvt_pk_bf16_f32 v210, v77, v209
	ds_read_b32 v77, v179
	ds_read_b32 v209, v180
	ds_read_b32 v212, v181
	ds_read_b32 v213, v182
	ds_read_b32 v214, v183
	ds_read_b32 v215, v184
	ds_read_b32 v216, v185
	ds_read_b32 v217, v186
	s_waitcnt lgkmcnt(7)
	v_mul_f32_e32 v77, v70, v77
	s_waitcnt lgkmcnt(6)
	v_mul_f32_e32 v209, v71, v209
	v_cvt_pk_bf16_f32 v211, v77, v209
	s_waitcnt lgkmcnt(5)
	v_mul_f32_e32 v77, v64, v212
	s_waitcnt lgkmcnt(4)
	v_mul_f32_e32 v209, v65, v213
	v_cvt_pk_bf16_f32 v212, v77, v209
	s_waitcnt lgkmcnt(3)
	v_mul_f32_e32 v77, v66, v214
	s_waitcnt lgkmcnt(2)
	v_mul_f32_e32 v209, v67, v215
	v_cvt_pk_bf16_f32 v213, v77, v209
	v_add_u32_e32 v77, s28, v142
	v_mad_i64_i32 v[214:215], s[8:9], s27, v77, 0
	v_lshl_add_u64 v[214:215], v[214:215], 1, s[2:3]
	v_lshl_add_u64 v[214:215], v[214:215], 0, s[6:7]
	v_lshl_add_u64 v[214:215], v[214:215], 0, v[72:73]
	global_store_dwordx4 v[214:215], v[210:213], off nt
	s_waitcnt lgkmcnt(1)
	v_mul_f32_e32 v77, v68, v216
	s_waitcnt lgkmcnt(0)
	v_mul_f32_e32 v209, v69, v217
	v_cvt_pk_bf16_f32 v210, v77, v209
	ds_read_b32 v77, v187
	ds_read_b32 v209, v188
	ds_read_b32 v212, v189
	ds_read_b32 v213, v190
	ds_read_b32 v214, v191
	ds_read_b32 v215, v192
	ds_read_b32 v216, v193
	ds_read_b32 v217, v194
	s_waitcnt lgkmcnt(7)
	v_mul_f32_e32 v77, v70, v77
	s_waitcnt lgkmcnt(6)
	v_mul_f32_e32 v209, v71, v209
	v_cvt_pk_bf16_f32 v211, v77, v209
	s_waitcnt lgkmcnt(5)
	v_mul_f32_e32 v77, v64, v212
	s_waitcnt lgkmcnt(4)
	v_mul_f32_e32 v209, v65, v213
	v_cvt_pk_bf16_f32 v212, v77, v209
	s_waitcnt lgkmcnt(3)
	v_mul_f32_e32 v77, v66, v214
	s_waitcnt lgkmcnt(2)
	v_mul_f32_e32 v209, v67, v215
	v_cvt_pk_bf16_f32 v213, v77, v209
	v_add_u32_e32 v77, s28, v143
	v_mad_i64_i32 v[214:215], s[8:9], s27, v77, 0
	v_lshl_add_u64 v[214:215], v[214:215], 1, s[2:3]
	v_lshl_add_u64 v[214:215], v[214:215], 0, s[6:7]
	v_lshl_add_u64 v[214:215], v[214:215], 0, v[72:73]
	global_store_dwordx4 v[214:215], v[210:213], off nt
	s_waitcnt lgkmcnt(1)
	v_mul_f32_e32 v77, v68, v216
	s_waitcnt lgkmcnt(0)
	v_mul_f32_e32 v209, v69, v217
	v_cvt_pk_bf16_f32 v210, v77, v209
	ds_read_b32 v77, v195
	ds_read_b32 v209, v196
	ds_read_b32 v212, v197
	ds_read_b32 v213, v198
	ds_read_b32 v214, v199
	ds_read_b32 v215, v200
	ds_read_b32 v216, v201
	ds_read_b32 v217, v202
	s_waitcnt lgkmcnt(7)
	v_mul_f32_e32 v77, v70, v77
	s_waitcnt lgkmcnt(6)
	v_mul_f32_e32 v209, v71, v209
	v_cvt_pk_bf16_f32 v211, v77, v209
	s_waitcnt lgkmcnt(5)
	v_mul_f32_e32 v77, v64, v212
	s_waitcnt lgkmcnt(4)
	v_mul_f32_e32 v209, v65, v213
	v_cvt_pk_bf16_f32 v212, v77, v209
	s_waitcnt lgkmcnt(3)
	v_mul_f32_e32 v77, v66, v214
	s_waitcnt lgkmcnt(2)
	v_mul_f32_e32 v209, v67, v215
	v_cvt_pk_bf16_f32 v213, v77, v209
	v_add_u32_e32 v77, s28, v144
	v_mad_i64_i32 v[214:215], s[8:9], s27, v77, 0
	v_lshl_add_u64 v[214:215], v[214:215], 1, s[2:3]
	v_lshl_add_u64 v[214:215], v[214:215], 0, s[6:7]
	v_lshl_add_u64 v[214:215], v[214:215], 0, v[72:73]
	global_store_dwordx4 v[214:215], v[210:213], off nt
	ds_read_b32 v77, v203
	ds_read_b32 v209, v204
	ds_read_b32 v210, v205
	ds_read_b32 v211, v206
	ds_read_b32 v212, v207
	ds_read_b32 v213, v208
	s_waitcnt lgkmcnt(7)
	v_mul_f32_e32 v68, v68, v216
	s_waitcnt lgkmcnt(6)
	v_mul_f32_e32 v69, v69, v217
	v_cvt_pk_bf16_f32 v68, v68, v69
	s_waitcnt lgkmcnt(5)
	v_mul_f32_e32 v69, v70, v77
	s_waitcnt lgkmcnt(4)
	v_mul_f32_e32 v70, v71, v209
	s_waitcnt lgkmcnt(3)
	v_mul_f32_e32 v64, v64, v210
	v_cvt_pk_bf16_f32 v69, v69, v70
	s_waitcnt lgkmcnt(2)
	v_mul_f32_e32 v65, v65, v211
	v_cvt_pk_bf16_f32 v70, v64, v65
	s_waitcnt lgkmcnt(1)
	v_mul_f32_e32 v64, v66, v212
	s_waitcnt lgkmcnt(0)
	v_mul_f32_e32 v65, v67, v213
	v_cvt_pk_bf16_f32 v71, v64, v65
	v_add_u32_e32 v64, s28, v145
	v_mad_i64_i32 v[64:65], s[8:9], s27, v64, 0
	v_lshl_add_u64 v[64:65], v[64:65], 1, s[2:3]
	v_lshl_add_u64 v[64:65], v[64:65], 0, s[6:7]
	v_lshl_add_u64 v[64:65], v[64:65], 0, v[72:73]
	global_store_dwordx4 v[64:65], v[68:71], off nt
	s_waitcnt lgkmcnt(0)
	s_cmpk_lt_i32 s53, 0x800
	s_mov_b32 s28, s24
	s_mov_b64 s[2:3], s[12:13]
	s_mov_b64 s[6:7], s[14:15]
	s_mov_b32 s27, s54
	s_mov_b32 s8, s18
	s_cbranch_scc0 .LBB0_1329

.LBB0_1408:
	v_mov_b32_e32 v150, 0
	v_mov_b32_e32 v151, 0
	v_mov_b32_e32 v152, 0
	v_mov_b32_e32 v153, 0
	v_cvt_pk_fp8_f32 v150, v124, v125
	v_cvt_pk_fp8_f32 v151, v120, v121
	v_cvt_pk_fp8_f32 v152, v116, v117
	v_cvt_pk_fp8_f32 v153, v108, v109
	v_cvt_pk_fp8_f32 v150, v126, v127 op_sel:[0,0,1]
	v_cvt_pk_fp8_f32 v151, v122, v123 op_sel:[0,0,1]
	v_cvt_pk_fp8_f32 v152, v118, v119 op_sel:[0,0,1]
	v_cvt_pk_fp8_f32 v153, v110, v111 op_sel:[0,0,1]
	v_lshl_add_u32 v158, s57, 8, v144
	v_lshl_or_b32 v154, s58, 8, v146
	v_mov_b64_e32 v[156:157], s[8:9]
	v_ashrrev_i32_e32 v155, 31, v154
	v_mad_i64_i32 v[108:109], s[20:21], v158, s54, v[156:157]
	v_lshl_add_u64 v[108:109], v[108:109], 0, v[154:155]
	global_store_dwordx4 v[108:109], v[150:153], off nt
	v_mov_b32_e32 v108, 0
	v_mov_b32_e32 v109, 0
	v_mov_b32_e32 v110, 0
	v_mov_b32_e32 v111, 0
	v_cvt_pk_fp8_f32 v108, v112, v113
	v_cvt_pk_fp8_f32 v109, v104, v105
	v_cvt_pk_fp8_f32 v110, v100, v101
	v_cvt_pk_fp8_f32 v111, v92, v93
	v_cvt_pk_fp8_f32 v108, v114, v115 op_sel:[0,0,1]
	v_cvt_pk_fp8_f32 v109, v106, v107 op_sel:[0,0,1]
	v_cvt_pk_fp8_f32 v110, v102, v103 op_sel:[0,0,1]
	v_cvt_pk_fp8_f32 v111, v94, v95 op_sel:[0,0,1]
	v_or_b32_e32 v116, 16, v158
	v_mad_i64_i32 v[92:93], s[20:21], v116, s54, v[156:157]
	v_lshl_add_u64 v[92:93], v[92:93], 0, v[154:155]
	global_store_dwordx4 v[92:93], v[108:111], off nt
	v_mov_b32_e32 v92, 0
	v_mov_b32_e32 v93, 0
	v_mov_b32_e32 v94, 0
	v_mov_b32_e32 v95, 0
	v_cvt_pk_fp8_f32 v92, v96, v97
	v_cvt_pk_fp8_f32 v93, v88, v89
	v_cvt_pk_fp8_f32 v94, v84, v85
	v_cvt_pk_fp8_f32 v95, v76, v77
	v_cvt_pk_fp8_f32 v92, v98, v99 op_sel:[0,0,1]
	v_cvt_pk_fp8_f32 v93, v90, v91 op_sel:[0,0,1]
	v_cvt_pk_fp8_f32 v94, v86, v87 op_sel:[0,0,1]
	v_cvt_pk_fp8_f32 v95, v78, v79 op_sel:[0,0,1]
	v_or_b32_e32 v100, 32, v158
	v_mad_i64_i32 v[76:77], s[20:21], v100, s54, v[156:157]
	v_lshl_add_u64 v[76:77], v[76:77], 0, v[154:155]
	global_store_dwordx4 v[76:77], v[92:95], off nt
	v_mov_b32_e32 v76, 0
	v_mov_b32_e32 v77, 0
	v_mov_b32_e32 v78, 0
	v_mov_b32_e32 v79, 0
	v_cvt_pk_fp8_f32 v76, v80, v81
	v_cvt_pk_fp8_f32 v77, v72, v73
	v_cvt_pk_fp8_f32 v78, v68, v69
	v_cvt_pk_fp8_f32 v79, v64, v65
	v_cvt_pk_fp8_f32 v76, v82, v83 op_sel:[0,0,1]
	v_cvt_pk_fp8_f32 v77, v74, v75 op_sel:[0,0,1]
	v_cvt_pk_fp8_f32 v78, v70, v71 op_sel:[0,0,1]
	v_cvt_pk_fp8_f32 v79, v66, v67 op_sel:[0,0,1]
	v_or_b32_e32 v84, 48, v158
	v_mad_i64_i32 v[64:65], s[20:21], v84, s54, v[156:157]
	v_lshl_add_u64 v[64:65], v[64:65], 0, v[154:155]
	global_store_dwordx4 v[64:65], v[76:79], off nt
	v_mov_b32_e32 v64, 0
	v_mov_b32_e32 v65, 0
	v_mov_b32_e32 v66, 0
	v_mov_b32_e32 v67, 0
	v_cvt_pk_fp8_f32 v64, v60, v61
	v_cvt_pk_fp8_f32 v65, v56, v57
	v_cvt_pk_fp8_f32 v66, v52, v53
	v_cvt_pk_fp8_f32 v67, v44, v45
	v_cvt_pk_fp8_f32 v64, v62, v63 op_sel:[0,0,1]
	v_cvt_pk_fp8_f32 v65, v58, v59 op_sel:[0,0,1]
	v_cvt_pk_fp8_f32 v66, v54, v55 op_sel:[0,0,1]
	v_cvt_pk_fp8_f32 v67, v46, v47 op_sel:[0,0,1]
	v_add_u32_e32 v68, 0x80, v158
	v_mad_i64_i32 v[44:45], s[20:21], v68, s54, v[156:157]
	v_lshl_add_u64 v[44:45], v[44:45], 0, v[154:155]
	global_store_dwordx4 v[44:45], v[64:67], off nt
	v_mov_b32_e32 v44, 0
	v_mov_b32_e32 v45, 0
	v_mov_b32_e32 v46, 0
	v_mov_b32_e32 v47, 0
	v_cvt_pk_fp8_f32 v44, v48, v49
	v_cvt_pk_fp8_f32 v45, v40, v41
	v_cvt_pk_fp8_f32 v46, v36, v37
	v_cvt_pk_fp8_f32 v47, v28, v29
	v_cvt_pk_fp8_f32 v44, v50, v51 op_sel:[0,0,1]
	v_cvt_pk_fp8_f32 v45, v42, v43 op_sel:[0,0,1]
	v_cvt_pk_fp8_f32 v46, v38, v39 op_sel:[0,0,1]
	v_cvt_pk_fp8_f32 v47, v30, v31 op_sel:[0,0,1]
	v_add_u32_e32 v52, 0x90, v158
	v_mad_i64_i32 v[28:29], s[20:21], v52, s54, v[156:157]
	v_lshl_add_u64 v[28:29], v[28:29], 0, v[154:155]
	global_store_dwordx4 v[28:29], v[44:47], off nt
	v_mov_b32_e32 v28, 0
	v_mov_b32_e32 v29, 0
	v_mov_b32_e32 v30, 0
	v_mov_b32_e32 v31, 0
	v_cvt_pk_fp8_f32 v28, v32, v33
	v_cvt_pk_fp8_f32 v29, v24, v25
	v_cvt_pk_fp8_f32 v30, v20, v21
	v_cvt_pk_fp8_f32 v31, v12, v13
	v_cvt_pk_fp8_f32 v28, v34, v35 op_sel:[0,0,1]
	v_cvt_pk_fp8_f32 v29, v26, v27 op_sel:[0,0,1]
	v_cvt_pk_fp8_f32 v30, v22, v23 op_sel:[0,0,1]
	v_cvt_pk_fp8_f32 v31, v14, v15 op_sel:[0,0,1]
	v_add_u32_e32 v36, 0xa0, v158
	v_mad_i64_i32 v[12:13], s[20:21], v36, s54, v[156:157]
	v_lshl_add_u64 v[12:13], v[12:13], 0, v[154:155]
	global_store_dwordx4 v[12:13], v[28:31], off nt
	v_mov_b32_e32 v12, 0
	v_mov_b32_e32 v13, 0
	v_mov_b32_e32 v14, 0
	v_mov_b32_e32 v15, 0
	v_cvt_pk_fp8_f32 v12, v16, v17
	v_cvt_pk_fp8_f32 v13, v8, v9
	v_cvt_pk_fp8_f32 v14, v4, v5
	v_cvt_pk_fp8_f32 v15, v0, v1
	v_cvt_pk_fp8_f32 v12, v18, v19 op_sel:[0,0,1]
	v_cvt_pk_fp8_f32 v13, v10, v11 op_sel:[0,0,1]
	v_cvt_pk_fp8_f32 v14, v6, v7 op_sel:[0,0,1]
	v_cvt_pk_fp8_f32 v15, v2, v3 op_sel:[0,0,1]
	v_add_u32_e32 v20, 0xb0, v158
	v_mad_i64_i32 v[0:1], s[20:21], v20, s54, v[156:157]
	v_lshl_add_u64 v[0:1], v[0:1], 0, v[154:155]
	s_andn2_b64 vcc, exec, s[2:3]
	s_mov_b64 s[2:3], -1
	global_store_dwordx4 v[0:1], v[12:15], off nt
	s_cbranch_vccnz .LBB0_1401
	s_andn2_b64 vcc, exec, s[6:7]
	s_cbranch_vccnz .LBB0_1400
	s_barrier
	s_branch .LBB0_1400

.LBB0_1432:
	v_mov_b32_e32 v149, 0
	v_lshl_add_u32 v150, s68, 8, v140
	v_cvt_pk_fp8_f32 v149, v112, v113
	v_ashrrev_i32_e32 v151, 31, v150
	v_lshl_or_b32 v152, s69, 8, v142
	v_lshlrev_b64 v[112:113], 11, v[150:151]
	v_ashrrev_i32_e32 v153, 31, v152
	v_mov_b32_e32 v148, 0
	v_lshl_add_u64 v[112:113], s[8:9], 0, v[112:113]
	v_cvt_pk_fp8_f32 v148, v116, v117
	v_cvt_pk_fp8_f32 v149, v114, v115 op_sel:[0,0,1]
	v_lshl_add_u64 v[116:117], v[112:113], 0, v[152:153]
	v_mov_b32_e32 v112, 0
	v_mov_b32_e32 v113, 0
	v_mov_b32_e32 v114, 0
	v_mov_b32_e32 v115, 0
	v_cvt_pk_fp8_f32 v112, v108, v109
	v_cvt_pk_fp8_f32 v113, v104, v105
	v_cvt_pk_fp8_f32 v114, v100, v101
	v_cvt_pk_fp8_f32 v115, v96, v97
	v_cvt_pk_fp8_f32 v148, v118, v119 op_sel:[0,0,1]
	v_or_b32_e32 v118, 16, v150
	v_ashrrev_i32_e32 v119, 31, v118
	v_cvt_pk_fp8_f32 v112, v110, v111 op_sel:[0,0,1]
	v_cvt_pk_fp8_f32 v113, v106, v107 op_sel:[0,0,1]
	v_cvt_pk_fp8_f32 v114, v102, v103 op_sel:[0,0,1]
	v_cvt_pk_fp8_f32 v115, v98, v99 op_sel:[0,0,1]
	v_lshlrev_b64 v[96:97], 11, v[118:119]
	v_lshl_add_u64 v[96:97], s[8:9], 0, v[96:97]
	v_lshl_add_u64 v[96:97], v[96:97], 0, v[152:153]
	global_store_dwordx4 v[96:97], v[112:115], off nt
	v_mov_b32_e32 v96, 0
	v_mov_b32_e32 v97, 0
	v_mov_b32_e32 v98, 0
	v_mov_b32_e32 v99, 0
	v_cvt_pk_fp8_f32 v96, v92, v93
	v_cvt_pk_fp8_f32 v97, v88, v89
	v_cvt_pk_fp8_f32 v98, v84, v85
	v_cvt_pk_fp8_f32 v99, v80, v81
	v_or_b32_e32 v100, 32, v150
	v_ashrrev_i32_e32 v101, 31, v100
	v_cvt_pk_fp8_f32 v96, v94, v95 op_sel:[0,0,1]
	v_cvt_pk_fp8_f32 v97, v90, v91 op_sel:[0,0,1]
	v_cvt_pk_fp8_f32 v98, v86, v87 op_sel:[0,0,1]
	v_cvt_pk_fp8_f32 v99, v82, v83 op_sel:[0,0,1]
	v_lshlrev_b64 v[80:81], 11, v[100:101]
	v_lshl_add_u64 v[80:81], s[8:9], 0, v[80:81]
	v_lshl_add_u64 v[80:81], v[80:81], 0, v[152:153]
	global_store_dwordx4 v[80:81], v[96:99], off nt
	v_mov_b32_e32 v80, 0
	v_mov_b32_e32 v81, 0
	v_mov_b32_e32 v82, 0
	v_mov_b32_e32 v83, 0
	v_cvt_pk_fp8_f32 v80, v76, v77
	v_cvt_pk_fp8_f32 v81, v72, v73
	v_cvt_pk_fp8_f32 v82, v68, v69
	v_cvt_pk_fp8_f32 v83, v64, v65
	v_or_b32_e32 v84, 48, v150
	v_ashrrev_i32_e32 v85, 31, v84
	v_cvt_pk_fp8_f32 v80, v78, v79 op_sel:[0,0,1]
	v_cvt_pk_fp8_f32 v81, v74, v75 op_sel:[0,0,1]
	v_cvt_pk_fp8_f32 v82, v70, v71 op_sel:[0,0,1]
	v_cvt_pk_fp8_f32 v83, v66, v67 op_sel:[0,0,1]
	v_lshlrev_b64 v[64:65], 11, v[84:85]
	v_lshl_add_u64 v[64:65], s[8:9], 0, v[64:65]
	v_lshl_add_u64 v[64:65], v[64:65], 0, v[152:153]
	global_store_dwordx4 v[64:65], v[80:83], off nt
	v_mov_b32_e32 v64, 0
	v_mov_b32_e32 v65, 0
	v_mov_b32_e32 v66, 0
	v_mov_b32_e32 v67, 0
	v_cvt_pk_fp8_f32 v64, v60, v61
	v_cvt_pk_fp8_f32 v65, v56, v57
	v_cvt_pk_fp8_f32 v66, v52, v53
	v_cvt_pk_fp8_f32 v67, v44, v45
	v_cvt_pk_fp8_f32 v64, v62, v63 op_sel:[0,0,1]
	v_cvt_pk_fp8_f32 v65, v58, v59 op_sel:[0,0,1]
	v_cvt_pk_fp8_f32 v66, v54, v55 op_sel:[0,0,1]
	v_cvt_pk_fp8_f32 v67, v46, v47 op_sel:[0,0,1]
	v_add_co_u32_e32 v44, vcc, s64, v116
	v_mov_b32_e32 v46, 0
	s_nop 0
	v_addc_co_u32_e32 v45, vcc, 0, v117, vcc
	global_store_dwordx4 v[44:45], v[64:67], off nt
	v_mov_b32_e32 v44, 0
	v_mov_b32_e32 v45, 0
	v_mov_b32_e32 v47, 0
	v_cvt_pk_fp8_f32 v44, v48, v49
	v_cvt_pk_fp8_f32 v45, v40, v41
	v_cvt_pk_fp8_f32 v46, v36, v37
	v_cvt_pk_fp8_f32 v47, v28, v29
	v_cvt_pk_fp8_f32 v44, v50, v51 op_sel:[0,0,1]
	v_cvt_pk_fp8_f32 v45, v42, v43 op_sel:[0,0,1]
	v_cvt_pk_fp8_f32 v46, v38, v39 op_sel:[0,0,1]
	v_cvt_pk_fp8_f32 v47, v30, v31 op_sel:[0,0,1]
	v_add_co_u32_e32 v28, vcc, s65, v116
	v_mov_b32_e32 v30, 0
	s_nop 0
	v_addc_co_u32_e32 v29, vcc, 0, v117, vcc
	global_store_dwordx4 v[28:29], v[44:47], off nt
	v_mov_b32_e32 v28, 0
	v_mov_b32_e32 v29, 0
	v_mov_b32_e32 v31, 0
	v_cvt_pk_fp8_f32 v28, v32, v33
	v_cvt_pk_fp8_f32 v29, v24, v25
	v_cvt_pk_fp8_f32 v30, v20, v21
	v_cvt_pk_fp8_f32 v31, v12, v13
	v_cvt_pk_fp8_f32 v28, v34, v35 op_sel:[0,0,1]
	v_cvt_pk_fp8_f32 v29, v26, v27 op_sel:[0,0,1]
	v_cvt_pk_fp8_f32 v30, v22, v23 op_sel:[0,0,1]
	v_cvt_pk_fp8_f32 v31, v14, v15 op_sel:[0,0,1]
	v_add_co_u32_e32 v12, vcc, s66, v116
	v_mov_b32_e32 v146, 0
	s_nop 0
	v_addc_co_u32_e32 v13, vcc, 0, v117, vcc
	v_mov_b32_e32 v147, 0
	global_store_dwordx4 v[12:13], v[28:31], off nt
	v_mov_b32_e32 v12, 0
	v_mov_b32_e32 v13, 0
	v_mov_b32_e32 v14, 0
	v_mov_b32_e32 v15, 0
	v_cvt_pk_fp8_f32 v146, v124, v125
	v_cvt_pk_fp8_f32 v147, v120, v121
	v_cvt_pk_fp8_f32 v12, v16, v17
	v_cvt_pk_fp8_f32 v13, v8, v9
	v_cvt_pk_fp8_f32 v14, v4, v5
	v_cvt_pk_fp8_f32 v15, v0, v1
	v_cvt_pk_fp8_f32 v146, v126, v127 op_sel:[0,0,1]
	v_cvt_pk_fp8_f32 v147, v122, v123 op_sel:[0,0,1]
	v_cvt_pk_fp8_f32 v12, v18, v19 op_sel:[0,0,1]
	v_cvt_pk_fp8_f32 v13, v10, v11 op_sel:[0,0,1]
	v_cvt_pk_fp8_f32 v14, v6, v7 op_sel:[0,0,1]
	v_cvt_pk_fp8_f32 v15, v2, v3 op_sel:[0,0,1]
	v_add_co_u32_e32 v0, vcc, 0x58000, v116
	global_store_dwordx4 v[116:117], v[146:149], off nt
	s_nop 0
	v_addc_co_u32_e32 v1, vcc, 0, v117, vcc
	s_andn2_b64 vcc, exec, s[2:3]
	s_mov_b64 s[2:3], -1
	global_store_dwordx4 v[0:1], v[12:15], off nt
	s_cbranch_vccnz .LBB0_1421
	s_andn2_b64 vcc, exec, s[6:7]
	s_cbranch_vccnz .LBB0_1420
	s_barrier
	s_branch .LBB0_1420

.LBB0_1511:
	v_and_b32_e32 v50, 0xffff0000, v88
	v_lshlrev_b32_e32 v49, 16, v88
	v_mul_f32_e32 v50, v50, v50
	v_fmac_f32_e32 v50, v49, v49
	v_lshlrev_b32_e32 v49, 16, v89
	v_fmac_f32_e32 v50, v49, v49
	v_and_b32_e32 v49, 0xffff0000, v89
	v_fmac_f32_e32 v50, v49, v49
	v_lshlrev_b32_e32 v49, 16, v90
	v_fmac_f32_e32 v50, v49, v49
	v_and_b32_e32 v49, 0xffff0000, v90
	v_fmac_f32_e32 v50, v49, v49
	v_lshlrev_b32_e32 v49, 16, v91
	v_fmac_f32_e32 v50, v49, v49
	v_and_b32_e32 v49, 0xffff0000, v91
	v_and_b32_e32 v51, 0xffff0000, v84
	v_fmac_f32_e32 v50, v49, v49
	v_lshlrev_b32_e32 v49, 16, v84
	v_mul_f32_e32 v51, v51, v51
	v_fmac_f32_e32 v51, v49, v49
	v_lshlrev_b32_e32 v49, 16, v85
	v_fmac_f32_e32 v51, v49, v49
	v_and_b32_e32 v49, 0xffff0000, v85
	v_fmac_f32_e32 v51, v49, v49
	v_lshlrev_b32_e32 v49, 16, v86
	v_fmac_f32_e32 v51, v49, v49
	v_and_b32_e32 v49, 0xffff0000, v86
	v_fmac_f32_e32 v51, v49, v49
	v_lshlrev_b32_e32 v49, 16, v87
	v_fmac_f32_e32 v51, v49, v49
	v_and_b32_e32 v49, 0xffff0000, v87
	v_fmac_f32_e32 v51, v49, v49
	v_cndmask_b32_e64 v49, 0, v50, s[4:5]
	v_cndmask_b32_e64 v50, 0, v50, s[6:7]
	v_cndmask_b32_e64 v51, 0, v51, s[8:9]
	v_add_f32_e32 v50, v51, v50
	ds_bpermute_b32 v51, v126, v50
	ds_bpermute_b32 v84, v126, v49
	v_cvt_f32_i32_e32 v95, v145
	v_cvt_pk_f32_fp8_sdwa v[86:87], v80 src0_sel:WORD_1
	v_cvt_pk_f32_fp8_e32 v[88:89], v81
	s_waitcnt lgkmcnt(1)
	v_add_f32_e32 v50, v50, v51
	ds_bpermute_b32 v51, v127, v50
	s_waitcnt lgkmcnt(1)
	v_add_f32_e32 v49, v49, v84
	ds_bpermute_b32 v84, v127, v49
	v_pk_mul_f32 v[152:153], v[86:87], v[86:87]
	v_cvt_pk_f32_fp8_e32 v[90:91], v82
	s_waitcnt lgkmcnt(1)
	v_add_f32_e32 v50, v50, v51
	ds_bpermute_b32 v51, v128, v50
	s_waitcnt lgkmcnt(1)
	v_add_f32_e32 v49, v49, v84
	ds_bpermute_b32 v84, v128, v49
	v_pk_mul_f32 v[154:155], v[88:89], v[88:89]
	v_cvt_pk_f32_fp8_sdwa v[116:117], v82 src0_sel:WORD_1
	s_waitcnt lgkmcnt(1)
	v_add_f32_e32 v50, v50, v51
	ds_bpermute_b32 v51, v129, v50
	s_waitcnt lgkmcnt(1)
	v_add_f32_e32 v49, v49, v84
	ds_bpermute_b32 v84, v129, v49
	v_cvt_pk_f32_fp8_e32 v[118:119], v83
	v_pk_mul_f32 v[158:159], v[90:91], v[90:91]
	s_waitcnt lgkmcnt(1)
	v_add_f32_e32 v50, v50, v51
	ds_bpermute_b32 v51, v130, v50
	s_waitcnt lgkmcnt(1)
	v_add_f32_e32 v49, v49, v84
	ds_bpermute_b32 v84, v130, v49
	v_cvt_pk_f32_fp8_sdwa v[82:83], v83 src0_sel:WORD_1
	v_pk_mul_f32 v[160:161], v[116:117], v[116:117]
	s_waitcnt lgkmcnt(1)
	v_add_f32_e32 v50, v50, v51
	ds_bpermute_b32 v51, v131, v50
	s_waitcnt lgkmcnt(1)
	v_add_f32_e32 v49, v49, v84
	ds_bpermute_b32 v84, v131, v49
	v_cvt_pk_f32_fp8_e32 v[146:147], v144
	v_pk_mul_f32 v[162:163], v[118:119], v[118:119]
	s_waitcnt lgkmcnt(1)
	v_add_f32_e32 v50, v50, v51
	v_fmamk_f32 v174, v50, 0x3b800000, v135
	v_mul_f32_e32 v50, v120, v95
	v_cvt_f64_f32_e32 v[50:51], v50
	s_waitcnt lgkmcnt(0)
	v_add_f32_e32 v49, v49, v84
	v_mul_f64 v[84:85], v[50:51], s[22:23]
	v_floor_f64_e32 v[84:85], v[84:85]
	v_fma_f64 v[50:51], v[50:51], s[22:23], -v[84:85]
	v_cvt_f32_f64_e32 v50, v[50:51]
	v_cos_f32_e32 v175, v50
	v_sin_f32_e32 v176, v50
	v_mul_f32_e32 v50, v121, v95
	v_cvt_f64_f32_e32 v[50:51], v50
	v_mul_f64 v[84:85], v[50:51], s[22:23]
	v_floor_f64_e32 v[84:85], v[84:85]
	v_fma_f64 v[50:51], v[50:51], s[22:23], -v[84:85]
	v_cvt_f32_f64_e32 v50, v[50:51]
	v_cos_f32_e32 v177, v50
	v_sin_f32_e32 v178, v50
	v_mul_f32_e32 v50, v122, v95
	v_cvt_f64_f32_e32 v[50:51], v50
	v_mul_f64 v[84:85], v[50:51], s[22:23]
	v_floor_f64_e32 v[84:85], v[84:85]
	v_fma_f64 v[50:51], v[50:51], s[22:23], -v[84:85]
	v_cvt_pk_f32_fp8_e32 v[84:85], v80
	v_cvt_f32_f64_e32 v50, v[50:51]
	v_cos_f32_e32 v179, v50
	v_sin_f32_e32 v180, v50
	v_pk_mul_f32 v[50:51], v[84:85], v[84:85]
	v_cvt_pk_f32_fp8_sdwa v[80:81], v81 src0_sel:WORD_1
	v_add_f32_e32 v50, v50, v51
	v_add_f32_e32 v50, v50, v152
	v_add_f32_e32 v50, v153, v50
	v_add_f32_e32 v50, v154, v50
	v_pk_mul_f32 v[156:157], v[80:81], v[80:81]
	v_add_f32_e32 v50, v155, v50
	v_add_f32_e32 v50, v156, v50
	v_add_f32_e32 v50, v157, v50
	v_add_f32_e32 v50, v158, v50
	v_add_f32_e32 v50, v159, v50
	v_add_f32_e32 v50, v160, v50
	v_add_f32_e32 v50, v161, v50
	v_add_f32_e32 v50, v162, v50
	v_cvt_pk_f32_fp8_sdwa v[144:145], v144 src0_sel:WORD_1
	v_pk_mul_f32 v[164:165], v[82:83], v[82:83]
	v_add_f32_e32 v50, v163, v50
	v_add_f32_e32 v50, v164, v50
	v_cvt_pk_f32_fp8_e32 v[148:149], v143
	v_pk_mul_f32 v[166:167], v[146:147], v[146:147]
	v_add_f32_e32 v50, v165, v50
	v_add_f32_e32 v50, v166, v50
	v_cvt_pk_f32_fp8_sdwa v[150:151], v143 src0_sel:WORD_1
	v_pk_mul_f32 v[168:169], v[144:145], v[144:145]
	v_add_f32_e32 v50, v167, v50
	v_add_f32_e32 v50, v168, v50
	v_pk_mul_f32 v[170:171], v[148:149], v[148:149]
	v_add_f32_e32 v50, v169, v50
	v_add_f32_e32 v50, v170, v50
	v_pk_mul_f32 v[172:173], v[150:151], v[150:151]
	v_add_f32_e32 v50, v171, v50
	v_add_f32_e32 v50, v172, v50
	v_add_f32_e32 v143, v173, v50
	ds_bpermute_b32 v154, v126, v143
	v_mul_f32_e32 v50, v125, v95
	v_fmamk_f32 v49, v49, 0x3b2aaaab, v135
	v_rsq_f32_e32 v49, v49
	v_cvt_f64_f32_e32 v[50:51], v50
	s_waitcnt lgkmcnt(0)
	v_add_f32_e32 v95, v143, v154
	ds_bpermute_b32 v143, v127, v95
	v_mul_f64 v[152:153], v[50:51], s[22:23]
	s_lshl_b32 s16, s48, 6
	v_floor_f64_e32 v[152:153], v[152:153]
	s_add_i32 s16, s16, s49
	s_waitcnt lgkmcnt(0)
	v_add_f32_e32 v95, v95, v143
	ds_bpermute_b32 v143, v128, v95
	v_fma_f64 v[50:51], v[50:51], s[22:23], -v[152:153]
	s_and_b32 s24, s16, 0x3fff
	v_cvt_f32_f64_e32 v50, v[50:51]
	s_ashr_i32 s16, s16, 11
	s_waitcnt lgkmcnt(0)
	v_add_f32_e32 v95, v95, v143
	v_mul_f32_e32 v143, v49, v49
	v_mul_f32_e32 v95, v143, v95
	v_fmamk_f32 v95, v95, 0x3baaaaab, v135
	v_rsq_f32_e32 v95, v95
	v_cos_f32_e32 v152, v50
	v_sin_f32_e32 v153, v50
	v_and_or_b32 v50, s16, -8, v123
	v_mul_f32_e32 v49, v49, v95
	v_mul_f32_e32 v49, 0x3f553b94, v49
	v_mul_f32_e32 v95, v12, v49
	v_mul_f32_e32 v84, v84, v95
	v_mul_f32_e32 v95, v13, v49
	v_mul_f32_e32 v85, v85, v95
	v_mul_f32_e32 v95, v14, v49
	v_mul_f32_e32 v86, v86, v95
	v_mul_f32_e32 v95, v15, v49
	v_mul_f32_e32 v87, v87, v95
	v_mul_f32_e32 v95, v8, v49
	v_mul_f32_e32 v88, v88, v95
	v_mul_f32_e32 v95, v9, v49
	v_mul_f32_e32 v89, v89, v95
	v_mul_f32_e32 v95, v10, v49
	v_mul_f32_e32 v95, v80, v95
	v_mul_f32_e32 v80, v11, v49
	v_mul_f32_e32 v154, v81, v80
	v_mul_f32_e32 v80, v4, v49
	v_mul_f32_e32 v90, v90, v80
	v_mul_f32_e32 v80, v5, v49
	v_mul_f32_e32 v91, v91, v80
	v_mul_f32_e32 v80, v6, v49
	v_mul_f32_e32 v116, v116, v80
	v_mul_f32_e32 v80, v7, v49
	v_mul_f32_e32 v117, v117, v80
	v_mul_f32_e32 v80, v0, v49
	v_mul_f32_e32 v118, v118, v80
	v_mul_f32_e32 v80, v1, v49
	v_mul_f32_e32 v119, v119, v80
	v_mul_f32_e32 v80, v2, v49
	v_mul_f32_e32 v155, v82, v80
	v_mul_f32_e32 v80, v3, v49
	v_mul_f32_e32 v156, v83, v80
	v_mul_f32_e32 v80, v32, v49
	v_mul_f32_e32 v146, v146, v80
	v_mul_f32_e32 v80, v33, v49
	v_mul_f32_e32 v147, v147, v80
	v_mul_f32_e32 v80, v34, v49
	v_mul_f32_e32 v144, v144, v80
	v_mul_f32_e32 v80, v35, v49
	v_mul_f32_e32 v145, v145, v80
	v_mul_f32_e32 v80, v36, v49
	v_mul_f32_e32 v148, v148, v80
	v_mul_f32_e32 v80, v37, v49
	v_mul_f32_e32 v149, v149, v80
	v_mul_f32_e32 v80, v38, v49
	v_mul_f32_e32 v150, v150, v80
	v_mov_b32_e32 v80, v48
	v_mov_b32_e32 v81, v48
	v_mov_b32_e32 v82, v48
	v_mov_b32_e32 v83, v48
	v_cvt_pk_fp8_f32 v80, v84, v85
	v_cvt_pk_fp8_f32 v81, v88, v89
	v_cvt_pk_fp8_f32 v82, v90, v91
	v_cvt_pk_fp8_f32 v83, v118, v119
	v_ashrrev_i32_e32 v51, 31, v50
	v_lshlrev_b64 v[50:51], 14, v[50:51]
	v_or_b32_e32 v50, s24, v50
	v_cvt_pk_fp8_f32 v80, v86, v87 op_sel:[0,0,1]
	v_cvt_pk_fp8_f32 v81, v95, v154 op_sel:[0,0,1]
	v_cvt_pk_fp8_f32 v82, v116, v117 op_sel:[0,0,1]
	v_cvt_pk_fp8_f32 v83, v155, v156 op_sel:[0,0,1]
	v_mov_b64_e32 v[84:85], s[18:19]
	v_mad_u64_u32 v[84:85], s[24:25], v50, s15, v[84:85]
	v_mad_i32_i24 v85, v51, s15, v85
	v_lshl_add_u64 v[86:87], v[84:85], 0, v[92:93]
	global_store_dwordx4 v[86:87], v[80:83], off nt
	v_mul_f32_e32 v86, v180, v150
	v_fma_f32 v95, v179, v144, -v86
	v_mul_f32_e32 v80, v176, v148
	v_mul_f32_e32 v81, v176, v146
	v_mul_f32_e32 v82, v178, v149
	v_mul_f32_e32 v83, v178, v147
	v_fma_f32 v80, v175, v146, -v80
	v_fmac_f32_e32 v81, v175, v148
	v_fma_f32 v82, v177, v147, -v82
	v_fmac_f32_e32 v83, v177, v149
	v_mul_f32_e32 v118, v180, v144
	v_mov_b32_e32 v144, v48
	v_mov_b32_e32 v146, v48
	v_rsq_f32_e32 v143, v174
	v_cvt_pk_fp8_f32 v144, v80, v82
	v_cvt_pk_fp8_f32 v146, v81, v83
	v_cvt_pk_f32_fp8_e32 v[80:81], v76
	v_mul_f32_e32 v49, v39, v49
	v_mul_f32_e32 v49, v151, v49
	v_cvt_pk_f32_fp8_sdwa v[82:83], v76 src0_sel:WORD_1
	v_mul_f32_e32 v86, v153, v49
	v_fma_f32 v119, v152, v145, -v86
	v_cvt_pk_f32_fp8_e32 v[86:87], v77
	v_mul_f32_e32 v154, v143, v81
	v_mul_f32_e32 v151, v143, v80
	v_mul_f32_e32 v80, v154, v154
	v_cvt_pk_f32_fp8_sdwa v[76:77], v77 src0_sel:WORD_1
	v_mul_f32_e32 v155, v143, v82
	v_fmac_f32_e32 v80, v151, v151
	v_mul_f32_e32 v156, v143, v83
	v_fmac_f32_e32 v80, v155, v155
	v_cvt_pk_f32_fp8_e32 v[88:89], v78
	v_mul_f32_e32 v157, v143, v86
	v_fmac_f32_e32 v80, v156, v156
	v_mul_f32_e32 v158, v143, v87
	v_fmac_f32_e32 v80, v157, v157
	v_cvt_pk_f32_fp8_sdwa v[90:91], v78 src0_sel:WORD_1
	v_mul_f32_e32 v159, v143, v76
	v_fmac_f32_e32 v80, v158, v158
	v_mul_f32_e32 v160, v143, v77
	v_fmac_f32_e32 v80, v159, v159
	v_cvt_pk_f32_fp8_e32 v[116:117], v79
	v_mul_f32_e32 v161, v143, v88
	v_fmac_f32_e32 v80, v160, v160
	v_mul_f32_e32 v162, v143, v89
	v_fmac_f32_e32 v80, v161, v161
	v_cvt_pk_f32_fp8_sdwa v[78:79], v79 src0_sel:WORD_1
	v_mul_f32_e32 v163, v143, v90
	v_fmac_f32_e32 v80, v162, v162
	v_mul_f32_e32 v164, v143, v91
	v_fmac_f32_e32 v80, v163, v163
	v_mul_f32_e32 v116, v143, v116
	v_fmac_f32_e32 v80, v164, v164
	v_mul_f32_e32 v117, v143, v117
	v_fmac_f32_e32 v80, v116, v116
	v_mul_f32_e32 v165, v143, v78
	v_fmac_f32_e32 v80, v117, v117
	v_mul_f32_e32 v166, v143, v79
	v_fmac_f32_e32 v80, v165, v165
	v_lshlrev_b32_e32 v147, 16, v114
	v_fmac_f32_e32 v80, v166, v166
	v_and_b32_e32 v114, 0xffff0000, v114
	v_fmac_f32_e32 v80, v147, v147
	v_lshlrev_b32_e32 v148, 16, v115
	v_fmac_f32_e32 v80, v114, v114
	v_and_b32_e32 v115, 0xffff0000, v115
	v_fmac_f32_e32 v80, v148, v148
	v_lshlrev_b32_e32 v149, 16, v112
	v_fmac_f32_e32 v80, v115, v115
	v_fmac_f32_e32 v118, v179, v150
	v_and_b32_e32 v150, 0xffff0000, v112
	v_fmac_f32_e32 v80, v149, v149
	v_and_b32_e32 v76, 0xffff0000, v113
	v_lshlrev_b32_e32 v77, 16, v113
	v_fmac_f32_e32 v80, v150, v150
	v_pk_mul_f32 v[78:79], v[76:77], v[76:77]
	v_cvt_pk_fp8_f32 v144, v95, v119 op_sel:[0,0,1]
	v_add_f32_e32 v79, v79, v80
	v_add_f32_e32 v78, v78, v79
	ds_bpermute_b32 v79, v126, v78
	v_mul_f32_e32 v80, v153, v145
	v_fmac_f32_e32 v80, v152, v49
	v_cvt_pk_fp8_f32 v146, v118, v80 op_sel:[0,0,1]
	v_cvt_pk_f32_fp8_e32 v[82:83], v73
	s_waitcnt lgkmcnt(0)
	v_add_f32_e32 v49, v78, v79
	ds_bpermute_b32 v80, v127, v49
	v_lshl_add_u64 v[78:79], v[84:85], 0, v[96:97]
	global_store_dword v[78:79], v144, off offset:128
	global_store_dword v[78:79], v146, off offset:160
	v_cvt_pk_f32_fp8_e32 v[78:79], v72
	v_cvt_pk_f32_fp8_sdwa v[84:85], v73 src0_sel:WORD_1
	s_waitcnt lgkmcnt(0)
	v_add_f32_e32 v49, v49, v80
	ds_bpermute_b32 v88, v128, v49
	v_cvt_pk_f32_fp8_sdwa v[80:81], v72 src0_sel:WORD_1
	v_cvt_pk_f32_fp8_e32 v[86:87], v74
	v_cvt_pk_f32_fp8_e32 v[90:91], v75
	v_cvt_pk_f32_fp8_sdwa v[112:113], v75 src0_sel:WORD_1
	s_waitcnt lgkmcnt(0)
	v_add_f32_e32 v49, v49, v88
	v_fmamk_f32 v49, v49, 0x3baaaaab, v135
	v_rsq_f32_e32 v49, v49
	v_cvt_pk_f32_fp8_sdwa v[88:89], v74 src0_sel:WORD_1
	s_ashr_i32 s16, s48, 5
	s_add_i32 s14, s14, s50
	v_mul_f32_e32 v72, v28, v49
	v_mul_f32_e32 v73, v151, v72
	v_mul_f32_e32 v72, v29, v49
	v_mul_f32_e32 v74, v154, v72
	v_mul_f32_e32 v72, v30, v49
	v_mul_f32_e32 v95, v155, v72
	v_mul_f32_e32 v72, v31, v49
	v_mul_f32_e32 v118, v156, v72
	v_mul_f32_e32 v72, v24, v49
	v_mul_f32_e32 v75, v157, v72
	v_mul_f32_e32 v72, v25, v49
	v_mul_f32_e32 v119, v158, v72
	v_mul_f32_e32 v72, v26, v49
	v_mul_f32_e32 v144, v159, v72
	v_mul_f32_e32 v72, v27, v49
	v_mul_f32_e32 v145, v160, v72
	v_mul_f32_e32 v72, v20, v49
	v_mul_f32_e32 v146, v161, v72
	v_mul_f32_e32 v72, v21, v49
	v_mul_f32_e32 v151, v162, v72
	v_mul_f32_e32 v72, v22, v49
	v_mul_f32_e32 v154, v163, v72
	v_mul_f32_e32 v72, v23, v49
	v_mul_f32_e32 v155, v164, v72
	v_mul_f32_e32 v72, v16, v49
	v_mul_f32_e32 v116, v116, v72
	v_mul_f32_e32 v72, v17, v49
	v_mul_f32_e32 v117, v117, v72
	v_mul_f32_e32 v72, v18, v49
	v_mul_f32_e32 v156, v165, v72
	v_mul_f32_e32 v72, v19, v49
	v_mul_f32_e32 v157, v166, v72
	v_mul_f32_e32 v72, v40, v49
	v_mul_f32_e32 v147, v72, v147
	v_mul_f32_e32 v72, v41, v49
	v_mul_f32_e32 v114, v72, v114
	v_mul_f32_e32 v72, v42, v49
	v_mul_f32_e32 v148, v72, v148
	v_mul_f32_e32 v72, v43, v49
	v_mul_f32_e32 v115, v72, v115
	v_mul_f32_e32 v72, v44, v49
	v_mul_f32_e32 v149, v72, v149
	v_mul_f32_e32 v72, v45, v49
	v_mul_f32_e32 v150, v72, v150
	v_mul_f32_e32 v72, v46, v49
	v_mul_f32_e32 v158, v72, v77
	v_mov_b32_e32 v72, v48
	v_cvt_pk_fp8_f32 v72, v73, v74
	v_mov_b32_e32 v73, v48
	v_cvt_pk_fp8_f32 v73, v75, v119
	v_mov_b32_e32 v74, v48
	v_mov_b32_e32 v75, v48
	v_cvt_pk_fp8_f32 v74, v146, v151
	v_cvt_pk_fp8_f32 v75, v116, v117
	v_mul_f32_e32 v49, v47, v49
	v_mul_f32_e32 v49, v49, v76
	v_cvt_pk_fp8_f32 v72, v95, v118 op_sel:[0,0,1]
	v_cvt_pk_fp8_f32 v73, v144, v145 op_sel:[0,0,1]
	v_cvt_pk_fp8_f32 v74, v154, v155 op_sel:[0,0,1]
	v_cvt_pk_fp8_f32 v75, v156, v157 op_sel:[0,0,1]
	v_mov_b64_e32 v[76:77], s[20:21]
	v_mad_u64_u32 v[76:77], s[24:25], v50, s15, v[76:77]
	v_mad_i32_i24 v77, v51, s15, v77
	v_lshl_add_u64 v[50:51], v[76:77], 0, v[92:93]
	global_store_dwordx4 v[50:51], v[72:75], off nt
	v_mul_f32_e32 v51, v176, v147
	v_fmac_f32_e32 v51, v175, v149
	v_mul_f32_e32 v73, v178, v114
	v_fmac_f32_e32 v73, v177, v150
	v_mov_b32_e32 v116, v48
	v_mul_f32_e32 v50, v176, v149
	v_mul_f32_e32 v72, v178, v150
	v_cvt_pk_fp8_f32 v116, v51, v73
	v_fma_f32 v50, v175, v147, -v50
	v_fma_f32 v72, v177, v114, -v72
	v_mov_b32_e32 v114, v48
	v_mul_f32_e32 v75, v180, v148
	v_cvt_pk_fp8_f32 v114, v50, v72
	v_mul_f32_e32 v50, v153, v115
	v_fmac_f32_e32 v75, v179, v158
	v_fmac_f32_e32 v50, v152, v49
	v_mul_f32_e32 v95, v153, v49
	v_cvt_pk_fp8_f32 v116, v75, v50 op_sel:[0,0,1]
	v_mul_f32_e32 v49, v143, v78
	v_mul_f32_e32 v50, v143, v79
	v_mov_b32_e32 v72, v48
	v_cvt_pk_fp8_f32 v72, v49, v50
	v_mul_f32_e32 v49, v143, v82
	v_mul_f32_e32 v50, v143, v83
	v_mov_b32_e32 v73, v48
	v_cvt_pk_fp8_f32 v73, v49, v50
	v_mul_f32_e32 v74, v180, v158
	v_fma_f32 v74, v179, v148, -v74
	v_fma_f32 v95, v152, v115, -v95
	v_cvt_pk_fp8_f32 v114, v74, v95 op_sel:[0,0,1]
	v_mul_f32_e32 v51, v143, v80
	v_mul_f32_e32 v74, v143, v81
	v_mul_f32_e32 v49, v143, v84
	v_mul_f32_e32 v50, v143, v85
	v_cvt_pk_fp8_f32 v72, v51, v74 op_sel:[0,0,1]
	v_cvt_pk_fp8_f32 v73, v49, v50 op_sel:[0,0,1]
	v_mul_f32_e32 v49, v143, v86
	v_mul_f32_e32 v50, v143, v87
	v_mov_b32_e32 v74, v48
	v_cvt_pk_fp8_f32 v74, v49, v50
	v_mul_f32_e32 v49, v143, v90
	v_mul_f32_e32 v50, v143, v91
	v_mov_b32_e32 v75, v48
	v_cvt_pk_fp8_f32 v75, v49, v50
	v_mul_f32_e32 v51, v143, v88
	v_mul_f32_e32 v78, v143, v89
	v_mul_f32_e32 v49, v143, v112
	v_mul_f32_e32 v50, v143, v113
	v_cvt_pk_fp8_f32 v74, v51, v78 op_sel:[0,0,1]
	v_cvt_pk_fp8_f32 v75, v49, v50 op_sel:[0,0,1]
	v_lshl_add_u64 v[50:51], v[76:77], 0, v[96:97]
	global_store_dword v[50:51], v114, off offset:128
	global_store_dword v[50:51], v116, off offset:160
	s_and_b32 s24, s16, -8
	ds_write_b128 v136, v[72:75]
	s_waitcnt lgkmcnt(0)
	s_barrier
	ds_read_b32 v49, v137
	ds_read_b32 v72, v137 offset:1040
	ds_read_b32 v73, v137 offset:2080
	ds_read_b32 v74, v137 offset:3120
	ds_read_b32 v75, v137 offset:8320
	ds_read_b32 v77, v137 offset:9360
	ds_read_b32 v78, v137 offset:10400
	ds_read_b32 v79, v137 offset:11440
	s_waitcnt lgkmcnt(6)
	v_perm_b32 v76, v72, v49, s55
	v_perm_b32 v49, v72, v49, s56
	s_waitcnt lgkmcnt(4)
	v_perm_b32 v80, v74, v73, s55
	v_perm_b32 v73, v74, v73, s56
	v_perm_b32 v72, v80, v76, s57
	v_perm_b32 v76, v80, v76, s58
	v_perm_b32 v80, v73, v49, s57
	v_perm_b32 v84, v73, v49, s58
	s_waitcnt lgkmcnt(2)
	v_perm_b32 v49, v77, v75, s55
	v_perm_b32 v74, v77, v75, s56
	s_waitcnt lgkmcnt(0)
	v_perm_b32 v75, v79, v78, s55
	v_perm_b32 v78, v79, v78, s56
	v_perm_b32 v73, v75, v49, s57
	v_perm_b32 v77, v75, v49, s58
	v_perm_b32 v81, v78, v74, s57
	v_perm_b32 v85, v78, v74, s58
	ds_read_b32 v49, v137 offset:16640
	ds_read_b32 v74, v137 offset:17680
	ds_read_b32 v75, v137 offset:18720
	ds_read_b32 v78, v137 offset:19760
	ds_read_b32 v79, v137 offset:24960
	ds_read_b32 v83, v137 offset:26000
	ds_read_b32 v87, v137 offset:27040
	ds_read_b32 v88, v137 offset:28080
	s_waitcnt lgkmcnt(6)
	v_perm_b32 v82, v74, v49, s55
	v_perm_b32 v49, v74, v49, s56
	s_waitcnt lgkmcnt(4)
	v_perm_b32 v86, v78, v75, s55
	v_perm_b32 v75, v78, v75, s56
	s_lshl_b32 s16, s48, 13
	v_perm_b32 v74, v86, v82, s57
	v_perm_b32 v78, v86, v82, s58
	v_perm_b32 v82, v75, v49, s57
	v_perm_b32 v86, v75, v49, s58
	s_waitcnt lgkmcnt(2)
	v_perm_b32 v49, v83, v79, s55
	v_perm_b32 v89, v83, v79, s56
	s_waitcnt lgkmcnt(0)
	v_perm_b32 v79, v88, v87, s55
	v_perm_b32 v87, v88, v87, s56
	v_add_u32_e32 v88, s24, v132
	s_and_b32 s16, s16, 0x1fe000
	v_perm_b32 v83, v87, v89, s57
	v_perm_b32 v87, v87, v89, s58
	v_ashrrev_i32_e32 v89, 31, v88
	v_lshl_add_u64 v[50:51], v[100:101], 0, s[16:17]
	v_lshlrev_b64 v[88:89], 21, v[88:89]
	v_perm_b32 v75, v79, v49, s57
	v_lshl_add_u64 v[88:89], v[50:51], 0, v[88:89]
	v_perm_b32 v79, v79, v49, s58
	global_store_dwordx4 v[88:89], v[72:75], off nt
	global_store_dwordx4 v[88:89], v[76:79], off offset:64 nt
	global_store_dwordx4 v[88:89], v[80:83], off offset:128 nt
	global_store_dwordx4 v[88:89], v[84:87], off offset:192 nt
	ds_read_b32 v49, v138
	ds_read_b32 v72, v138 offset:1040
	ds_read_b32 v73, v138 offset:2080
	ds_read_b32 v74, v138 offset:3120
	ds_read_b32 v75, v138 offset:8320
	ds_read_b32 v77, v138 offset:9360
	ds_read_b32 v78, v138 offset:10400
	ds_read_b32 v79, v138 offset:11440
	s_waitcnt lgkmcnt(6)
	v_perm_b32 v76, v72, v49, s55
	v_perm_b32 v49, v72, v49, s56
	s_waitcnt lgkmcnt(4)
	v_perm_b32 v80, v74, v73, s55
	v_perm_b32 v73, v74, v73, s56
	v_perm_b32 v72, v80, v76, s57
	v_perm_b32 v76, v80, v76, s58
	v_perm_b32 v80, v73, v49, s57
	v_perm_b32 v84, v73, v49, s58
	s_waitcnt lgkmcnt(2)
	v_perm_b32 v49, v77, v75, s55
	v_perm_b32 v74, v77, v75, s56
	s_waitcnt lgkmcnt(0)
	v_perm_b32 v75, v79, v78, s55
	v_perm_b32 v78, v79, v78, s56
	v_perm_b32 v73, v75, v49, s57
	v_perm_b32 v77, v75, v49, s58
	v_perm_b32 v81, v78, v74, s57
	v_perm_b32 v85, v78, v74, s58
	ds_read_b32 v49, v138 offset:16640
	ds_read_b32 v74, v138 offset:17680
	ds_read_b32 v75, v138 offset:18720
	ds_read_b32 v78, v138 offset:19760
	ds_read_b32 v79, v138 offset:24960
	ds_read_b32 v83, v138 offset:26000
	ds_read_b32 v87, v138 offset:27040
	ds_read_b32 v88, v138 offset:28080
	s_waitcnt lgkmcnt(6)
	v_perm_b32 v82, v74, v49, s55
	v_perm_b32 v49, v74, v49, s56
	s_waitcnt lgkmcnt(4)
	v_perm_b32 v86, v78, v75, s55
	v_perm_b32 v75, v78, v75, s56
	v_perm_b32 v74, v86, v82, s57
	v_perm_b32 v78, v86, v82, s58
	v_perm_b32 v82, v75, v49, s57
	v_perm_b32 v86, v75, v49, s58
	s_waitcnt lgkmcnt(2)
	v_perm_b32 v49, v83, v79, s55
	v_perm_b32 v89, v83, v79, s56
	s_waitcnt lgkmcnt(0)
	v_perm_b32 v79, v88, v87, s55
	v_perm_b32 v87, v88, v87, s56
	v_add_u32_e32 v88, s24, v133
	v_perm_b32 v83, v87, v89, s57
	v_perm_b32 v87, v87, v89, s58
	v_ashrrev_i32_e32 v89, 31, v88
	v_lshlrev_b64 v[88:89], 21, v[88:89]
	s_add_i32 s51, s51, s50
	v_perm_b32 v75, v79, v49, s57
	v_lshl_add_u64 v[50:51], v[50:51], 0, v[88:89]
	s_cmpk_gt_i32 s36, 0x1ff
	s_mov_b32 s48, s36
	v_perm_b32 v79, v79, v49, s58
	global_store_dwordx4 v[50:51], v[72:75], off nt
	global_store_dwordx4 v[50:51], v[76:79], off offset:64 nt
	global_store_dwordx4 v[50:51], v[80:83], off offset:128 nt
	global_store_dwordx4 v[50:51], v[84:87], off offset:192 nt
	s_barrier
	s_cbranch_scc1 .LBB0_1523

.LBB0_1519:
	v_and_b32_e32 v50, 0xffff0000, v52
	v_lshlrev_b32_e32 v49, 16, v52
	v_mul_f32_e32 v50, v50, v50
	v_fmac_f32_e32 v50, v49, v49
	v_lshlrev_b32_e32 v49, 16, v53
	v_fmac_f32_e32 v50, v49, v49
	v_and_b32_e32 v49, 0xffff0000, v53
	v_fmac_f32_e32 v50, v49, v49
	v_lshlrev_b32_e32 v49, 16, v54
	v_fmac_f32_e32 v50, v49, v49
	v_and_b32_e32 v49, 0xffff0000, v54
	v_fmac_f32_e32 v50, v49, v49
	v_lshlrev_b32_e32 v49, 16, v55
	v_fmac_f32_e32 v50, v49, v49
	v_and_b32_e32 v49, 0xffff0000, v55
	v_and_b32_e32 v51, 0xffff0000, v56
	v_fmac_f32_e32 v50, v49, v49
	v_lshlrev_b32_e32 v49, 16, v56
	v_mul_f32_e32 v51, v51, v51
	v_fmac_f32_e32 v51, v49, v49
	v_lshlrev_b32_e32 v49, 16, v57
	v_fmac_f32_e32 v51, v49, v49
	v_and_b32_e32 v49, 0xffff0000, v57
	v_fmac_f32_e32 v51, v49, v49
	v_lshlrev_b32_e32 v49, 16, v58
	v_fmac_f32_e32 v51, v49, v49
	v_and_b32_e32 v49, 0xffff0000, v58
	v_fmac_f32_e32 v51, v49, v49
	v_lshlrev_b32_e32 v49, 16, v59
	v_fmac_f32_e32 v51, v49, v49
	v_and_b32_e32 v49, 0xffff0000, v59
	v_fmac_f32_e32 v51, v49, v49
	v_cndmask_b32_e64 v49, 0, v50, s[4:5]
	v_cndmask_b32_e64 v50, 0, v50, s[6:7]
	v_cndmask_b32_e64 v51, 0, v51, s[8:9]
	v_add_f32_e32 v50, v51, v50
	ds_bpermute_b32 v51, v126, v50
	ds_bpermute_b32 v52, v126, v49
	v_cvt_pk_f32_fp8_e32 v[54:55], v68
	v_cvt_pk_f32_fp8_sdwa v[56:57], v68 src0_sel:WORD_1
	v_cvt_pk_f32_fp8_e32 v[58:59], v69
	s_waitcnt lgkmcnt(1)
	v_add_f32_e32 v50, v50, v51
	ds_bpermute_b32 v51, v127, v50
	s_waitcnt lgkmcnt(1)
	v_add_f32_e32 v49, v49, v52
	ds_bpermute_b32 v52, v127, v49
	v_pk_mul_f32 v[160:161], v[54:55], v[54:55]
	v_cvt_pk_f32_fp8_sdwa v[68:69], v69 src0_sel:WORD_1
	s_waitcnt lgkmcnt(1)
	v_add_f32_e32 v50, v50, v51
	ds_bpermute_b32 v51, v128, v50
	s_waitcnt lgkmcnt(1)
	v_add_f32_e32 v49, v49, v52
	ds_bpermute_b32 v52, v128, v49
	v_pk_mul_f32 v[162:163], v[56:57], v[56:57]
	v_add_f32_e32 v160, v160, v161
	s_waitcnt lgkmcnt(1)
	v_add_f32_e32 v50, v50, v51
	ds_bpermute_b32 v51, v129, v50
	s_waitcnt lgkmcnt(1)
	v_add_f32_e32 v49, v49, v52
	ds_bpermute_b32 v52, v129, v49
	v_add_f32_e32 v160, v160, v162
	v_cvt_pk_f32_fp8_e32 v[148:149], v70
	v_pk_mul_f32 v[164:165], v[58:59], v[58:59]
	v_add_f32_e32 v160, v163, v160
	s_waitcnt lgkmcnt(1)
	v_add_f32_e32 v50, v50, v51
	v_add_f32_e32 v160, v164, v160
	ds_bpermute_b32 v51, v130, v50
	v_cvt_pk_f32_fp8_sdwa v[150:151], v70 src0_sel:WORD_1
	v_pk_mul_f32 v[166:167], v[68:69], v[68:69]
	v_add_f32_e32 v160, v165, v160
	v_add_f32_e32 v160, v166, v160
	s_waitcnt lgkmcnt(1)
	v_add_f32_e32 v49, v49, v52
	v_cvt_pk_f32_fp8_e32 v[152:153], v71
	v_pk_mul_f32 v[168:169], v[148:149], v[148:149]
	v_add_f32_e32 v160, v167, v160
	ds_bpermute_b32 v52, v130, v49
	v_add_f32_e32 v160, v168, v160
	v_cvt_pk_f32_fp8_sdwa v[70:71], v71 src0_sel:WORD_1
	v_pk_mul_f32 v[170:171], v[150:151], v[150:151]
	v_add_f32_e32 v160, v169, v160
	s_waitcnt lgkmcnt(1)
	v_add_f32_e32 v50, v50, v51
	v_add_f32_e32 v160, v170, v160
	ds_bpermute_b32 v51, v131, v50
	v_cvt_pk_f32_fp8_e32 v[154:155], v141
	v_pk_mul_f32 v[172:173], v[152:153], v[152:153]
	v_add_f32_e32 v160, v171, v160
	v_add_f32_e32 v160, v172, v160
	s_waitcnt lgkmcnt(1)
	v_add_f32_e32 v49, v49, v52
	v_cvt_f32_i32_e32 v95, v142
	v_cvt_pk_f32_fp8_sdwa v[156:157], v141 src0_sel:WORD_1
	v_pk_mul_f32 v[174:175], v[70:71], v[70:71]
	v_add_f32_e32 v160, v173, v160
	ds_bpermute_b32 v52, v131, v49
	v_add_f32_e32 v160, v174, v160
	v_cvt_pk_f32_fp8_e32 v[158:159], v140
	v_pk_mul_f32 v[176:177], v[154:155], v[154:155]
	v_add_f32_e32 v160, v175, v160
	s_waitcnt lgkmcnt(1)
	v_add_f32_e32 v50, v50, v51
	v_add_f32_e32 v160, v176, v160
	v_fmamk_f32 v142, v50, 0x3b800000, v135
	v_mul_f32_e32 v50, v120, v95
	v_cvt_pk_f32_fp8_sdwa v[140:141], v140 src0_sel:WORD_1
	v_pk_mul_f32 v[178:179], v[156:157], v[156:157]
	v_add_f32_e32 v160, v177, v160
	v_cvt_f64_f32_e32 v[50:51], v50
	v_add_f32_e32 v160, v178, v160
	s_waitcnt lgkmcnt(0)
	v_add_f32_e32 v49, v49, v52
	v_mul_f64 v[52:53], v[50:51], s[22:23]
	v_pk_mul_f32 v[180:181], v[158:159], v[158:159]
	v_add_f32_e32 v160, v179, v160
	v_floor_f64_e32 v[52:53], v[52:53]
	v_add_f32_e32 v160, v180, v160
	v_fma_f64 v[50:51], v[50:51], s[22:23], -v[52:53]
	v_pk_mul_f32 v[182:183], v[140:141], v[140:141]
	v_add_f32_e32 v160, v181, v160
	v_cvt_f32_f64_e32 v50, v[50:51]
	v_add_f32_e32 v160, v182, v160
	v_cos_f32_e32 v147, v50
	v_sin_f32_e32 v184, v50
	v_mul_f32_e32 v50, v121, v95
	v_add_f32_e32 v160, v183, v160
	v_cvt_f64_f32_e32 v[50:51], v50
	ds_bpermute_b32 v161, v126, v160
	v_mul_f64 v[52:53], v[50:51], s[22:23]
	v_floor_f64_e32 v[52:53], v[52:53]
	v_fma_f64 v[50:51], v[50:51], s[22:23], -v[52:53]
	v_cvt_f32_f64_e32 v50, v[50:51]
	v_cos_f32_e32 v185, v50
	v_sin_f32_e32 v186, v50
	v_mul_f32_e32 v50, v122, v95
	s_waitcnt lgkmcnt(0)
	v_add_f32_e32 v160, v160, v161
	v_cvt_f64_f32_e32 v[50:51], v50
	ds_bpermute_b32 v161, v127, v160
	v_mul_f64 v[52:53], v[50:51], s[22:23]
	v_floor_f64_e32 v[52:53], v[52:53]
	v_fma_f64 v[50:51], v[50:51], s[22:23], -v[52:53]
	v_cvt_f32_f64_e32 v50, v[50:51]
	v_cos_f32_e32 v162, v50
	v_sin_f32_e32 v163, v50
	v_mul_f32_e32 v50, v125, v95
	s_waitcnt lgkmcnt(0)
	v_add_f32_e32 v95, v160, v161
	v_fmamk_f32 v49, v49, 0x3b2aaaab, v135
	ds_bpermute_b32 v160, v128, v95
	v_cvt_f64_f32_e32 v[50:51], v50
	v_rsq_f32_e32 v49, v49
	v_mul_f64 v[52:53], v[50:51], s[22:23]
	v_floor_f64_e32 v[52:53], v[52:53]
	v_fma_f64 v[50:51], v[50:51], s[22:23], -v[52:53]
	v_cvt_f32_f64_e32 v50, v[50:51]
	s_waitcnt lgkmcnt(0)
	v_add_f32_e32 v51, v95, v160
	v_mul_f32_e32 v52, v49, v49
	v_mul_f32_e32 v51, v52, v51
	v_fmamk_f32 v51, v51, 0x3baaaaab, v135
	v_rsq_f32_e32 v51, v51
	v_cos_f32_e32 v161, v50
	v_sin_f32_e32 v95, v50
	s_ashr_i32 s16, s28, 11
	v_mul_f32_e32 v49, v49, v51
	v_mul_f32_e32 v49, 0x3f553b94, v49
	v_mul_f32_e32 v50, v12, v49
	v_mul_f32_e32 v51, v54, v50
	v_mul_f32_e32 v50, v13, v49
	v_mul_f32_e32 v52, v55, v50
	v_mul_f32_e32 v50, v14, v49
	v_mul_f32_e32 v54, v56, v50
	v_mul_f32_e32 v50, v15, v49
	v_mul_f32_e32 v55, v57, v50
	v_mul_f32_e32 v50, v8, v49
	v_mul_f32_e32 v53, v58, v50
	v_mul_f32_e32 v50, v9, v49
	v_mul_f32_e32 v56, v59, v50
	v_mul_f32_e32 v50, v10, v49
	v_mul_f32_e32 v57, v68, v50
	v_mul_f32_e32 v50, v11, v49
	v_mul_f32_e32 v58, v69, v50
	v_mul_f32_e32 v50, v4, v49
	v_mul_f32_e32 v59, v148, v50
	v_mul_f32_e32 v50, v5, v49
	v_mul_f32_e32 v68, v149, v50
	v_mul_f32_e32 v50, v6, v49
	v_mul_f32_e32 v69, v150, v50
	v_mul_f32_e32 v50, v7, v49
	v_mul_f32_e32 v148, v151, v50
	v_mul_f32_e32 v50, v0, v49
	v_mul_f32_e32 v149, v152, v50
	v_mul_f32_e32 v50, v1, v49
	v_mul_f32_e32 v150, v153, v50
	v_mul_f32_e32 v50, v2, v49
	v_mul_f32_e32 v70, v70, v50
	v_mul_f32_e32 v50, v3, v49
	v_mul_f32_e32 v71, v71, v50
	v_mul_f32_e32 v50, v32, v49
	v_mul_f32_e32 v151, v154, v50
	v_mul_f32_e32 v50, v33, v49
	v_mul_f32_e32 v152, v155, v50
	v_mul_f32_e32 v50, v34, v49
	v_mul_f32_e32 v153, v156, v50
	v_mul_f32_e32 v50, v35, v49
	v_mul_f32_e32 v154, v157, v50
	v_mul_f32_e32 v50, v36, v49
	v_mul_f32_e32 v155, v158, v50
	v_mul_f32_e32 v50, v37, v49
	v_mul_f32_e32 v156, v159, v50
	v_mul_f32_e32 v50, v38, v49
	v_mul_f32_e32 v140, v140, v50
	v_mov_b32_e32 v50, v48
	v_cvt_pk_fp8_f32 v50, v51, v52
	v_mov_b32_e32 v51, v48
	v_cvt_pk_fp8_f32 v51, v53, v56
	v_mov_b32_e32 v52, v48
	v_mov_b32_e32 v53, v48
	v_cvt_pk_fp8_f32 v52, v59, v68
	v_cvt_pk_fp8_f32 v53, v149, v150
	v_cvt_pk_fp8_f32 v50, v54, v55 op_sel:[0,0,1]
	v_and_or_b32 v56, s16, -8, v123
	v_mov_b64_e32 v[54:55], s[24:25]
	v_cvt_pk_fp8_f32 v51, v57, v58 op_sel:[0,0,1]
	v_cvt_pk_fp8_f32 v52, v69, v148 op_sel:[0,0,1]
	v_cvt_pk_fp8_f32 v53, v70, v71 op_sel:[0,0,1]
	v_mad_i64_i32 v[54:55], s[28:29], v56, s52, v[54:55]
	v_lshl_add_u64 v[56:57], v[118:119], 0, v[54:55]
	v_add_co_u32_e32 v58, vcc, s53, v56
	v_mul_f32_e32 v49, v39, v49
	s_nop 0
	v_addc_co_u32_e32 v59, vcc, 0, v57, vcc
	global_store_dwordx4 v[58:59], v[50:53], off nt
	v_mul_f32_e32 v58, v163, v140
	v_mul_f32_e32 v49, v141, v49
	v_mul_f32_e32 v50, v184, v155
	v_mul_f32_e32 v51, v184, v151
	v_mul_f32_e32 v52, v186, v156
	v_mul_f32_e32 v53, v186, v152
	v_fma_f32 v50, v147, v151, -v50
	v_fmac_f32_e32 v51, v147, v155
	v_fma_f32 v52, v185, v152, -v52
	v_fmac_f32_e32 v53, v185, v156
	v_fma_f32 v148, v162, v153, -v58
	v_mul_f32_e32 v149, v163, v153
	v_mov_b32_e32 v152, v48
	v_mov_b32_e32 v153, v48
	v_rsq_f32_e32 v142, v142
	v_mul_f32_e32 v58, v95, v49
	v_cvt_pk_fp8_f32 v152, v50, v52
	v_cvt_pk_fp8_f32 v153, v51, v53
	v_cvt_pk_f32_fp8_e32 v[50:51], v64
	v_fma_f32 v150, v161, v154, -v58
	v_cvt_pk_f32_fp8_e32 v[58:59], v65
	v_cvt_pk_f32_fp8_sdwa v[52:53], v64 src0_sel:WORD_1
	v_mul_f32_e32 v159, v142, v51
	v_mul_f32_e32 v158, v142, v50
	v_mul_f32_e32 v165, v142, v58
	v_mul_f32_e32 v58, v159, v159
	v_cvt_pk_f32_fp8_sdwa v[64:65], v65 src0_sel:WORD_1
	v_mul_f32_e32 v160, v142, v52
	v_fmac_f32_e32 v58, v158, v158
	v_mul_f32_e32 v164, v142, v53
	v_fmac_f32_e32 v58, v160, v160
	v_cvt_pk_f32_fp8_e32 v[68:69], v66
	v_fmac_f32_e32 v58, v164, v164
	v_mul_f32_e32 v166, v142, v59
	v_fmac_f32_e32 v58, v165, v165
	v_cvt_pk_f32_fp8_sdwa v[70:71], v66 src0_sel:WORD_1
	v_mul_f32_e32 v167, v142, v64
	v_fmac_f32_e32 v58, v166, v166
	v_mul_f32_e32 v168, v142, v65
	v_fmac_f32_e32 v58, v167, v167
	v_fmac_f32_e32 v149, v162, v140
	v_cvt_pk_f32_fp8_e32 v[140:141], v67
	v_mul_f32_e32 v169, v142, v68
	v_fmac_f32_e32 v58, v168, v168
	v_mul_f32_e32 v170, v142, v69
	v_fmac_f32_e32 v58, v169, v169
	v_cvt_pk_f32_fp8_sdwa v[66:67], v67 src0_sel:WORD_1
	v_mul_f32_e32 v171, v142, v70
	v_fmac_f32_e32 v58, v170, v170
	v_mul_f32_e32 v172, v142, v71
	v_fmac_f32_e32 v58, v171, v171
	v_mul_f32_e32 v140, v142, v140
	v_fmac_f32_e32 v58, v172, v172
	v_mul_f32_e32 v141, v142, v141
	v_fmac_f32_e32 v58, v140, v140
	v_mul_f32_e32 v173, v142, v66
	v_fmac_f32_e32 v58, v141, v141
	v_mul_f32_e32 v174, v142, v67
	v_fmac_f32_e32 v58, v173, v173
	v_mul_f32_e32 v151, v95, v154
	v_lshlrev_b32_e32 v154, 16, v110
	v_fmac_f32_e32 v58, v174, v174
	v_and_b32_e32 v110, 0xffff0000, v110
	v_fmac_f32_e32 v58, v154, v154
	v_lshlrev_b32_e32 v155, 16, v111
	v_fmac_f32_e32 v58, v110, v110
	v_and_b32_e32 v111, 0xffff0000, v111
	v_fmac_f32_e32 v58, v155, v155
	v_lshlrev_b32_e32 v156, 16, v108
	v_fmac_f32_e32 v58, v111, v111
	v_and_b32_e32 v157, 0xffff0000, v108
	v_fmac_f32_e32 v58, v156, v156
	v_and_b32_e32 v50, 0xffff0000, v109
	v_lshlrev_b32_e32 v51, 16, v109
	v_fmac_f32_e32 v58, v157, v157
	v_pk_mul_f32 v[52:53], v[50:51], v[50:51]
	v_fmac_f32_e32 v151, v161, v49
	v_add_f32_e32 v53, v53, v58
	v_add_f32_e32 v52, v52, v53
	ds_bpermute_b32 v53, v126, v52
	v_cvt_pk_fp8_f32 v152, v148, v150 op_sel:[0,0,1]
	v_lshl_add_u64 v[54:55], v[116:117], 0, v[54:55]
	v_cvt_pk_fp8_f32 v153, v149, v151 op_sel:[0,0,1]
	v_cvt_pk_f32_fp8_e32 v[58:59], v60
	s_waitcnt lgkmcnt(0)
	v_add_f32_e32 v49, v52, v53
	ds_bpermute_b32 v64, v127, v49
	v_add_co_u32_e32 v52, vcc, s53, v54
	v_cvt_pk_f32_fp8_e32 v[66:67], v61
	s_nop 0
	v_addc_co_u32_e32 v53, vcc, 0, v55, vcc
	s_waitcnt lgkmcnt(0)
	v_add_f32_e32 v49, v49, v64
	global_store_dword v[52:53], v152, off offset:128
	global_store_dword v[52:53], v153, off offset:160
	ds_bpermute_b32 v52, v128, v49
	v_add_co_u32_e32 v56, vcc, s54, v56
	v_cvt_pk_f32_fp8_sdwa v[64:65], v60 src0_sel:WORD_1
	s_nop 0
	v_addc_co_u32_e32 v57, vcc, 0, v57, vcc
	s_waitcnt lgkmcnt(0)
	v_add_f32_e32 v49, v49, v52
	v_fmamk_f32 v49, v49, 0x3baaaaab, v135
	v_rsq_f32_e32 v49, v49
	v_cvt_pk_f32_fp8_sdwa v[60:61], v61 src0_sel:WORD_1
	v_cvt_pk_f32_fp8_e32 v[68:69], v62
	v_cvt_pk_f32_fp8_e32 v[108:109], v63
	v_mul_f32_e32 v152, v26, v49
	v_mul_f32_e32 v152, v167, v152
	v_mul_f32_e32 v167, v40, v49
	v_mul_f32_e32 v154, v167, v154
	v_mul_f32_e32 v167, v41, v49
	v_mul_f32_e32 v110, v167, v110
	v_mul_f32_e32 v167, v42, v49
	v_mul_f32_e32 v150, v24, v49
	v_mul_f32_e32 v155, v167, v155
	v_mul_f32_e32 v167, v43, v49
	v_mul_f32_e32 v150, v165, v150
	v_mul_f32_e32 v165, v16, v49
	v_mul_f32_e32 v111, v167, v111
	v_mul_f32_e32 v167, v44, v49
	v_mul_f32_e32 v52, v28, v49
	v_mul_f32_e32 v53, v29, v49
	v_mul_f32_e32 v148, v30, v49
	v_mul_f32_e32 v149, v31, v49
	v_mul_f32_e32 v151, v25, v49
	v_mul_f32_e32 v140, v140, v165
	v_mul_f32_e32 v165, v17, v49
	v_mul_f32_e32 v156, v167, v156
	v_mul_f32_e32 v167, v45, v49
	v_mul_f32_e32 v52, v158, v52
	v_mul_f32_e32 v53, v159, v53
	v_mul_f32_e32 v148, v160, v148
	v_mul_f32_e32 v149, v164, v149
	v_mul_f32_e32 v151, v166, v151
	v_mul_f32_e32 v153, v27, v49
	v_mul_f32_e32 v158, v20, v49
	v_mul_f32_e32 v159, v21, v49
	v_mul_f32_e32 v160, v22, v49
	v_mul_f32_e32 v164, v23, v49
	v_mul_f32_e32 v141, v141, v165
	v_mul_f32_e32 v165, v18, v49
	v_mul_f32_e32 v166, v19, v49
	v_mul_f32_e32 v157, v167, v157
	v_mul_f32_e32 v167, v46, v49
	v_mul_f32_e32 v49, v47, v49
	v_mul_f32_e32 v49, v49, v50
	v_mov_b32_e32 v50, v48
	v_mul_f32_e32 v158, v169, v158
	v_mul_f32_e32 v159, v170, v159
	v_mul_f32_e32 v167, v167, v51
	v_cvt_pk_fp8_f32 v50, v52, v53
	v_mov_b32_e32 v51, v48
	v_mov_b32_e32 v52, v48
	v_mov_b32_e32 v53, v48
	v_cvt_pk_fp8_f32 v51, v150, v151
	v_cvt_pk_fp8_f32 v52, v158, v159
	v_cvt_pk_fp8_f32 v53, v140, v141
	v_mul_f32_e32 v153, v168, v153
	v_mul_f32_e32 v160, v171, v160
	v_mul_f32_e32 v164, v172, v164
	v_mul_f32_e32 v165, v173, v165
	v_mul_f32_e32 v166, v174, v166
	v_cvt_pk_fp8_f32 v50, v148, v149 op_sel:[0,0,1]
	v_cvt_pk_fp8_f32 v51, v152, v153 op_sel:[0,0,1]
	v_cvt_pk_fp8_f32 v52, v160, v164 op_sel:[0,0,1]
	v_cvt_pk_fp8_f32 v53, v165, v166 op_sel:[0,0,1]
	v_mov_b32_e32 v141, v48
	v_mov_b32_e32 v140, v48
	v_cvt_pk_f32_fp8_sdwa v[70:71], v62 src0_sel:WORD_1
	global_store_dwordx4 v[56:57], v[50:53], off nt
	v_mul_f32_e32 v57, v163, v155
	v_mul_f32_e32 v56, v163, v167
	v_mul_f32_e32 v51, v184, v154
	v_mul_f32_e32 v53, v186, v110
	v_mul_f32_e32 v50, v184, v156
	v_fmac_f32_e32 v51, v147, v156
	v_mul_f32_e32 v52, v186, v157
	v_fmac_f32_e32 v53, v185, v157
	v_fma_f32 v50, v147, v154, -v50
	v_fma_f32 v52, v185, v110, -v52
	v_cvt_pk_fp8_f32 v141, v51, v53
	v_cvt_pk_fp8_f32 v140, v50, v52
	v_mul_f32_e32 v50, v95, v111
	v_fmac_f32_e32 v57, v162, v167
	v_mul_f32_e32 v110, v95, v49
	v_fmac_f32_e32 v50, v161, v49
	v_fma_f32 v56, v162, v155, -v56
	v_fma_f32 v110, v161, v111, -v110
	v_cvt_pk_fp8_f32 v141, v57, v50 op_sel:[0,0,1]
	v_mul_f32_e32 v49, v142, v58
	v_mul_f32_e32 v51, v142, v59
	v_mov_b32_e32 v50, v48
	v_cvt_pk_fp8_f32 v140, v56, v110 op_sel:[0,0,1]
	v_cvt_pk_fp8_f32 v50, v49, v51
	v_mul_f32_e32 v49, v142, v66
	v_mul_f32_e32 v56, v142, v67
	v_mov_b32_e32 v51, v48
	v_cvt_pk_fp8_f32 v51, v49, v56
	v_mul_f32_e32 v52, v142, v64
	v_mul_f32_e32 v53, v142, v65
	v_cvt_pk_fp8_f32 v50, v52, v53 op_sel:[0,0,1]
	v_mul_f32_e32 v49, v142, v60
	v_mul_f32_e32 v52, v142, v61
	v_cvt_pk_fp8_f32 v51, v49, v52 op_sel:[0,0,1]
	v_mul_f32_e32 v49, v142, v68
	v_mul_f32_e32 v53, v142, v69
	v_mov_b32_e32 v52, v48
	v_cvt_pk_f32_fp8_sdwa v[62:63], v63 src0_sel:WORD_1
	v_cvt_pk_fp8_f32 v52, v49, v53
	v_mul_f32_e32 v49, v142, v108
	v_mul_f32_e32 v58, v142, v109
	v_mov_b32_e32 v53, v48
	v_cvt_pk_fp8_f32 v53, v49, v58
	v_mul_f32_e32 v56, v142, v70
	v_mul_f32_e32 v57, v142, v71
	v_cvt_pk_fp8_f32 v52, v56, v57 op_sel:[0,0,1]
	v_mul_f32_e32 v49, v142, v62
	v_mul_f32_e32 v56, v142, v63
	v_cvt_pk_fp8_f32 v53, v49, v56 op_sel:[0,0,1]
	v_add_co_u32_e32 v54, vcc, s54, v54
	s_add_u32 s24, s24, 0xc0
	s_nop 0
	v_addc_co_u32_e32 v55, vcc, 0, v55, vcc
	s_addc_u32 s25, s25, 0
	global_store_dword v[54:55], v140, off offset:128
	global_store_dword v[54:55], v141, off offset:160
	ds_write_b128 v146, v[50:53]
	s_cmpk_eq_i32 s24, 0x540
	v_add_u32_e32 v146, 0x410, v146
	s_cbranch_scc0 .LBB0_1513
	s_add_i32 s36, s48, s44
	s_lshl_b32 s16, s36, 6
	s_add_i32 s24, s16, s47
	s_waitcnt vmcnt(9)
	v_mov_b64_e32 v[60:61], v[72:73]
	v_mov_b64_e32 v[52:53], v[88:89]
	v_mov_b64_e32 v[56:57], v[84:85]
	v_mov_b64_e32 v[68:69], v[80:81]
	v_mov_b64_e32 v[64:65], v[76:77]
	s_cmpk_gt_i32 s24, 0x7fff
	s_waitcnt vmcnt(6)
	v_mov_b32_e32 v142, v145
	v_mov_b32_e32 v140, v143
	v_mov_b32_e32 v141, v144
	v_mov_b64_e32 v[108:109], v[112:113]
	v_mov_b64_e32 v[110:111], v[114:115]
	v_mov_b64_e32 v[62:63], v[74:75]
	v_mov_b64_e32 v[54:55], v[90:91]
	v_mov_b64_e32 v[58:59], v[86:87]
	v_mov_b64_e32 v[70:71], v[82:83]
	v_mov_b64_e32 v[66:67], v[78:79]
	s_cbranch_scc1 .LBB0_1511
	s_mul_i32 s28, s24, 0x600
	s_mul_hi_i32 s29, s24, 0x600
	s_add_u32 s26, s45, s28
	s_addc_u32 s27, s46, s29
	global_load_dwordx4 v[52:55], v94, s[26:27]
	v_mov_b32_e32 v50, v48
	v_mov_b32_e32 v51, v48
	v_mov_b32_e32 v49, v48
	v_mov_b64_e32 v[58:59], v[50:51]
	v_mov_b64_e32 v[56:57], v[48:49]
	s_and_saveexec_b64 s[30:31], s[2:3]
	s_cbranch_execz .LBB0_1510
	v_mov_b32_e32 v95, v48
	v_lshl_add_u64 v[50:51], s[26:27], 0, v[94:95]
	global_load_dwordx4 v[56:59], v[50:51], off offset:1024
	s_branch .LBB0_1510

.LBB0_1592:
	s_or_b64 exec, exec, s[4:5]
	s_waitcnt lgkmcnt(6)
	v_mfma_f32_32x32x64_f8f6f4 v[0:15], v[112:119], v[88:95], v[0:15]
	s_lshl_b32 s2, s44, 11
	s_waitcnt lgkmcnt(0)
	s_and_b32 s2, s2, 0xffffc000
	ds_read_b128 v[88:91], v197 offset:60416
	s_add_i32 s2, s2, s63
	s_ashr_i32 s3, s2, 31
	s_lshl_b64 s[2:3], s[2:3], 11
	s_add_u32 s2, s61, s2
	s_addc_u32 s3, s62, s3
	s_lshl_b32 s4, s44, 8
	s_waitcnt lgkmcnt(0)
	v_rcp_f32_e32 v96, v88
	s_and_b32 s4, s4, 0x700
	s_add_u32 s2, s2, s4
	s_addc_u32 s3, s3, 0
	s_lshl_b32 s4, s43, 13
	v_mfma_f32_32x32x64_f8f6f4 v[16:31], v[112:119], v[80:87], v[16:31]
	s_add_i32 s4, s4, 0
	s_nop 2
	v_mul_f32_e32 v0, v0, v96
	ds_read_b128 v[92:95], v197 offset:60448
	v_rcp_f32_e32 v97, v89
	v_rcp_f32_e32 v98, v90
	v_rcp_f32_e32 v99, v91
	ds_read_b128 v[88:91], v197 offset:60480
	ds_read_b128 v[80:83], v197 offset:60512
	s_waitcnt lgkmcnt(0)
	s_barrier
	v_rcp_f32_e32 v92, v92
	v_rcp_f32_e32 v93, v93
	v_rcp_f32_e32 v94, v94
	v_rcp_f32_e32 v84, v95
	v_mfma_f32_32x32x64_f8f6f4 v[32:47], v[112:119], v[72:79], v[32:47]
	v_lshlrev_b32_e32 v72, 1, v194
	v_lshlrev_b32_e32 v73, 8, v195
	v_add3_u32 v72, s4, v72, v73
	v_bfe_u32 v73, v0, 16, 1
	v_add3_u32 v0, v0, v73, s59
	ds_write_b16_d16_hi v72, v0
	v_mul_f32_e32 v0, v16, v96
	v_bfe_u32 v16, v0, 16, 1
	v_add3_u32 v0, v0, v16, s59
	ds_write_b16_d16_hi v72, v0 offset:64
	v_rcp_f32_e32 v85, v88
	v_rcp_f32_e32 v86, v89
	v_rcp_f32_e32 v87, v90
	v_rcp_f32_e32 v88, v91
	v_rcp_f32_e32 v80, v80
	v_mfma_f32_32x32x64_f8f6f4 v[48:63], v[112:119], v[64:71], v[48:63]
	s_nop 3
	v_mul_f32_e32 v0, v32, v96
	v_bfe_u32 v16, v0, 16, 1
	v_add3_u32 v0, v0, v16, s59
	ds_write_b16_d16_hi v72, v0 offset:128
	v_rcp_f32_e32 v81, v81
	v_rcp_f32_e32 v82, v82
	v_rcp_f32_e32 v83, v83
	s_ashr_i32 s43, s42, 31
	s_lshl_b64 s[6:7], s[42:43], 11
	s_add_u32 s2, s2, s6
	s_addc_u32 s3, s3, s7
	s_add_i32 s60, s60, 1
	s_nop 3
	v_mul_f32_e32 v0, v48, v96
	v_bfe_u32 v16, v0, 16, 1
	v_add3_u32 v0, v0, v16, s59
	ds_write_b16_d16_hi v72, v0 offset:192
	v_mul_f32_e32 v0, v1, v97
	v_bfe_u32 v1, v0, 16, 1
	v_add3_u32 v0, v0, v1, s59
	ds_write_b16_d16_hi v72, v0 offset:256
	v_mul_f32_e32 v0, v17, v97
	v_bfe_u32 v1, v0, 16, 1
	v_add3_u32 v0, v0, v1, s59
	ds_write_b16_d16_hi v72, v0 offset:320
	v_mul_f32_e32 v0, v33, v97
	v_bfe_u32 v1, v0, 16, 1
	v_add3_u32 v0, v0, v1, s59
	ds_write_b16_d16_hi v72, v0 offset:384
	v_mul_f32_e32 v0, v49, v97
	v_bfe_u32 v1, v0, 16, 1
	v_add3_u32 v0, v0, v1, s59
	ds_write_b16_d16_hi v72, v0 offset:448
	v_mul_f32_e32 v0, v2, v98
	v_bfe_u32 v1, v0, 16, 1
	v_add3_u32 v0, v0, v1, s59
	ds_write_b16_d16_hi v72, v0 offset:512
	v_mul_f32_e32 v0, v18, v98
	v_bfe_u32 v1, v0, 16, 1
	v_add3_u32 v0, v0, v1, s59
	ds_write_b16_d16_hi v72, v0 offset:576
	v_mul_f32_e32 v0, v34, v98
	v_bfe_u32 v1, v0, 16, 1
	v_add3_u32 v0, v0, v1, s59
	ds_write_b16_d16_hi v72, v0 offset:640
	v_mul_f32_e32 v0, v50, v98
	v_bfe_u32 v1, v0, 16, 1
	v_add3_u32 v0, v0, v1, s59
	ds_write_b16_d16_hi v72, v0 offset:704
	v_mul_f32_e32 v0, v3, v99
	v_bfe_u32 v1, v0, 16, 1
	v_add3_u32 v0, v0, v1, s59
	ds_write_b16_d16_hi v72, v0 offset:768
	v_mul_f32_e32 v0, v19, v99
	v_bfe_u32 v1, v0, 16, 1
	v_add3_u32 v0, v0, v1, s59
	ds_write_b16_d16_hi v72, v0 offset:832
	v_mul_f32_e32 v0, v35, v99
	v_bfe_u32 v1, v0, 16, 1
	v_add3_u32 v0, v0, v1, s59
	ds_write_b16_d16_hi v72, v0 offset:896
	v_mul_f32_e32 v0, v51, v99
	v_bfe_u32 v1, v0, 16, 1
	v_add3_u32 v0, v0, v1, s59
	ds_write_b16_d16_hi v72, v0 offset:960
	v_mul_f32_e32 v0, v4, v92
	v_bfe_u32 v1, v0, 16, 1
	v_add3_u32 v0, v0, v1, s59
	ds_write_b16_d16_hi v72, v0 offset:2048
	v_mul_f32_e32 v0, v20, v92
	v_bfe_u32 v1, v0, 16, 1
	v_add3_u32 v0, v0, v1, s59
	ds_write_b16_d16_hi v72, v0 offset:2112
	v_mul_f32_e32 v0, v36, v92
	v_bfe_u32 v1, v0, 16, 1
	v_add3_u32 v0, v0, v1, s59
	ds_write_b16_d16_hi v72, v0 offset:2176
	v_mul_f32_e32 v0, v52, v92
	v_bfe_u32 v1, v0, 16, 1
	v_add3_u32 v0, v0, v1, s59
	ds_write_b16_d16_hi v72, v0 offset:2240
	v_mul_f32_e32 v0, v5, v93
	v_bfe_u32 v1, v0, 16, 1
	v_add3_u32 v0, v0, v1, s59
	ds_write_b16_d16_hi v72, v0 offset:2304
	v_mul_f32_e32 v0, v21, v93
	v_bfe_u32 v1, v0, 16, 1
	v_add3_u32 v0, v0, v1, s59
	ds_write_b16_d16_hi v72, v0 offset:2368
	v_mul_f32_e32 v0, v37, v93
	v_bfe_u32 v1, v0, 16, 1
	v_add3_u32 v0, v0, v1, s59
	ds_write_b16_d16_hi v72, v0 offset:2432
	v_mul_f32_e32 v0, v53, v93
	v_bfe_u32 v1, v0, 16, 1
	v_add3_u32 v0, v0, v1, s59
	ds_write_b16_d16_hi v72, v0 offset:2496
	v_mul_f32_e32 v0, v6, v94
	v_bfe_u32 v1, v0, 16, 1
	v_add3_u32 v0, v0, v1, s59
	ds_write_b16_d16_hi v72, v0 offset:2560
	v_mul_f32_e32 v0, v22, v94
	v_bfe_u32 v1, v0, 16, 1
	v_add3_u32 v0, v0, v1, s59
	ds_write_b16_d16_hi v72, v0 offset:2624
	v_mul_f32_e32 v0, v38, v94
	v_bfe_u32 v1, v0, 16, 1
	v_add3_u32 v0, v0, v1, s59
	ds_write_b16_d16_hi v72, v0 offset:2688
	v_mul_f32_e32 v0, v54, v94
	v_bfe_u32 v1, v0, 16, 1
	v_add3_u32 v0, v0, v1, s59
	ds_write_b16_d16_hi v72, v0 offset:2752
	v_mul_f32_e32 v0, v7, v84
	v_bfe_u32 v1, v0, 16, 1
	v_add3_u32 v0, v0, v1, s59
	ds_write_b16_d16_hi v72, v0 offset:2816
	v_mul_f32_e32 v0, v23, v84
	v_bfe_u32 v1, v0, 16, 1
	v_add3_u32 v0, v0, v1, s59
	ds_write_b16_d16_hi v72, v0 offset:2880
	v_mul_f32_e32 v0, v39, v84
	v_bfe_u32 v1, v0, 16, 1
	v_add3_u32 v0, v0, v1, s59
	ds_write_b16_d16_hi v72, v0 offset:2944
	v_mul_f32_e32 v0, v55, v84
	v_bfe_u32 v1, v0, 16, 1
	v_add3_u32 v0, v0, v1, s59
	ds_write_b16_d16_hi v72, v0 offset:3008
	v_mul_f32_e32 v0, v8, v85
	v_bfe_u32 v1, v0, 16, 1
	v_add3_u32 v0, v0, v1, s59
	ds_write_b16_d16_hi v72, v0 offset:4096
	v_mul_f32_e32 v0, v24, v85
	v_bfe_u32 v1, v0, 16, 1
	v_add3_u32 v0, v0, v1, s59
	ds_write_b16_d16_hi v72, v0 offset:4160
	v_mul_f32_e32 v0, v40, v85
	v_bfe_u32 v1, v0, 16, 1
	v_add3_u32 v0, v0, v1, s59
	ds_write_b16_d16_hi v72, v0 offset:4224
	v_mul_f32_e32 v0, v56, v85
	v_bfe_u32 v1, v0, 16, 1
	v_add3_u32 v0, v0, v1, s59
	ds_write_b16_d16_hi v72, v0 offset:4288
	v_mul_f32_e32 v0, v9, v86
	v_bfe_u32 v1, v0, 16, 1
	v_add3_u32 v0, v0, v1, s59
	ds_write_b16_d16_hi v72, v0 offset:4352
	v_mul_f32_e32 v0, v25, v86
	v_bfe_u32 v1, v0, 16, 1
	v_add3_u32 v0, v0, v1, s59
	ds_write_b16_d16_hi v72, v0 offset:4416
	v_mul_f32_e32 v0, v41, v86
	v_bfe_u32 v1, v0, 16, 1
	v_add3_u32 v0, v0, v1, s59
	ds_write_b16_d16_hi v72, v0 offset:4480
	v_mul_f32_e32 v0, v57, v86
	v_bfe_u32 v1, v0, 16, 1
	v_add3_u32 v0, v0, v1, s59
	ds_write_b16_d16_hi v72, v0 offset:4544
	v_mul_f32_e32 v0, v10, v87
	v_bfe_u32 v1, v0, 16, 1
	v_add3_u32 v0, v0, v1, s59
	ds_write_b16_d16_hi v72, v0 offset:4608
	v_mul_f32_e32 v0, v26, v87
	v_bfe_u32 v1, v0, 16, 1
	v_add3_u32 v0, v0, v1, s59
	ds_write_b16_d16_hi v72, v0 offset:4672
	v_mul_f32_e32 v0, v42, v87
	v_bfe_u32 v1, v0, 16, 1
	v_add3_u32 v0, v0, v1, s59
	ds_write_b16_d16_hi v72, v0 offset:4736
	v_mul_f32_e32 v0, v58, v87
	v_bfe_u32 v1, v0, 16, 1
	v_add3_u32 v0, v0, v1, s59
	ds_write_b16_d16_hi v72, v0 offset:4800
	v_mul_f32_e32 v0, v11, v88
	v_bfe_u32 v1, v0, 16, 1
	v_add3_u32 v0, v0, v1, s59
	ds_write_b16_d16_hi v72, v0 offset:4864
	v_mul_f32_e32 v0, v27, v88
	v_bfe_u32 v1, v0, 16, 1
	v_add3_u32 v0, v0, v1, s59
	ds_write_b16_d16_hi v72, v0 offset:4928
	v_mul_f32_e32 v0, v43, v88
	v_bfe_u32 v1, v0, 16, 1
	v_add3_u32 v0, v0, v1, s59
	ds_write_b16_d16_hi v72, v0 offset:4992
	v_mul_f32_e32 v0, v59, v88
	v_bfe_u32 v1, v0, 16, 1
	v_add3_u32 v0, v0, v1, s59
	ds_write_b16_d16_hi v72, v0 offset:5056
	v_mul_f32_e32 v0, v12, v80
	v_bfe_u32 v1, v0, 16, 1
	v_add3_u32 v0, v0, v1, s59
	ds_write_b16_d16_hi v72, v0 offset:6144
	v_mul_f32_e32 v0, v28, v80
	v_bfe_u32 v1, v0, 16, 1
	v_add3_u32 v0, v0, v1, s59
	ds_write_b16_d16_hi v72, v0 offset:6208
	v_mul_f32_e32 v0, v44, v80
	v_bfe_u32 v1, v0, 16, 1
	v_add3_u32 v0, v0, v1, s59
	ds_write_b16_d16_hi v72, v0 offset:6272
	v_mul_f32_e32 v0, v60, v80
	v_bfe_u32 v1, v0, 16, 1
	v_add3_u32 v0, v0, v1, s59
	ds_write_b16_d16_hi v72, v0 offset:6336
	v_mul_f32_e32 v0, v13, v81
	v_bfe_u32 v1, v0, 16, 1
	v_add3_u32 v0, v0, v1, s59
	ds_write_b16_d16_hi v72, v0 offset:6400
	v_mul_f32_e32 v0, v29, v81
	v_bfe_u32 v1, v0, 16, 1
	v_add3_u32 v0, v0, v1, s59
	ds_write_b16_d16_hi v72, v0 offset:6464
	v_mul_f32_e32 v0, v45, v81
	v_bfe_u32 v1, v0, 16, 1
	v_add3_u32 v0, v0, v1, s59
	ds_write_b16_d16_hi v72, v0 offset:6528
	v_mul_f32_e32 v0, v61, v81
	v_bfe_u32 v1, v0, 16, 1
	v_add3_u32 v0, v0, v1, s59
	ds_write_b16_d16_hi v72, v0 offset:6592
	v_mul_f32_e32 v0, v14, v82
	v_bfe_u32 v1, v0, 16, 1
	v_add3_u32 v0, v0, v1, s59
	ds_write_b16_d16_hi v72, v0 offset:6656
	v_mul_f32_e32 v0, v30, v82
	v_bfe_u32 v1, v0, 16, 1
	v_add3_u32 v0, v0, v1, s59
	ds_write_b16_d16_hi v72, v0 offset:6720
	v_mul_f32_e32 v0, v46, v82
	v_bfe_u32 v1, v0, 16, 1
	v_add3_u32 v0, v0, v1, s59
	ds_write_b16_d16_hi v72, v0 offset:6784
	v_mul_f32_e32 v0, v62, v82
	v_bfe_u32 v1, v0, 16, 1
	v_add3_u32 v0, v0, v1, s59
	ds_write_b16_d16_hi v72, v0 offset:6848
	v_mul_f32_e32 v0, v15, v83
	v_bfe_u32 v1, v0, 16, 1
	v_add3_u32 v0, v0, v1, s59
	ds_write_b16_d16_hi v72, v0 offset:6912
	v_mul_f32_e32 v0, v31, v83
	v_bfe_u32 v1, v0, 16, 1
	v_add3_u32 v0, v0, v1, s59
	ds_write_b16_d16_hi v72, v0 offset:6976
	v_mul_f32_e32 v0, v47, v83
	v_bfe_u32 v1, v0, 16, 1
	v_add3_u32 v0, v0, v1, s59
	ds_write_b16_d16_hi v72, v0 offset:7040
	v_mul_f32_e32 v0, v63, v83
	v_bfe_u32 v1, v0, 16, 1
	v_add3_u32 v0, v0, v1, s59
	ds_write_b16_d16_hi v72, v0 offset:7104
	v_lshlrev_b32_e32 v0, 4, v192
	v_and_b32_e32 v184, 0xf0, v0
	v_add_u32_e32 v12, s4, v184
	v_lshl_add_u64 v[0:1], s[2:3], 0, v[184:185]
	v_lshrrev_b32_e32 v13, 4, v193
	s_waitcnt lgkmcnt(0)
	v_lshl_add_u64 v[8:9], v[0:1], 0, s[40:41]
	v_lshl_add_u32 v0, v13, 8, v12
	v_or_b32_e32 v14, 4, v13
	ds_read_b128 v[0:3], v0
	v_lshl_add_u32 v4, v14, 8, v12
	ds_read_b128 v[4:7], v4
	v_lshlrev_b32_e32 v184, 11, v13
	v_lshl_add_u64 v[10:11], v[8:9], 0, v[184:185]
	v_lshlrev_b32_e32 v184, 11, v14
	s_waitcnt lgkmcnt(1)
	global_store_dwordx4 v[10:11], v[0:3], off nt
	v_or_b32_e32 v14, 12, v13
	s_mov_b64 s[4:5], 0
	v_lshl_add_u64 v[0:1], v[8:9], 0, v[184:185]
	s_waitcnt lgkmcnt(0)
	global_store_dwordx4 v[0:1], v[4:7], off nt
	s_nop 1
	v_or_b32_e32 v4, 8, v13
	v_lshl_add_u32 v0, v4, 8, v12
	ds_read_b128 v[0:3], v0
	v_lshlrev_b32_e32 v184, 11, v4
	v_lshl_add_u32 v4, v14, 8, v12
	ds_read_b128 v[4:7], v4
	v_lshl_add_u64 v[10:11], v[8:9], 0, v[184:185]
	v_lshlrev_b32_e32 v184, 11, v14
	s_waitcnt lgkmcnt(1)
	global_store_dwordx4 v[10:11], v[0:3], off nt
	v_or_b32_e32 v14, 20, v13
	s_nop 0
	v_lshl_add_u64 v[0:1], v[8:9], 0, v[184:185]
	s_waitcnt lgkmcnt(0)
	global_store_dwordx4 v[0:1], v[4:7], off nt
	s_nop 1
	v_or_b32_e32 v4, 16, v13
	v_lshl_add_u32 v0, v4, 8, v12
	ds_read_b128 v[0:3], v0
	v_lshlrev_b32_e32 v184, 11, v4
	v_lshl_add_u32 v4, v14, 8, v12
	ds_read_b128 v[4:7], v4
	v_lshl_add_u64 v[10:11], v[8:9], 0, v[184:185]
	v_lshlrev_b32_e32 v184, 11, v14
	s_waitcnt lgkmcnt(1)
	global_store_dwordx4 v[10:11], v[0:3], off nt
	s_nop 1
	v_lshl_add_u64 v[0:1], v[8:9], 0, v[184:185]
	s_waitcnt lgkmcnt(0)
	global_store_dwordx4 v[0:1], v[4:7], off nt
	s_nop 1
	v_or_b32_e32 v4, 24, v13
	v_lshl_add_u32 v0, v4, 8, v12
	v_or_b32_e32 v13, 28, v13
	ds_read_b128 v[0:3], v0
	v_lshlrev_b32_e32 v184, 11, v4
	v_lshl_add_u32 v4, v13, 8, v12
	ds_read_b128 v[4:7], v4
	v_lshl_add_u64 v[10:11], v[8:9], 0, v[184:185]
	v_lshlrev_b32_e32 v184, 11, v13
	s_waitcnt lgkmcnt(1)
	global_store_dwordx4 v[10:11], v[0:3], off nt
	s_nop 1
	v_lshl_add_u64 v[0:1], v[8:9], 0, v[184:185]
	s_waitcnt lgkmcnt(0)
	global_store_dwordx4 v[0:1], v[4:7], off nt
	s_barrier

.LBB0_2613:
	s_or_b64 exec, exec, s[22:23]
	v_lshlrev_b32_e32 v46, 2, v22
	global_load_dwordx4 v[22:25], v46, s[12:13]
	global_load_dwordx4 v[26:29], v46, s[18:19]
	global_load_dwordx4 v[30:33], v46, s[12:13] offset:16
	global_load_dwordx4 v[34:37], v46, s[18:19] offset:16
	global_load_dwordx4 v[38:41], v46, s[16:17]
	global_load_dwordx4 v[42:45], v46, s[16:17] offset:16
	s_waitcnt vmcnt(6)
	v_lshlrev_b32_e32 v52, 16, v4
	v_lshlrev_b32_e32 v53, 16, v0
	v_lshlrev_b32_e32 v47, 16, v12
	v_lshlrev_b32_e32 v46, 16, v8
	v_and_b32_e32 v54, 0xffff0000, v4
	v_and_b32_e32 v55, 0xffff0000, v0
	v_and_b32_e32 v49, 0xffff0000, v12
	v_and_b32_e32 v48, 0xffff0000, v8
	v_lshlrev_b32_e32 v56, 16, v5
	v_lshlrev_b32_e32 v57, 16, v1
	v_lshlrev_b32_e32 v50, 16, v9
	v_lshlrev_b32_e32 v51, 16, v13
	v_and_b32_e32 v58, 0xffff0000, v5
	v_and_b32_e32 v59, 0xffff0000, v1
	v_and_b32_e32 v1, 0xffff0000, v13
	v_and_b32_e32 v0, 0xffff0000, v9
	v_lshlrev_b32_e32 v60, 16, v6
	v_lshlrev_b32_e32 v61, 16, v2
	v_lshlrev_b32_e32 v5, 16, v14
	v_lshlrev_b32_e32 v4, 16, v10
	v_and_b32_e32 v62, 0xffff0000, v6
	v_and_b32_e32 v63, 0xffff0000, v2
	v_and_b32_e32 v9, 0xffff0000, v14
	v_and_b32_e32 v8, 0xffff0000, v10
	v_lshlrev_b32_e32 v64, 16, v7
	v_lshlrev_b32_e32 v65, 16, v3
	v_lshlrev_b32_e32 v12, 16, v11
	v_lshlrev_b32_e32 v13, 16, v15
	v_and_b32_e32 v66, 0xffff0000, v7
	v_and_b32_e32 v67, 0xffff0000, v3
	v_and_b32_e32 v3, 0xffff0000, v15
	v_and_b32_e32 v2, 0xffff0000, v11
	v_lshlrev_b64 v[18:19], 10, v[18:19]
	v_add_u32_e32 v20, s26, v20
	v_cmp_lt_i32_e32 vcc, s29, v20
	s_or_b64 s[20:21], vcc, s[20:21]
	v_add_u32_e32 v21, s27, v21
	s_waitcnt vmcnt(5)
	v_mov_b32_e32 v6, v22
	s_waitcnt vmcnt(4)
	v_mov_b32_e32 v7, v26
	v_mov_b32_e32 v26, v23
	v_mov_b32_e32 v11, v28
	v_mov_b32_e32 v28, v25
	s_waitcnt vmcnt(3)
	v_mov_b32_e32 v14, v30
	s_waitcnt vmcnt(2)
	v_mov_b32_e32 v15, v34
	v_mov_b32_e32 v34, v31
	v_mov_b32_e32 v22, v32
	v_mov_b32_e32 v23, v36
	v_mov_b32_e32 v10, v24
	v_mov_b32_e32 v36, v33
	v_pk_mul_f32 v[6:7], v[6:7], v[46:47]
	v_pk_mul_f32 v[0:1], v[28:29], v[0:1]
	v_pk_mul_f32 v[4:5], v[14:15], v[4:5]
	v_pk_mul_f32 v[8:9], v[34:35], v[8:9]
	v_pk_mul_f32 v[12:13], v[22:23], v[12:13]
	v_pk_mul_f32 v[24:25], v[26:27], v[48:49]
	v_pk_mul_f32 v[10:11], v[10:11], v[50:51]
	v_pk_mul_f32 v[2:3], v[36:37], v[2:3]
	s_waitcnt vmcnt(1)
	v_fma_f32 v6, v38, v53, v6
	v_fma_f32 v0, v41, v59, v0
	s_waitcnt vmcnt(0)
	v_fma_f32 v4, v42, v61, v4
	v_fma_f32 v8, v43, v63, v8
	v_fma_f32 v12, v44, v65, v12
	v_fma_f32 v14, v39, v55, v24
	v_fma_f32 v10, v40, v57, v10
	v_fma_f32 v2, v45, v67, v2
	v_add_f32_e32 v6, v6, v7
	v_add_f32_e32 v0, v0, v1
	v_add_f32_e32 v1, v4, v5
	v_add_f32_e32 v4, v8, v9
	v_add_f32_e32 v5, v12, v13
	v_add_f32_e32 v7, v14, v25
	v_add_f32_e32 v10, v10, v11
	v_add_f32_e32 v2, v2, v3
	v_mul_f32_e32 v3, v6, v52
	v_mul_f32_e32 v4, v4, v62
	v_mul_f32_e32 v5, v5, v64
	v_mul_f32_e32 v6, v7, v54
	v_mul_f32_e32 v7, v10, v56
	v_mul_f32_e32 v8, v0, v58
	v_mul_f32_e32 v9, v1, v60
	v_mul_f32_e32 v10, v2, v66
	v_cvt_pk_bf16_f32 v0, v3, v6
	v_cvt_pk_bf16_f32 v2, v9, v4
	v_cvt_pk_bf16_f32 v3, v5, v10
	v_lshl_add_u64 v[4:5], v[18:19], 1, s[14:15]
	v_lshl_add_u64 v[4:5], v[4:5], 0, v[16:17]
	v_cvt_pk_bf16_f32 v1, v7, v8
	global_store_dwordx4 v[4:5], v[0:3], off nt
	s_andn2_b64 exec, exec, s[20:21]
	s_cbranch_execz .LBB0_2618

.LBB0_3212:
	ds_read2_b32 v[214:215], v146 offset1:32
	s_add_i32 s44, s44, s29
	s_add_i32 s28, s28, s29
	s_add_i32 s54, s54, s29
	s_add_i32 s55, s55, s56
	s_waitcnt vmcnt(0) lgkmcnt(0)
	v_mul_f32_e32 v77, v68, v214
	ds_read_b32 v209, v147
	ds_read_b32 v211, v148
	ds_read_b32 v212, v149
	ds_read_b32 v213, v150
	ds_read_b32 v214, v151
	ds_read_b32 v216, v152
	ds_read_b32 v217, v153
	ds_read_b32 v218, v154
	s_waitcnt lgkmcnt(7)
	v_mul_f32_e32 v209, v69, v209
	v_cvt_pk_bf16_f32 v210, v77, v209
	s_waitcnt lgkmcnt(6)
	v_mul_f32_e32 v77, v70, v211
	s_waitcnt lgkmcnt(5)
	v_mul_f32_e32 v209, v71, v212
	v_cvt_pk_bf16_f32 v211, v77, v209
	s_waitcnt lgkmcnt(4)
	v_mul_f32_e32 v77, v64, v213
	s_waitcnt lgkmcnt(3)
	v_mul_f32_e32 v209, v65, v214
	v_cvt_pk_bf16_f32 v212, v77, v209
	s_waitcnt lgkmcnt(2)
	v_mul_f32_e32 v77, v66, v216
	s_waitcnt lgkmcnt(1)
	v_mul_f32_e32 v209, v67, v217
	v_cvt_pk_bf16_f32 v213, v77, v209
	v_add_u32_e32 v77, s27, v138
	v_mad_i64_i32 v[216:217], s[6:7], s26, v77, 0
	v_lshl_add_u64 v[216:217], v[216:217], 1, s[2:3]
	s_lshl_b64 s[6:7], s[8:9], 1
	v_lshl_add_u64 v[216:217], v[216:217], 0, s[6:7]
	v_lshl_add_u64 v[216:217], v[216:217], 0, v[72:73]
	global_store_dwordx4 v[216:217], v[210:213], off nt
	s_waitcnt lgkmcnt(0)
	v_mul_f32_e32 v77, v68, v218
	ds_read_b32 v209, v155
	ds_read_b32 v211, v156
	ds_read_b32 v212, v157
	ds_read_b32 v213, v158
	ds_read_b32 v214, v159
	ds_read_b32 v216, v160
	ds_read_b32 v217, v161
	ds_read_b32 v218, v162
	s_waitcnt lgkmcnt(7)
	v_mul_f32_e32 v209, v69, v209
	v_cvt_pk_bf16_f32 v210, v77, v209
	s_waitcnt lgkmcnt(6)
	v_mul_f32_e32 v77, v70, v211
	s_waitcnt lgkmcnt(5)
	v_mul_f32_e32 v209, v71, v212
	v_cvt_pk_bf16_f32 v211, v77, v209
	s_waitcnt lgkmcnt(4)
	v_mul_f32_e32 v77, v64, v213
	s_waitcnt lgkmcnt(3)
	v_mul_f32_e32 v209, v65, v214
	v_cvt_pk_bf16_f32 v212, v77, v209
	s_waitcnt lgkmcnt(2)
	v_mul_f32_e32 v77, v66, v216
	s_waitcnt lgkmcnt(1)
	v_mul_f32_e32 v209, v67, v217
	v_cvt_pk_bf16_f32 v213, v77, v209
	v_add_u32_e32 v77, s27, v139
	v_mad_i64_i32 v[216:217], s[8:9], s26, v77, 0
	v_lshl_add_u64 v[216:217], v[216:217], 1, s[2:3]
	v_lshl_add_u64 v[216:217], v[216:217], 0, s[6:7]
	v_lshl_add_u64 v[216:217], v[216:217], 0, v[72:73]
	global_store_dwordx4 v[216:217], v[210:213], off nt
	s_waitcnt lgkmcnt(0)
	v_mul_f32_e32 v77, v68, v218
	ds_read_b32 v209, v163
	ds_read_b32 v211, v164
	ds_read_b32 v212, v165
	ds_read_b32 v213, v166
	ds_read_b32 v214, v167
	ds_read_b32 v216, v168
	ds_read_b32 v217, v169
	ds_read_b32 v218, v170
	s_waitcnt lgkmcnt(7)
	v_mul_f32_e32 v209, v69, v209
	v_cvt_pk_bf16_f32 v210, v77, v209
	s_waitcnt lgkmcnt(6)
	v_mul_f32_e32 v77, v70, v211
	s_waitcnt lgkmcnt(5)
	v_mul_f32_e32 v209, v71, v212
	v_cvt_pk_bf16_f32 v211, v77, v209
	s_waitcnt lgkmcnt(4)
	v_mul_f32_e32 v77, v64, v213
	s_waitcnt lgkmcnt(3)
	v_mul_f32_e32 v209, v65, v214
	v_cvt_pk_bf16_f32 v212, v77, v209
	s_waitcnt lgkmcnt(2)
	v_mul_f32_e32 v77, v66, v216
	s_waitcnt lgkmcnt(1)
	v_mul_f32_e32 v209, v67, v217
	v_cvt_pk_bf16_f32 v213, v77, v209
	v_add_u32_e32 v77, s27, v140
	v_mad_i64_i32 v[216:217], s[8:9], s26, v77, 0
	v_lshl_add_u64 v[216:217], v[216:217], 1, s[2:3]
	v_lshl_add_u64 v[216:217], v[216:217], 0, s[6:7]
	v_lshl_add_u64 v[216:217], v[216:217], 0, v[72:73]
	global_store_dwordx4 v[216:217], v[210:213], off nt
	s_waitcnt lgkmcnt(0)
	v_mul_f32_e32 v77, v68, v218
	ds_read_b32 v209, v171
	ds_read_b32 v211, v172
	ds_read_b32 v212, v173
	ds_read_b32 v213, v174
	ds_read_b32 v214, v175
	ds_read_b32 v216, v176
	ds_read_b32 v217, v177
	ds_read_b32 v218, v178
	s_waitcnt lgkmcnt(7)
	v_mul_f32_e32 v209, v69, v209
	v_cvt_pk_bf16_f32 v210, v77, v209
	s_waitcnt lgkmcnt(6)
	v_mul_f32_e32 v77, v70, v211
	s_waitcnt lgkmcnt(5)
	v_mul_f32_e32 v209, v71, v212
	v_cvt_pk_bf16_f32 v211, v77, v209
	s_waitcnt lgkmcnt(4)
	v_mul_f32_e32 v77, v64, v213
	s_waitcnt lgkmcnt(3)
	v_mul_f32_e32 v209, v65, v214
	v_cvt_pk_bf16_f32 v212, v77, v209
	s_waitcnt lgkmcnt(2)
	v_mul_f32_e32 v77, v66, v216
	s_waitcnt lgkmcnt(1)
	v_mul_f32_e32 v209, v67, v217
	v_cvt_pk_bf16_f32 v213, v77, v209
	v_add_u32_e32 v77, s27, v141
	v_mad_i64_i32 v[216:217], s[8:9], s26, v77, 0
	v_lshl_add_u64 v[216:217], v[216:217], 1, s[2:3]
	v_lshl_add_u64 v[216:217], v[216:217], 0, s[6:7]
	v_lshl_add_u64 v[216:217], v[216:217], 0, v[72:73]
	global_store_dwordx4 v[216:217], v[210:213], off nt
	v_mul_f32_e32 v77, v68, v215
	s_waitcnt lgkmcnt(0)
	v_mul_f32_e32 v209, v69, v218
	v_cvt_pk_bf16_f32 v210, v77, v209
	ds_read_b32 v77, v179
	ds_read_b32 v209, v180
	ds_read_b32 v212, v181
	ds_read_b32 v213, v182
	ds_read_b32 v214, v183
	ds_read_b32 v215, v184
	ds_read_b32 v216, v185
	ds_read_b32 v217, v186
	s_waitcnt lgkmcnt(7)
	v_mul_f32_e32 v77, v70, v77
	s_waitcnt lgkmcnt(6)
	v_mul_f32_e32 v209, v71, v209
	v_cvt_pk_bf16_f32 v211, v77, v209
	s_waitcnt lgkmcnt(5)
	v_mul_f32_e32 v77, v64, v212
	s_waitcnt lgkmcnt(4)
	v_mul_f32_e32 v209, v65, v213
	v_cvt_pk_bf16_f32 v212, v77, v209
	s_waitcnt lgkmcnt(3)
	v_mul_f32_e32 v77, v66, v214
	s_waitcnt lgkmcnt(2)
	v_mul_f32_e32 v209, v67, v215
	v_cvt_pk_bf16_f32 v213, v77, v209
	v_add_u32_e32 v77, s27, v142
	v_mad_i64_i32 v[214:215], s[8:9], s26, v77, 0
	v_lshl_add_u64 v[214:215], v[214:215], 1, s[2:3]
	v_lshl_add_u64 v[214:215], v[214:215], 0, s[6:7]
	v_lshl_add_u64 v[214:215], v[214:215], 0, v[72:73]
	global_store_dwordx4 v[214:215], v[210:213], off nt
	s_waitcnt lgkmcnt(1)
	v_mul_f32_e32 v77, v68, v216
	s_waitcnt lgkmcnt(0)
	v_mul_f32_e32 v209, v69, v217
	v_cvt_pk_bf16_f32 v210, v77, v209
	ds_read_b32 v77, v187
	ds_read_b32 v209, v188
	ds_read_b32 v212, v189
	ds_read_b32 v213, v190
	ds_read_b32 v214, v191
	ds_read_b32 v215, v192
	ds_read_b32 v216, v193
	ds_read_b32 v217, v194
	s_waitcnt lgkmcnt(7)
	v_mul_f32_e32 v77, v70, v77
	s_waitcnt lgkmcnt(6)
	v_mul_f32_e32 v209, v71, v209
	v_cvt_pk_bf16_f32 v211, v77, v209
	s_waitcnt lgkmcnt(5)
	v_mul_f32_e32 v77, v64, v212
	s_waitcnt lgkmcnt(4)
	v_mul_f32_e32 v209, v65, v213
	v_cvt_pk_bf16_f32 v212, v77, v209
	s_waitcnt lgkmcnt(3)
	v_mul_f32_e32 v77, v66, v214
	s_waitcnt lgkmcnt(2)
	v_mul_f32_e32 v209, v67, v215
	v_cvt_pk_bf16_f32 v213, v77, v209
	v_add_u32_e32 v77, s27, v143
	v_mad_i64_i32 v[214:215], s[8:9], s26, v77, 0
	v_lshl_add_u64 v[214:215], v[214:215], 1, s[2:3]
	v_lshl_add_u64 v[214:215], v[214:215], 0, s[6:7]
	v_lshl_add_u64 v[214:215], v[214:215], 0, v[72:73]
	global_store_dwordx4 v[214:215], v[210:213], off nt
	s_waitcnt lgkmcnt(1)
	v_mul_f32_e32 v77, v68, v216
	s_waitcnt lgkmcnt(0)
	v_mul_f32_e32 v209, v69, v217
	v_cvt_pk_bf16_f32 v210, v77, v209
	ds_read_b32 v77, v195
	ds_read_b32 v209, v196
	ds_read_b32 v212, v197
	ds_read_b32 v213, v198
	ds_read_b32 v214, v199
	ds_read_b32 v215, v200
	ds_read_b32 v216, v201
	ds_read_b32 v217, v202
	s_waitcnt lgkmcnt(7)
	v_mul_f32_e32 v77, v70, v77
	s_waitcnt lgkmcnt(6)
	v_mul_f32_e32 v209, v71, v209
	v_cvt_pk_bf16_f32 v211, v77, v209
	s_waitcnt lgkmcnt(5)
	v_mul_f32_e32 v77, v64, v212
	s_waitcnt lgkmcnt(4)
	v_mul_f32_e32 v209, v65, v213
	v_cvt_pk_bf16_f32 v212, v77, v209
	s_waitcnt lgkmcnt(3)
	v_mul_f32_e32 v77, v66, v214
	s_waitcnt lgkmcnt(2)
	v_mul_f32_e32 v209, v67, v215
	v_cvt_pk_bf16_f32 v213, v77, v209
	v_add_u32_e32 v77, s27, v144
	v_mad_i64_i32 v[214:215], s[8:9], s26, v77, 0
	v_lshl_add_u64 v[214:215], v[214:215], 1, s[2:3]
	v_lshl_add_u64 v[214:215], v[214:215], 0, s[6:7]
	v_lshl_add_u64 v[214:215], v[214:215], 0, v[72:73]
	global_store_dwordx4 v[214:215], v[210:213], off nt
	ds_read_b32 v77, v203
	ds_read_b32 v209, v204
	ds_read_b32 v210, v205
	ds_read_b32 v211, v206
	ds_read_b32 v212, v207
	ds_read_b32 v213, v208
	s_waitcnt lgkmcnt(7)
	v_mul_f32_e32 v68, v68, v216
	s_waitcnt lgkmcnt(6)
	v_mul_f32_e32 v69, v69, v217
	v_cvt_pk_bf16_f32 v68, v68, v69
	s_waitcnt lgkmcnt(5)
	v_mul_f32_e32 v69, v70, v77
	s_waitcnt lgkmcnt(4)
	v_mul_f32_e32 v70, v71, v209
	s_waitcnt lgkmcnt(3)
	v_mul_f32_e32 v64, v64, v210
	v_cvt_pk_bf16_f32 v69, v69, v70
	s_waitcnt lgkmcnt(2)
	v_mul_f32_e32 v65, v65, v211
	v_cvt_pk_bf16_f32 v70, v64, v65
	s_waitcnt lgkmcnt(1)
	v_mul_f32_e32 v64, v66, v212
	s_waitcnt lgkmcnt(0)
	v_mul_f32_e32 v65, v67, v213
	v_cvt_pk_bf16_f32 v71, v64, v65
	v_add_u32_e32 v64, s27, v145
	v_mad_i64_i32 v[64:65], s[8:9], s26, v64, 0
	v_lshl_add_u64 v[64:65], v[64:65], 1, s[2:3]
	v_lshl_add_u64 v[64:65], v[64:65], 0, s[6:7]
	v_lshl_add_u64 v[64:65], v[64:65], 0, v[72:73]
	global_store_dwordx4 v[64:65], v[68:71], off nt
	s_waitcnt lgkmcnt(0)
	s_add_i32 s2, s53, s44
	s_cmpk_gt_i32 s2, 0x13ff
	s_mov_b32 s27, s24
	s_mov_b64 s[2:3], s[12:13]
	s_mov_b64 s[6:7], s[14:15]
	s_mov_b32 s26, s57
	s_mov_b32 s8, s18
	s_cbranch_scc1 .LBB0_3246

.LBB0_4358:
	v_add_u32_e32 v140, s64, v137
	v_ashrrev_i32_e32 v141, 31, v140
	v_lshl_add_u64 v[134:135], v[140:141], 2, s[16:17]
	global_load_dword v142, v[134:135], off
	v_mov_b32_e32 v162, v120
	v_add_u32_e32 v120, 16, v140
	v_mov_b32_e32 v163, v112
	v_mov_b32_e32 v112, v121
	v_ashrrev_i32_e32 v121, 31, v120
	v_lshl_add_u64 v[120:121], v[120:121], 2, s[16:17]
	global_load_dword v174, v[120:121], off
	v_mov_b32_e32 v160, v124
	v_mov_b32_e32 v164, v126
	v_mov_b32_e32 v166, v122
	v_add_u32_e32 v122, 32, v140
	v_add_u32_e32 v124, 48, v140
	v_add_u32_e32 v126, 0x80, v140
	v_mov_b32_e32 v161, v116
	v_mov_b32_e32 v116, v125
	v_mov_b32_e32 v165, v118
	v_mov_b32_e32 v167, v114
	v_mov_b32_e32 v118, v127
	v_mov_b32_e32 v114, v123
	v_add_u32_e32 v168, 0x90, v140
	v_add_u32_e32 v170, 0xa0, v140
	v_add_u32_e32 v140, 0xb0, v140
	v_ashrrev_i32_e32 v123, 31, v122
	v_ashrrev_i32_e32 v125, 31, v124
	v_ashrrev_i32_e32 v127, 31, v126
	v_ashrrev_i32_e32 v169, 31, v168
	v_ashrrev_i32_e32 v171, 31, v170
	v_ashrrev_i32_e32 v141, 31, v140
	v_lshl_add_u64 v[120:121], v[122:123], 2, s[16:17]
	v_lshl_add_u64 v[122:123], v[124:125], 2, s[16:17]
	v_lshl_add_u64 v[124:125], v[126:127], 2, s[16:17]
	v_lshl_add_u64 v[168:169], v[168:169], 2, s[16:17]
	v_lshl_add_u64 v[170:171], v[170:171], 2, s[16:17]
	v_lshl_add_u64 v[140:141], v[140:141], 2, s[16:17]
	global_load_dword v136, v[120:121], off
	global_load_dword v132, v[122:123], off
	global_load_dword v126, v[124:125], off
	s_nop 0
	global_load_dword v124, v[168:169], off
	global_load_dword v122, v[170:171], off
	global_load_dword v120, v[140:141], off
	v_lshl_or_b32 v144, s28, 7, v151
	v_lshl_add_u32 v138, s63, 8, v137
	v_mov_b64_e32 v[134:135], s[14:15]
	v_ashrrev_i32_e32 v145, 31, v144
	v_mad_i64_i32 v[172:173], s[30:31], v138, s58, v[134:135]
	s_and_b64 vcc, exec, s[2:3]
	s_mov_b64 s[2:3], -1
	s_waitcnt vmcnt(0)
	v_pk_mul_f32 v[116:117], v[116:117], v[142:143] op_sel_hi:[1,0]
	v_pk_mul_f32 v[112:113], v[112:113], v[142:143] op_sel_hi:[1,0]
	v_mul_f32_e32 v125, 0xbfb8aa3b, v117
	v_mul_f32_e32 v127, 0xbfb8aa3b, v113
	v_exp_f32_e32 v125, v125
	v_exp_f32_e32 v127, v127
	v_pk_mul_f32 v[140:141], v[160:161], v[142:143] op_sel_hi:[1,0]
	v_pk_mul_f32 v[160:161], v[162:163], v[142:143] op_sel_hi:[1,0]
	v_pk_mul_f32 v[162:163], v[164:165], v[142:143] op_sel_hi:[1,0]
	v_pk_mul_f32 v[164:165], v[166:167], v[142:143] op_sel_hi:[1,0]
	v_pk_mul_f32 v[118:119], v[118:119], v[142:143] op_sel_hi:[1,0]
	v_pk_mul_f32 v[114:115], v[114:115], v[142:143] op_sel_hi:[1,0]
	v_mul_f32_e32 v121, 0xbfb8aa3b, v141
	v_mul_f32_e32 v143, 0xbfb8aa3b, v165
	v_add_f32_e32 v125, 1.0, v125
	v_add_f32_e32 v127, 1.0, v127
	v_mul_f32_e32 v159, 0xbfb8aa3b, v119
	v_exp_f32_e32 v121, v121
	v_exp_f32_e32 v143, v143
	v_rcp_f32_e32 v125, v125
	v_rcp_f32_e32 v127, v127
	v_mul_f32_e32 v166, 0xbfb8aa3b, v115
	v_exp_f32_e32 v159, v159
	v_mul_f32_e32 v142, 0xbfb8aa3b, v163
	v_exp_f32_e32 v166, v166
	v_mul_f32_e32 v123, 0xbfb8aa3b, v161
	v_exp_f32_e32 v142, v142
	v_exp_f32_e32 v123, v123
	v_add_f32_e32 v121, 1.0, v121
	v_add_f32_e32 v143, 1.0, v143
	v_mul_f32_e32 v117, v117, v125
	v_mul_f32_e32 v113, v113, v127
	v_rcp_f32_e32 v121, v121
	v_rcp_f32_e32 v143, v143
	v_mul_f32_e32 v116, v116, v117
	v_mul_f32_e32 v117, v112, v113
	v_add_f32_e32 v113, 1.0, v159
	v_rcp_f32_e32 v113, v113
	v_add_f32_e32 v127, 1.0, v166
	v_add_f32_e32 v142, 1.0, v142
	v_rcp_f32_e32 v127, v127
	v_add_f32_e32 v123, 1.0, v123
	v_rcp_f32_e32 v142, v142
	v_rcp_f32_e32 v123, v123
	v_mul_f32_e32 v121, v141, v121
	v_mul_f32_e32 v112, v165, v143
	v_mul_f32_e32 v121, v140, v121
	v_mul_f32_e32 v140, v164, v112
	v_mul_f32_e32 v112, v119, v113
	v_mul_f32_e32 v141, v118, v112
	v_mul_f32_e32 v112, v115, v127
	v_mul_f32_e32 v125, v163, v142
	v_mul_f32_e32 v127, v114, v112
	v_lshlrev_b64 v[112:113], 1, v[144:145]
	v_mul_f32_e32 v123, v161, v123
	v_mul_f32_e32 v125, v162, v125
	v_lshl_add_u64 v[118:119], v[172:173], 0, v[112:113]
	v_cvt_pk_bf16_f32 v114, v121, v116
	v_cvt_pk_bf16_f32 v115, v125, v141
	v_mul_f32_e32 v123, v160, v123
	v_cvt_pk_bf16_f32 v116, v123, v117
	v_cvt_pk_bf16_f32 v117, v140, v127
	global_store_dwordx4 v[118:119], v[114:117], off nt
	s_nop 1
	v_mov_b32_e32 v114, v100
	v_mov_b32_e32 v115, v108
	v_pk_mul_f32 v[114:115], v[114:115], v[174:175] op_sel_hi:[1,0]
	v_mov_b32_e32 v116, v96
	v_mul_f32_e32 v100, 0xbfb8aa3b, v115
	v_mov_b32_e32 v117, v104
	v_exp_f32_e32 v100, v100
	v_pk_mul_f32 v[116:117], v[116:117], v[174:175] op_sel_hi:[1,0]
	v_mov_b32_e32 v108, v101
	v_mul_f32_e32 v96, 0xbfb8aa3b, v117
	v_exp_f32_e32 v96, v96
	v_add_f32_e32 v100, 1.0, v100
	v_rcp_f32_e32 v100, v100
	v_or_b32_e32 v104, 16, v138
	v_add_f32_e32 v96, 1.0, v96
	v_rcp_f32_e32 v96, v96
	v_mul_f32_e32 v100, v115, v100
	v_mul_f32_e32 v114, v114, v100
	v_pk_mul_f32 v[100:101], v[108:109], v[174:175] op_sel_hi:[1,0]
	v_mad_i64_i32 v[118:119], s[30:31], v104, s58, v[134:135]
	v_mul_f32_e32 v115, v117, v96
	v_mul_f32_e32 v96, 0xbfb8aa3b, v101
	v_mov_b32_e32 v104, v97
	v_exp_f32_e32 v108, v96
	v_pk_mul_f32 v[96:97], v[104:105], v[174:175] op_sel_hi:[1,0]
	v_mul_f32_e32 v109, v116, v115
	v_mul_f32_e32 v104, 0xbfb8aa3b, v97
	v_exp_f32_e32 v104, v104
	v_add_f32_e32 v105, 1.0, v108
	v_rcp_f32_e32 v108, v105
	v_mov_b32_e32 v105, v110
	v_add_f32_e32 v104, 1.0, v104
	v_rcp_f32_e32 v115, v104
	v_mov_b32_e32 v104, v102
	v_pk_mul_f32 v[104:105], v[104:105], v[174:175] op_sel_hi:[1,0]
	v_mul_f32_e32 v101, v101, v108
	v_mul_f32_e32 v102, 0xbfb8aa3b, v105
	v_exp_f32_e32 v102, v102
	v_mul_f32_e32 v108, v100, v101
	v_mov_b32_e32 v101, v106
	v_mul_f32_e32 v97, v97, v115
	v_add_f32_e32 v100, 1.0, v102
	v_rcp_f32_e32 v102, v100
	v_mov_b32_e32 v100, v98
	v_pk_mul_f32 v[100:101], v[100:101], v[174:175] op_sel_hi:[1,0]
	v_mul_f32_e32 v115, v96, v97
	v_mul_f32_e32 v98, 0xbfb8aa3b, v101
	v_exp_f32_e32 v98, v98
	v_mul_f32_e32 v96, v105, v102
	v_mul_f32_e32 v102, v104, v96
	v_mov_b32_e32 v110, v103
	v_add_f32_e32 v96, 1.0, v98
	v_rcp_f32_e32 v104, v96
	v_pk_mul_f32 v[96:97], v[110:111], v[174:175] op_sel_hi:[1,0]
	v_mov_b32_e32 v106, v99
	v_mul_f32_e32 v98, 0xbfb8aa3b, v97
	v_exp_f32_e32 v103, v98
	v_pk_mul_f32 v[98:99], v[106:107], v[174:175] op_sel_hi:[1,0]
	v_mul_f32_e32 v101, v101, v104
	v_mul_f32_e32 v105, 0xbfb8aa3b, v99
	v_exp_f32_e32 v105, v105
	v_add_f32_e32 v103, 1.0, v103
	v_rcp_f32_e32 v103, v103
	v_add_f32_e32 v104, 1.0, v105
	v_rcp_f32_e32 v104, v104
	v_mul_f32_e32 v97, v97, v103
	v_mul_f32_e32 v97, v96, v97
	v_mul_f32_e32 v105, v100, v101
	v_mul_f32_e32 v96, v99, v104
	v_mul_f32_e32 v99, v98, v96
	v_lshl_add_u64 v[100:101], v[118:119], 0, v[112:113]
	v_cvt_pk_bf16_f32 v96, v114, v108
	v_cvt_pk_bf16_f32 v97, v102, v97
	v_cvt_pk_bf16_f32 v98, v109, v115
	v_cvt_pk_bf16_f32 v99, v105, v99
	global_store_dwordx4 v[100:101], v[96:99], off nt
	s_nop 1
	v_mov_b32_e32 v96, v84
	v_mov_b32_e32 v97, v92
	v_pk_mul_f32 v[96:97], v[96:97], v[136:137] op_sel_hi:[1,0]
	v_mov_b32_e32 v98, v80
	v_mul_f32_e32 v84, 0xbfb8aa3b, v97
	v_mov_b32_e32 v99, v88
	v_exp_f32_e32 v84, v84
	v_pk_mul_f32 v[98:99], v[98:99], v[136:137] op_sel_hi:[1,0]
	v_mov_b32_e32 v92, v85
	v_mul_f32_e32 v80, 0xbfb8aa3b, v99
	v_exp_f32_e32 v80, v80
	v_add_f32_e32 v84, 1.0, v84
	v_rcp_f32_e32 v84, v84
	v_or_b32_e32 v88, 32, v138
	v_add_f32_e32 v80, 1.0, v80
	v_rcp_f32_e32 v80, v80
	v_mul_f32_e32 v84, v97, v84
	v_mul_f32_e32 v96, v96, v84
	v_pk_mul_f32 v[84:85], v[92:93], v[136:137] op_sel_hi:[1,0]
	v_mad_i64_i32 v[100:101], s[30:31], v88, s58, v[134:135]
	v_mul_f32_e32 v97, v99, v80
	v_mul_f32_e32 v80, 0xbfb8aa3b, v85
	v_mov_b32_e32 v88, v81
	v_exp_f32_e32 v92, v80
	v_pk_mul_f32 v[80:81], v[88:89], v[136:137] op_sel_hi:[1,0]
	v_mul_f32_e32 v93, v98, v97
	v_mul_f32_e32 v88, 0xbfb8aa3b, v81
	v_exp_f32_e32 v88, v88
	v_add_f32_e32 v89, 1.0, v92
	v_rcp_f32_e32 v92, v89
	v_mov_b32_e32 v89, v94
	v_add_f32_e32 v88, 1.0, v88
	v_rcp_f32_e32 v97, v88
	v_mov_b32_e32 v88, v86
	v_pk_mul_f32 v[88:89], v[88:89], v[136:137] op_sel_hi:[1,0]
	v_mul_f32_e32 v85, v85, v92
	v_mul_f32_e32 v86, 0xbfb8aa3b, v89
	v_exp_f32_e32 v86, v86
	v_mul_f32_e32 v92, v84, v85
	v_mov_b32_e32 v85, v90
	v_mul_f32_e32 v81, v81, v97
	v_add_f32_e32 v84, 1.0, v86
	v_rcp_f32_e32 v86, v84
	v_mov_b32_e32 v84, v82
	v_pk_mul_f32 v[84:85], v[84:85], v[136:137] op_sel_hi:[1,0]
	v_mul_f32_e32 v97, v80, v81
	v_mul_f32_e32 v82, 0xbfb8aa3b, v85
	v_exp_f32_e32 v82, v82
	v_mul_f32_e32 v80, v89, v86
	v_mul_f32_e32 v86, v88, v80
	v_mov_b32_e32 v94, v87
	v_add_f32_e32 v80, 1.0, v82
	v_rcp_f32_e32 v88, v80
	v_pk_mul_f32 v[80:81], v[94:95], v[136:137] op_sel_hi:[1,0]
	v_mov_b32_e32 v90, v83
	v_mul_f32_e32 v82, 0xbfb8aa3b, v81
	v_exp_f32_e32 v87, v82
	v_pk_mul_f32 v[82:83], v[90:91], v[136:137] op_sel_hi:[1,0]
	v_mul_f32_e32 v85, v85, v88
	v_mul_f32_e32 v89, 0xbfb8aa3b, v83
	v_exp_f32_e32 v89, v89
	v_add_f32_e32 v87, 1.0, v87
	v_rcp_f32_e32 v87, v87
	v_add_f32_e32 v88, 1.0, v89
	v_rcp_f32_e32 v88, v88
	v_mul_f32_e32 v81, v81, v87
	v_mul_f32_e32 v81, v80, v81
	v_mul_f32_e32 v89, v84, v85
	v_mul_f32_e32 v80, v83, v88
	v_mul_f32_e32 v83, v82, v80
	v_lshl_add_u64 v[84:85], v[100:101], 0, v[112:113]
	v_cvt_pk_bf16_f32 v80, v96, v92
	v_cvt_pk_bf16_f32 v81, v86, v81
	v_cvt_pk_bf16_f32 v82, v93, v97
	v_cvt_pk_bf16_f32 v83, v89, v83
	global_store_dwordx4 v[84:85], v[80:83], off nt
	s_nop 1
	v_mov_b32_e32 v80, v68
	v_mov_b32_e32 v81, v76
	v_pk_mul_f32 v[80:81], v[80:81], v[132:133] op_sel_hi:[1,0]
	v_mov_b32_e32 v82, v64
	v_mul_f32_e32 v68, 0xbfb8aa3b, v81
	v_mov_b32_e32 v83, v72
	v_exp_f32_e32 v68, v68
	v_pk_mul_f32 v[82:83], v[82:83], v[132:133] op_sel_hi:[1,0]
	v_mov_b32_e32 v76, v69
	v_mul_f32_e32 v64, 0xbfb8aa3b, v83
	v_exp_f32_e32 v64, v64
	v_add_f32_e32 v68, 1.0, v68
	v_rcp_f32_e32 v68, v68
	v_or_b32_e32 v72, 48, v138
	v_add_f32_e32 v64, 1.0, v64
	v_rcp_f32_e32 v64, v64
	v_mul_f32_e32 v68, v81, v68
	v_mul_f32_e32 v80, v80, v68
	v_pk_mul_f32 v[68:69], v[76:77], v[132:133] op_sel_hi:[1,0]
	v_mad_i64_i32 v[84:85], s[30:31], v72, s58, v[134:135]
	v_mul_f32_e32 v81, v83, v64
	v_mul_f32_e32 v64, 0xbfb8aa3b, v69
	v_mov_b32_e32 v72, v65
	v_exp_f32_e32 v76, v64
	v_pk_mul_f32 v[64:65], v[72:73], v[132:133] op_sel_hi:[1,0]
	v_mul_f32_e32 v77, v82, v81
	v_mul_f32_e32 v72, 0xbfb8aa3b, v65
	v_exp_f32_e32 v72, v72
	v_add_f32_e32 v73, 1.0, v76
	v_rcp_f32_e32 v76, v73
	v_mov_b32_e32 v73, v78
	v_add_f32_e32 v72, 1.0, v72
	v_rcp_f32_e32 v81, v72
	v_mov_b32_e32 v72, v70
	v_pk_mul_f32 v[72:73], v[72:73], v[132:133] op_sel_hi:[1,0]
	v_mul_f32_e32 v69, v69, v76
	v_mul_f32_e32 v70, 0xbfb8aa3b, v73
	v_exp_f32_e32 v70, v70
	v_mul_f32_e32 v76, v68, v69
	v_mov_b32_e32 v69, v74
	v_mul_f32_e32 v65, v65, v81
	v_add_f32_e32 v68, 1.0, v70
	v_rcp_f32_e32 v70, v68
	v_mov_b32_e32 v68, v66
	v_pk_mul_f32 v[68:69], v[68:69], v[132:133] op_sel_hi:[1,0]
	v_mul_f32_e32 v81, v64, v65
	v_mul_f32_e32 v66, 0xbfb8aa3b, v69
	v_exp_f32_e32 v66, v66
	v_mul_f32_e32 v64, v73, v70
	v_mul_f32_e32 v70, v72, v64
	v_mov_b32_e32 v78, v71
	v_add_f32_e32 v64, 1.0, v66
	v_rcp_f32_e32 v72, v64
	v_pk_mul_f32 v[64:65], v[78:79], v[132:133] op_sel_hi:[1,0]
	v_mov_b32_e32 v74, v67
	v_mul_f32_e32 v66, 0xbfb8aa3b, v65
	v_exp_f32_e32 v71, v66
	v_pk_mul_f32 v[66:67], v[74:75], v[132:133] op_sel_hi:[1,0]
	v_mul_f32_e32 v69, v69, v72
	v_mul_f32_e32 v73, 0xbfb8aa3b, v67
	v_exp_f32_e32 v73, v73
	v_add_f32_e32 v71, 1.0, v71
	v_rcp_f32_e32 v71, v71
	v_add_f32_e32 v72, 1.0, v73
	v_rcp_f32_e32 v72, v72
	v_mul_f32_e32 v65, v65, v71
	v_mul_f32_e32 v65, v64, v65
	v_mul_f32_e32 v73, v68, v69
	v_mul_f32_e32 v64, v67, v72
	v_mul_f32_e32 v67, v66, v64
	v_lshl_add_u64 v[68:69], v[84:85], 0, v[112:113]
	v_cvt_pk_bf16_f32 v64, v80, v76
	v_cvt_pk_bf16_f32 v65, v70, v65
	v_cvt_pk_bf16_f32 v66, v77, v81
	v_cvt_pk_bf16_f32 v67, v73, v67
	global_store_dwordx4 v[68:69], v[64:67], off nt
	s_nop 1
	v_mov_b32_e32 v64, v52
	v_mov_b32_e32 v65, v60
	v_pk_mul_f32 v[64:65], v[64:65], v[126:127] op_sel_hi:[1,0]
	v_mov_b32_e32 v66, v48
	v_mul_f32_e32 v52, 0xbfb8aa3b, v65
	v_mov_b32_e32 v67, v56
	v_exp_f32_e32 v52, v52
	v_pk_mul_f32 v[66:67], v[66:67], v[126:127] op_sel_hi:[1,0]
	v_mov_b32_e32 v60, v53
	v_mul_f32_e32 v48, 0xbfb8aa3b, v67
	v_exp_f32_e32 v48, v48
	v_add_f32_e32 v52, 1.0, v52
	v_rcp_f32_e32 v52, v52
	v_add_u32_e32 v56, 0x80, v138
	v_add_f32_e32 v48, 1.0, v48
	v_rcp_f32_e32 v48, v48
	v_mul_f32_e32 v52, v65, v52
	v_mul_f32_e32 v64, v64, v52
	v_pk_mul_f32 v[52:53], v[60:61], v[126:127] op_sel_hi:[1,0]
	v_mad_i64_i32 v[68:69], s[30:31], v56, s58, v[134:135]
	v_mul_f32_e32 v65, v67, v48
	v_mul_f32_e32 v48, 0xbfb8aa3b, v53
	v_mov_b32_e32 v56, v49
	v_exp_f32_e32 v60, v48
	v_pk_mul_f32 v[48:49], v[56:57], v[126:127] op_sel_hi:[1,0]
	v_mul_f32_e32 v61, v66, v65
	v_mul_f32_e32 v56, 0xbfb8aa3b, v49
	v_exp_f32_e32 v56, v56
	v_add_f32_e32 v57, 1.0, v60
	v_rcp_f32_e32 v60, v57
	v_mov_b32_e32 v57, v62
	v_add_f32_e32 v56, 1.0, v56
	v_rcp_f32_e32 v65, v56
	v_mov_b32_e32 v56, v54
	v_pk_mul_f32 v[56:57], v[56:57], v[126:127] op_sel_hi:[1,0]
	v_mul_f32_e32 v53, v53, v60
	v_mul_f32_e32 v54, 0xbfb8aa3b, v57
	v_exp_f32_e32 v54, v54
	v_mul_f32_e32 v60, v52, v53
	v_mov_b32_e32 v53, v58
	v_mul_f32_e32 v49, v49, v65
	v_add_f32_e32 v52, 1.0, v54
	v_rcp_f32_e32 v54, v52
	v_mov_b32_e32 v52, v50
	v_pk_mul_f32 v[52:53], v[52:53], v[126:127] op_sel_hi:[1,0]
	v_mul_f32_e32 v65, v48, v49
	v_mul_f32_e32 v50, 0xbfb8aa3b, v53
	v_exp_f32_e32 v50, v50
	v_mul_f32_e32 v48, v57, v54
	v_mul_f32_e32 v54, v56, v48
	v_mov_b32_e32 v62, v55
	v_add_f32_e32 v48, 1.0, v50
	v_rcp_f32_e32 v56, v48
	v_pk_mul_f32 v[48:49], v[62:63], v[126:127] op_sel_hi:[1,0]
	v_mov_b32_e32 v58, v51
	v_mul_f32_e32 v50, 0xbfb8aa3b, v49
	v_exp_f32_e32 v55, v50
	v_pk_mul_f32 v[50:51], v[58:59], v[126:127] op_sel_hi:[1,0]
	v_mul_f32_e32 v53, v53, v56
	v_mul_f32_e32 v57, 0xbfb8aa3b, v51
	v_exp_f32_e32 v57, v57
	v_add_f32_e32 v55, 1.0, v55
	v_rcp_f32_e32 v55, v55
	v_add_f32_e32 v56, 1.0, v57
	v_rcp_f32_e32 v56, v56
	v_mul_f32_e32 v49, v49, v55
	v_mul_f32_e32 v49, v48, v49
	v_mul_f32_e32 v57, v52, v53
	v_mul_f32_e32 v48, v51, v56
	v_mul_f32_e32 v51, v50, v48
	v_lshl_add_u64 v[52:53], v[68:69], 0, v[112:113]
	v_cvt_pk_bf16_f32 v48, v64, v60
	v_cvt_pk_bf16_f32 v49, v54, v49
	v_cvt_pk_bf16_f32 v50, v61, v65
	v_cvt_pk_bf16_f32 v51, v57, v51
	global_store_dwordx4 v[52:53], v[48:51], off nt
	s_nop 1
	v_mov_b32_e32 v48, v36
	v_mov_b32_e32 v49, v44
	v_pk_mul_f32 v[48:49], v[48:49], v[124:125] op_sel_hi:[1,0]
	v_mov_b32_e32 v50, v32
	v_mul_f32_e32 v36, 0xbfb8aa3b, v49
	v_mov_b32_e32 v51, v40
	v_exp_f32_e32 v36, v36
	v_pk_mul_f32 v[50:51], v[50:51], v[124:125] op_sel_hi:[1,0]
	v_mov_b32_e32 v44, v37
	v_mul_f32_e32 v32, 0xbfb8aa3b, v51
	v_exp_f32_e32 v32, v32
	v_add_f32_e32 v36, 1.0, v36
	v_rcp_f32_e32 v36, v36
	v_add_u32_e32 v40, 0x90, v138
	v_add_f32_e32 v32, 1.0, v32
	v_rcp_f32_e32 v32, v32
	v_mul_f32_e32 v36, v49, v36
	v_mul_f32_e32 v48, v48, v36
	v_pk_mul_f32 v[36:37], v[44:45], v[124:125] op_sel_hi:[1,0]
	v_mad_i64_i32 v[52:53], s[30:31], v40, s58, v[134:135]
	v_mul_f32_e32 v49, v51, v32
	v_mul_f32_e32 v32, 0xbfb8aa3b, v37
	v_mov_b32_e32 v40, v33
	v_exp_f32_e32 v44, v32
	v_pk_mul_f32 v[32:33], v[40:41], v[124:125] op_sel_hi:[1,0]
	v_mul_f32_e32 v45, v50, v49
	v_mul_f32_e32 v40, 0xbfb8aa3b, v33
	v_exp_f32_e32 v40, v40
	v_add_f32_e32 v41, 1.0, v44
	v_rcp_f32_e32 v44, v41
	v_mov_b32_e32 v41, v46
	v_add_f32_e32 v40, 1.0, v40
	v_rcp_f32_e32 v49, v40
	v_mov_b32_e32 v40, v38
	v_pk_mul_f32 v[40:41], v[40:41], v[124:125] op_sel_hi:[1,0]
	v_mul_f32_e32 v37, v37, v44
	v_mul_f32_e32 v38, 0xbfb8aa3b, v41
	v_exp_f32_e32 v38, v38
	v_mul_f32_e32 v44, v36, v37
	v_mov_b32_e32 v37, v42
	v_mul_f32_e32 v33, v33, v49
	v_add_f32_e32 v36, 1.0, v38
	v_rcp_f32_e32 v38, v36
	v_mov_b32_e32 v36, v34
	v_pk_mul_f32 v[36:37], v[36:37], v[124:125] op_sel_hi:[1,0]
	v_mul_f32_e32 v49, v32, v33
	v_mul_f32_e32 v34, 0xbfb8aa3b, v37
	v_exp_f32_e32 v34, v34
	v_mul_f32_e32 v32, v41, v38
	v_mul_f32_e32 v38, v40, v32
	v_mov_b32_e32 v46, v39
	v_add_f32_e32 v32, 1.0, v34
	v_rcp_f32_e32 v40, v32
	v_pk_mul_f32 v[32:33], v[46:47], v[124:125] op_sel_hi:[1,0]
	v_mov_b32_e32 v42, v35
	v_mul_f32_e32 v34, 0xbfb8aa3b, v33
	v_exp_f32_e32 v39, v34
	v_pk_mul_f32 v[34:35], v[42:43], v[124:125] op_sel_hi:[1,0]
	v_mul_f32_e32 v37, v37, v40
	v_mul_f32_e32 v41, 0xbfb8aa3b, v35
	v_exp_f32_e32 v41, v41
	v_add_f32_e32 v39, 1.0, v39
	v_rcp_f32_e32 v39, v39
	v_add_f32_e32 v40, 1.0, v41
	v_rcp_f32_e32 v40, v40
	v_mul_f32_e32 v33, v33, v39
	v_mul_f32_e32 v33, v32, v33
	v_mul_f32_e32 v41, v36, v37
	v_mul_f32_e32 v32, v35, v40
	v_mul_f32_e32 v35, v34, v32
	v_lshl_add_u64 v[36:37], v[52:53], 0, v[112:113]
	v_cvt_pk_bf16_f32 v32, v48, v44
	v_cvt_pk_bf16_f32 v33, v38, v33
	v_cvt_pk_bf16_f32 v34, v45, v49
	v_cvt_pk_bf16_f32 v35, v41, v35
	global_store_dwordx4 v[36:37], v[32:35], off nt
	s_nop 1
	v_mov_b32_e32 v32, v20
	v_mov_b32_e32 v33, v28
	v_pk_mul_f32 v[32:33], v[32:33], v[122:123] op_sel_hi:[1,0]
	v_mov_b32_e32 v34, v16
	v_mul_f32_e32 v20, 0xbfb8aa3b, v33
	v_mov_b32_e32 v35, v24
	v_exp_f32_e32 v20, v20
	v_pk_mul_f32 v[34:35], v[34:35], v[122:123] op_sel_hi:[1,0]
	v_mov_b32_e32 v28, v21
	v_mul_f32_e32 v16, 0xbfb8aa3b, v35
	v_exp_f32_e32 v16, v16
	v_add_f32_e32 v20, 1.0, v20
	v_rcp_f32_e32 v20, v20
	v_add_u32_e32 v24, 0xa0, v138
	v_add_f32_e32 v16, 1.0, v16
	v_rcp_f32_e32 v16, v16
	v_mul_f32_e32 v20, v33, v20
	v_mul_f32_e32 v32, v32, v20
	v_pk_mul_f32 v[20:21], v[28:29], v[122:123] op_sel_hi:[1,0]
	v_mad_i64_i32 v[36:37], s[30:31], v24, s58, v[134:135]
	v_mul_f32_e32 v33, v35, v16
	v_mul_f32_e32 v16, 0xbfb8aa3b, v21
	v_mov_b32_e32 v24, v17
	v_exp_f32_e32 v28, v16
	v_pk_mul_f32 v[16:17], v[24:25], v[122:123] op_sel_hi:[1,0]
	v_mul_f32_e32 v29, v34, v33
	v_mul_f32_e32 v24, 0xbfb8aa3b, v17
	v_exp_f32_e32 v24, v24
	v_add_f32_e32 v25, 1.0, v28
	v_rcp_f32_e32 v28, v25
	v_mov_b32_e32 v25, v30
	v_add_f32_e32 v24, 1.0, v24
	v_rcp_f32_e32 v33, v24
	v_mov_b32_e32 v24, v22
	v_pk_mul_f32 v[24:25], v[24:25], v[122:123] op_sel_hi:[1,0]
	v_mul_f32_e32 v21, v21, v28
	v_mul_f32_e32 v22, 0xbfb8aa3b, v25
	v_exp_f32_e32 v22, v22
	v_mul_f32_e32 v28, v20, v21
	v_mov_b32_e32 v21, v26
	v_mul_f32_e32 v17, v17, v33
	v_add_f32_e32 v20, 1.0, v22
	v_rcp_f32_e32 v22, v20
	v_mov_b32_e32 v20, v18
	v_pk_mul_f32 v[20:21], v[20:21], v[122:123] op_sel_hi:[1,0]
	v_mul_f32_e32 v33, v16, v17
	v_mul_f32_e32 v18, 0xbfb8aa3b, v21
	v_exp_f32_e32 v18, v18
	v_mul_f32_e32 v16, v25, v22
	v_mul_f32_e32 v22, v24, v16
	v_mov_b32_e32 v30, v23
	v_add_f32_e32 v16, 1.0, v18
	v_rcp_f32_e32 v24, v16
	v_pk_mul_f32 v[16:17], v[30:31], v[122:123] op_sel_hi:[1,0]
	v_mov_b32_e32 v26, v19
	v_mul_f32_e32 v18, 0xbfb8aa3b, v17
	v_exp_f32_e32 v23, v18
	v_pk_mul_f32 v[18:19], v[26:27], v[122:123] op_sel_hi:[1,0]
	v_mul_f32_e32 v21, v21, v24
	v_mul_f32_e32 v25, 0xbfb8aa3b, v19
	v_exp_f32_e32 v25, v25
	v_add_f32_e32 v23, 1.0, v23
	v_rcp_f32_e32 v23, v23
	v_add_f32_e32 v24, 1.0, v25
	v_rcp_f32_e32 v24, v24
	v_mul_f32_e32 v17, v17, v23
	v_mul_f32_e32 v17, v16, v17
	v_mul_f32_e32 v25, v20, v21
	v_mul_f32_e32 v16, v19, v24
	v_mul_f32_e32 v19, v18, v16
	v_lshl_add_u64 v[20:21], v[36:37], 0, v[112:113]
	v_cvt_pk_bf16_f32 v16, v32, v28
	v_cvt_pk_bf16_f32 v17, v22, v17
	v_cvt_pk_bf16_f32 v18, v29, v33
	v_cvt_pk_bf16_f32 v19, v25, v19
	global_store_dwordx4 v[20:21], v[16:19], off nt
	s_nop 1
	v_mov_b32_e32 v16, v4
	v_mov_b32_e32 v17, v12
	v_pk_mul_f32 v[16:17], v[16:17], v[120:121] op_sel_hi:[1,0]
	v_mov_b32_e32 v18, v0
	v_mul_f32_e32 v4, 0xbfb8aa3b, v17
	v_mov_b32_e32 v19, v8
	v_exp_f32_e32 v4, v4
	v_pk_mul_f32 v[18:19], v[18:19], v[120:121] op_sel_hi:[1,0]
	v_mov_b32_e32 v12, v5
	v_mul_f32_e32 v0, 0xbfb8aa3b, v19
	v_exp_f32_e32 v0, v0
	v_add_f32_e32 v4, 1.0, v4
	v_rcp_f32_e32 v4, v4
	v_add_u32_e32 v8, 0xb0, v138
	v_add_f32_e32 v0, 1.0, v0
	v_rcp_f32_e32 v0, v0
	v_mul_f32_e32 v4, v17, v4
	v_mul_f32_e32 v16, v16, v4
	v_pk_mul_f32 v[4:5], v[12:13], v[120:121] op_sel_hi:[1,0]
	v_mad_i64_i32 v[20:21], s[30:31], v8, s58, v[134:135]
	v_mul_f32_e32 v17, v19, v0
	v_mul_f32_e32 v0, 0xbfb8aa3b, v5
	v_mov_b32_e32 v8, v1
	v_exp_f32_e32 v12, v0
	v_pk_mul_f32 v[0:1], v[8:9], v[120:121] op_sel_hi:[1,0]
	v_mul_f32_e32 v13, v18, v17
	v_mul_f32_e32 v8, 0xbfb8aa3b, v1
	v_exp_f32_e32 v8, v8
	v_add_f32_e32 v9, 1.0, v12
	v_rcp_f32_e32 v12, v9
	v_mov_b32_e32 v9, v14
	v_add_f32_e32 v8, 1.0, v8
	v_rcp_f32_e32 v17, v8
	v_mov_b32_e32 v8, v6
	v_pk_mul_f32 v[8:9], v[8:9], v[120:121] op_sel_hi:[1,0]
	v_mul_f32_e32 v5, v5, v12
	v_mul_f32_e32 v6, 0xbfb8aa3b, v9
	v_exp_f32_e32 v6, v6
	v_mul_f32_e32 v12, v4, v5
	v_mov_b32_e32 v5, v10
	v_mul_f32_e32 v1, v1, v17
	v_add_f32_e32 v4, 1.0, v6
	v_rcp_f32_e32 v6, v4
	v_mov_b32_e32 v4, v2
	v_pk_mul_f32 v[4:5], v[4:5], v[120:121] op_sel_hi:[1,0]
	v_mul_f32_e32 v17, v0, v1
	v_mul_f32_e32 v2, 0xbfb8aa3b, v5
	v_exp_f32_e32 v2, v2
	v_mul_f32_e32 v0, v9, v6
	v_mul_f32_e32 v6, v8, v0
	v_mov_b32_e32 v14, v7
	v_add_f32_e32 v0, 1.0, v2
	v_rcp_f32_e32 v8, v0
	v_pk_mul_f32 v[0:1], v[14:15], v[120:121] op_sel_hi:[1,0]
	v_mov_b32_e32 v10, v3
	v_mul_f32_e32 v2, 0xbfb8aa3b, v1
	v_exp_f32_e32 v7, v2
	v_pk_mul_f32 v[2:3], v[10:11], v[120:121] op_sel_hi:[1,0]
	v_mul_f32_e32 v5, v5, v8
	v_mul_f32_e32 v9, 0xbfb8aa3b, v3
	v_exp_f32_e32 v9, v9
	v_add_f32_e32 v7, 1.0, v7
	v_rcp_f32_e32 v7, v7
	v_add_f32_e32 v8, 1.0, v9
	v_rcp_f32_e32 v8, v8
	v_mul_f32_e32 v1, v1, v7
	v_mul_f32_e32 v1, v0, v1
	v_mul_f32_e32 v9, v4, v5
	v_mul_f32_e32 v0, v3, v8
	v_mul_f32_e32 v3, v2, v0
	v_lshl_add_u64 v[4:5], v[20:21], 0, v[112:113]
	v_cvt_pk_bf16_f32 v0, v16, v12
	v_cvt_pk_bf16_f32 v1, v6, v1
	v_cvt_pk_bf16_f32 v2, v13, v17
	v_cvt_pk_bf16_f32 v3, v9, v3
	global_store_dwordx4 v[4:5], v[0:3], off nt
	s_cbranch_vccnz .LBB0_4341
	s_andn2_b64 vcc, exec, s[12:13]
	s_cbranch_vccnz .LBB0_4340
	s_barrier
	s_branch .LBB0_4340

.LBB0_4461:
	v_lshl_or_b32 v136, s66, 8, v148
	v_ashrrev_i32_e32 v137, 31, v136
	v_add_u32_e32 v192, s48, v138
	v_ashrrev_i32_e32 v193, 31, v192
	v_lshlrev_b64 v[192:193], 2, v[192:193]
	v_lshl_add_u64 v[194:195], s[12:13], 0, v[192:193]
	v_lshl_add_u64 v[192:193], s[8:9], 0, v[192:193]
	v_cmp_gt_i32_e32 vcc, s51, v138
	s_and_saveexec_b64 s[36:37], vcc
	global_load_dword v160, v[192:193], off
	global_load_dword v162, v[194:195], off
	s_or_b64 exec, exec, s[36:37]
	v_add_u32_e32 v196, 16, v138
	v_cmp_gt_i32_e32 vcc, s51, v196
	s_and_saveexec_b64 s[36:37], vcc
	global_load_dword v164, v[192:193], off offset:64
	global_load_dword v166, v[194:195], off offset:64
	s_or_b64 exec, exec, s[36:37]
	v_add_u32_e32 v196, 32, v138
	v_cmp_gt_i32_e32 vcc, s51, v196
	s_and_saveexec_b64 s[36:37], vcc
	global_load_dword v168, v[192:193], off offset:128
	global_load_dword v170, v[194:195], off offset:128
	s_or_b64 exec, exec, s[36:37]
	v_add_u32_e32 v196, 48, v138
	v_cmp_gt_i32_e32 vcc, s51, v196
	s_and_saveexec_b64 s[36:37], vcc
	global_load_dword v172, v[192:193], off offset:192
	global_load_dword v174, v[194:195], off offset:192
	s_or_b64 exec, exec, s[36:37]
	v_add_u32_e32 v196, 128, v138
	v_cmp_gt_i32_e32 vcc, s51, v196
	s_and_saveexec_b64 s[36:37], vcc
	global_load_dword v176, v[192:193], off offset:512
	global_load_dword v178, v[194:195], off offset:512
	s_or_b64 exec, exec, s[36:37]
	v_add_u32_e32 v196, 144, v138
	v_cmp_gt_i32_e32 vcc, s51, v196
	s_and_saveexec_b64 s[36:37], vcc
	global_load_dword v180, v[192:193], off offset:576
	global_load_dword v182, v[194:195], off offset:576
	s_or_b64 exec, exec, s[36:37]
	v_add_u32_e32 v196, 160, v138
	v_cmp_gt_i32_e32 vcc, s51, v196
	s_and_saveexec_b64 s[36:37], vcc
	global_load_dword v184, v[192:193], off offset:640
	global_load_dword v186, v[194:195], off offset:640
	s_or_b64 exec, exec, s[36:37]
	v_add_u32_e32 v196, 176, v138
	v_cmp_gt_i32_e32 vcc, s51, v196
	s_and_saveexec_b64 s[36:37], vcc
	global_load_dword v188, v[192:193], off offset:704
	global_load_dword v190, v[194:195], off offset:704
	s_or_b64 exec, exec, s[36:37]
	s_waitcnt vmcnt(0)
	v_cmp_gt_i32_e32 vcc, s51, v138
	s_and_saveexec_b64 s[36:37], vcc
	s_cbranch_execz .LBB0_4463
	v_mov_b32_e32 v152, 0
	v_mov_b32_e32 v153, 0
	v_mov_b32_e32 v154, 0
	v_mov_b32_e32 v155, 0
	v_ashrrev_i32_e32 v161, 31, v160
	v_mul_f32_e32 v162, 0x41800000, v162
	v_pk_mul_f32 v[112:113], v[112:113], v[162:163] op_sel_hi:[1,0]
	v_pk_mul_f32 v[116:117], v[116:117], v[162:163] op_sel_hi:[1,0]
	v_pk_mul_f32 v[120:121], v[120:121], v[162:163] op_sel_hi:[1,0]
	v_pk_mul_f32 v[124:125], v[124:125], v[162:163] op_sel_hi:[1,0]
	v_cvt_pk_fp8_f32 v152, v112, v113
	v_cvt_pk_fp8_f32 v153, v116, v117
	v_cvt_pk_fp8_f32 v154, v120, v121
	v_cvt_pk_fp8_f32 v155, v124, v125
	v_pk_mul_f32 v[114:115], v[114:115], v[162:163] op_sel_hi:[1,0]
	v_pk_mul_f32 v[118:119], v[118:119], v[162:163] op_sel_hi:[1,0]
	v_pk_mul_f32 v[122:123], v[122:123], v[162:163] op_sel_hi:[1,0]
	v_pk_mul_f32 v[126:127], v[126:127], v[162:163] op_sel_hi:[1,0]
	v_cvt_pk_fp8_f32 v152, v114, v115 op_sel:[0,0,1]
	v_cvt_pk_fp8_f32 v153, v118, v119 op_sel:[0,0,1]
	v_cvt_pk_fp8_f32 v154, v122, v123 op_sel:[0,0,1]
	v_cvt_pk_fp8_f32 v155, v126, v127 op_sel:[0,0,1]
	v_lshlrev_b64 v[112:113], 10, v[160:161]
	v_lshl_add_u64 v[112:113], s[6:7], 0, v[112:113]
	v_lshl_add_u64 v[112:113], v[112:113], 0, v[136:137]
	global_store_dwordx4 v[112:113], v[152:155], off nt
.LBB0_4463:
	s_or_b64 exec, exec, s[36:37]
	v_or_b32_e32 v112, 16, v138
	v_cmp_gt_i32_e32 vcc, s51, v112
	s_and_saveexec_b64 s[36:37], vcc
	s_cbranch_execz .LBB0_4465
	v_mov_b32_e32 v112, 0
	v_mov_b32_e32 v113, 0
	v_mov_b32_e32 v114, 0
	v_mov_b32_e32 v115, 0
	v_ashrrev_i32_e32 v165, 31, v164
	v_mul_f32_e32 v166, 0x41800000, v166
	v_pk_mul_f32 v[96:97], v[96:97], v[166:167] op_sel_hi:[1,0]
	v_pk_mul_f32 v[100:101], v[100:101], v[166:167] op_sel_hi:[1,0]
	v_pk_mul_f32 v[104:105], v[104:105], v[166:167] op_sel_hi:[1,0]
	v_pk_mul_f32 v[108:109], v[108:109], v[166:167] op_sel_hi:[1,0]
	v_cvt_pk_fp8_f32 v112, v96, v97
	v_cvt_pk_fp8_f32 v113, v100, v101
	v_cvt_pk_fp8_f32 v114, v104, v105
	v_cvt_pk_fp8_f32 v115, v108, v109
	v_pk_mul_f32 v[98:99], v[98:99], v[166:167] op_sel_hi:[1,0]
	v_pk_mul_f32 v[102:103], v[102:103], v[166:167] op_sel_hi:[1,0]
	v_pk_mul_f32 v[106:107], v[106:107], v[166:167] op_sel_hi:[1,0]
	v_pk_mul_f32 v[110:111], v[110:111], v[166:167] op_sel_hi:[1,0]
	v_cvt_pk_fp8_f32 v112, v98, v99 op_sel:[0,0,1]
	v_cvt_pk_fp8_f32 v113, v102, v103 op_sel:[0,0,1]
	v_cvt_pk_fp8_f32 v114, v106, v107 op_sel:[0,0,1]
	v_cvt_pk_fp8_f32 v115, v110, v111 op_sel:[0,0,1]
	v_lshlrev_b64 v[96:97], 10, v[164:165]
	v_lshl_add_u64 v[96:97], s[6:7], 0, v[96:97]
	v_lshl_add_u64 v[96:97], v[96:97], 0, v[136:137]
	global_store_dwordx4 v[96:97], v[112:115], off nt
.LBB0_4465:
	s_or_b64 exec, exec, s[36:37]
	v_or_b32_e32 v96, 32, v138
	v_cmp_gt_i32_e32 vcc, s51, v96
	s_and_saveexec_b64 s[36:37], vcc
	s_cbranch_execz .LBB0_4467
	v_mov_b32_e32 v96, 0
	v_mov_b32_e32 v97, 0
	v_mov_b32_e32 v98, 0
	v_mov_b32_e32 v99, 0
	v_ashrrev_i32_e32 v169, 31, v168
	v_mul_f32_e32 v170, 0x41800000, v170
	v_pk_mul_f32 v[80:81], v[80:81], v[170:171] op_sel_hi:[1,0]
	v_pk_mul_f32 v[84:85], v[84:85], v[170:171] op_sel_hi:[1,0]
	v_pk_mul_f32 v[88:89], v[88:89], v[170:171] op_sel_hi:[1,0]
	v_pk_mul_f32 v[92:93], v[92:93], v[170:171] op_sel_hi:[1,0]
	v_cvt_pk_fp8_f32 v96, v80, v81
	v_cvt_pk_fp8_f32 v97, v84, v85
	v_cvt_pk_fp8_f32 v98, v88, v89
	v_cvt_pk_fp8_f32 v99, v92, v93
	v_pk_mul_f32 v[82:83], v[82:83], v[170:171] op_sel_hi:[1,0]
	v_pk_mul_f32 v[86:87], v[86:87], v[170:171] op_sel_hi:[1,0]
	v_pk_mul_f32 v[90:91], v[90:91], v[170:171] op_sel_hi:[1,0]
	v_pk_mul_f32 v[94:95], v[94:95], v[170:171] op_sel_hi:[1,0]
	v_cvt_pk_fp8_f32 v96, v82, v83 op_sel:[0,0,1]
	v_cvt_pk_fp8_f32 v97, v86, v87 op_sel:[0,0,1]
	v_cvt_pk_fp8_f32 v98, v90, v91 op_sel:[0,0,1]
	v_cvt_pk_fp8_f32 v99, v94, v95 op_sel:[0,0,1]
	v_lshlrev_b64 v[80:81], 10, v[168:169]
	v_lshl_add_u64 v[80:81], s[6:7], 0, v[80:81]
	v_lshl_add_u64 v[80:81], v[80:81], 0, v[136:137]
	global_store_dwordx4 v[80:81], v[96:99], off nt
.LBB0_4467:
	s_or_b64 exec, exec, s[36:37]
	v_or_b32_e32 v80, 48, v138
	v_cmp_gt_i32_e32 vcc, s51, v80
	s_and_saveexec_b64 s[36:37], vcc
	s_cbranch_execz .LBB0_4469
	v_mov_b32_e32 v80, 0
	v_mov_b32_e32 v81, 0
	v_mov_b32_e32 v82, 0
	v_mov_b32_e32 v83, 0
	v_ashrrev_i32_e32 v173, 31, v172
	v_mul_f32_e32 v174, 0x41800000, v174
	v_pk_mul_f32 v[64:65], v[64:65], v[174:175] op_sel_hi:[1,0]
	v_pk_mul_f32 v[68:69], v[68:69], v[174:175] op_sel_hi:[1,0]
	v_pk_mul_f32 v[72:73], v[72:73], v[174:175] op_sel_hi:[1,0]
	v_pk_mul_f32 v[76:77], v[76:77], v[174:175] op_sel_hi:[1,0]
	v_cvt_pk_fp8_f32 v80, v64, v65
	v_cvt_pk_fp8_f32 v81, v68, v69
	v_cvt_pk_fp8_f32 v82, v72, v73
	v_cvt_pk_fp8_f32 v83, v76, v77
	v_pk_mul_f32 v[66:67], v[66:67], v[174:175] op_sel_hi:[1,0]
	v_pk_mul_f32 v[70:71], v[70:71], v[174:175] op_sel_hi:[1,0]
	v_pk_mul_f32 v[74:75], v[74:75], v[174:175] op_sel_hi:[1,0]
	v_pk_mul_f32 v[78:79], v[78:79], v[174:175] op_sel_hi:[1,0]
	v_cvt_pk_fp8_f32 v80, v66, v67 op_sel:[0,0,1]
	v_cvt_pk_fp8_f32 v81, v70, v71 op_sel:[0,0,1]
	v_cvt_pk_fp8_f32 v82, v74, v75 op_sel:[0,0,1]
	v_cvt_pk_fp8_f32 v83, v78, v79 op_sel:[0,0,1]
	v_lshlrev_b64 v[64:65], 10, v[172:173]
	v_lshl_add_u64 v[64:65], s[6:7], 0, v[64:65]
	v_lshl_add_u64 v[64:65], v[64:65], 0, v[136:137]
	global_store_dwordx4 v[64:65], v[80:83], off nt
.LBB0_4469:
	s_or_b64 exec, exec, s[36:37]
	v_add_u32_e32 v64, 0x80, v138
	v_cmp_gt_i32_e32 vcc, s51, v64
	s_and_saveexec_b64 s[36:37], vcc
	s_cbranch_execz .LBB0_4471
	v_mov_b32_e32 v64, 0
	v_mov_b32_e32 v65, 0
	v_mov_b32_e32 v66, 0
	v_mov_b32_e32 v67, 0
	v_ashrrev_i32_e32 v177, 31, v176
	v_mul_f32_e32 v178, 0x41800000, v178
	v_pk_mul_f32 v[48:49], v[48:49], v[178:179] op_sel_hi:[1,0]
	v_pk_mul_f32 v[52:53], v[52:53], v[178:179] op_sel_hi:[1,0]
	v_pk_mul_f32 v[56:57], v[56:57], v[178:179] op_sel_hi:[1,0]
	v_pk_mul_f32 v[60:61], v[60:61], v[178:179] op_sel_hi:[1,0]
	v_cvt_pk_fp8_f32 v64, v48, v49
	v_cvt_pk_fp8_f32 v65, v52, v53
	v_cvt_pk_fp8_f32 v66, v56, v57
	v_cvt_pk_fp8_f32 v67, v60, v61
	v_pk_mul_f32 v[50:51], v[50:51], v[178:179] op_sel_hi:[1,0]
	v_pk_mul_f32 v[54:55], v[54:55], v[178:179] op_sel_hi:[1,0]
	v_pk_mul_f32 v[58:59], v[58:59], v[178:179] op_sel_hi:[1,0]
	v_pk_mul_f32 v[62:63], v[62:63], v[178:179] op_sel_hi:[1,0]
	v_cvt_pk_fp8_f32 v64, v50, v51 op_sel:[0,0,1]
	v_cvt_pk_fp8_f32 v65, v54, v55 op_sel:[0,0,1]
	v_cvt_pk_fp8_f32 v66, v58, v59 op_sel:[0,0,1]
	v_cvt_pk_fp8_f32 v67, v62, v63 op_sel:[0,0,1]
	v_lshlrev_b64 v[48:49], 10, v[176:177]
	v_lshl_add_u64 v[48:49], s[6:7], 0, v[48:49]
	v_lshl_add_u64 v[48:49], v[48:49], 0, v[136:137]
	global_store_dwordx4 v[48:49], v[64:67], off nt
.LBB0_4471:
	s_or_b64 exec, exec, s[36:37]
	v_add_u32_e32 v48, 0x90, v138
	v_cmp_gt_i32_e32 vcc, s51, v48
	s_and_saveexec_b64 s[36:37], vcc
	s_cbranch_execz .LBB0_4473
	v_mov_b32_e32 v48, 0
	v_mov_b32_e32 v49, 0
	v_mov_b32_e32 v50, 0
	v_mov_b32_e32 v51, 0
	v_ashrrev_i32_e32 v181, 31, v180
	v_mul_f32_e32 v182, 0x41800000, v182
	v_pk_mul_f32 v[32:33], v[32:33], v[182:183] op_sel_hi:[1,0]
	v_pk_mul_f32 v[36:37], v[36:37], v[182:183] op_sel_hi:[1,0]
	v_pk_mul_f32 v[40:41], v[40:41], v[182:183] op_sel_hi:[1,0]
	v_pk_mul_f32 v[44:45], v[44:45], v[182:183] op_sel_hi:[1,0]
	v_cvt_pk_fp8_f32 v48, v32, v33
	v_cvt_pk_fp8_f32 v49, v36, v37
	v_cvt_pk_fp8_f32 v50, v40, v41
	v_cvt_pk_fp8_f32 v51, v44, v45
	v_pk_mul_f32 v[34:35], v[34:35], v[182:183] op_sel_hi:[1,0]
	v_pk_mul_f32 v[38:39], v[38:39], v[182:183] op_sel_hi:[1,0]
	v_pk_mul_f32 v[42:43], v[42:43], v[182:183] op_sel_hi:[1,0]
	v_pk_mul_f32 v[46:47], v[46:47], v[182:183] op_sel_hi:[1,0]
	v_cvt_pk_fp8_f32 v48, v34, v35 op_sel:[0,0,1]
	v_cvt_pk_fp8_f32 v49, v38, v39 op_sel:[0,0,1]
	v_cvt_pk_fp8_f32 v50, v42, v43 op_sel:[0,0,1]
	v_cvt_pk_fp8_f32 v51, v46, v47 op_sel:[0,0,1]
	v_lshlrev_b64 v[32:33], 10, v[180:181]
	v_lshl_add_u64 v[32:33], s[6:7], 0, v[32:33]
	v_lshl_add_u64 v[32:33], v[32:33], 0, v[136:137]
	global_store_dwordx4 v[32:33], v[48:51], off nt
.LBB0_4473:
	s_or_b64 exec, exec, s[36:37]
	v_cmp_gt_i32_e32 vcc, s51, v151
	s_and_saveexec_b64 s[36:37], vcc
	s_cbranch_execz .LBB0_4475
	v_mov_b32_e32 v32, 0
	v_mov_b32_e32 v33, 0
	v_mov_b32_e32 v34, 0
	v_mov_b32_e32 v35, 0
	v_ashrrev_i32_e32 v185, 31, v184
	v_mul_f32_e32 v186, 0x41800000, v186
	v_pk_mul_f32 v[16:17], v[16:17], v[186:187] op_sel_hi:[1,0]
	v_pk_mul_f32 v[20:21], v[20:21], v[186:187] op_sel_hi:[1,0]
	v_pk_mul_f32 v[24:25], v[24:25], v[186:187] op_sel_hi:[1,0]
	v_pk_mul_f32 v[28:29], v[28:29], v[186:187] op_sel_hi:[1,0]
	v_cvt_pk_fp8_f32 v32, v16, v17
	v_cvt_pk_fp8_f32 v33, v20, v21
	v_cvt_pk_fp8_f32 v34, v24, v25
	v_cvt_pk_fp8_f32 v35, v28, v29
	v_pk_mul_f32 v[18:19], v[18:19], v[186:187] op_sel_hi:[1,0]
	v_pk_mul_f32 v[22:23], v[22:23], v[186:187] op_sel_hi:[1,0]
	v_pk_mul_f32 v[26:27], v[26:27], v[186:187] op_sel_hi:[1,0]
	v_pk_mul_f32 v[30:31], v[30:31], v[186:187] op_sel_hi:[1,0]
	v_cvt_pk_fp8_f32 v32, v18, v19 op_sel:[0,0,1]
	v_cvt_pk_fp8_f32 v33, v22, v23 op_sel:[0,0,1]
	v_cvt_pk_fp8_f32 v34, v26, v27 op_sel:[0,0,1]
	v_cvt_pk_fp8_f32 v35, v30, v31 op_sel:[0,0,1]
	v_lshlrev_b64 v[16:17], 10, v[184:185]
	v_lshl_add_u64 v[16:17], s[6:7], 0, v[16:17]
	v_lshl_add_u64 v[16:17], v[16:17], 0, v[136:137]
	global_store_dwordx4 v[16:17], v[32:35], off nt
.LBB0_4475:
	s_or_b64 exec, exec, s[36:37]
	v_cmp_gt_i32_e32 vcc, s51, v141
	s_and_saveexec_b64 s[36:37], vcc
	s_cbranch_execz .LBB0_4477
	v_mov_b32_e32 v16, 0
	v_mov_b32_e32 v17, 0
	v_mov_b32_e32 v18, 0
	v_mov_b32_e32 v19, 0
	v_ashrrev_i32_e32 v189, 31, v188
	v_mul_f32_e32 v190, 0x41800000, v190
	v_pk_mul_f32 v[0:1], v[0:1], v[190:191] op_sel_hi:[1,0]
	v_pk_mul_f32 v[4:5], v[4:5], v[190:191] op_sel_hi:[1,0]
	v_pk_mul_f32 v[8:9], v[8:9], v[190:191] op_sel_hi:[1,0]
	v_pk_mul_f32 v[12:13], v[12:13], v[190:191] op_sel_hi:[1,0]
	v_cvt_pk_fp8_f32 v16, v0, v1
	v_cvt_pk_fp8_f32 v17, v4, v5
	v_cvt_pk_fp8_f32 v18, v8, v9
	v_cvt_pk_fp8_f32 v19, v12, v13
	v_pk_mul_f32 v[2:3], v[2:3], v[190:191] op_sel_hi:[1,0]
	v_pk_mul_f32 v[6:7], v[6:7], v[190:191] op_sel_hi:[1,0]
	v_pk_mul_f32 v[10:11], v[10:11], v[190:191] op_sel_hi:[1,0]
	v_pk_mul_f32 v[14:15], v[14:15], v[190:191] op_sel_hi:[1,0]
	v_cvt_pk_fp8_f32 v16, v2, v3 op_sel:[0,0,1]
	v_cvt_pk_fp8_f32 v17, v6, v7 op_sel:[0,0,1]
	v_cvt_pk_fp8_f32 v18, v10, v11 op_sel:[0,0,1]
	v_cvt_pk_fp8_f32 v19, v14, v15 op_sel:[0,0,1]
	v_lshlrev_b64 v[0:1], 10, v[188:189]
	v_lshl_add_u64 v[0:1], s[6:7], 0, v[0:1]
	v_lshl_add_u64 v[0:1], v[0:1], 0, v[136:137]
	global_store_dwordx4 v[0:1], v[16:19], off nt

.LBB0_4554:
	s_ashr_i32 s5, s4, 31
	s_lshl_b64 s[12:13], s[4:5], 10
	v_lshl_add_u64 v[12:13], v[0:1], 0, s[12:13]
	global_load_dwordx2 v[6:7], v[2:3], off
	global_load_dwordx2 v[8:9], v[2:3], off offset:512
	global_load_dwordx2 v[10:11], v[2:3], off offset:1024
	global_load_dword v30, v[12:13], off
	global_load_dword v31, v[12:13], off offset:1024
	global_load_dword v32, v[12:13], off offset:256
	global_load_dword v36, v[12:13], off offset:1280
	global_load_dword v40, v[12:13], off offset:512
	global_load_dword v44, v[12:13], off offset:1536
	global_load_dword v52, v[12:13], off offset:1792
	global_load_dword v48, v[12:13], off offset:768
	global_load_dwordx2 v[14:15], v[2:3], off offset:1536
	s_add_i32 s0, s0, s2
	s_add_i32 s4, s4, s11
	v_lshl_add_u64 v[2:3], v[2:3], 0, s[6:7]
	s_cmp_lt_i32 s0, 0x8000
	s_waitcnt vmcnt(5)
	v_cvt_pk_f32_fp8_e32 v[34:35], v36
	v_cvt_pk_f32_fp8_sdwa v[36:37], v36 src0_sel:WORD_1
	v_lshlrev_b32_e32 v12, 16, v6
	v_and_b32_e32 v13, 0xffff0000, v6
	v_lshlrev_b32_e32 v16, 16, v7
	v_and_b32_e32 v17, 0xffff0000, v7
	v_lshlrev_b32_e32 v18, 16, v8
	v_and_b32_e32 v19, 0xffff0000, v8
	v_lshlrev_b32_e32 v20, 16, v9
	v_and_b32_e32 v21, 0xffff0000, v9
	v_lshlrev_b32_e32 v22, 16, v10
	v_and_b32_e32 v23, 0xffff0000, v10
	v_lshlrev_b32_e32 v24, 16, v11
	v_and_b32_e32 v25, 0xffff0000, v11
	s_waitcnt vmcnt(0)
	v_lshlrev_b32_e32 v26, 16, v14
	v_and_b32_e32 v27, 0xffff0000, v14
	v_lshlrev_b32_e32 v28, 16, v15
	v_and_b32_e32 v29, 0xffff0000, v15
	v_cvt_pk_f32_fp8_e32 v[6:7], v30
	v_cvt_pk_f32_fp8_sdwa v[8:9], v30 src0_sel:WORD_1
	v_cvt_pk_f32_fp8_e32 v[10:11], v31
	v_cvt_pk_f32_fp8_sdwa v[14:15], v31 src0_sel:WORD_1
	v_cvt_pk_f32_fp8_e32 v[30:31], v32
	v_cvt_pk_f32_fp8_sdwa v[32:33], v32 src0_sel:WORD_1
	v_cvt_pk_f32_fp8_e32 v[38:39], v40
	v_cvt_pk_f32_fp8_sdwa v[40:41], v40 src0_sel:WORD_1
	v_cvt_pk_f32_fp8_e32 v[42:43], v44
	v_cvt_pk_f32_fp8_sdwa v[44:45], v44 src0_sel:WORD_1
	v_cvt_pk_f32_fp8_e32 v[46:47], v48
	v_cvt_pk_f32_fp8_sdwa v[48:49], v48 src0_sel:WORD_1
	v_cvt_pk_f32_fp8_e32 v[50:51], v52
	v_cvt_pk_f32_fp8_sdwa v[52:53], v52 src0_sel:WORD_1
	v_pk_add_f32 v[6:7], v[6:7], v[10:11]
	v_pk_add_f32 v[8:9], v[8:9], v[14:15]
	v_pk_add_f32 v[10:11], v[30:31], v[34:35]
	v_pk_add_f32 v[14:15], v[32:33], v[36:37]
	v_pk_add_f32 v[30:31], v[38:39], v[42:43]
	v_pk_add_f32 v[32:33], v[40:41], v[44:45]
	v_pk_add_f32 v[34:35], v[46:47], v[50:51]
	v_pk_add_f32 v[36:37], v[48:49], v[52:53]
	v_pk_fma_f32 v[6:7], v[6:7], s[10:11], v[12:13] op_sel_hi:[1,0,1]
	v_pk_fma_f32 v[8:9], v[8:9], s[10:11], v[16:17] op_sel_hi:[1,0,1]
	v_pk_fma_f32 v[10:11], v[10:11], s[10:11], v[18:19] op_sel_hi:[1,0,1]
	v_pk_fma_f32 v[12:13], v[14:15], s[10:11], v[20:21] op_sel_hi:[1,0,1]
	v_pk_fma_f32 v[14:15], v[30:31], s[10:11], v[22:23] op_sel_hi:[1,0,1]
	v_pk_fma_f32 v[16:17], v[32:33], s[10:11], v[24:25] op_sel_hi:[1,0,1]
	v_pk_fma_f32 v[18:19], v[34:35], s[10:11], v[26:27] op_sel_hi:[1,0,1]
	v_pk_fma_f32 v[20:21], v[36:37], s[10:11], v[28:29] op_sel_hi:[1,0,1]
	global_store_dwordx4 v[4:5], v[6:9], off offset:-3072 nt
	global_store_dwordx4 v[4:5], v[10:13], off offset:-2048 nt
	global_store_dwordx4 v[4:5], v[14:17], off offset:-1024 nt
	global_store_dwordx4 v[4:5], v[18:21], off nt
	v_lshl_add_u64 v[4:5], v[4:5], 0, s[8:9]
	s_cbranch_scc1 .LBB0_4554
